# hand-written agg kernel: the wave's two columns gathered concurrently in half-waves (2 dependent round trips instead of 4), 4-byte weight write-back; K1 as baseline
# speedup vs baseline: 1.0908x; 1.0253x over previous
_Z9k1_kernelPKfS0_S0_PDF16_PiPfP15HIP_vector_typeIiLj2EES6_:
	v_and_b32_e32 v80, 63, v0
	v_lshrrev_b32_e32 v81, 6, v0
	s_cmpk_lt_u32 s2, 0x60
	s_mov_b64 s[4:5], -1
	s_cbranch_scc0 .LBB0_4
	v_lshlrev_b32_e32 v1, 4, v0
	v_and_b32_e32 v4, 0x70, v1
	v_and_b32_e32 v2, 0x1f0, v1
	v_and_b32_e32 v8, 0xe00, v1
	v_or_b32_e32 v1, 0x100, v0
	v_lshrrev_b32_e32 v9, 3, v1
	v_lshlrev_b32_e32 v1, 4, v1
	v_and_b32_e32 v11, 0x1e00, v1
	v_or_b32_e32 v1, 0x200, v0
	v_lshrrev_b32_e32 v12, 3, v1
	v_lshlrev_b32_e32 v1, 4, v1
	v_and_b32_e32 v14, 0x2e00, v1
	v_or_b32_e32 v1, 0x300, v0
	s_load_dwordx4 s[4:7], s[0:1], 0x8
	s_load_dwordx2 s[8:9], s[0:1], 0x18
	v_or_b32_e32 v5, 0x4200, v2
	v_lshrrev_b32_e32 v2, 5, v80
	v_lshlrev_b32_e32 v83, 5, v81
	v_and_b32_e32 v84, 31, v0
	v_lshrrev_b32_e32 v15, 3, v1
	v_lshlrev_b32_e32 v1, 4, v1
	v_or_b32_e32 v3, v83, v84
	s_movk_i32 s10, 0x84
	v_and_b32_e32 v17, 0x3e00, v1
	v_lshlrev_b32_e32 v1, 2, v2
	v_mad_u32_u24 v85, v3, s10, v1
	v_lshlrev_b32_e32 v1, 4, v84
	v_lshlrev_b32_e32 v18, 9, v2
	v_or_b32_e32 v2, v8, v1
	v_mov_b32_e32 v3, 0
	s_waitcnt lgkmcnt(0)
	v_lshl_add_u64 v[66:67], s[6:7], 0, v[2:3]
	v_or_b32_e32 v2, v17, v1
	s_lshl_b32 s3, s2, 7
	v_lshrrev_b32_e32 v82, 3, v0
	v_lshl_add_u64 v[68:69], s[6:7], 0, v[2:3]
	v_or_b32_e32 v2, v14, v1
	v_and_b32_e32 v0, 7, v0
	v_or_b32_e32 v16, s3, v15
	v_lshl_add_u64 v[70:71], s[6:7], 0, v[2:3]
	v_or_b32_e32 v2, v11, v1
	v_lshlrev_b32_e32 v34, 4, v0
	v_or_b32_e32 v13, s3, v12
	v_lshl_add_u64 v[72:73], s[6:7], 0, v[2:3]
	v_lshl_or_b32 v2, v16, 10, v34
	v_or_b32_e32 v10, s3, v9
	v_lshl_add_u64 v[0:1], s[4:5], 0, v[2:3]
	v_lshl_or_b32 v2, v13, 10, v34
	v_lshl_add_u64 v[74:75], s[4:5], 0, v[2:3]
	v_lshl_or_b32 v2, v10, 10, v34
	v_mov_b32_e32 v6, 0x4200
	v_lshl_add_u64 v[76:77], s[4:5], 0, v[2:3]
	s_lshl_b32 s6, s2, 17
	v_lshlrev_b32_e32 v2, 10, v82
	v_lshl_or_b32 v6, v84, 2, v6
	v_mul_u32_u24_e32 v7, 0x84, v82
	v_mul_u32_u24_e32 v9, 0x84, v9
	v_mul_u32_u24_e32 v12, 0x84, v12
	v_mul_u32_u24_e32 v15, 0x84, v15
	v_or_b32_e32 v19, 0x400, v18
	v_or_b32_e32 v20, 0x800, v18
	v_or_b32_e32 v21, 0xc00, v18
	v_or_b32_e32 v22, 0x1000, v18
	v_or_b32_e32 v23, 0x1400, v18
	v_or_b32_e32 v24, 0x1800, v18
	v_or_b32_e32 v25, 0x1c00, v18
	v_or_b32_e32 v26, 0x2000, v18
	v_or_b32_e32 v27, 0x2400, v18
	v_or_b32_e32 v28, 0x2800, v18
	v_or_b32_e32 v29, 0x2c00, v18
	v_or_b32_e32 v30, 0x3000, v18
	v_or_b32_e32 v31, 0x3400, v18
	v_or_b32_e32 v32, 0x3800, v18
	v_or_b32_e32 v33, 0x3c00, v18
	v_or3_b32 v2, s6, v2, v34
	v_lshl_add_u64 v[78:79], s[4:5], 0, v[2:3]
	s_mov_b64 s[4:5], 0
	v_add_u32_e32 v86, v4, v7
	v_add_u32_e32 v87, v5, v8
	v_add_u32_e32 v88, v4, v9
	v_add_u32_e32 v89, v5, v11
	v_add_u32_e32 v90, v4, v12
	v_add_u32_e32 v91, v5, v14
	v_add_u32_e32 v92, v4, v15
	v_add_u32_e32 v93, v5, v17
	v_add_u32_e32 v94, v6, v18
	v_add_u32_e32 v95, v6, v19
	v_add_u32_e32 v96, v6, v20
	v_add_u32_e32 v97, v6, v21
	v_add_u32_e32 v98, v6, v22
	v_add_u32_e32 v99, v6, v23
	v_add_u32_e32 v100, v6, v24
	v_add_u32_e32 v101, v6, v25
	v_add_u32_e32 v102, v6, v26
	v_add_u32_e32 v103, v6, v27
	v_add_u32_e32 v104, v6, v28
	v_add_u32_e32 v105, v6, v29
	v_add_u32_e32 v106, v6, v30
	v_add_u32_e32 v107, v6, v31
	v_add_u32_e32 v108, v6, v32
	v_add_u32_e32 v109, v6, v33
	s_mov_b64 s[6:7], 0x80
	v_mov_b32_e32 v2, v3
	v_mov_b32_e32 v4, v3
	v_mov_b32_e32 v5, v3
	v_mov_b32_e32 v6, v3
	v_mov_b32_e32 v7, v3
	v_mov_b32_e32 v8, v3
	v_mov_b32_e32 v9, v3
	v_mov_b32_e32 v10, v3
	v_mov_b32_e32 v11, v3
	v_mov_b32_e32 v12, v3
	v_mov_b32_e32 v13, v3
	v_mov_b32_e32 v14, v3
	v_mov_b32_e32 v15, v3
	v_mov_b32_e32 v16, v3
	v_mov_b32_e32 v17, v3
	v_mov_b32_e32 v18, v3
	v_mov_b32_e32 v19, v3
	v_mov_b32_e32 v20, v3
	v_mov_b32_e32 v21, v3
	v_mov_b32_e32 v22, v3
	v_mov_b32_e32 v23, v3
	v_mov_b32_e32 v24, v3
	v_mov_b32_e32 v25, v3
	v_mov_b32_e32 v26, v3
	v_mov_b32_e32 v27, v3
	v_mov_b32_e32 v28, v3
	v_mov_b32_e32 v29, v3
	v_mov_b32_e32 v30, v3
	v_mov_b32_e32 v31, v3
	v_mov_b32_e32 v32, v3
	v_mov_b32_e32 v33, v3
	v_mov_b32_e32 v34, v3
	v_mov_b32_e32 v35, v3
	v_mov_b32_e32 v36, v3
	v_mov_b32_e32 v37, v3
	v_mov_b32_e32 v38, v3
	v_mov_b32_e32 v39, v3
	v_mov_b32_e32 v40, v3
	v_mov_b32_e32 v41, v3
	v_mov_b32_e32 v42, v3
	v_mov_b32_e32 v43, v3
	v_mov_b32_e32 v44, v3
	v_mov_b32_e32 v45, v3
	v_mov_b32_e32 v46, v3
	v_mov_b32_e32 v47, v3
	v_mov_b32_e32 v48, v3
	v_mov_b32_e32 v49, v3
	v_mov_b32_e32 v50, v3
	v_mov_b32_e32 v51, v3
	v_mov_b32_e32 v52, v3
	v_mov_b32_e32 v53, v3
	v_mov_b32_e32 v54, v3
	v_mov_b32_e32 v55, v3
	v_mov_b32_e32 v56, v3
	v_mov_b32_e32 v57, v3
	v_mov_b32_e32 v58, v3
	v_mov_b32_e32 v59, v3
	v_mov_b32_e32 v60, v3
	v_mov_b32_e32 v61, v3
	v_mov_b32_e32 v62, v3
	v_mov_b32_e32 v63, v3
	v_mov_b32_e32 v64, v3
	v_mov_b32_e32 v65, v3
.LBB0_2:
	s_barrier
	global_load_dwordx4 v[110:113], v[78:79], off
	v_lshl_add_u64 v[114:115], v[66:67], 0, s[4:5]
	global_load_dwordx4 v[114:117], v[114:115], off
	v_lshl_add_u64 v[78:79], v[78:79], 0, s[6:7]
	s_waitcnt vmcnt(1)
	ds_write2_b32 v86, v110, v111 offset1:1
	ds_write2_b32 v86, v112, v113 offset0:2 offset1:3
	s_waitcnt vmcnt(0)
	ds_write_b128 v87, v[114:117]
	global_load_dwordx4 v[110:113], v[76:77], off
	v_lshl_add_u64 v[114:115], v[72:73], 0, s[4:5]
	global_load_dwordx4 v[114:117], v[114:115], off
	v_lshl_add_u64 v[76:77], v[76:77], 0, s[6:7]
	s_waitcnt vmcnt(1)
	ds_write2_b32 v88, v110, v111 offset1:1
	ds_write2_b32 v88, v112, v113 offset0:2 offset1:3
	s_waitcnt vmcnt(0)
	ds_write_b128 v89, v[114:117]
	global_load_dwordx4 v[110:113], v[74:75], off
	v_lshl_add_u64 v[114:115], v[70:71], 0, s[4:5]
	global_load_dwordx4 v[114:117], v[114:115], off
	v_lshl_add_u64 v[74:75], v[74:75], 0, s[6:7]
	s_waitcnt vmcnt(1)
	ds_write2_b32 v90, v110, v111 offset1:1
	ds_write2_b32 v90, v112, v113 offset0:2 offset1:3
	s_waitcnt vmcnt(0)
	ds_write_b128 v91, v[114:117]
	global_load_dwordx4 v[110:113], v[0:1], off
	v_lshl_add_u64 v[114:115], v[68:69], 0, s[4:5]
	global_load_dwordx4 v[114:117], v[114:115], off
	s_add_u32 s4, s4, 0x4000
	s_addc_u32 s5, s5, 0
	v_lshl_add_u64 v[0:1], v[0:1], 0, s[6:7]
	s_cmp_eq_u32 s4, 0x20000
	s_waitcnt vmcnt(1)
	ds_write2_b32 v92, v110, v111 offset1:1
	ds_write2_b32 v92, v112, v113 offset0:2 offset1:3
	s_waitcnt vmcnt(0)
	ds_write_b128 v93, v[114:117]
	s_waitcnt lgkmcnt(0)
	s_barrier
	ds_read2_b32 v[110:111], v94 offset1:32
	ds_read2_b32 v[112:113], v85 offset1:2
	ds_read2_b32 v[114:115], v85 offset0:4 offset1:6
	ds_read2_b32 v[116:117], v85 offset0:8 offset1:10
	ds_read2_b32 v[118:119], v85 offset0:12 offset1:14
	s_waitcnt lgkmcnt(3)
	v_mfma_f32_32x32x2_f32 v[50:65], v112, v110, v[50:65]
	v_mfma_f32_32x32x2_f32 v[34:49], v112, v111, v[34:49]
	ds_read2_b32 v[110:111], v94 offset0:64 offset1:96
	s_waitcnt lgkmcnt(0)
	v_mfma_f32_32x32x2_f32 v[18:33], v112, v110, v[18:33]
	v_mfma_f32_32x32x2_f32 v[2:17], v112, v111, v[2:17]
	ds_read2_b32 v[110:111], v95 offset1:32
	s_waitcnt lgkmcnt(0)
	v_mfma_f32_32x32x2_f32 v[50:65], v113, v110, v[50:65]
	v_mfma_f32_32x32x2_f32 v[34:49], v113, v111, v[34:49]
	ds_read2_b32 v[110:111], v95 offset0:64 offset1:96
	s_waitcnt lgkmcnt(0)
	v_mfma_f32_32x32x2_f32 v[18:33], v113, v110, v[18:33]
	v_mfma_f32_32x32x2_f32 v[2:17], v113, v111, v[2:17]
	ds_read2_b32 v[110:111], v96 offset1:32
	s_waitcnt lgkmcnt(0)
	v_mfma_f32_32x32x2_f32 v[50:65], v114, v110, v[50:65]
	v_mfma_f32_32x32x2_f32 v[34:49], v114, v111, v[34:49]
	ds_read2_b32 v[110:111], v96 offset0:64 offset1:96
	s_waitcnt lgkmcnt(0)
	v_mfma_f32_32x32x2_f32 v[18:33], v114, v110, v[18:33]
	v_mfma_f32_32x32x2_f32 v[2:17], v114, v111, v[2:17]
	ds_read2_b32 v[110:111], v97 offset1:32
	s_waitcnt lgkmcnt(0)
	v_mfma_f32_32x32x2_f32 v[50:65], v115, v110, v[50:65]
	v_mfma_f32_32x32x2_f32 v[34:49], v115, v111, v[34:49]
	ds_read2_b32 v[110:111], v97 offset0:64 offset1:96
	s_waitcnt lgkmcnt(0)
	v_mfma_f32_32x32x2_f32 v[18:33], v115, v110, v[18:33]
	v_mfma_f32_32x32x2_f32 v[2:17], v115, v111, v[2:17]
	ds_read2_b32 v[110:111], v98 offset1:32
	s_waitcnt lgkmcnt(0)
	v_mfma_f32_32x32x2_f32 v[50:65], v116, v110, v[50:65]
	v_mfma_f32_32x32x2_f32 v[34:49], v116, v111, v[34:49]
	ds_read2_b32 v[110:111], v98 offset0:64 offset1:96
	s_waitcnt lgkmcnt(0)
	v_mfma_f32_32x32x2_f32 v[18:33], v116, v110, v[18:33]
	v_mfma_f32_32x32x2_f32 v[2:17], v116, v111, v[2:17]
	ds_read2_b32 v[110:111], v99 offset1:32
	s_waitcnt lgkmcnt(0)
	v_mfma_f32_32x32x2_f32 v[50:65], v117, v110, v[50:65]
	v_mfma_f32_32x32x2_f32 v[34:49], v117, v111, v[34:49]
	ds_read2_b32 v[110:111], v99 offset0:64 offset1:96
	s_waitcnt lgkmcnt(0)
	v_mfma_f32_32x32x2_f32 v[18:33], v117, v110, v[18:33]
	v_mfma_f32_32x32x2_f32 v[2:17], v117, v111, v[2:17]
	ds_read2_b32 v[110:111], v100 offset1:32
	s_waitcnt lgkmcnt(0)
	v_mfma_f32_32x32x2_f32 v[50:65], v118, v110, v[50:65]
	v_mfma_f32_32x32x2_f32 v[34:49], v118, v111, v[34:49]
	ds_read2_b32 v[110:111], v100 offset0:64 offset1:96
	s_waitcnt lgkmcnt(0)
	v_mfma_f32_32x32x2_f32 v[18:33], v118, v110, v[18:33]
	v_mfma_f32_32x32x2_f32 v[2:17], v118, v111, v[2:17]
	ds_read2_b32 v[110:111], v101 offset1:32
	s_waitcnt lgkmcnt(0)
	v_mfma_f32_32x32x2_f32 v[50:65], v119, v110, v[50:65]
	v_mfma_f32_32x32x2_f32 v[34:49], v119, v111, v[34:49]
	ds_read2_b32 v[110:111], v101 offset0:64 offset1:96
	s_waitcnt lgkmcnt(0)
	v_mfma_f32_32x32x2_f32 v[18:33], v119, v110, v[18:33]
	v_mfma_f32_32x32x2_f32 v[2:17], v119, v111, v[2:17]
	ds_read2_b32 v[110:111], v85 offset0:16 offset1:18
	ds_read2_b32 v[112:113], v102 offset1:32
	s_waitcnt lgkmcnt(0)
	v_mfma_f32_32x32x2_f32 v[50:65], v110, v112, v[50:65]
	v_mfma_f32_32x32x2_f32 v[34:49], v110, v113, v[34:49]
	ds_read2_b32 v[112:113], v102 offset0:64 offset1:96
	s_waitcnt lgkmcnt(0)
	v_mfma_f32_32x32x2_f32 v[18:33], v110, v112, v[18:33]
	v_mfma_f32_32x32x2_f32 v[2:17], v110, v113, v[2:17]
	ds_read2_b32 v[112:113], v103 offset1:32
	s_waitcnt lgkmcnt(0)
	v_mfma_f32_32x32x2_f32 v[50:65], v111, v112, v[50:65]
	v_mfma_f32_32x32x2_f32 v[34:49], v111, v113, v[34:49]
	ds_read2_b32 v[112:113], v103 offset0:64 offset1:96
	s_waitcnt lgkmcnt(0)
	v_mfma_f32_32x32x2_f32 v[18:33], v111, v112, v[18:33]
	v_mfma_f32_32x32x2_f32 v[2:17], v111, v113, v[2:17]
	ds_read2_b32 v[110:111], v85 offset0:20 offset1:22
	ds_read2_b32 v[112:113], v104 offset1:32
	s_waitcnt lgkmcnt(0)
	v_mfma_f32_32x32x2_f32 v[50:65], v110, v112, v[50:65]
	v_mfma_f32_32x32x2_f32 v[34:49], v110, v113, v[34:49]
	ds_read2_b32 v[112:113], v104 offset0:64 offset1:96
	s_waitcnt lgkmcnt(0)
	v_mfma_f32_32x32x2_f32 v[18:33], v110, v112, v[18:33]
	v_mfma_f32_32x32x2_f32 v[2:17], v110, v113, v[2:17]
	ds_read2_b32 v[112:113], v105 offset1:32
	s_waitcnt lgkmcnt(0)
	v_mfma_f32_32x32x2_f32 v[50:65], v111, v112, v[50:65]
	v_mfma_f32_32x32x2_f32 v[34:49], v111, v113, v[34:49]
	ds_read2_b32 v[112:113], v105 offset0:64 offset1:96
	s_waitcnt lgkmcnt(0)
	v_mfma_f32_32x32x2_f32 v[18:33], v111, v112, v[18:33]
	v_mfma_f32_32x32x2_f32 v[2:17], v111, v113, v[2:17]
	ds_read2_b32 v[110:111], v85 offset0:24 offset1:26
	ds_read2_b32 v[112:113], v106 offset1:32
	s_waitcnt lgkmcnt(0)
	v_mfma_f32_32x32x2_f32 v[50:65], v110, v112, v[50:65]
	v_mfma_f32_32x32x2_f32 v[34:49], v110, v113, v[34:49]
	ds_read2_b32 v[112:113], v106 offset0:64 offset1:96
	s_waitcnt lgkmcnt(0)
	v_mfma_f32_32x32x2_f32 v[18:33], v110, v112, v[18:33]
	v_mfma_f32_32x32x2_f32 v[2:17], v110, v113, v[2:17]
	ds_read2_b32 v[112:113], v107 offset1:32
	s_waitcnt lgkmcnt(0)
	v_mfma_f32_32x32x2_f32 v[50:65], v111, v112, v[50:65]
	v_mfma_f32_32x32x2_f32 v[34:49], v111, v113, v[34:49]
	ds_read2_b32 v[112:113], v107 offset0:64 offset1:96
	s_waitcnt lgkmcnt(0)
	v_mfma_f32_32x32x2_f32 v[18:33], v111, v112, v[18:33]
	v_mfma_f32_32x32x2_f32 v[2:17], v111, v113, v[2:17]
	ds_read2_b32 v[110:111], v85 offset0:28 offset1:30
	ds_read2_b32 v[112:113], v108 offset1:32
	s_waitcnt lgkmcnt(0)
	v_mfma_f32_32x32x2_f32 v[50:65], v110, v112, v[50:65]
	v_mfma_f32_32x32x2_f32 v[34:49], v110, v113, v[34:49]
	ds_read2_b32 v[112:113], v108 offset0:64 offset1:96
	s_waitcnt lgkmcnt(0)
	v_mfma_f32_32x32x2_f32 v[18:33], v110, v112, v[18:33]
	v_mfma_f32_32x32x2_f32 v[2:17], v110, v113, v[2:17]
	ds_read2_b32 v[112:113], v109 offset1:32
	s_waitcnt lgkmcnt(0)
	v_mfma_f32_32x32x2_f32 v[50:65], v111, v112, v[50:65]
	v_mfma_f32_32x32x2_f32 v[34:49], v111, v113, v[34:49]
	ds_read2_b32 v[112:113], v109 offset0:64 offset1:96
	s_waitcnt lgkmcnt(0)
	v_mfma_f32_32x32x2_f32 v[18:33], v111, v112, v[18:33]
	v_mfma_f32_32x32x2_f32 v[2:17], v111, v113, v[2:17]
	s_cbranch_scc0 .LBB0_2
	v_add_u32_e32 v66, s3, v83
	v_lshlrev_b32_e32 v0, 1, v84
	v_mov_b32_e32 v1, 0
	s_nop 8
	v_cvt_f16_f32_e32 v50, v50
	v_lshl_add_u64 v[68:69], s[8:9], 0, v[0:1]
	v_and_or_b32 v0, v82, 4, v66
	v_cvt_f16_f32_e32 v51, v51
	v_lshlrev_b32_e32 v0, 8, v0
	v_cvt_f16_f32_e32 v52, v52
	v_lshl_add_u64 v[66:67], v[68:69], 0, v[0:1]
	v_cvt_f16_f32_e32 v53, v53
	global_store_short v[66:67], v50, off
	global_store_short v[66:67], v51, off offset:256
	global_store_short v[66:67], v52, off offset:512
	global_store_short v[66:67], v53, off offset:768
	v_cvt_f16_f32_e32 v50, v54
	v_cvt_f16_f32_e32 v51, v55
	v_cvt_f16_f32_e32 v52, v56
	v_cvt_f16_f32_e32 v54, v58
	v_cvt_f16_f32_e32 v53, v57
	global_store_short v[66:67], v50, off offset:2048
	global_store_short v[66:67], v51, off offset:2304
	global_store_short v[66:67], v52, off offset:2560
	global_store_short v[66:67], v53, off offset:2816
	v_or_b32_e32 v50, 0x1000, v0
	v_mov_b32_e32 v51, v1
	v_cvt_f16_f32_e32 v56, v59
	v_lshl_add_u64 v[52:53], v[68:69], 0, v[50:51]
	global_store_short v[52:53], v54, off
	v_or_b32_e32 v52, 0x1100, v0
	v_mov_b32_e32 v53, v1
	v_cvt_f16_f32_e32 v58, v60
	v_lshl_add_u64 v[54:55], v[68:69], 0, v[52:53]
	global_store_short v[54:55], v56, off
	v_or_b32_e32 v54, 0x1200, v0
	v_mov_b32_e32 v55, v1
	v_cvt_f16_f32_e32 v60, v61
	v_lshl_add_u64 v[56:57], v[68:69], 0, v[54:55]
	global_store_short v[56:57], v58, off
	v_or_b32_e32 v56, 0x1300, v0
	v_mov_b32_e32 v57, v1
	v_cvt_f16_f32_e32 v62, v62
	v_lshl_add_u64 v[58:59], v[68:69], 0, v[56:57]
	global_store_short v[58:59], v60, off
	v_or_b32_e32 v58, 0x1800, v0
	v_mov_b32_e32 v59, v1
	v_cvt_f16_f32_e32 v70, v63
	v_cvt_f16_f32_e32 v34, v34
	v_lshl_add_u64 v[60:61], v[68:69], 0, v[58:59]
	global_store_short v[60:61], v62, off
	v_or_b32_e32 v62, 0x1900, v0
	v_mov_b32_e32 v63, v1
	v_cvt_f16_f32_e32 v64, v64
	v_lshl_add_u64 v[60:61], v[68:69], 0, v[62:63]
	v_cvt_f16_f32_e32 v72, v65
	v_cvt_f16_f32_e32 v35, v35
	global_store_short v[60:61], v70, off
	v_or_b32_e32 v60, 0x1a00, v0
	v_mov_b32_e32 v61, v1
	v_cvt_f16_f32_e32 v36, v36
	global_store_short v[66:67], v34, off offset:64
	v_cvt_f16_f32_e32 v34, v37
	v_lshl_add_u64 v[70:71], v[68:69], 0, v[60:61]
	v_or_b32_e32 v0, 0x1b00, v0
	global_store_short v[70:71], v64, off
	v_lshl_add_u64 v[64:65], v[68:69], 0, v[0:1]
	global_store_short v[64:65], v72, off
	global_store_short v[66:67], v35, off offset:320
	global_store_short v[66:67], v36, off offset:576
	v_cvt_f16_f32_e32 v35, v38
	global_store_short v[66:67], v34, off offset:832
	v_cvt_f16_f32_e32 v34, v39
	v_cvt_f16_f32_e32 v36, v40
	global_store_short v[66:67], v35, off offset:2112
	v_cvt_f16_f32_e32 v35, v41
	global_store_short v[66:67], v34, off offset:2368
	global_store_short v[66:67], v36, off offset:2624
	v_cvt_f16_f32_e32 v36, v42
	v_cvt_f16_f32_e32 v37, v43
	v_lshl_add_u64 v[64:65], v[68:69], 0, 64
	global_store_short v[66:67], v35, off offset:2880
	v_lshl_add_u64 v[34:35], v[64:65], 0, v[50:51]
	global_store_short v[34:35], v36, off
	v_lshl_add_u64 v[34:35], v[64:65], 0, v[52:53]
	v_cvt_f16_f32_e32 v36, v44
	global_store_short v[34:35], v37, off
	v_cvt_f16_f32_e32 v37, v45
	v_lshl_add_u64 v[34:35], v[64:65], 0, v[54:55]
	global_store_short v[34:35], v36, off
	v_lshl_add_u64 v[34:35], v[64:65], 0, v[56:57]
	v_cvt_f16_f32_e32 v36, v46
	global_store_short v[34:35], v37, off
	v_cvt_f16_f32_e32 v37, v47
	v_cvt_f16_f32_e32 v18, v18
	v_lshl_add_u64 v[34:35], v[64:65], 0, v[58:59]
	global_store_short v[34:35], v36, off
	v_lshl_add_u64 v[34:35], v[64:65], 0, v[62:63]
	v_cvt_f16_f32_e32 v36, v48
	global_store_short v[34:35], v37, off
	v_cvt_f16_f32_e32 v37, v49
	v_cvt_f16_f32_e32 v19, v19
	v_cvt_f16_f32_e32 v20, v20
	global_store_short v[66:67], v18, off offset:128
	v_cvt_f16_f32_e32 v18, v21
	v_lshl_add_u64 v[34:35], v[64:65], 0, v[60:61]
	global_store_short v[34:35], v36, off
	v_lshl_add_u64 v[34:35], v[64:65], 0, v[0:1]
	global_store_short v[34:35], v37, off
	global_store_short v[66:67], v19, off offset:384
	global_store_short v[66:67], v20, off offset:640
	v_cvt_f16_f32_e32 v19, v22
	global_store_short v[66:67], v18, off offset:896
	v_cvt_f16_f32_e32 v18, v23
	v_cvt_f16_f32_e32 v20, v24
	global_store_short v[66:67], v19, off offset:2176
	v_cvt_f16_f32_e32 v19, v25
	global_store_short v[66:67], v18, off offset:2432
	global_store_short v[66:67], v20, off offset:2688
	v_cvt_f16_f32_e32 v20, v26
	s_mov_b64 s[4:5], 0x80
	v_cvt_f16_f32_e32 v21, v27
	v_lshl_add_u64 v[34:35], v[68:69], 0, s[4:5]
	global_store_short v[66:67], v19, off offset:2944
	v_lshl_add_u64 v[18:19], v[34:35], 0, v[50:51]
	global_store_short v[18:19], v20, off
	v_lshl_add_u64 v[18:19], v[34:35], 0, v[52:53]
	v_cvt_f16_f32_e32 v20, v28
	global_store_short v[18:19], v21, off
	v_cvt_f16_f32_e32 v21, v29
	v_lshl_add_u64 v[18:19], v[34:35], 0, v[54:55]
	global_store_short v[18:19], v20, off
	v_lshl_add_u64 v[18:19], v[34:35], 0, v[56:57]
	v_cvt_f16_f32_e32 v20, v30
	global_store_short v[18:19], v21, off
	v_cvt_f16_f32_e32 v21, v31
	v_cvt_f16_f32_e32 v2, v2
	v_lshl_add_u64 v[18:19], v[34:35], 0, v[58:59]
	global_store_short v[18:19], v20, off
	v_lshl_add_u64 v[18:19], v[34:35], 0, v[62:63]
	v_cvt_f16_f32_e32 v20, v32
	global_store_short v[18:19], v21, off
	v_cvt_f16_f32_e32 v21, v33
	v_cvt_f16_f32_e32 v3, v3
	v_cvt_f16_f32_e32 v4, v4
	global_store_short v[66:67], v2, off offset:192
	v_cvt_f16_f32_e32 v2, v5
	v_lshl_add_u64 v[18:19], v[34:35], 0, v[60:61]
	global_store_short v[18:19], v20, off
	v_lshl_add_u64 v[18:19], v[34:35], 0, v[0:1]
	global_store_short v[18:19], v21, off
	global_store_short v[66:67], v3, off offset:448
	global_store_short v[66:67], v4, off offset:704
	v_cvt_f16_f32_e32 v3, v6
	global_store_short v[66:67], v2, off offset:960
	v_cvt_f16_f32_e32 v2, v7
	v_cvt_f16_f32_e32 v4, v8
	global_store_short v[66:67], v3, off offset:2240
	v_cvt_f16_f32_e32 v3, v9
	global_store_short v[66:67], v2, off offset:2496
	global_store_short v[66:67], v4, off offset:2752
	v_cvt_f16_f32_e32 v4, v10
	s_mov_b64 s[4:5], 0xc0
	v_cvt_f16_f32_e32 v5, v11
	v_lshl_add_u64 v[18:19], v[68:69], 0, s[4:5]
	global_store_short v[66:67], v3, off offset:3008
	v_lshl_add_u64 v[2:3], v[18:19], 0, v[50:51]
	global_store_short v[2:3], v4, off
	v_lshl_add_u64 v[2:3], v[18:19], 0, v[52:53]
	v_cvt_f16_f32_e32 v4, v12
	global_store_short v[2:3], v5, off
	v_cvt_f16_f32_e32 v5, v13
	v_lshl_add_u64 v[2:3], v[18:19], 0, v[54:55]
	global_store_short v[2:3], v4, off
	v_lshl_add_u64 v[2:3], v[18:19], 0, v[56:57]
	v_cvt_f16_f32_e32 v4, v14
	global_store_short v[2:3], v5, off
	v_cvt_f16_f32_e32 v5, v15
	v_lshl_add_u64 v[2:3], v[18:19], 0, v[58:59]
	global_store_short v[2:3], v4, off
	v_lshl_add_u64 v[2:3], v[18:19], 0, v[62:63]
	v_cvt_f16_f32_e32 v4, v16
	global_store_short v[2:3], v5, off
	v_cvt_f16_f32_e32 v5, v17
	v_lshl_add_u64 v[2:3], v[18:19], 0, v[60:61]
	v_lshl_add_u64 v[0:1], v[18:19], 0, v[0:1]
	s_mov_b64 s[4:5], 0
	global_store_short v[2:3], v4, off
	global_store_short v[0:1], v5, off
.LBB0_4:
	s_and_b64 vcc, exec, s[4:5]
	s_cbranch_vccz .LBB0_1207
	s_load_dwordx2 s[12:13], s[0:1], 0x0
	s_load_dwordx4 s[4:7], s[0:1], 0x20
	s_load_dwordx2 s[10:11], s[0:1], 0x38
	v_cmp_eq_u32_e32 vcc, 0, v80
	s_and_saveexec_b64 s[8:9], vcc
	v_lshlrev_b32_e32 v0, 2, v81
	v_mov_b32_e32 v1, 0
	ds_write_b32 v0, v1 offset:37376
	s_or_b64 exec, exec, s[8:9]
	s_load_dwordx2 s[8:9], s[0:1], 0x30
	v_mov_b32_e32 v0, 0x9200
	s_lshl_b32 s0, s2, 2
	v_lshl_or_b32 v77, v81, 2, v0
	v_mov_b32_e32 v0, 0x8200
	s_addk_i32 s0, 0xfe80
	v_lshl_or_b32 v76, v81, 10, v0
	v_or_b32_e32 v0, s0, v81
	v_mul_lo_u32 v79, v0, 6
	s_mov_b32 s2, 0xc000
	s_waitcnt lgkmcnt(0)
	v_mov_b64_e32 v[0:1], s[12:13]
	v_mad_i64_i32 v[0:1], s[0:1], v79, s2, v[0:1]
	v_lshlrev_b32_e32 v64, 4, v80
	v_mov_b32_e32 v65, 0
	v_mad_i64_i32 v[66:67], s[0:1], v79, s2, 0
	v_lshl_add_u64 v[0:1], v[0:1], 0, v[64:65]
	s_waitcnt vmcnt(63) expcnt(7) lgkmcnt(15)
	s_barrier
	s_movk_i32 s0, 0x1000
	v_add_co_u32_e32 v2, vcc, s0, v0
	s_movk_i32 s0, 0x2000
	s_nop 0
	v_addc_co_u32_e32 v3, vcc, 0, v1, vcc
	v_add_co_u32_e32 v4, vcc, s0, v0
	global_load_dwordx4 v[60:63], v[0:1], off nt
	global_load_dwordx4 v[56:59], v[0:1], off offset:1024 nt
	global_load_dwordx4 v[52:55], v[0:1], off offset:2048 nt
	global_load_dwordx4 v[48:51], v[0:1], off offset:3072 nt
	v_addc_co_u32_e32 v5, vcc, 0, v1, vcc
	global_load_dwordx4 v[36:39], v[2:3], off offset:1024 nt
	global_load_dwordx4 v[28:31], v[2:3], off offset:2048 nt
	global_load_dwordx4 v[44:47], v[4:5], off offset:-4096 nt
	global_load_dwordx4 v[20:23], v[2:3], off offset:3072 nt
	s_movk_i32 s0, 0x3000
	v_add_co_u32_e32 v0, vcc, s0, v0
	global_load_dwordx4 v[40:43], v[4:5], off nt
	global_load_dwordx4 v[32:35], v[4:5], off offset:1024 nt
	global_load_dwordx4 v[24:27], v[4:5], off offset:2048 nt
	global_load_dwordx4 v[16:19], v[4:5], off offset:3072 nt
	v_addc_co_u32_e32 v1, vcc, 0, v1, vcc
	global_load_dwordx4 v[12:15], v[0:1], off nt
	global_load_dwordx4 v[8:11], v[0:1], off offset:1024 nt
	global_load_dwordx4 v[4:7], v[0:1], off offset:2048 nt
	s_nop 0
	global_load_dwordx4 v[0:3], v[0:1], off offset:3072 nt
	v_or_b32_e32 v66, v66, v64
	v_lshl_add_u64 v[66:67], s[12:13], 0, v[66:67]
	s_mov_b64 s[0:1], 0x4000
	v_lshlrev_b32_e32 v78, 2, v80
	v_lshl_add_u64 v[66:67], v[66:67], 0, s[0:1]
	s_mov_b32 s20, -2
	v_mov_b32_e32 v81, 1
	s_movk_i32 s21, 0x7f
	s_mov_b32 s22, 0x18000
	s_branch .LBB0_9
.LBB0_8:
	s_or_b64 exec, exec, s[2:3]
	v_add_co_u32_e32 v0, vcc, 0x2000, v66
	s_nop 1
	v_addc_co_u32_e32 v1, vcc, 0, v67, vcc
	global_load_dwordx4 v[40:43], v[0:1], off nt
	global_load_dwordx4 v[32:35], v[0:1], off offset:1024 nt
	global_load_dwordx4 v[24:27], v[0:1], off offset:2048 nt
	global_load_dwordx4 v[16:19], v[0:1], off offset:3072 nt
	v_add_co_u32_e32 v0, vcc, 0x3000, v66
	s_nop 1
	v_addc_co_u32_e32 v1, vcc, 0, v67, vcc
	global_load_dwordx4 v[12:15], v[0:1], off nt
	global_load_dwordx4 v[8:11], v[0:1], off offset:1024 nt
	global_load_dwordx4 v[4:7], v[0:1], off offset:2048 nt
	s_nop 0
	global_load_dwordx4 v[0:3], v[0:1], off offset:3072 nt
	s_cmp_gt_u32 s20, 31
	v_lshl_add_u64 v[66:67], v[66:67], 0, s[0:1]
	s_cbranch_scc1 .LBB0_604
.LBB0_9:
	s_waitcnt vmcnt(8)
	v_mov_b32_e32 v71, v20
	v_mov_b32_e32 v69, v22
	v_or_b32_e32 v68, v53, v52
	v_or3_b32 v70, v68, v55, v54
	v_or_b32_e32 v68, v48, v49
	v_or3_b32 v68, v68, v51, v50
	v_or3_b32 v72, v68, v45, v44
	v_or3_b32 v72, v72, v47, v46
	v_or3_b32 v72, v72, v37, v36
	v_or3_b32 v72, v72, v39, v38
	v_or3_b32 v72, v72, v29, v28
	v_or3_b32 v72, v72, v31, v30
	s_add_i32 s20, s20, 2
	v_or3_b32 v72, v72, v21, v71
	s_and_b32 s2, s20, 0xff
	v_or3_b32 v72, v72, v23, v69
	s_mulk_i32 s2, 0xab
	v_or_b32_e32 v64, v61, v60
	v_or3_b32 v72, v72, v57, v56
	s_lshr_b32 s12, s2, 10
	v_or3_b32 v64, v64, v63, v62
	v_or3_b32 v72, v72, v59, v58
	v_add_u32_e32 v82, s12, v79
	v_or3_b32 v72, v72, v70, v64
	v_cmp_ne_u32_e32 vcc, 0, v72
	v_lshlrev_b32_e32 v83, 14, v82
	s_and_saveexec_b64 s[2:3], vcc
	s_cbranch_execz .LBB0_307
	s_mul_i32 s12, s12, 6
	s_sub_i32 s12, s20, s12
	s_and_b32 s12, s12, 0xff
	v_lshl_or_b32 v84, s12, 11, v78
	v_cmp_ne_u32_e32 vcc, 0, v64
	s_and_saveexec_b64 s[12:13], vcc
	s_cbranch_execz .LBB0_48
	v_cmp_neq_f32_e32 vcc, 0, v60
	s_and_saveexec_b64 s[14:15], vcc
	s_cbranch_execz .LBB0_21
	ds_add_rtn_u32 v64, v77, v81
	s_waitcnt lgkmcnt(0)
	v_cmp_lt_i32_e32 vcc, s21, v64
	s_and_saveexec_b64 s[16:17], vcc
	s_xor_b64 s[16:17], exec, s[16:17]
	s_cbranch_execz .LBB0_19
	v_lshlrev_b32_e32 v85, 2, v84
	global_atomic_add v72, v85, v81, s[4:5] sc0
	s_waitcnt vmcnt(0)
	v_cmp_lt_i32_e32 vcc, 63, v72
	s_and_saveexec_b64 s[18:19], vcc
	s_xor_b64 s[18:19], exec, s[18:19]
	s_cbranch_execz .LBB0_16
	v_mov_b64_e32 v[74:75], s[10:11]
	v_mov_b32_e32 v73, v65
	v_mad_u64_u32 v[74:75], s[24:25], v84, s22, v[74:75]
	v_lshl_add_u64 v[74:75], v[72:73], 3, v[74:75]
	global_store_dword v[74:75], v82, off
.LBB0_16:
	s_andn2_saveexec_b64 s[18:19], s[18:19]
	s_cbranch_execz .LBB0_18
	v_lshlrev_b32_e32 v64, 9, v84
	v_ashrrev_i32_e32 v73, 31, v72
	v_lshl_add_u64 v[74:75], s[8:9], 0, v[64:65]
	v_lshl_add_u64 v[74:75], v[72:73], 3, v[74:75]
	global_store_dword v[74:75], v82, off
.LBB0_18:
	s_or_b64 exec, exec, s[18:19]
	global_store_dword v[74:75], v60, off offset:4
	global_atomic_add_f32 v85, v60, s[6:7]
.LBB0_19:
	s_andn2_saveexec_b64 s[16:17], s[16:17]
	v_or_b32_e32 v72, v84, v83
	v_lshl_add_u32 v64, v64, 3, v76
	v_mov_b32_e32 v73, v60
	ds_write_b64 v64, v[72:73]
.LBB0_21:
	s_or_b64 exec, exec, s[14:15]
	v_cmp_neq_f32_e32 vcc, 0, v61
	s_and_saveexec_b64 s[14:15], vcc
	s_cbranch_execz .LBB0_30
	ds_add_rtn_u32 v64, v77, v81
	v_or_b32_e32 v60, 1, v84
	s_waitcnt lgkmcnt(0)
	v_cmp_lt_i32_e32 vcc, s21, v64
	s_and_saveexec_b64 s[16:17], vcc
	s_xor_b64 s[16:17], exec, s[16:17]
	s_cbranch_execz .LBB0_28
	v_lshlrev_b32_e32 v74, 2, v84
	global_atomic_add v64, v74, v81, s[4:5] offset:4 sc0
	s_waitcnt vmcnt(0)
	v_cmp_lt_i32_e32 vcc, 63, v64
	s_and_saveexec_b64 s[18:19], vcc
	s_xor_b64 s[18:19], exec, s[18:19]
	s_cbranch_execz .LBB0_25
	v_mov_b64_e32 v[72:73], s[10:11]
	v_mad_u64_u32 v[72:73], s[24:25], v60, s22, v[72:73]
	v_lshl_add_u64 v[72:73], v[64:65], 3, v[72:73]
	global_store_dword v[72:73], v82, off
.LBB0_25:
	s_andn2_saveexec_b64 s[18:19], s[18:19]
	s_cbranch_execz .LBB0_27
	v_ashrrev_i32_e32 v73, 31, v64
	v_mov_b32_e32 v72, v64
	v_lshlrev_b32_e32 v64, 9, v60
	v_lshl_add_u64 v[86:87], s[8:9], 0, v[64:65]
	v_lshl_add_u64 v[72:73], v[72:73], 3, v[86:87]
	global_store_dword v[72:73], v82, off
.LBB0_27:
	s_or_b64 exec, exec, s[18:19]
	global_store_dword v[72:73], v61, off offset:4
	global_atomic_add_f32 v74, v61, s[6:7] offset:4
.LBB0_28:
	s_andn2_saveexec_b64 s[16:17], s[16:17]
	v_or_b32_e32 v60, v60, v83
	v_lshl_add_u32 v64, v64, 3, v76
	ds_write_b64 v64, v[60:61]
.LBB0_30:
	s_or_b64 exec, exec, s[14:15]
	v_cmp_neq_f32_e32 vcc, 0, v62
	s_and_saveexec_b64 s[14:15], vcc
	s_cbranch_execz .LBB0_39
	ds_add_rtn_u32 v60, v77, v81
	v_or_b32_e32 v72, 2, v84
	s_waitcnt lgkmcnt(0)
	v_cmp_lt_i32_e32 vcc, s21, v60
	s_and_saveexec_b64 s[16:17], vcc
	s_xor_b64 s[16:17], exec, s[16:17]
	s_cbranch_execz .LBB0_37
	v_lshlrev_b32_e32 v73, 2, v84
	global_atomic_add v64, v73, v81, s[4:5] offset:8 sc0
	s_waitcnt vmcnt(0)
	v_cmp_lt_i32_e32 vcc, 63, v64
	s_and_saveexec_b64 s[18:19], vcc
	s_xor_b64 s[18:19], exec, s[18:19]
	s_cbranch_execz .LBB0_34
	v_mov_b64_e32 v[60:61], s[10:11]
	v_mad_u64_u32 v[60:61], s[24:25], v72, s22, v[60:61]
	v_lshl_add_u64 v[60:61], v[64:65], 3, v[60:61]
	global_store_dword v[60:61], v82, off
.LBB0_34:
	s_andn2_saveexec_b64 s[18:19], s[18:19]
	s_cbranch_execz .LBB0_36
	v_ashrrev_i32_e32 v61, 31, v64
	v_mov_b32_e32 v60, v64
	v_lshlrev_b32_e32 v64, 9, v72
	v_lshl_add_u64 v[74:75], s[8:9], 0, v[64:65]
	v_lshl_add_u64 v[60:61], v[60:61], 3, v[74:75]
	global_store_dword v[60:61], v82, off
.LBB0_36:
	s_or_b64 exec, exec, s[18:19]
	global_store_dword v[60:61], v62, off offset:4
	global_atomic_add_f32 v73, v62, s[6:7] offset:8
.LBB0_37:
	s_andn2_saveexec_b64 s[16:17], s[16:17]
	v_or_b32_e32 v72, v72, v83
	v_lshl_add_u32 v60, v60, 3, v76
	v_mov_b32_e32 v73, v62
	ds_write_b64 v60, v[72:73]
.LBB0_39:
	s_or_b64 exec, exec, s[14:15]
	v_cmp_neq_f32_e32 vcc, 0, v63
	s_and_b64 exec, exec, vcc
	s_cbranch_execz .LBB0_48
	ds_add_rtn_u32 v60, v77, v81
	v_or_b32_e32 v62, 3, v84
	s_waitcnt lgkmcnt(0)
	v_cmp_lt_i32_e32 vcc, s21, v60
	s_and_saveexec_b64 s[14:15], vcc
	s_xor_b64 s[14:15], exec, s[14:15]
	s_cbranch_execz .LBB0_46
	v_lshlrev_b32_e32 v72, 2, v84
	global_atomic_add v64, v72, v81, s[4:5] offset:12 sc0
	s_waitcnt vmcnt(0)
	v_cmp_lt_i32_e32 vcc, 63, v64
	s_and_saveexec_b64 s[16:17], vcc
	s_xor_b64 s[16:17], exec, s[16:17]
	s_cbranch_execz .LBB0_43
	v_mov_b64_e32 v[60:61], s[10:11]
	v_mad_u64_u32 v[60:61], s[18:19], v62, s22, v[60:61]
	v_lshl_add_u64 v[60:61], v[64:65], 3, v[60:61]
	global_store_dword v[60:61], v82, off
.LBB0_43:
	s_andn2_saveexec_b64 s[16:17], s[16:17]
	s_cbranch_execz .LBB0_45
	v_ashrrev_i32_e32 v61, 31, v64
	v_mov_b32_e32 v60, v64
	v_lshlrev_b32_e32 v64, 9, v62
	v_lshl_add_u64 v[74:75], s[8:9], 0, v[64:65]
	v_lshl_add_u64 v[60:61], v[60:61], 3, v[74:75]
	global_store_dword v[60:61], v82, off
.LBB0_45:
	s_or_b64 exec, exec, s[16:17]
	global_store_dword v[60:61], v63, off offset:4
	global_atomic_add_f32 v72, v63, s[6:7] offset:12
.LBB0_46:
	s_andn2_saveexec_b64 s[14:15], s[14:15]
	v_or_b32_e32 v62, v62, v83
	v_lshl_add_u32 v60, v60, 3, v76
	ds_write_b64 v60, v[62:63]
.LBB0_48:
	s_or_b64 exec, exec, s[12:13]
	v_or_b32_e32 v60, v56, v57
	v_or3_b32 v60, v60, v59, v58
	v_cmp_ne_u32_e32 vcc, 0, v60
	s_and_saveexec_b64 s[12:13], vcc
	s_cbranch_execz .LBB0_85
	v_cmp_neq_f32_e32 vcc, 0, v56
	s_and_saveexec_b64 s[14:15], vcc
	s_cbranch_execz .LBB0_58
	ds_add_rtn_u32 v60, v77, v81
	v_or_b32_e32 v62, 0x100, v84
	s_waitcnt lgkmcnt(0)
	v_cmp_lt_i32_e32 vcc, s21, v60
	s_and_saveexec_b64 s[16:17], vcc
	s_xor_b64 s[16:17], exec, s[16:17]
	s_cbranch_execz .LBB0_56
	v_lshlrev_b32_e32 v63, 2, v84
	global_atomic_add v64, v63, v81, s[4:5] offset:1024 sc0
	s_waitcnt vmcnt(0)
	v_cmp_lt_i32_e32 vcc, 63, v64
	s_and_saveexec_b64 s[18:19], vcc
	s_xor_b64 s[18:19], exec, s[18:19]
	s_cbranch_execz .LBB0_53
	v_mov_b64_e32 v[60:61], s[10:11]
	v_mad_u64_u32 v[60:61], s[24:25], v62, s22, v[60:61]
	v_lshl_add_u64 v[60:61], v[64:65], 3, v[60:61]
	global_store_dword v[60:61], v82, off
.LBB0_53:
	s_andn2_saveexec_b64 s[18:19], s[18:19]
	s_cbranch_execz .LBB0_55
	v_ashrrev_i32_e32 v61, 31, v64
	v_mov_b32_e32 v60, v64
	v_lshlrev_b32_e32 v64, 9, v62
	v_lshl_add_u64 v[72:73], s[8:9], 0, v[64:65]
	v_lshl_add_u64 v[60:61], v[60:61], 3, v[72:73]
	global_store_dword v[60:61], v82, off
.LBB0_55:
	s_or_b64 exec, exec, s[18:19]
	global_store_dword v[60:61], v56, off offset:4
	global_atomic_add_f32 v63, v56, s[6:7] offset:1024
.LBB0_56:
	s_andn2_saveexec_b64 s[16:17], s[16:17]
	v_or_b32_e32 v62, v62, v83
	v_lshl_add_u32 v60, v60, 3, v76
	v_mov_b32_e32 v63, v56
	ds_write_b64 v60, v[62:63]
.LBB0_58:
	s_or_b64 exec, exec, s[14:15]
	v_cmp_neq_f32_e32 vcc, 0, v57
	s_and_saveexec_b64 s[14:15], vcc
	s_cbranch_execz .LBB0_67
	ds_add_rtn_u32 v60, v77, v81
	v_or_b32_e32 v56, 0x101, v84
	s_waitcnt lgkmcnt(0)
	v_cmp_lt_i32_e32 vcc, s21, v60
	s_and_saveexec_b64 s[16:17], vcc
	s_xor_b64 s[16:17], exec, s[16:17]
	s_cbranch_execz .LBB0_65
	v_lshlrev_b32_e32 v62, 2, v84
	global_atomic_add v64, v62, v81, s[4:5] offset:1028 sc0
	s_waitcnt vmcnt(0)
	v_cmp_lt_i32_e32 vcc, 63, v64
	s_and_saveexec_b64 s[18:19], vcc
	s_xor_b64 s[18:19], exec, s[18:19]
	s_cbranch_execz .LBB0_62
	v_mov_b64_e32 v[60:61], s[10:11]
	v_mad_u64_u32 v[60:61], s[24:25], v56, s22, v[60:61]
	v_lshl_add_u64 v[60:61], v[64:65], 3, v[60:61]
	global_store_dword v[60:61], v82, off
.LBB0_62:
	s_andn2_saveexec_b64 s[18:19], s[18:19]
	s_cbranch_execz .LBB0_64
	v_ashrrev_i32_e32 v61, 31, v64
	v_mov_b32_e32 v60, v64
	v_lshlrev_b32_e32 v64, 9, v56
	v_lshl_add_u64 v[72:73], s[8:9], 0, v[64:65]
	v_lshl_add_u64 v[60:61], v[60:61], 3, v[72:73]
	global_store_dword v[60:61], v82, off
.LBB0_64:
	s_or_b64 exec, exec, s[18:19]
	global_store_dword v[60:61], v57, off offset:4
	global_atomic_add_f32 v62, v57, s[6:7] offset:1028
.LBB0_65:
	s_andn2_saveexec_b64 s[16:17], s[16:17]
	v_or_b32_e32 v56, v56, v83
	v_lshl_add_u32 v60, v60, 3, v76
	ds_write_b64 v60, v[56:57]
.LBB0_67:
	s_or_b64 exec, exec, s[14:15]
	v_cmp_neq_f32_e32 vcc, 0, v58
	s_and_saveexec_b64 s[14:15], vcc
	s_cbranch_execz .LBB0_76
	ds_add_rtn_u32 v56, v77, v81
	v_or_b32_e32 v60, 0x102, v84
	s_waitcnt lgkmcnt(0)
	v_cmp_lt_i32_e32 vcc, s21, v56
	s_and_saveexec_b64 s[16:17], vcc
	s_xor_b64 s[16:17], exec, s[16:17]
	s_cbranch_execz .LBB0_74
	v_lshlrev_b32_e32 v61, 2, v84
	global_atomic_add v64, v61, v81, s[4:5] offset:1032 sc0
	s_waitcnt vmcnt(0)
	v_cmp_lt_i32_e32 vcc, 63, v64
	s_and_saveexec_b64 s[18:19], vcc
	s_xor_b64 s[18:19], exec, s[18:19]
	s_cbranch_execz .LBB0_71
	v_mov_b64_e32 v[56:57], s[10:11]
	v_mad_u64_u32 v[56:57], s[24:25], v60, s22, v[56:57]
	v_lshl_add_u64 v[56:57], v[64:65], 3, v[56:57]
	global_store_dword v[56:57], v82, off
.LBB0_71:
	s_andn2_saveexec_b64 s[18:19], s[18:19]
	s_cbranch_execz .LBB0_73
	v_ashrrev_i32_e32 v57, 31, v64
	v_mov_b32_e32 v56, v64
	v_lshlrev_b32_e32 v64, 9, v60
	v_lshl_add_u64 v[62:63], s[8:9], 0, v[64:65]
	v_lshl_add_u64 v[56:57], v[56:57], 3, v[62:63]
	global_store_dword v[56:57], v82, off
.LBB0_73:
	s_or_b64 exec, exec, s[18:19]
	global_store_dword v[56:57], v58, off offset:4
	global_atomic_add_f32 v61, v58, s[6:7] offset:1032
.LBB0_74:
	s_andn2_saveexec_b64 s[16:17], s[16:17]
	v_or_b32_e32 v60, v60, v83
	v_lshl_add_u32 v56, v56, 3, v76
	v_mov_b32_e32 v61, v58
	ds_write_b64 v56, v[60:61]
.LBB0_76:
	s_or_b64 exec, exec, s[14:15]
	v_cmp_neq_f32_e32 vcc, 0, v59
	s_and_b64 exec, exec, vcc
	s_cbranch_execz .LBB0_85
	ds_add_rtn_u32 v56, v77, v81
	v_or_b32_e32 v58, 0x103, v84
	s_waitcnt lgkmcnt(0)
	v_cmp_lt_i32_e32 vcc, s21, v56
	s_and_saveexec_b64 s[14:15], vcc
	s_xor_b64 s[14:15], exec, s[14:15]
	s_cbranch_execz .LBB0_83
	v_lshlrev_b32_e32 v60, 2, v84
	global_atomic_add v64, v60, v81, s[4:5] offset:1036 sc0
	s_waitcnt vmcnt(0)
	v_cmp_lt_i32_e32 vcc, 63, v64
	s_and_saveexec_b64 s[16:17], vcc
	s_xor_b64 s[16:17], exec, s[16:17]
	s_cbranch_execz .LBB0_80
	v_mov_b64_e32 v[56:57], s[10:11]
	v_mad_u64_u32 v[56:57], s[18:19], v58, s22, v[56:57]
	v_lshl_add_u64 v[56:57], v[64:65], 3, v[56:57]
	global_store_dword v[56:57], v82, off
.LBB0_80:
	s_andn2_saveexec_b64 s[16:17], s[16:17]
	s_cbranch_execz .LBB0_82
	v_ashrrev_i32_e32 v57, 31, v64
	v_mov_b32_e32 v56, v64
	v_lshlrev_b32_e32 v64, 9, v58
	v_lshl_add_u64 v[62:63], s[8:9], 0, v[64:65]
	v_lshl_add_u64 v[56:57], v[56:57], 3, v[62:63]
	global_store_dword v[56:57], v82, off
.LBB0_82:
	s_or_b64 exec, exec, s[16:17]
	global_store_dword v[56:57], v59, off offset:4
	global_atomic_add_f32 v60, v59, s[6:7] offset:1036
.LBB0_83:
	s_andn2_saveexec_b64 s[14:15], s[14:15]
	v_or_b32_e32 v58, v58, v83
	v_lshl_add_u32 v56, v56, 3, v76
	ds_write_b64 v56, v[58:59]
.LBB0_85:
	s_or_b64 exec, exec, s[12:13]
	v_cmp_ne_u32_e32 vcc, 0, v70
	s_and_saveexec_b64 s[12:13], vcc
	s_cbranch_execz .LBB0_122
	v_cmp_neq_f32_e32 vcc, 0, v52
	s_and_saveexec_b64 s[14:15], vcc
	s_cbranch_execz .LBB0_95
	ds_add_rtn_u32 v56, v77, v81
	v_or_b32_e32 v58, 0x200, v84
	s_waitcnt lgkmcnt(0)
	v_cmp_lt_i32_e32 vcc, s21, v56
	s_and_saveexec_b64 s[16:17], vcc
	s_xor_b64 s[16:17], exec, s[16:17]
	s_cbranch_execz .LBB0_93
	v_lshlrev_b32_e32 v59, 2, v84
	global_atomic_add v64, v59, v81, s[4:5] offset:2048 sc0
	s_waitcnt vmcnt(0)
	v_cmp_lt_i32_e32 vcc, 63, v64
	s_and_saveexec_b64 s[18:19], vcc
	s_xor_b64 s[18:19], exec, s[18:19]
	s_cbranch_execz .LBB0_90
	v_mov_b64_e32 v[56:57], s[10:11]
	v_mad_u64_u32 v[56:57], s[24:25], v58, s22, v[56:57]
	v_lshl_add_u64 v[56:57], v[64:65], 3, v[56:57]
	global_store_dword v[56:57], v82, off
.LBB0_90:
	s_andn2_saveexec_b64 s[18:19], s[18:19]
	s_cbranch_execz .LBB0_92
	v_ashrrev_i32_e32 v57, 31, v64
	v_mov_b32_e32 v56, v64
	v_lshlrev_b32_e32 v64, 9, v58
	v_lshl_add_u64 v[60:61], s[8:9], 0, v[64:65]
	v_lshl_add_u64 v[56:57], v[56:57], 3, v[60:61]
	global_store_dword v[56:57], v82, off
.LBB0_92:
	s_or_b64 exec, exec, s[18:19]
	global_store_dword v[56:57], v52, off offset:4
	global_atomic_add_f32 v59, v52, s[6:7] offset:2048
.LBB0_93:
	s_andn2_saveexec_b64 s[16:17], s[16:17]
	v_or_b32_e32 v58, v58, v83
	v_lshl_add_u32 v56, v56, 3, v76
	v_mov_b32_e32 v59, v52
	ds_write_b64 v56, v[58:59]
.LBB0_95:
	s_or_b64 exec, exec, s[14:15]
	v_cmp_neq_f32_e32 vcc, 0, v53
	s_and_saveexec_b64 s[14:15], vcc
	s_cbranch_execz .LBB0_104
	ds_add_rtn_u32 v56, v77, v81
	v_or_b32_e32 v52, 0x201, v84
	s_waitcnt lgkmcnt(0)
	v_cmp_lt_i32_e32 vcc, s21, v56
	s_and_saveexec_b64 s[16:17], vcc
	s_xor_b64 s[16:17], exec, s[16:17]
	s_cbranch_execz .LBB0_102
	v_lshlrev_b32_e32 v58, 2, v84
	global_atomic_add v64, v58, v81, s[4:5] offset:2052 sc0
	s_waitcnt vmcnt(0)
	v_cmp_lt_i32_e32 vcc, 63, v64
	s_and_saveexec_b64 s[18:19], vcc
	s_xor_b64 s[18:19], exec, s[18:19]
	s_cbranch_execz .LBB0_99
	v_mov_b64_e32 v[56:57], s[10:11]
	v_mad_u64_u32 v[56:57], s[24:25], v52, s22, v[56:57]
	v_lshl_add_u64 v[56:57], v[64:65], 3, v[56:57]
	global_store_dword v[56:57], v82, off
.LBB0_99:
	s_andn2_saveexec_b64 s[18:19], s[18:19]
	s_cbranch_execz .LBB0_101
	v_ashrrev_i32_e32 v57, 31, v64
	v_mov_b32_e32 v56, v64
	v_lshlrev_b32_e32 v64, 9, v52
	v_lshl_add_u64 v[60:61], s[8:9], 0, v[64:65]
	v_lshl_add_u64 v[56:57], v[56:57], 3, v[60:61]
	global_store_dword v[56:57], v82, off
.LBB0_101:
	s_or_b64 exec, exec, s[18:19]
	global_store_dword v[56:57], v53, off offset:4
	global_atomic_add_f32 v58, v53, s[6:7] offset:2052
.LBB0_102:
	s_andn2_saveexec_b64 s[16:17], s[16:17]
	v_or_b32_e32 v52, v52, v83
	v_lshl_add_u32 v56, v56, 3, v76
	ds_write_b64 v56, v[52:53]
.LBB0_104:
	s_or_b64 exec, exec, s[14:15]
	v_cmp_neq_f32_e32 vcc, 0, v54
	s_and_saveexec_b64 s[14:15], vcc
	s_cbranch_execz .LBB0_113
	ds_add_rtn_u32 v52, v77, v81
	v_or_b32_e32 v56, 0x202, v84
	s_waitcnt lgkmcnt(0)
	v_cmp_lt_i32_e32 vcc, s21, v52
	s_and_saveexec_b64 s[16:17], vcc
	s_xor_b64 s[16:17], exec, s[16:17]
	s_cbranch_execz .LBB0_111
	v_lshlrev_b32_e32 v57, 2, v84
	global_atomic_add v64, v57, v81, s[4:5] offset:2056 sc0
	s_waitcnt vmcnt(0)
	v_cmp_lt_i32_e32 vcc, 63, v64
	s_and_saveexec_b64 s[18:19], vcc
	s_xor_b64 s[18:19], exec, s[18:19]
	s_cbranch_execz .LBB0_108
	v_mov_b64_e32 v[52:53], s[10:11]
	v_mad_u64_u32 v[52:53], s[24:25], v56, s22, v[52:53]
	v_lshl_add_u64 v[52:53], v[64:65], 3, v[52:53]
	global_store_dword v[52:53], v82, off
.LBB0_108:
	s_andn2_saveexec_b64 s[18:19], s[18:19]
	s_cbranch_execz .LBB0_110
	v_ashrrev_i32_e32 v53, 31, v64
	v_mov_b32_e32 v52, v64
	v_lshlrev_b32_e32 v64, 9, v56
	v_lshl_add_u64 v[58:59], s[8:9], 0, v[64:65]
	v_lshl_add_u64 v[52:53], v[52:53], 3, v[58:59]
	global_store_dword v[52:53], v82, off
.LBB0_110:
	s_or_b64 exec, exec, s[18:19]
	global_store_dword v[52:53], v54, off offset:4
	global_atomic_add_f32 v57, v54, s[6:7] offset:2056
.LBB0_111:
	s_andn2_saveexec_b64 s[16:17], s[16:17]
	v_or_b32_e32 v56, v56, v83
	v_lshl_add_u32 v52, v52, 3, v76
	v_mov_b32_e32 v57, v54
	ds_write_b64 v52, v[56:57]
.LBB0_113:
	s_or_b64 exec, exec, s[14:15]
	v_cmp_neq_f32_e32 vcc, 0, v55
	s_and_b64 exec, exec, vcc
	s_cbranch_execz .LBB0_122
	ds_add_rtn_u32 v52, v77, v81
	v_or_b32_e32 v54, 0x203, v84
	s_waitcnt lgkmcnt(0)
	v_cmp_lt_i32_e32 vcc, s21, v52
	s_and_saveexec_b64 s[14:15], vcc
	s_xor_b64 s[14:15], exec, s[14:15]
	s_cbranch_execz .LBB0_120
	v_lshlrev_b32_e32 v56, 2, v84
	global_atomic_add v64, v56, v81, s[4:5] offset:2060 sc0
	s_waitcnt vmcnt(0)
	v_cmp_lt_i32_e32 vcc, 63, v64
	s_and_saveexec_b64 s[16:17], vcc
	s_xor_b64 s[16:17], exec, s[16:17]
	s_cbranch_execz .LBB0_117
	v_mov_b64_e32 v[52:53], s[10:11]
	v_mad_u64_u32 v[52:53], s[18:19], v54, s22, v[52:53]
	v_lshl_add_u64 v[52:53], v[64:65], 3, v[52:53]
	global_store_dword v[52:53], v82, off
.LBB0_117:
	s_andn2_saveexec_b64 s[16:17], s[16:17]
	s_cbranch_execz .LBB0_119
	v_ashrrev_i32_e32 v53, 31, v64
	v_mov_b32_e32 v52, v64
	v_lshlrev_b32_e32 v64, 9, v54
	v_lshl_add_u64 v[58:59], s[8:9], 0, v[64:65]
	v_lshl_add_u64 v[52:53], v[52:53], 3, v[58:59]
	global_store_dword v[52:53], v82, off
.LBB0_119:
	s_or_b64 exec, exec, s[16:17]
	global_store_dword v[52:53], v55, off offset:4
	global_atomic_add_f32 v56, v55, s[6:7] offset:2060
.LBB0_120:
	s_andn2_saveexec_b64 s[14:15], s[14:15]
	v_or_b32_e32 v54, v54, v83
	v_lshl_add_u32 v52, v52, 3, v76
	ds_write_b64 v52, v[54:55]
.LBB0_122:
	s_or_b64 exec, exec, s[12:13]
	v_cmp_ne_u32_e32 vcc, 0, v68
	s_and_saveexec_b64 s[12:13], vcc
	s_cbranch_execz .LBB0_159
	v_cmp_neq_f32_e32 vcc, 0, v48
	s_and_saveexec_b64 s[14:15], vcc
	s_cbranch_execz .LBB0_132
	ds_add_rtn_u32 v52, v77, v81
	v_or_b32_e32 v54, 0x300, v84
	s_waitcnt lgkmcnt(0)
	v_cmp_lt_i32_e32 vcc, s21, v52
	s_and_saveexec_b64 s[16:17], vcc
	s_xor_b64 s[16:17], exec, s[16:17]
	s_cbranch_execz .LBB0_130
	v_lshlrev_b32_e32 v55, 2, v84
	global_atomic_add v64, v55, v81, s[4:5] offset:3072 sc0
	s_waitcnt vmcnt(0)
	v_cmp_lt_i32_e32 vcc, 63, v64
	s_and_saveexec_b64 s[18:19], vcc
	s_xor_b64 s[18:19], exec, s[18:19]
	s_cbranch_execz .LBB0_127
	v_mov_b64_e32 v[52:53], s[10:11]
	v_mad_u64_u32 v[52:53], s[24:25], v54, s22, v[52:53]
	v_lshl_add_u64 v[52:53], v[64:65], 3, v[52:53]
	global_store_dword v[52:53], v82, off
.LBB0_127:
	s_andn2_saveexec_b64 s[18:19], s[18:19]
	s_cbranch_execz .LBB0_129
	v_ashrrev_i32_e32 v53, 31, v64
	v_mov_b32_e32 v52, v64
	v_lshlrev_b32_e32 v64, 9, v54
	v_lshl_add_u64 v[56:57], s[8:9], 0, v[64:65]
	v_lshl_add_u64 v[52:53], v[52:53], 3, v[56:57]
	global_store_dword v[52:53], v82, off
.LBB0_129:
	s_or_b64 exec, exec, s[18:19]
	global_store_dword v[52:53], v48, off offset:4
	global_atomic_add_f32 v55, v48, s[6:7] offset:3072
.LBB0_130:
	s_andn2_saveexec_b64 s[16:17], s[16:17]
	v_or_b32_e32 v54, v54, v83
	v_lshl_add_u32 v52, v52, 3, v76
	v_mov_b32_e32 v55, v48
	ds_write_b64 v52, v[54:55]
.LBB0_132:
	s_or_b64 exec, exec, s[14:15]
	v_cmp_neq_f32_e32 vcc, 0, v49
	s_and_saveexec_b64 s[14:15], vcc
	s_cbranch_execz .LBB0_141
	ds_add_rtn_u32 v52, v77, v81
	v_or_b32_e32 v48, 0x301, v84
	s_waitcnt lgkmcnt(0)
	v_cmp_lt_i32_e32 vcc, s21, v52
	s_and_saveexec_b64 s[16:17], vcc
	s_xor_b64 s[16:17], exec, s[16:17]
	s_cbranch_execz .LBB0_139
	v_lshlrev_b32_e32 v54, 2, v84
	global_atomic_add v64, v54, v81, s[4:5] offset:3076 sc0
	s_waitcnt vmcnt(0)
	v_cmp_lt_i32_e32 vcc, 63, v64
	s_and_saveexec_b64 s[18:19], vcc
	s_xor_b64 s[18:19], exec, s[18:19]
	s_cbranch_execz .LBB0_136
	v_mov_b64_e32 v[52:53], s[10:11]
	v_mad_u64_u32 v[52:53], s[24:25], v48, s22, v[52:53]
	v_lshl_add_u64 v[52:53], v[64:65], 3, v[52:53]
	global_store_dword v[52:53], v82, off
.LBB0_136:
	s_andn2_saveexec_b64 s[18:19], s[18:19]
	s_cbranch_execz .LBB0_138
	v_ashrrev_i32_e32 v53, 31, v64
	v_mov_b32_e32 v52, v64
	v_lshlrev_b32_e32 v64, 9, v48
	v_lshl_add_u64 v[56:57], s[8:9], 0, v[64:65]
	v_lshl_add_u64 v[52:53], v[52:53], 3, v[56:57]
	global_store_dword v[52:53], v82, off
.LBB0_138:
	s_or_b64 exec, exec, s[18:19]
	global_store_dword v[52:53], v49, off offset:4
	global_atomic_add_f32 v54, v49, s[6:7] offset:3076
.LBB0_139:
	s_andn2_saveexec_b64 s[16:17], s[16:17]
	v_or_b32_e32 v48, v48, v83
	v_lshl_add_u32 v52, v52, 3, v76
	ds_write_b64 v52, v[48:49]
.LBB0_141:
	s_or_b64 exec, exec, s[14:15]
	v_cmp_neq_f32_e32 vcc, 0, v50
	s_and_saveexec_b64 s[14:15], vcc
	s_cbranch_execz .LBB0_150
	ds_add_rtn_u32 v48, v77, v81
	v_or_b32_e32 v52, 0x302, v84
	s_waitcnt lgkmcnt(0)
	v_cmp_lt_i32_e32 vcc, s21, v48
	s_and_saveexec_b64 s[16:17], vcc
	s_xor_b64 s[16:17], exec, s[16:17]
	s_cbranch_execz .LBB0_148
	v_lshlrev_b32_e32 v53, 2, v84
	global_atomic_add v64, v53, v81, s[4:5] offset:3080 sc0
	s_waitcnt vmcnt(0)
	v_cmp_lt_i32_e32 vcc, 63, v64
	s_and_saveexec_b64 s[18:19], vcc
	s_xor_b64 s[18:19], exec, s[18:19]
	s_cbranch_execz .LBB0_145
	v_mov_b64_e32 v[48:49], s[10:11]
	v_mad_u64_u32 v[48:49], s[24:25], v52, s22, v[48:49]
	v_lshl_add_u64 v[48:49], v[64:65], 3, v[48:49]
	global_store_dword v[48:49], v82, off
.LBB0_145:
	s_andn2_saveexec_b64 s[18:19], s[18:19]
	s_cbranch_execz .LBB0_147
	v_ashrrev_i32_e32 v49, 31, v64
	v_mov_b32_e32 v48, v64
	v_lshlrev_b32_e32 v64, 9, v52
	v_lshl_add_u64 v[54:55], s[8:9], 0, v[64:65]
	v_lshl_add_u64 v[48:49], v[48:49], 3, v[54:55]
	global_store_dword v[48:49], v82, off
.LBB0_147:
	s_or_b64 exec, exec, s[18:19]
	global_store_dword v[48:49], v50, off offset:4
	global_atomic_add_f32 v53, v50, s[6:7] offset:3080
.LBB0_148:
	s_andn2_saveexec_b64 s[16:17], s[16:17]
	v_or_b32_e32 v52, v52, v83
	v_lshl_add_u32 v48, v48, 3, v76
	v_mov_b32_e32 v53, v50
	ds_write_b64 v48, v[52:53]
.LBB0_150:
	s_or_b64 exec, exec, s[14:15]
	v_cmp_neq_f32_e32 vcc, 0, v51
	s_and_b64 exec, exec, vcc
	s_cbranch_execz .LBB0_159
	ds_add_rtn_u32 v48, v77, v81
	v_or_b32_e32 v50, 0x303, v84
	s_waitcnt lgkmcnt(0)
	v_cmp_lt_i32_e32 vcc, s21, v48
	s_and_saveexec_b64 s[14:15], vcc
	s_xor_b64 s[14:15], exec, s[14:15]
	s_cbranch_execz .LBB0_157
	v_lshlrev_b32_e32 v52, 2, v84
	global_atomic_add v64, v52, v81, s[4:5] offset:3084 sc0
	s_waitcnt vmcnt(0)
	v_cmp_lt_i32_e32 vcc, 63, v64
	s_and_saveexec_b64 s[16:17], vcc
	s_xor_b64 s[16:17], exec, s[16:17]
	s_cbranch_execz .LBB0_154
	v_mov_b64_e32 v[48:49], s[10:11]
	v_mad_u64_u32 v[48:49], s[18:19], v50, s22, v[48:49]
	v_lshl_add_u64 v[48:49], v[64:65], 3, v[48:49]
	global_store_dword v[48:49], v82, off
.LBB0_154:
	s_andn2_saveexec_b64 s[16:17], s[16:17]
	s_cbranch_execz .LBB0_156
	v_ashrrev_i32_e32 v49, 31, v64
	v_mov_b32_e32 v48, v64
	v_lshlrev_b32_e32 v64, 9, v50
	v_lshl_add_u64 v[54:55], s[8:9], 0, v[64:65]
	v_lshl_add_u64 v[48:49], v[48:49], 3, v[54:55]
	global_store_dword v[48:49], v82, off
.LBB0_156:
	s_or_b64 exec, exec, s[16:17]
	global_store_dword v[48:49], v51, off offset:4
	global_atomic_add_f32 v52, v51, s[6:7] offset:3084
.LBB0_157:
	s_andn2_saveexec_b64 s[14:15], s[14:15]
	v_or_b32_e32 v50, v50, v83
	v_lshl_add_u32 v48, v48, 3, v76
	ds_write_b64 v48, v[50:51]
.LBB0_159:
	s_or_b64 exec, exec, s[12:13]
	v_or_b32_e32 v48, v44, v45
	v_or3_b32 v48, v48, v47, v46
	v_cmp_ne_u32_e32 vcc, 0, v48
	s_and_saveexec_b64 s[12:13], vcc
	s_cbranch_execz .LBB0_196
	v_cmp_neq_f32_e32 vcc, 0, v44
	s_and_saveexec_b64 s[14:15], vcc
	s_cbranch_execz .LBB0_169
	ds_add_rtn_u32 v48, v77, v81
	v_or_b32_e32 v50, 0x400, v84
	s_waitcnt lgkmcnt(0)
	v_cmp_lt_i32_e32 vcc, s21, v48
	s_and_saveexec_b64 s[16:17], vcc
	s_xor_b64 s[16:17], exec, s[16:17]
	s_cbranch_execz .LBB0_167
	v_lshlrev_b32_e32 v51, 2, v50
	global_atomic_add v64, v51, v81, s[4:5] sc0
	s_waitcnt vmcnt(0)
	v_cmp_lt_i32_e32 vcc, 63, v64
	s_and_saveexec_b64 s[18:19], vcc
	s_xor_b64 s[18:19], exec, s[18:19]
	s_cbranch_execz .LBB0_164
	v_mov_b64_e32 v[48:49], s[10:11]
	v_mad_u64_u32 v[48:49], s[24:25], v50, s22, v[48:49]
	v_lshl_add_u64 v[48:49], v[64:65], 3, v[48:49]
	global_store_dword v[48:49], v82, off
.LBB0_164:
	s_andn2_saveexec_b64 s[18:19], s[18:19]
	s_cbranch_execz .LBB0_166
	v_ashrrev_i32_e32 v49, 31, v64
	v_mov_b32_e32 v48, v64
	v_lshlrev_b32_e32 v64, 9, v50
	v_lshl_add_u64 v[52:53], s[8:9], 0, v[64:65]
	v_lshl_add_u64 v[48:49], v[48:49], 3, v[52:53]
	global_store_dword v[48:49], v82, off
.LBB0_166:
	s_or_b64 exec, exec, s[18:19]
	global_store_dword v[48:49], v44, off offset:4
	global_atomic_add_f32 v51, v44, s[6:7]
.LBB0_167:
	s_andn2_saveexec_b64 s[16:17], s[16:17]
	v_or_b32_e32 v50, v50, v83
	v_lshl_add_u32 v48, v48, 3, v76
	v_mov_b32_e32 v51, v44
	ds_write_b64 v48, v[50:51]
.LBB0_169:
	s_or_b64 exec, exec, s[14:15]
	v_cmp_neq_f32_e32 vcc, 0, v45
	s_and_saveexec_b64 s[14:15], vcc
	s_cbranch_execz .LBB0_178
	ds_add_rtn_u32 v48, v77, v81
	v_or_b32_e32 v44, 0x401, v84
	s_waitcnt lgkmcnt(0)
	v_cmp_lt_i32_e32 vcc, s21, v48
	s_and_saveexec_b64 s[16:17], vcc
	s_xor_b64 s[16:17], exec, s[16:17]
	s_cbranch_execz .LBB0_176
	v_lshlrev_b32_e32 v50, 2, v44
	global_atomic_add v64, v50, v81, s[4:5] sc0
	s_waitcnt vmcnt(0)
	v_cmp_lt_i32_e32 vcc, 63, v64
	s_and_saveexec_b64 s[18:19], vcc
	s_xor_b64 s[18:19], exec, s[18:19]
	s_cbranch_execz .LBB0_173
	v_mov_b64_e32 v[48:49], s[10:11]
	v_mad_u64_u32 v[48:49], s[24:25], v44, s22, v[48:49]
	v_lshl_add_u64 v[48:49], v[64:65], 3, v[48:49]
	global_store_dword v[48:49], v82, off
.LBB0_173:
	s_andn2_saveexec_b64 s[18:19], s[18:19]
	s_cbranch_execz .LBB0_175
	v_ashrrev_i32_e32 v49, 31, v64
	v_mov_b32_e32 v48, v64
	v_lshlrev_b32_e32 v64, 9, v44
	v_lshl_add_u64 v[52:53], s[8:9], 0, v[64:65]
	v_lshl_add_u64 v[48:49], v[48:49], 3, v[52:53]
	global_store_dword v[48:49], v82, off
.LBB0_175:
	s_or_b64 exec, exec, s[18:19]
	global_store_dword v[48:49], v45, off offset:4
	global_atomic_add_f32 v50, v45, s[6:7]
.LBB0_176:
	s_andn2_saveexec_b64 s[16:17], s[16:17]
	v_or_b32_e32 v44, v44, v83
	v_lshl_add_u32 v48, v48, 3, v76
	ds_write_b64 v48, v[44:45]
.LBB0_178:
	s_or_b64 exec, exec, s[14:15]
	v_cmp_neq_f32_e32 vcc, 0, v46
	s_and_saveexec_b64 s[14:15], vcc
	s_cbranch_execz .LBB0_187
	ds_add_rtn_u32 v44, v77, v81
	v_or_b32_e32 v48, 0x402, v84
	s_waitcnt lgkmcnt(0)
	v_cmp_lt_i32_e32 vcc, s21, v44
	s_and_saveexec_b64 s[16:17], vcc
	s_xor_b64 s[16:17], exec, s[16:17]
	s_cbranch_execz .LBB0_185
	v_lshlrev_b32_e32 v49, 2, v48
	global_atomic_add v64, v49, v81, s[4:5] sc0
	s_waitcnt vmcnt(0)
	v_cmp_lt_i32_e32 vcc, 63, v64
	s_and_saveexec_b64 s[18:19], vcc
	s_xor_b64 s[18:19], exec, s[18:19]
	s_cbranch_execz .LBB0_182
	v_mov_b64_e32 v[44:45], s[10:11]
	v_mad_u64_u32 v[44:45], s[24:25], v48, s22, v[44:45]
	v_lshl_add_u64 v[44:45], v[64:65], 3, v[44:45]
	global_store_dword v[44:45], v82, off
.LBB0_182:
	s_andn2_saveexec_b64 s[18:19], s[18:19]
	s_cbranch_execz .LBB0_184
	v_ashrrev_i32_e32 v45, 31, v64
	v_mov_b32_e32 v44, v64
	v_lshlrev_b32_e32 v64, 9, v48
	v_lshl_add_u64 v[50:51], s[8:9], 0, v[64:65]
	v_lshl_add_u64 v[44:45], v[44:45], 3, v[50:51]
	global_store_dword v[44:45], v82, off
.LBB0_184:
	s_or_b64 exec, exec, s[18:19]
	global_store_dword v[44:45], v46, off offset:4
	global_atomic_add_f32 v49, v46, s[6:7]
.LBB0_185:
	s_andn2_saveexec_b64 s[16:17], s[16:17]
	v_or_b32_e32 v48, v48, v83
	v_lshl_add_u32 v44, v44, 3, v76
	v_mov_b32_e32 v49, v46
	ds_write_b64 v44, v[48:49]
.LBB0_187:
	s_or_b64 exec, exec, s[14:15]
	v_cmp_neq_f32_e32 vcc, 0, v47
	s_and_b64 exec, exec, vcc
	s_cbranch_execz .LBB0_196
	ds_add_rtn_u32 v44, v77, v81
	v_or_b32_e32 v46, 0x403, v84
	s_waitcnt lgkmcnt(0)
	v_cmp_lt_i32_e32 vcc, s21, v44
	s_and_saveexec_b64 s[14:15], vcc
	s_xor_b64 s[14:15], exec, s[14:15]
	s_cbranch_execz .LBB0_194
	v_lshlrev_b32_e32 v48, 2, v46
	global_atomic_add v64, v48, v81, s[4:5] sc0
	s_waitcnt vmcnt(0)
	v_cmp_lt_i32_e32 vcc, 63, v64
	s_and_saveexec_b64 s[16:17], vcc
	s_xor_b64 s[16:17], exec, s[16:17]
	s_cbranch_execz .LBB0_191
	v_mov_b64_e32 v[44:45], s[10:11]
	v_mad_u64_u32 v[44:45], s[18:19], v46, s22, v[44:45]
	v_lshl_add_u64 v[44:45], v[64:65], 3, v[44:45]
	global_store_dword v[44:45], v82, off
.LBB0_191:
	s_andn2_saveexec_b64 s[16:17], s[16:17]
	s_cbranch_execz .LBB0_193
	v_ashrrev_i32_e32 v45, 31, v64
	v_mov_b32_e32 v44, v64
	v_lshlrev_b32_e32 v64, 9, v46
	v_lshl_add_u64 v[50:51], s[8:9], 0, v[64:65]
	v_lshl_add_u64 v[44:45], v[44:45], 3, v[50:51]
	global_store_dword v[44:45], v82, off
.LBB0_193:
	s_or_b64 exec, exec, s[16:17]
	global_store_dword v[44:45], v47, off offset:4
	global_atomic_add_f32 v48, v47, s[6:7]
.LBB0_194:
	s_andn2_saveexec_b64 s[14:15], s[14:15]
	v_or_b32_e32 v46, v46, v83
	v_lshl_add_u32 v44, v44, 3, v76
	ds_write_b64 v44, v[46:47]
.LBB0_196:
	s_or_b64 exec, exec, s[12:13]
	v_or_b32_e32 v44, v36, v37
	v_or3_b32 v44, v44, v39, v38
	v_cmp_ne_u32_e32 vcc, 0, v44
	s_and_saveexec_b64 s[12:13], vcc
	s_cbranch_execz .LBB0_233
	v_cmp_neq_f32_e32 vcc, 0, v36
	s_and_saveexec_b64 s[14:15], vcc
	s_cbranch_execz .LBB0_206
	ds_add_rtn_u32 v44, v77, v81
	v_or_b32_e32 v46, 0x500, v84
	s_waitcnt lgkmcnt(0)
	v_cmp_lt_i32_e32 vcc, s21, v44
	s_and_saveexec_b64 s[16:17], vcc
	s_xor_b64 s[16:17], exec, s[16:17]
	s_cbranch_execz .LBB0_204
	v_lshlrev_b32_e32 v47, 2, v46
	global_atomic_add v64, v47, v81, s[4:5] sc0
	s_waitcnt vmcnt(0)
	v_cmp_lt_i32_e32 vcc, 63, v64
	s_and_saveexec_b64 s[18:19], vcc
	s_xor_b64 s[18:19], exec, s[18:19]
	s_cbranch_execz .LBB0_201
	v_mov_b64_e32 v[44:45], s[10:11]
	v_mad_u64_u32 v[44:45], s[24:25], v46, s22, v[44:45]
	v_lshl_add_u64 v[44:45], v[64:65], 3, v[44:45]
	global_store_dword v[44:45], v82, off
.LBB0_201:
	s_andn2_saveexec_b64 s[18:19], s[18:19]
	s_cbranch_execz .LBB0_203
	v_ashrrev_i32_e32 v45, 31, v64
	v_mov_b32_e32 v44, v64
	v_lshlrev_b32_e32 v64, 9, v46
	v_lshl_add_u64 v[48:49], s[8:9], 0, v[64:65]
	v_lshl_add_u64 v[44:45], v[44:45], 3, v[48:49]
	global_store_dword v[44:45], v82, off
.LBB0_203:
	s_or_b64 exec, exec, s[18:19]
	global_store_dword v[44:45], v36, off offset:4
	global_atomic_add_f32 v47, v36, s[6:7]
.LBB0_204:
	s_andn2_saveexec_b64 s[16:17], s[16:17]
	v_or_b32_e32 v46, v46, v83
	v_lshl_add_u32 v44, v44, 3, v76
	v_mov_b32_e32 v47, v36
	ds_write_b64 v44, v[46:47]
.LBB0_206:
	s_or_b64 exec, exec, s[14:15]
	v_cmp_neq_f32_e32 vcc, 0, v37
	s_and_saveexec_b64 s[14:15], vcc
	s_cbranch_execz .LBB0_215
	ds_add_rtn_u32 v44, v77, v81
	v_or_b32_e32 v36, 0x501, v84
	s_waitcnt lgkmcnt(0)
	v_cmp_lt_i32_e32 vcc, s21, v44
	s_and_saveexec_b64 s[16:17], vcc
	s_xor_b64 s[16:17], exec, s[16:17]
	s_cbranch_execz .LBB0_213
	v_lshlrev_b32_e32 v46, 2, v36
	global_atomic_add v64, v46, v81, s[4:5] sc0
	s_waitcnt vmcnt(0)
	v_cmp_lt_i32_e32 vcc, 63, v64
	s_and_saveexec_b64 s[18:19], vcc
	s_xor_b64 s[18:19], exec, s[18:19]
	s_cbranch_execz .LBB0_210
	v_mov_b64_e32 v[44:45], s[10:11]
	v_mad_u64_u32 v[44:45], s[24:25], v36, s22, v[44:45]
	v_lshl_add_u64 v[44:45], v[64:65], 3, v[44:45]
	global_store_dword v[44:45], v82, off
.LBB0_210:
	s_andn2_saveexec_b64 s[18:19], s[18:19]
	s_cbranch_execz .LBB0_212
	v_ashrrev_i32_e32 v45, 31, v64
	v_mov_b32_e32 v44, v64
	v_lshlrev_b32_e32 v64, 9, v36
	v_lshl_add_u64 v[48:49], s[8:9], 0, v[64:65]
	v_lshl_add_u64 v[44:45], v[44:45], 3, v[48:49]
	global_store_dword v[44:45], v82, off
.LBB0_212:
	s_or_b64 exec, exec, s[18:19]
	global_store_dword v[44:45], v37, off offset:4
	global_atomic_add_f32 v46, v37, s[6:7]
.LBB0_213:
	s_andn2_saveexec_b64 s[16:17], s[16:17]
	v_or_b32_e32 v36, v36, v83
	v_lshl_add_u32 v44, v44, 3, v76
	ds_write_b64 v44, v[36:37]
.LBB0_215:
	s_or_b64 exec, exec, s[14:15]
	v_cmp_neq_f32_e32 vcc, 0, v38
	s_and_saveexec_b64 s[14:15], vcc
	s_cbranch_execz .LBB0_224
	ds_add_rtn_u32 v36, v77, v81
	v_or_b32_e32 v44, 0x502, v84
	s_waitcnt lgkmcnt(0)
	v_cmp_lt_i32_e32 vcc, s21, v36
	s_and_saveexec_b64 s[16:17], vcc
	s_xor_b64 s[16:17], exec, s[16:17]
	s_cbranch_execz .LBB0_222
	v_lshlrev_b32_e32 v45, 2, v44
	global_atomic_add v64, v45, v81, s[4:5] sc0
	s_waitcnt vmcnt(0)
	v_cmp_lt_i32_e32 vcc, 63, v64
	s_and_saveexec_b64 s[18:19], vcc
	s_xor_b64 s[18:19], exec, s[18:19]
	s_cbranch_execz .LBB0_219
	v_mov_b64_e32 v[36:37], s[10:11]
	v_mad_u64_u32 v[36:37], s[24:25], v44, s22, v[36:37]
	v_lshl_add_u64 v[36:37], v[64:65], 3, v[36:37]
	global_store_dword v[36:37], v82, off
.LBB0_219:
	s_andn2_saveexec_b64 s[18:19], s[18:19]
	s_cbranch_execz .LBB0_221
	v_ashrrev_i32_e32 v37, 31, v64
	v_mov_b32_e32 v36, v64
	v_lshlrev_b32_e32 v64, 9, v44
	v_lshl_add_u64 v[46:47], s[8:9], 0, v[64:65]
	v_lshl_add_u64 v[36:37], v[36:37], 3, v[46:47]
	global_store_dword v[36:37], v82, off
.LBB0_221:
	s_or_b64 exec, exec, s[18:19]
	global_store_dword v[36:37], v38, off offset:4
	global_atomic_add_f32 v45, v38, s[6:7]
.LBB0_222:
	s_andn2_saveexec_b64 s[16:17], s[16:17]
	v_or_b32_e32 v44, v44, v83
	v_lshl_add_u32 v36, v36, 3, v76
	v_mov_b32_e32 v45, v38
	ds_write_b64 v36, v[44:45]
.LBB0_224:
	s_or_b64 exec, exec, s[14:15]
	v_cmp_neq_f32_e32 vcc, 0, v39
	s_and_b64 exec, exec, vcc
	s_cbranch_execz .LBB0_233
	ds_add_rtn_u32 v36, v77, v81
	v_or_b32_e32 v38, 0x503, v84
	s_waitcnt lgkmcnt(0)
	v_cmp_lt_i32_e32 vcc, s21, v36
	s_and_saveexec_b64 s[14:15], vcc
	s_xor_b64 s[14:15], exec, s[14:15]
	s_cbranch_execz .LBB0_231
	v_lshlrev_b32_e32 v44, 2, v38
	global_atomic_add v64, v44, v81, s[4:5] sc0
	s_waitcnt vmcnt(0)
	v_cmp_lt_i32_e32 vcc, 63, v64
	s_and_saveexec_b64 s[16:17], vcc
	s_xor_b64 s[16:17], exec, s[16:17]
	s_cbranch_execz .LBB0_228
	v_mov_b64_e32 v[36:37], s[10:11]
	v_mad_u64_u32 v[36:37], s[18:19], v38, s22, v[36:37]
	v_lshl_add_u64 v[36:37], v[64:65], 3, v[36:37]
	global_store_dword v[36:37], v82, off
.LBB0_228:
	s_andn2_saveexec_b64 s[16:17], s[16:17]
	s_cbranch_execz .LBB0_230
	v_ashrrev_i32_e32 v37, 31, v64
	v_mov_b32_e32 v36, v64
	v_lshlrev_b32_e32 v64, 9, v38
	v_lshl_add_u64 v[46:47], s[8:9], 0, v[64:65]
	v_lshl_add_u64 v[36:37], v[36:37], 3, v[46:47]
	global_store_dword v[36:37], v82, off
.LBB0_230:
	s_or_b64 exec, exec, s[16:17]
	global_store_dword v[36:37], v39, off offset:4
	global_atomic_add_f32 v44, v39, s[6:7]
.LBB0_231:
	s_andn2_saveexec_b64 s[14:15], s[14:15]
	v_or_b32_e32 v38, v38, v83
	v_lshl_add_u32 v36, v36, 3, v76
	ds_write_b64 v36, v[38:39]
.LBB0_233:
	s_or_b64 exec, exec, s[12:13]
	v_or_b32_e32 v36, v28, v29
	v_or3_b32 v36, v36, v31, v30
	v_cmp_ne_u32_e32 vcc, 0, v36
	s_and_saveexec_b64 s[12:13], vcc
	s_cbranch_execz .LBB0_270
	v_cmp_neq_f32_e32 vcc, 0, v28
	s_and_saveexec_b64 s[14:15], vcc
	s_cbranch_execz .LBB0_243
	ds_add_rtn_u32 v36, v77, v81
	v_or_b32_e32 v38, 0x600, v84
	s_waitcnt lgkmcnt(0)
	v_cmp_lt_i32_e32 vcc, s21, v36
	s_and_saveexec_b64 s[16:17], vcc
	s_xor_b64 s[16:17], exec, s[16:17]
	s_cbranch_execz .LBB0_241
	v_lshlrev_b32_e32 v39, 2, v38
	global_atomic_add v64, v39, v81, s[4:5] sc0
	s_waitcnt vmcnt(0)
	v_cmp_lt_i32_e32 vcc, 63, v64
	s_and_saveexec_b64 s[18:19], vcc
	s_xor_b64 s[18:19], exec, s[18:19]
	s_cbranch_execz .LBB0_238
	v_mov_b64_e32 v[36:37], s[10:11]
	v_mad_u64_u32 v[36:37], s[24:25], v38, s22, v[36:37]
	v_lshl_add_u64 v[36:37], v[64:65], 3, v[36:37]
	global_store_dword v[36:37], v82, off
.LBB0_238:
	s_andn2_saveexec_b64 s[18:19], s[18:19]
	s_cbranch_execz .LBB0_240
	v_ashrrev_i32_e32 v37, 31, v64
	v_mov_b32_e32 v36, v64
	v_lshlrev_b32_e32 v64, 9, v38
	v_lshl_add_u64 v[44:45], s[8:9], 0, v[64:65]
	v_lshl_add_u64 v[36:37], v[36:37], 3, v[44:45]
	global_store_dword v[36:37], v82, off
.LBB0_240:
	s_or_b64 exec, exec, s[18:19]
	global_store_dword v[36:37], v28, off offset:4
	global_atomic_add_f32 v39, v28, s[6:7]
.LBB0_241:
	s_andn2_saveexec_b64 s[16:17], s[16:17]
	v_or_b32_e32 v38, v38, v83
	v_lshl_add_u32 v36, v36, 3, v76
	v_mov_b32_e32 v39, v28
	ds_write_b64 v36, v[38:39]
.LBB0_243:
	s_or_b64 exec, exec, s[14:15]
	v_cmp_neq_f32_e32 vcc, 0, v29
	s_and_saveexec_b64 s[14:15], vcc
	s_cbranch_execz .LBB0_252
	ds_add_rtn_u32 v36, v77, v81
	v_or_b32_e32 v28, 0x601, v84
	s_waitcnt lgkmcnt(0)
	v_cmp_lt_i32_e32 vcc, s21, v36
	s_and_saveexec_b64 s[16:17], vcc
	s_xor_b64 s[16:17], exec, s[16:17]
	s_cbranch_execz .LBB0_250
	v_lshlrev_b32_e32 v38, 2, v28
	global_atomic_add v64, v38, v81, s[4:5] sc0
	s_waitcnt vmcnt(0)
	v_cmp_lt_i32_e32 vcc, 63, v64
	s_and_saveexec_b64 s[18:19], vcc
	s_xor_b64 s[18:19], exec, s[18:19]
	s_cbranch_execz .LBB0_247
	v_mov_b64_e32 v[36:37], s[10:11]
	v_mad_u64_u32 v[36:37], s[24:25], v28, s22, v[36:37]
	v_lshl_add_u64 v[36:37], v[64:65], 3, v[36:37]
	global_store_dword v[36:37], v82, off
.LBB0_247:
	s_andn2_saveexec_b64 s[18:19], s[18:19]
	s_cbranch_execz .LBB0_249
	v_ashrrev_i32_e32 v37, 31, v64
	v_mov_b32_e32 v36, v64
	v_lshlrev_b32_e32 v64, 9, v28
	v_lshl_add_u64 v[44:45], s[8:9], 0, v[64:65]
	v_lshl_add_u64 v[36:37], v[36:37], 3, v[44:45]
	global_store_dword v[36:37], v82, off
.LBB0_249:
	s_or_b64 exec, exec, s[18:19]
	global_store_dword v[36:37], v29, off offset:4
	global_atomic_add_f32 v38, v29, s[6:7]
.LBB0_250:
	s_andn2_saveexec_b64 s[16:17], s[16:17]
	v_or_b32_e32 v28, v28, v83
	v_lshl_add_u32 v36, v36, 3, v76
	ds_write_b64 v36, v[28:29]
.LBB0_252:
	s_or_b64 exec, exec, s[14:15]
	v_cmp_neq_f32_e32 vcc, 0, v30
	s_and_saveexec_b64 s[14:15], vcc
	s_cbranch_execz .LBB0_261
	ds_add_rtn_u32 v28, v77, v81
	v_or_b32_e32 v36, 0x602, v84
	s_waitcnt lgkmcnt(0)
	v_cmp_lt_i32_e32 vcc, s21, v28
	s_and_saveexec_b64 s[16:17], vcc
	s_xor_b64 s[16:17], exec, s[16:17]
	s_cbranch_execz .LBB0_259
	v_lshlrev_b32_e32 v37, 2, v36
	global_atomic_add v64, v37, v81, s[4:5] sc0
	s_waitcnt vmcnt(0)
	v_cmp_lt_i32_e32 vcc, 63, v64
	s_and_saveexec_b64 s[18:19], vcc
	s_xor_b64 s[18:19], exec, s[18:19]
	s_cbranch_execz .LBB0_256
	v_mov_b64_e32 v[28:29], s[10:11]
	v_mad_u64_u32 v[28:29], s[24:25], v36, s22, v[28:29]
	v_lshl_add_u64 v[28:29], v[64:65], 3, v[28:29]
	global_store_dword v[28:29], v82, off
.LBB0_256:
	s_andn2_saveexec_b64 s[18:19], s[18:19]
	s_cbranch_execz .LBB0_258
	v_ashrrev_i32_e32 v29, 31, v64
	v_mov_b32_e32 v28, v64
	v_lshlrev_b32_e32 v64, 9, v36
	v_lshl_add_u64 v[38:39], s[8:9], 0, v[64:65]
	v_lshl_add_u64 v[28:29], v[28:29], 3, v[38:39]
	global_store_dword v[28:29], v82, off
.LBB0_258:
	s_or_b64 exec, exec, s[18:19]
	global_store_dword v[28:29], v30, off offset:4
	global_atomic_add_f32 v37, v30, s[6:7]
.LBB0_259:
	s_andn2_saveexec_b64 s[16:17], s[16:17]
	v_or_b32_e32 v36, v36, v83
	v_lshl_add_u32 v28, v28, 3, v76
	v_mov_b32_e32 v37, v30
	ds_write_b64 v28, v[36:37]
.LBB0_261:
	s_or_b64 exec, exec, s[14:15]
	v_cmp_neq_f32_e32 vcc, 0, v31
	s_and_b64 exec, exec, vcc
	s_cbranch_execz .LBB0_270
	ds_add_rtn_u32 v28, v77, v81
	v_or_b32_e32 v30, 0x603, v84
	s_waitcnt lgkmcnt(0)
	v_cmp_lt_i32_e32 vcc, s21, v28
	s_and_saveexec_b64 s[14:15], vcc
	s_xor_b64 s[14:15], exec, s[14:15]
	s_cbranch_execz .LBB0_268
	v_lshlrev_b32_e32 v36, 2, v30
	global_atomic_add v64, v36, v81, s[4:5] sc0
	s_waitcnt vmcnt(0)
	v_cmp_lt_i32_e32 vcc, 63, v64
	s_and_saveexec_b64 s[16:17], vcc
	s_xor_b64 s[16:17], exec, s[16:17]
	s_cbranch_execz .LBB0_265
	v_mov_b64_e32 v[28:29], s[10:11]
	v_mad_u64_u32 v[28:29], s[18:19], v30, s22, v[28:29]
	v_lshl_add_u64 v[28:29], v[64:65], 3, v[28:29]
	global_store_dword v[28:29], v82, off
.LBB0_265:
	s_andn2_saveexec_b64 s[16:17], s[16:17]
	s_cbranch_execz .LBB0_267
	v_ashrrev_i32_e32 v29, 31, v64
	v_mov_b32_e32 v28, v64
	v_lshlrev_b32_e32 v64, 9, v30
	v_lshl_add_u64 v[38:39], s[8:9], 0, v[64:65]
	v_lshl_add_u64 v[28:29], v[28:29], 3, v[38:39]
	global_store_dword v[28:29], v82, off
.LBB0_267:
	s_or_b64 exec, exec, s[16:17]
	global_store_dword v[28:29], v31, off offset:4
	global_atomic_add_f32 v36, v31, s[6:7]
.LBB0_268:
	s_andn2_saveexec_b64 s[14:15], s[14:15]
	v_or_b32_e32 v30, v30, v83
	v_lshl_add_u32 v28, v28, 3, v76
	ds_write_b64 v28, v[30:31]
.LBB0_270:
	s_or_b64 exec, exec, s[12:13]
	v_or_b32_e32 v28, v71, v21
	v_or3_b32 v28, v28, v23, v69
	v_cmp_ne_u32_e32 vcc, 0, v28
	s_and_b64 exec, exec, vcc
	s_cbranch_execz .LBB0_307
	v_cmp_neq_f32_e32 vcc, 0, v20
	s_and_saveexec_b64 s[12:13], vcc
	s_cbranch_execz .LBB0_280
	ds_add_rtn_u32 v28, v77, v81
	v_or_b32_e32 v30, 0x700, v84
	s_waitcnt lgkmcnt(0)
	v_cmp_lt_i32_e32 vcc, s21, v28
	s_and_saveexec_b64 s[14:15], vcc
	s_xor_b64 s[14:15], exec, s[14:15]
	s_cbranch_execz .LBB0_278
	v_lshlrev_b32_e32 v31, 2, v30
	global_atomic_add v64, v31, v81, s[4:5] sc0
	s_waitcnt vmcnt(0)
	v_cmp_lt_i32_e32 vcc, 63, v64
	s_and_saveexec_b64 s[16:17], vcc
	s_xor_b64 s[16:17], exec, s[16:17]
	s_cbranch_execz .LBB0_275
	v_mov_b64_e32 v[28:29], s[10:11]
	v_mad_u64_u32 v[28:29], s[18:19], v30, s22, v[28:29]
	v_lshl_add_u64 v[28:29], v[64:65], 3, v[28:29]
	global_store_dword v[28:29], v82, off
.LBB0_275:
	s_andn2_saveexec_b64 s[16:17], s[16:17]
	s_cbranch_execz .LBB0_277
	v_ashrrev_i32_e32 v29, 31, v64
	v_mov_b32_e32 v28, v64
	v_lshlrev_b32_e32 v64, 9, v30
	v_lshl_add_u64 v[36:37], s[8:9], 0, v[64:65]
	v_lshl_add_u64 v[28:29], v[28:29], 3, v[36:37]
	global_store_dword v[28:29], v82, off
.LBB0_277:
	s_or_b64 exec, exec, s[16:17]
	global_store_dword v[28:29], v20, off offset:4
	global_atomic_add_f32 v31, v20, s[6:7]
.LBB0_278:
	s_andn2_saveexec_b64 s[14:15], s[14:15]
	v_or_b32_e32 v70, v30, v83
	v_lshl_add_u32 v20, v28, 3, v76
	ds_write_b64 v20, v[70:71]
.LBB0_280:
	s_or_b64 exec, exec, s[12:13]
	v_cmp_neq_f32_e32 vcc, 0, v21
	s_and_saveexec_b64 s[12:13], vcc
	s_cbranch_execz .LBB0_289
	ds_add_rtn_u32 v28, v77, v81
	v_or_b32_e32 v20, 0x701, v84
	s_waitcnt lgkmcnt(0)
	v_cmp_lt_i32_e32 vcc, s21, v28
	s_and_saveexec_b64 s[14:15], vcc
	s_xor_b64 s[14:15], exec, s[14:15]
	s_cbranch_execz .LBB0_287
	v_lshlrev_b32_e32 v30, 2, v20
	global_atomic_add v64, v30, v81, s[4:5] sc0
	s_waitcnt vmcnt(0)
	v_cmp_lt_i32_e32 vcc, 63, v64
	s_and_saveexec_b64 s[16:17], vcc
	s_xor_b64 s[16:17], exec, s[16:17]
	s_cbranch_execz .LBB0_284
	v_mov_b64_e32 v[28:29], s[10:11]
	v_mad_u64_u32 v[28:29], s[18:19], v20, s22, v[28:29]
	v_lshl_add_u64 v[28:29], v[64:65], 3, v[28:29]
	global_store_dword v[28:29], v82, off
.LBB0_284:
	s_andn2_saveexec_b64 s[16:17], s[16:17]
	s_cbranch_execz .LBB0_286
	v_ashrrev_i32_e32 v29, 31, v64
	v_mov_b32_e32 v28, v64
	v_lshlrev_b32_e32 v64, 9, v20
	v_lshl_add_u64 v[36:37], s[8:9], 0, v[64:65]
	v_lshl_add_u64 v[28:29], v[28:29], 3, v[36:37]
	global_store_dword v[28:29], v82, off
.LBB0_286:
	s_or_b64 exec, exec, s[16:17]
	global_store_dword v[28:29], v21, off offset:4
	global_atomic_add_f32 v30, v21, s[6:7]
.LBB0_287:
	s_andn2_saveexec_b64 s[14:15], s[14:15]
	v_or_b32_e32 v20, v20, v83
	v_lshl_add_u32 v28, v28, 3, v76
	ds_write_b64 v28, v[20:21]
.LBB0_289:
	s_or_b64 exec, exec, s[12:13]
	v_cmp_neq_f32_e32 vcc, 0, v22
	s_and_saveexec_b64 s[12:13], vcc
	s_cbranch_execz .LBB0_298
	ds_add_rtn_u32 v20, v77, v81
	v_or_b32_e32 v28, 0x702, v84
	s_waitcnt lgkmcnt(0)
	v_cmp_lt_i32_e32 vcc, s21, v20
	s_and_saveexec_b64 s[14:15], vcc
	s_xor_b64 s[14:15], exec, s[14:15]
	s_cbranch_execz .LBB0_296
	v_lshlrev_b32_e32 v29, 2, v28
	global_atomic_add v64, v29, v81, s[4:5] sc0
	s_waitcnt vmcnt(0)
	v_cmp_lt_i32_e32 vcc, 63, v64
	s_and_saveexec_b64 s[16:17], vcc
	s_xor_b64 s[16:17], exec, s[16:17]
	s_cbranch_execz .LBB0_293
	v_mov_b64_e32 v[20:21], s[10:11]
	v_mad_u64_u32 v[20:21], s[18:19], v28, s22, v[20:21]
	v_lshl_add_u64 v[20:21], v[64:65], 3, v[20:21]
	global_store_dword v[20:21], v82, off
.LBB0_293:
	s_andn2_saveexec_b64 s[16:17], s[16:17]
	s_cbranch_execz .LBB0_295
	v_ashrrev_i32_e32 v21, 31, v64
	v_mov_b32_e32 v20, v64
	v_lshlrev_b32_e32 v64, 9, v28
	v_lshl_add_u64 v[30:31], s[8:9], 0, v[64:65]
	v_lshl_add_u64 v[20:21], v[20:21], 3, v[30:31]
	global_store_dword v[20:21], v82, off
.LBB0_295:
	s_or_b64 exec, exec, s[16:17]
	global_store_dword v[20:21], v22, off offset:4
	global_atomic_add_f32 v29, v22, s[6:7]
.LBB0_296:
	s_andn2_saveexec_b64 s[14:15], s[14:15]
	v_or_b32_e32 v68, v28, v83
	v_lshl_add_u32 v20, v20, 3, v76
	ds_write_b64 v20, v[68:69]
.LBB0_298:
	s_or_b64 exec, exec, s[12:13]
	v_cmp_neq_f32_e32 vcc, 0, v23
	s_and_b64 exec, exec, vcc
	s_cbranch_execz .LBB0_307
	ds_add_rtn_u32 v20, v77, v81
	v_or_b32_e32 v22, 0x703, v84
	s_waitcnt lgkmcnt(0)
	v_cmp_lt_i32_e32 vcc, s21, v20
	s_and_saveexec_b64 s[12:13], vcc
	s_xor_b64 s[12:13], exec, s[12:13]
	s_cbranch_execz .LBB0_305
	v_lshlrev_b32_e32 v28, 2, v22
	global_atomic_add v64, v28, v81, s[4:5] sc0
	s_waitcnt vmcnt(0)
	v_cmp_lt_i32_e32 vcc, 63, v64
	s_and_saveexec_b64 s[14:15], vcc
	s_xor_b64 s[14:15], exec, s[14:15]
	s_cbranch_execz .LBB0_302
	v_mov_b64_e32 v[20:21], s[10:11]
	v_mad_u64_u32 v[20:21], s[16:17], v22, s22, v[20:21]
	v_lshl_add_u64 v[20:21], v[64:65], 3, v[20:21]
	global_store_dword v[20:21], v82, off
.LBB0_302:
	s_andn2_saveexec_b64 s[14:15], s[14:15]
	s_cbranch_execz .LBB0_304
	v_ashrrev_i32_e32 v21, 31, v64
	v_mov_b32_e32 v20, v64
	v_lshlrev_b32_e32 v64, 9, v22
	v_lshl_add_u64 v[30:31], s[8:9], 0, v[64:65]
	v_lshl_add_u64 v[20:21], v[20:21], 3, v[30:31]
	global_store_dword v[20:21], v82, off
.LBB0_304:
	s_or_b64 exec, exec, s[14:15]
	global_store_dword v[20:21], v23, off offset:4
	global_atomic_add_f32 v28, v23, s[6:7]
.LBB0_305:
	s_andn2_saveexec_b64 s[12:13], s[12:13]
	v_or_b32_e32 v22, v22, v83
	v_lshl_add_u32 v20, v20, 3, v76
	ds_write_b64 v20, v[22:23]
.LBB0_307:
	s_or_b64 exec, exec, s[2:3]
	v_add_co_u32_e32 v20, vcc, 0x1000, v66
	global_load_dwordx4 v[60:63], v[66:67], off nt
	global_load_dwordx4 v[56:59], v[66:67], off offset:1024 nt
	global_load_dwordx4 v[52:55], v[66:67], off offset:2048 nt
	global_load_dwordx4 v[48:51], v[66:67], off offset:3072 nt
	v_addc_co_u32_e32 v21, vcc, 0, v67, vcc
	global_load_dwordx4 v[44:47], v[20:21], off nt
	global_load_dwordx4 v[36:39], v[20:21], off offset:1024 nt
	global_load_dwordx4 v[28:31], v[20:21], off offset:2048 nt
	s_nop 0
	global_load_dwordx4 v[20:23], v[20:21], off offset:3072 nt
	s_waitcnt vmcnt(13)
	v_or_b32_e32 v68, v25, v24
	v_or3_b32 v74, v68, v27, v26
	s_waitcnt vmcnt(8)
	v_or_b32_e32 v68, v0, v1
	v_or3_b32 v73, v68, v3, v2
	v_or3_b32 v68, v73, v5, v4
	v_or3_b32 v68, v68, v7, v6
	v_or3_b32 v68, v68, v9, v8
	v_or3_b32 v68, v68, v11, v10
	v_or3_b32 v68, v68, v13, v12
	v_or3_b32 v68, v68, v15, v14
	v_or3_b32 v68, v68, v17, v16
	v_or3_b32 v68, v68, v19, v18
	v_or_b32_e32 v64, v41, v40
	v_or3_b32 v68, v68, v33, v32
	v_or3_b32 v64, v64, v43, v42
	v_or3_b32 v68, v68, v35, v34
	v_or3_b32 v68, v68, v74, v64
	v_cmp_ne_u32_e32 vcc, 0, v68
	s_and_saveexec_b64 s[2:3], vcc
	s_cbranch_execz .LBB0_8
	s_or_b32 s12, s20, 1
	s_and_b32 s13, s12, 0xff
	s_mulk_i32 s13, 0xab
	s_bfe_u32 s13, s13, 0x6000a
	s_mul_i32 s13, s13, 6
	s_sub_i32 s12, s12, s13
	s_and_b32 s12, s12, 0xff
	v_lshl_or_b32 v72, s12, 11, v78
	v_cmp_ne_u32_e32 vcc, 0, v64
	s_and_saveexec_b64 s[12:13], vcc
	s_cbranch_execz .LBB0_345
	v_cmp_neq_f32_e32 vcc, 0, v40
	s_and_saveexec_b64 s[14:15], vcc
	s_cbranch_execz .LBB0_318
	ds_add_rtn_u32 v64, v77, v81
	s_waitcnt lgkmcnt(0)
	v_cmp_lt_i32_e32 vcc, s21, v64
	s_and_saveexec_b64 s[16:17], vcc
	s_xor_b64 s[16:17], exec, s[16:17]
	s_cbranch_execz .LBB0_316
	v_lshlrev_b32_e32 v75, 2, v72
	global_atomic_add v68, v75, v81, s[4:5] sc0
	s_waitcnt vmcnt(0)
	v_cmp_lt_i32_e32 vcc, 63, v68
	s_and_saveexec_b64 s[18:19], vcc
	s_xor_b64 s[18:19], exec, s[18:19]
	s_cbranch_execz .LBB0_313
	v_mov_b64_e32 v[70:71], s[10:11]
	v_mov_b32_e32 v69, v65
	v_mad_u64_u32 v[70:71], s[24:25], v72, s22, v[70:71]
	v_lshl_add_u64 v[70:71], v[68:69], 3, v[70:71]
	global_store_dword v[70:71], v82, off
.LBB0_313:
	s_andn2_saveexec_b64 s[18:19], s[18:19]
	s_cbranch_execz .LBB0_315
	v_lshlrev_b32_e32 v64, 9, v72
	v_ashrrev_i32_e32 v69, 31, v68
	v_lshl_add_u64 v[70:71], s[8:9], 0, v[64:65]
	v_lshl_add_u64 v[70:71], v[68:69], 3, v[70:71]
	global_store_dword v[70:71], v82, off
.LBB0_315:
	s_or_b64 exec, exec, s[18:19]
	global_store_dword v[70:71], v40, off offset:4
	global_atomic_add_f32 v75, v40, s[6:7]
.LBB0_316:
	s_andn2_saveexec_b64 s[16:17], s[16:17]
	v_or_b32_e32 v68, v72, v83
	v_lshl_add_u32 v64, v64, 3, v76
	v_mov_b32_e32 v69, v40
	ds_write_b64 v64, v[68:69]
.LBB0_318:
	s_or_b64 exec, exec, s[14:15]
	v_cmp_neq_f32_e32 vcc, 0, v41
	s_and_saveexec_b64 s[14:15], vcc
	s_cbranch_execz .LBB0_327
	ds_add_rtn_u32 v64, v77, v81
	v_or_b32_e32 v40, 1, v72
	s_waitcnt lgkmcnt(0)
	v_cmp_lt_i32_e32 vcc, s21, v64
	s_and_saveexec_b64 s[16:17], vcc
	s_xor_b64 s[16:17], exec, s[16:17]
	s_cbranch_execz .LBB0_325
	v_lshlrev_b32_e32 v70, 2, v72
	global_atomic_add v64, v70, v81, s[4:5] offset:4 sc0
	s_waitcnt vmcnt(0)
	v_cmp_lt_i32_e32 vcc, 63, v64
	s_and_saveexec_b64 s[18:19], vcc
	s_xor_b64 s[18:19], exec, s[18:19]
	s_cbranch_execz .LBB0_322
	v_mov_b64_e32 v[68:69], s[10:11]
	v_mad_u64_u32 v[68:69], s[24:25], v40, s22, v[68:69]
	v_lshl_add_u64 v[68:69], v[64:65], 3, v[68:69]
	global_store_dword v[68:69], v82, off
.LBB0_322:
	s_andn2_saveexec_b64 s[18:19], s[18:19]
	s_cbranch_execz .LBB0_324
	v_ashrrev_i32_e32 v69, 31, v64
	v_mov_b32_e32 v68, v64
	v_lshlrev_b32_e32 v64, 9, v40
	v_lshl_add_u64 v[84:85], s[8:9], 0, v[64:65]
	v_lshl_add_u64 v[68:69], v[68:69], 3, v[84:85]
	global_store_dword v[68:69], v82, off
.LBB0_324:
	s_or_b64 exec, exec, s[18:19]
	global_store_dword v[68:69], v41, off offset:4
	global_atomic_add_f32 v70, v41, s[6:7] offset:4
.LBB0_325:
	s_andn2_saveexec_b64 s[16:17], s[16:17]
	v_or_b32_e32 v40, v40, v83
	v_lshl_add_u32 v64, v64, 3, v76
	ds_write_b64 v64, v[40:41]
.LBB0_327:
	s_or_b64 exec, exec, s[14:15]
	v_cmp_neq_f32_e32 vcc, 0, v42
	s_and_saveexec_b64 s[14:15], vcc
	s_cbranch_execz .LBB0_336
	ds_add_rtn_u32 v40, v77, v81
	v_or_b32_e32 v68, 2, v72
	s_waitcnt lgkmcnt(0)
	v_cmp_lt_i32_e32 vcc, s21, v40
	s_and_saveexec_b64 s[16:17], vcc
	s_xor_b64 s[16:17], exec, s[16:17]
	s_cbranch_execz .LBB0_334
	v_lshlrev_b32_e32 v69, 2, v72
	global_atomic_add v64, v69, v81, s[4:5] offset:8 sc0
	s_waitcnt vmcnt(0)
	v_cmp_lt_i32_e32 vcc, 63, v64
	s_and_saveexec_b64 s[18:19], vcc
	s_xor_b64 s[18:19], exec, s[18:19]
	s_cbranch_execz .LBB0_331
	v_mov_b64_e32 v[40:41], s[10:11]
	v_mad_u64_u32 v[40:41], s[24:25], v68, s22, v[40:41]
	v_lshl_add_u64 v[40:41], v[64:65], 3, v[40:41]
	global_store_dword v[40:41], v82, off
.LBB0_331:
	s_andn2_saveexec_b64 s[18:19], s[18:19]
	s_cbranch_execz .LBB0_333
	v_ashrrev_i32_e32 v41, 31, v64
	v_mov_b32_e32 v40, v64
	v_lshlrev_b32_e32 v64, 9, v68
	v_lshl_add_u64 v[70:71], s[8:9], 0, v[64:65]
	v_lshl_add_u64 v[40:41], v[40:41], 3, v[70:71]
	global_store_dword v[40:41], v82, off
.LBB0_333:
	s_or_b64 exec, exec, s[18:19]
	global_store_dword v[40:41], v42, off offset:4
	global_atomic_add_f32 v69, v42, s[6:7] offset:8
.LBB0_334:
	s_andn2_saveexec_b64 s[16:17], s[16:17]
	v_or_b32_e32 v68, v68, v83
	v_lshl_add_u32 v40, v40, 3, v76
	v_mov_b32_e32 v69, v42
	ds_write_b64 v40, v[68:69]
.LBB0_336:
	s_or_b64 exec, exec, s[14:15]
	v_cmp_neq_f32_e32 vcc, 0, v43
	s_and_b64 exec, exec, vcc
	s_cbranch_execz .LBB0_345
	ds_add_rtn_u32 v64, v77, v81
	v_or_b32_e32 v68, 3, v72
	s_waitcnt lgkmcnt(0)
	v_cmp_lt_i32_e32 vcc, s21, v64
	s_and_saveexec_b64 s[14:15], vcc
	s_xor_b64 s[14:15], exec, s[14:15]
	s_cbranch_execz .LBB0_343
	v_lshlrev_b32_e32 v42, 2, v72
	global_atomic_add v64, v42, v81, s[4:5] offset:12 sc0
	s_waitcnt vmcnt(0)
	v_cmp_lt_i32_e32 vcc, 63, v64
	s_and_saveexec_b64 s[16:17], vcc
	s_xor_b64 s[16:17], exec, s[16:17]
	s_cbranch_execz .LBB0_340
	v_mov_b64_e32 v[40:41], s[10:11]
	v_mad_u64_u32 v[40:41], s[18:19], v68, s22, v[40:41]
	v_lshl_add_u64 v[40:41], v[64:65], 3, v[40:41]
	global_store_dword v[40:41], v82, off
.LBB0_340:
	s_andn2_saveexec_b64 s[16:17], s[16:17]
	s_cbranch_execz .LBB0_342
	v_ashrrev_i32_e32 v41, 31, v64
	v_mov_b32_e32 v40, v64
	v_lshlrev_b32_e32 v64, 9, v68
	v_lshl_add_u64 v[68:69], s[8:9], 0, v[64:65]
	v_lshl_add_u64 v[40:41], v[40:41], 3, v[68:69]
	global_store_dword v[40:41], v82, off
.LBB0_342:
	s_or_b64 exec, exec, s[16:17]
	global_store_dword v[40:41], v43, off offset:4
	global_atomic_add_f32 v42, v43, s[6:7] offset:12
.LBB0_343:
	s_andn2_saveexec_b64 s[14:15], s[14:15]
	v_or_b32_e32 v42, v68, v83
	v_lshl_add_u32 v40, v64, 3, v76
	ds_write_b64 v40, v[42:43]
.LBB0_345:
	s_or_b64 exec, exec, s[12:13]
	v_or_b32_e32 v40, v32, v33
	v_or3_b32 v40, v40, v35, v34
	v_cmp_ne_u32_e32 vcc, 0, v40
	s_and_saveexec_b64 s[12:13], vcc
	s_cbranch_execz .LBB0_382
	v_cmp_neq_f32_e32 vcc, 0, v32
	s_and_saveexec_b64 s[14:15], vcc
	s_cbranch_execz .LBB0_355
	ds_add_rtn_u32 v40, v77, v81
	v_or_b32_e32 v42, 0x100, v72
	s_waitcnt lgkmcnt(0)
	v_cmp_lt_i32_e32 vcc, s21, v40
	s_and_saveexec_b64 s[16:17], vcc
	s_xor_b64 s[16:17], exec, s[16:17]
	s_cbranch_execz .LBB0_353
	v_lshlrev_b32_e32 v43, 2, v72
	global_atomic_add v64, v43, v81, s[4:5] offset:1024 sc0
	s_waitcnt vmcnt(0)
	v_cmp_lt_i32_e32 vcc, 63, v64
	s_and_saveexec_b64 s[18:19], vcc
	s_xor_b64 s[18:19], exec, s[18:19]
	s_cbranch_execz .LBB0_350
	v_mov_b64_e32 v[40:41], s[10:11]
	v_mad_u64_u32 v[40:41], s[24:25], v42, s22, v[40:41]
	v_lshl_add_u64 v[40:41], v[64:65], 3, v[40:41]
	global_store_dword v[40:41], v82, off
.LBB0_350:
	s_andn2_saveexec_b64 s[18:19], s[18:19]
	s_cbranch_execz .LBB0_352
	v_ashrrev_i32_e32 v41, 31, v64
	v_mov_b32_e32 v40, v64
	v_lshlrev_b32_e32 v64, 9, v42
	v_lshl_add_u64 v[68:69], s[8:9], 0, v[64:65]
	v_lshl_add_u64 v[40:41], v[40:41], 3, v[68:69]
	global_store_dword v[40:41], v82, off
.LBB0_352:
	s_or_b64 exec, exec, s[18:19]
	global_store_dword v[40:41], v32, off offset:4
	global_atomic_add_f32 v43, v32, s[6:7] offset:1024
.LBB0_353:
	s_andn2_saveexec_b64 s[16:17], s[16:17]
	v_or_b32_e32 v42, v42, v83
	v_lshl_add_u32 v40, v40, 3, v76
	v_mov_b32_e32 v43, v32
	ds_write_b64 v40, v[42:43]
.LBB0_355:
	s_or_b64 exec, exec, s[14:15]
	v_cmp_neq_f32_e32 vcc, 0, v33
	s_and_saveexec_b64 s[14:15], vcc
	s_cbranch_execz .LBB0_364
	ds_add_rtn_u32 v40, v77, v81
	v_or_b32_e32 v32, 0x101, v72
	s_waitcnt lgkmcnt(0)
	v_cmp_lt_i32_e32 vcc, s21, v40
	s_and_saveexec_b64 s[16:17], vcc
	s_xor_b64 s[16:17], exec, s[16:17]
	s_cbranch_execz .LBB0_362
	v_lshlrev_b32_e32 v42, 2, v72
	global_atomic_add v64, v42, v81, s[4:5] offset:1028 sc0
	s_waitcnt vmcnt(0)
	v_cmp_lt_i32_e32 vcc, 63, v64
	s_and_saveexec_b64 s[18:19], vcc
	s_xor_b64 s[18:19], exec, s[18:19]
	s_cbranch_execz .LBB0_359
	v_mov_b64_e32 v[40:41], s[10:11]
	v_mad_u64_u32 v[40:41], s[24:25], v32, s22, v[40:41]
	v_lshl_add_u64 v[40:41], v[64:65], 3, v[40:41]
	global_store_dword v[40:41], v82, off
.LBB0_359:
	s_andn2_saveexec_b64 s[18:19], s[18:19]
	s_cbranch_execz .LBB0_361
	v_ashrrev_i32_e32 v41, 31, v64
	v_mov_b32_e32 v40, v64
	v_lshlrev_b32_e32 v64, 9, v32
	v_lshl_add_u64 v[68:69], s[8:9], 0, v[64:65]
	v_lshl_add_u64 v[40:41], v[40:41], 3, v[68:69]
	global_store_dword v[40:41], v82, off
.LBB0_361:
	s_or_b64 exec, exec, s[18:19]
	global_store_dword v[40:41], v33, off offset:4
	global_atomic_add_f32 v42, v33, s[6:7] offset:1028
.LBB0_362:
	s_andn2_saveexec_b64 s[16:17], s[16:17]
	v_or_b32_e32 v32, v32, v83
	v_lshl_add_u32 v40, v40, 3, v76
	ds_write_b64 v40, v[32:33]
.LBB0_364:
	s_or_b64 exec, exec, s[14:15]
	v_cmp_neq_f32_e32 vcc, 0, v34
	s_and_saveexec_b64 s[14:15], vcc
	s_cbranch_execz .LBB0_373
	ds_add_rtn_u32 v32, v77, v81
	v_or_b32_e32 v40, 0x102, v72
	s_waitcnt lgkmcnt(0)
	v_cmp_lt_i32_e32 vcc, s21, v32
	s_and_saveexec_b64 s[16:17], vcc
	s_xor_b64 s[16:17], exec, s[16:17]
	s_cbranch_execz .LBB0_371
	v_lshlrev_b32_e32 v41, 2, v72
	global_atomic_add v64, v41, v81, s[4:5] offset:1032 sc0
	s_waitcnt vmcnt(0)
	v_cmp_lt_i32_e32 vcc, 63, v64
	s_and_saveexec_b64 s[18:19], vcc
	s_xor_b64 s[18:19], exec, s[18:19]
	s_cbranch_execz .LBB0_368
	v_mov_b64_e32 v[32:33], s[10:11]
	v_mad_u64_u32 v[32:33], s[24:25], v40, s22, v[32:33]
	v_lshl_add_u64 v[32:33], v[64:65], 3, v[32:33]
	global_store_dword v[32:33], v82, off
.LBB0_368:
	s_andn2_saveexec_b64 s[18:19], s[18:19]
	s_cbranch_execz .LBB0_370
	v_ashrrev_i32_e32 v33, 31, v64
	v_mov_b32_e32 v32, v64
	v_lshlrev_b32_e32 v64, 9, v40
	v_lshl_add_u64 v[42:43], s[8:9], 0, v[64:65]
	v_lshl_add_u64 v[32:33], v[32:33], 3, v[42:43]
	global_store_dword v[32:33], v82, off
.LBB0_370:
	s_or_b64 exec, exec, s[18:19]
	global_store_dword v[32:33], v34, off offset:4
	global_atomic_add_f32 v41, v34, s[6:7] offset:1032
.LBB0_371:
	s_andn2_saveexec_b64 s[16:17], s[16:17]
	v_or_b32_e32 v40, v40, v83
	v_lshl_add_u32 v32, v32, 3, v76
	v_mov_b32_e32 v41, v34
	ds_write_b64 v32, v[40:41]
.LBB0_373:
	s_or_b64 exec, exec, s[14:15]
	v_cmp_neq_f32_e32 vcc, 0, v35
	s_and_b64 exec, exec, vcc
	s_cbranch_execz .LBB0_382
	ds_add_rtn_u32 v41, v77, v81
	v_or_b32_e32 v40, 0x103, v72
	s_waitcnt lgkmcnt(0)
	v_cmp_lt_i32_e32 vcc, s21, v41
	s_and_saveexec_b64 s[14:15], vcc
	s_xor_b64 s[14:15], exec, s[14:15]
	s_cbranch_execz .LBB0_380
	v_lshlrev_b32_e32 v34, 2, v72
	global_atomic_add v64, v34, v81, s[4:5] offset:1036 sc0
	s_waitcnt vmcnt(0)
	v_cmp_lt_i32_e32 vcc, 63, v64
	s_and_saveexec_b64 s[16:17], vcc
	s_xor_b64 s[16:17], exec, s[16:17]
	s_cbranch_execz .LBB0_377
	v_mov_b64_e32 v[32:33], s[10:11]
	v_mad_u64_u32 v[32:33], s[18:19], v40, s22, v[32:33]
	v_lshl_add_u64 v[32:33], v[64:65], 3, v[32:33]
	global_store_dword v[32:33], v82, off
.LBB0_377:
	s_andn2_saveexec_b64 s[16:17], s[16:17]
	s_cbranch_execz .LBB0_379
	v_ashrrev_i32_e32 v33, 31, v64
	v_mov_b32_e32 v32, v64
	v_lshlrev_b32_e32 v64, 9, v40
	v_lshl_add_u64 v[40:41], s[8:9], 0, v[64:65]
	v_lshl_add_u64 v[32:33], v[32:33], 3, v[40:41]
	global_store_dword v[32:33], v82, off
.LBB0_379:
	s_or_b64 exec, exec, s[16:17]
	global_store_dword v[32:33], v35, off offset:4
	global_atomic_add_f32 v34, v35, s[6:7] offset:1036
.LBB0_380:
	s_andn2_saveexec_b64 s[14:15], s[14:15]
	v_or_b32_e32 v34, v40, v83
	v_lshl_add_u32 v32, v41, 3, v76
	ds_write_b64 v32, v[34:35]
.LBB0_382:
	s_or_b64 exec, exec, s[12:13]
	v_cmp_ne_u32_e32 vcc, 0, v74
	s_and_saveexec_b64 s[12:13], vcc
	s_cbranch_execz .LBB0_419
	v_cmp_neq_f32_e32 vcc, 0, v24
	s_and_saveexec_b64 s[14:15], vcc
	s_cbranch_execz .LBB0_392
	ds_add_rtn_u32 v32, v77, v81
	v_or_b32_e32 v34, 0x200, v72
	s_waitcnt lgkmcnt(0)
	v_cmp_lt_i32_e32 vcc, s21, v32
	s_and_saveexec_b64 s[16:17], vcc
	s_xor_b64 s[16:17], exec, s[16:17]
	s_cbranch_execz .LBB0_390
	v_lshlrev_b32_e32 v35, 2, v72
	global_atomic_add v64, v35, v81, s[4:5] offset:2048 sc0
	s_waitcnt vmcnt(0)
	v_cmp_lt_i32_e32 vcc, 63, v64
	s_and_saveexec_b64 s[18:19], vcc
	s_xor_b64 s[18:19], exec, s[18:19]
	s_cbranch_execz .LBB0_387
	v_mov_b64_e32 v[32:33], s[10:11]
	v_mad_u64_u32 v[32:33], s[24:25], v34, s22, v[32:33]
	v_lshl_add_u64 v[32:33], v[64:65], 3, v[32:33]
	global_store_dword v[32:33], v82, off
.LBB0_387:
	s_andn2_saveexec_b64 s[18:19], s[18:19]
	s_cbranch_execz .LBB0_389
	v_ashrrev_i32_e32 v33, 31, v64
	v_mov_b32_e32 v32, v64
	v_lshlrev_b32_e32 v64, 9, v34
	v_lshl_add_u64 v[40:41], s[8:9], 0, v[64:65]
	v_lshl_add_u64 v[32:33], v[32:33], 3, v[40:41]
	global_store_dword v[32:33], v82, off
.LBB0_389:
	s_or_b64 exec, exec, s[18:19]
	global_store_dword v[32:33], v24, off offset:4
	global_atomic_add_f32 v35, v24, s[6:7] offset:2048
.LBB0_390:
	s_andn2_saveexec_b64 s[16:17], s[16:17]
	v_or_b32_e32 v34, v34, v83
	v_lshl_add_u32 v32, v32, 3, v76
	v_mov_b32_e32 v35, v24
	ds_write_b64 v32, v[34:35]
.LBB0_392:
	s_or_b64 exec, exec, s[14:15]
	v_cmp_neq_f32_e32 vcc, 0, v25
	s_and_saveexec_b64 s[14:15], vcc
	s_cbranch_execz .LBB0_401
	ds_add_rtn_u32 v32, v77, v81
	v_or_b32_e32 v24, 0x201, v72
	s_waitcnt lgkmcnt(0)
	v_cmp_lt_i32_e32 vcc, s21, v32
	s_and_saveexec_b64 s[16:17], vcc
	s_xor_b64 s[16:17], exec, s[16:17]
	s_cbranch_execz .LBB0_399
	v_lshlrev_b32_e32 v34, 2, v72
	global_atomic_add v64, v34, v81, s[4:5] offset:2052 sc0
	s_waitcnt vmcnt(0)
	v_cmp_lt_i32_e32 vcc, 63, v64
	s_and_saveexec_b64 s[18:19], vcc
	s_xor_b64 s[18:19], exec, s[18:19]
	s_cbranch_execz .LBB0_396
	v_mov_b64_e32 v[32:33], s[10:11]
	v_mad_u64_u32 v[32:33], s[24:25], v24, s22, v[32:33]
	v_lshl_add_u64 v[32:33], v[64:65], 3, v[32:33]
	global_store_dword v[32:33], v82, off
.LBB0_396:
	s_andn2_saveexec_b64 s[18:19], s[18:19]
	s_cbranch_execz .LBB0_398
	v_ashrrev_i32_e32 v33, 31, v64
	v_mov_b32_e32 v32, v64
	v_lshlrev_b32_e32 v64, 9, v24
	v_lshl_add_u64 v[40:41], s[8:9], 0, v[64:65]
	v_lshl_add_u64 v[32:33], v[32:33], 3, v[40:41]
	global_store_dword v[32:33], v82, off
.LBB0_398:
	s_or_b64 exec, exec, s[18:19]
	global_store_dword v[32:33], v25, off offset:4
	global_atomic_add_f32 v34, v25, s[6:7] offset:2052
.LBB0_399:
	s_andn2_saveexec_b64 s[16:17], s[16:17]
	v_or_b32_e32 v24, v24, v83
	v_lshl_add_u32 v32, v32, 3, v76
	ds_write_b64 v32, v[24:25]
.LBB0_401:
	s_or_b64 exec, exec, s[14:15]
	v_cmp_neq_f32_e32 vcc, 0, v26
	s_and_saveexec_b64 s[14:15], vcc
	s_cbranch_execz .LBB0_410
	ds_add_rtn_u32 v24, v77, v81
	v_or_b32_e32 v32, 0x202, v72
	s_waitcnt lgkmcnt(0)
	v_cmp_lt_i32_e32 vcc, s21, v24
	s_and_saveexec_b64 s[16:17], vcc
	s_xor_b64 s[16:17], exec, s[16:17]
	s_cbranch_execz .LBB0_408
	v_lshlrev_b32_e32 v33, 2, v72
	global_atomic_add v64, v33, v81, s[4:5] offset:2056 sc0
	s_waitcnt vmcnt(0)
	v_cmp_lt_i32_e32 vcc, 63, v64
	s_and_saveexec_b64 s[18:19], vcc
	s_xor_b64 s[18:19], exec, s[18:19]
	s_cbranch_execz .LBB0_405
	v_mov_b64_e32 v[24:25], s[10:11]
	v_mad_u64_u32 v[24:25], s[24:25], v32, s22, v[24:25]
	v_lshl_add_u64 v[24:25], v[64:65], 3, v[24:25]
	global_store_dword v[24:25], v82, off
.LBB0_405:
	s_andn2_saveexec_b64 s[18:19], s[18:19]
	s_cbranch_execz .LBB0_407
	v_ashrrev_i32_e32 v25, 31, v64
	v_mov_b32_e32 v24, v64
	v_lshlrev_b32_e32 v64, 9, v32
	v_lshl_add_u64 v[34:35], s[8:9], 0, v[64:65]
	v_lshl_add_u64 v[24:25], v[24:25], 3, v[34:35]
	global_store_dword v[24:25], v82, off
.LBB0_407:
	s_or_b64 exec, exec, s[18:19]
	global_store_dword v[24:25], v26, off offset:4
	global_atomic_add_f32 v33, v26, s[6:7] offset:2056
.LBB0_408:
	s_andn2_saveexec_b64 s[16:17], s[16:17]
	v_or_b32_e32 v32, v32, v83
	v_lshl_add_u32 v24, v24, 3, v76
	v_mov_b32_e32 v33, v26
	ds_write_b64 v24, v[32:33]
.LBB0_410:
	s_or_b64 exec, exec, s[14:15]
	v_cmp_neq_f32_e32 vcc, 0, v27
	s_and_b64 exec, exec, vcc
	s_cbranch_execz .LBB0_419
	ds_add_rtn_u32 v33, v77, v81
	v_or_b32_e32 v32, 0x203, v72
	s_waitcnt lgkmcnt(0)
	v_cmp_lt_i32_e32 vcc, s21, v33
	s_and_saveexec_b64 s[14:15], vcc
	s_xor_b64 s[14:15], exec, s[14:15]
	s_cbranch_execz .LBB0_417
	v_lshlrev_b32_e32 v26, 2, v72
	global_atomic_add v64, v26, v81, s[4:5] offset:2060 sc0
	s_waitcnt vmcnt(0)
	v_cmp_lt_i32_e32 vcc, 63, v64
	s_and_saveexec_b64 s[16:17], vcc
	s_xor_b64 s[16:17], exec, s[16:17]
	s_cbranch_execz .LBB0_414
	v_mov_b64_e32 v[24:25], s[10:11]
	v_mad_u64_u32 v[24:25], s[18:19], v32, s22, v[24:25]
	v_lshl_add_u64 v[24:25], v[64:65], 3, v[24:25]
	global_store_dword v[24:25], v82, off
.LBB0_414:
	s_andn2_saveexec_b64 s[16:17], s[16:17]
	s_cbranch_execz .LBB0_416
	v_ashrrev_i32_e32 v25, 31, v64
	v_mov_b32_e32 v24, v64
	v_lshlrev_b32_e32 v64, 9, v32
	v_lshl_add_u64 v[32:33], s[8:9], 0, v[64:65]
	v_lshl_add_u64 v[24:25], v[24:25], 3, v[32:33]
	global_store_dword v[24:25], v82, off
.LBB0_416:
	s_or_b64 exec, exec, s[16:17]
	global_store_dword v[24:25], v27, off offset:4
	global_atomic_add_f32 v26, v27, s[6:7] offset:2060
.LBB0_417:
	s_andn2_saveexec_b64 s[14:15], s[14:15]
	v_or_b32_e32 v26, v32, v83
	v_lshl_add_u32 v24, v33, 3, v76
	ds_write_b64 v24, v[26:27]
.LBB0_419:
	s_or_b64 exec, exec, s[12:13]
	v_or_b32_e32 v24, v16, v17
	v_or3_b32 v24, v24, v19, v18
	v_cmp_ne_u32_e32 vcc, 0, v24
	s_and_saveexec_b64 s[12:13], vcc
	s_cbranch_execz .LBB0_456
	v_cmp_neq_f32_e32 vcc, 0, v16
	s_and_saveexec_b64 s[14:15], vcc
	s_cbranch_execz .LBB0_429
	ds_add_rtn_u32 v24, v77, v81
	v_or_b32_e32 v26, 0x300, v72
	s_waitcnt lgkmcnt(0)
	v_cmp_lt_i32_e32 vcc, s21, v24
	s_and_saveexec_b64 s[16:17], vcc
	s_xor_b64 s[16:17], exec, s[16:17]
	s_cbranch_execz .LBB0_427
	v_lshlrev_b32_e32 v27, 2, v72
	global_atomic_add v64, v27, v81, s[4:5] offset:3072 sc0
	s_waitcnt vmcnt(0)
	v_cmp_lt_i32_e32 vcc, 63, v64
	s_and_saveexec_b64 s[18:19], vcc
	s_xor_b64 s[18:19], exec, s[18:19]
	s_cbranch_execz .LBB0_424
	v_mov_b64_e32 v[24:25], s[10:11]
	v_mad_u64_u32 v[24:25], s[24:25], v26, s22, v[24:25]
	v_lshl_add_u64 v[24:25], v[64:65], 3, v[24:25]
	global_store_dword v[24:25], v82, off
.LBB0_424:
	s_andn2_saveexec_b64 s[18:19], s[18:19]
	s_cbranch_execz .LBB0_426
	v_ashrrev_i32_e32 v25, 31, v64
	v_mov_b32_e32 v24, v64
	v_lshlrev_b32_e32 v64, 9, v26
	v_lshl_add_u64 v[32:33], s[8:9], 0, v[64:65]
	v_lshl_add_u64 v[24:25], v[24:25], 3, v[32:33]
	global_store_dword v[24:25], v82, off
.LBB0_426:
	s_or_b64 exec, exec, s[18:19]
	global_store_dword v[24:25], v16, off offset:4
	global_atomic_add_f32 v27, v16, s[6:7] offset:3072
.LBB0_427:
	s_andn2_saveexec_b64 s[16:17], s[16:17]
	v_or_b32_e32 v26, v26, v83
	v_lshl_add_u32 v24, v24, 3, v76
	v_mov_b32_e32 v27, v16
	ds_write_b64 v24, v[26:27]
.LBB0_429:
	s_or_b64 exec, exec, s[14:15]
	v_cmp_neq_f32_e32 vcc, 0, v17
	s_and_saveexec_b64 s[14:15], vcc
	s_cbranch_execz .LBB0_438
	ds_add_rtn_u32 v24, v77, v81
	v_or_b32_e32 v16, 0x301, v72
	s_waitcnt lgkmcnt(0)
	v_cmp_lt_i32_e32 vcc, s21, v24
	s_and_saveexec_b64 s[16:17], vcc
	s_xor_b64 s[16:17], exec, s[16:17]
	s_cbranch_execz .LBB0_436
	v_lshlrev_b32_e32 v26, 2, v72
	global_atomic_add v64, v26, v81, s[4:5] offset:3076 sc0
	s_waitcnt vmcnt(0)
	v_cmp_lt_i32_e32 vcc, 63, v64
	s_and_saveexec_b64 s[18:19], vcc
	s_xor_b64 s[18:19], exec, s[18:19]
	s_cbranch_execz .LBB0_433
	v_mov_b64_e32 v[24:25], s[10:11]
	v_mad_u64_u32 v[24:25], s[24:25], v16, s22, v[24:25]
	v_lshl_add_u64 v[24:25], v[64:65], 3, v[24:25]
	global_store_dword v[24:25], v82, off
.LBB0_433:
	s_andn2_saveexec_b64 s[18:19], s[18:19]
	s_cbranch_execz .LBB0_435
	v_ashrrev_i32_e32 v25, 31, v64
	v_mov_b32_e32 v24, v64
	v_lshlrev_b32_e32 v64, 9, v16
	v_lshl_add_u64 v[32:33], s[8:9], 0, v[64:65]
	v_lshl_add_u64 v[24:25], v[24:25], 3, v[32:33]
	global_store_dword v[24:25], v82, off
.LBB0_435:
	s_or_b64 exec, exec, s[18:19]
	global_store_dword v[24:25], v17, off offset:4
	global_atomic_add_f32 v26, v17, s[6:7] offset:3076
.LBB0_436:
	s_andn2_saveexec_b64 s[16:17], s[16:17]
	v_or_b32_e32 v16, v16, v83
	v_lshl_add_u32 v24, v24, 3, v76
	ds_write_b64 v24, v[16:17]
.LBB0_438:
	s_or_b64 exec, exec, s[14:15]
	v_cmp_neq_f32_e32 vcc, 0, v18
	s_and_saveexec_b64 s[14:15], vcc
	s_cbranch_execz .LBB0_447
	ds_add_rtn_u32 v16, v77, v81
	v_or_b32_e32 v24, 0x302, v72
	s_waitcnt lgkmcnt(0)
	v_cmp_lt_i32_e32 vcc, s21, v16
	s_and_saveexec_b64 s[16:17], vcc
	s_xor_b64 s[16:17], exec, s[16:17]
	s_cbranch_execz .LBB0_445
	v_lshlrev_b32_e32 v25, 2, v72
	global_atomic_add v64, v25, v81, s[4:5] offset:3080 sc0
	s_waitcnt vmcnt(0)
	v_cmp_lt_i32_e32 vcc, 63, v64
	s_and_saveexec_b64 s[18:19], vcc
	s_xor_b64 s[18:19], exec, s[18:19]
	s_cbranch_execz .LBB0_442
	v_mov_b64_e32 v[16:17], s[10:11]
	v_mad_u64_u32 v[16:17], s[24:25], v24, s22, v[16:17]
	v_lshl_add_u64 v[16:17], v[64:65], 3, v[16:17]
	global_store_dword v[16:17], v82, off
.LBB0_442:
	s_andn2_saveexec_b64 s[18:19], s[18:19]
	s_cbranch_execz .LBB0_444
	v_ashrrev_i32_e32 v17, 31, v64
	v_mov_b32_e32 v16, v64
	v_lshlrev_b32_e32 v64, 9, v24
	v_lshl_add_u64 v[26:27], s[8:9], 0, v[64:65]
	v_lshl_add_u64 v[16:17], v[16:17], 3, v[26:27]
	global_store_dword v[16:17], v82, off
.LBB0_444:
	s_or_b64 exec, exec, s[18:19]
	global_store_dword v[16:17], v18, off offset:4
	global_atomic_add_f32 v25, v18, s[6:7] offset:3080
.LBB0_445:
	s_andn2_saveexec_b64 s[16:17], s[16:17]
	v_or_b32_e32 v24, v24, v83
	v_lshl_add_u32 v16, v16, 3, v76
	v_mov_b32_e32 v25, v18
	ds_write_b64 v16, v[24:25]
.LBB0_447:
	s_or_b64 exec, exec, s[14:15]
	v_cmp_neq_f32_e32 vcc, 0, v19
	s_and_b64 exec, exec, vcc
	s_cbranch_execz .LBB0_456
	ds_add_rtn_u32 v25, v77, v81
	v_or_b32_e32 v24, 0x303, v72
	s_waitcnt lgkmcnt(0)
	v_cmp_lt_i32_e32 vcc, s21, v25
	s_and_saveexec_b64 s[14:15], vcc
	s_xor_b64 s[14:15], exec, s[14:15]
	s_cbranch_execz .LBB0_454
	v_lshlrev_b32_e32 v18, 2, v72
	global_atomic_add v64, v18, v81, s[4:5] offset:3084 sc0
	s_waitcnt vmcnt(0)
	v_cmp_lt_i32_e32 vcc, 63, v64
	s_and_saveexec_b64 s[16:17], vcc
	s_xor_b64 s[16:17], exec, s[16:17]
	s_cbranch_execz .LBB0_451
	v_mov_b64_e32 v[16:17], s[10:11]
	v_mad_u64_u32 v[16:17], s[18:19], v24, s22, v[16:17]
	v_lshl_add_u64 v[16:17], v[64:65], 3, v[16:17]
	global_store_dword v[16:17], v82, off
.LBB0_451:
	s_andn2_saveexec_b64 s[16:17], s[16:17]
	s_cbranch_execz .LBB0_453
	v_ashrrev_i32_e32 v17, 31, v64
	v_mov_b32_e32 v16, v64
	v_lshlrev_b32_e32 v64, 9, v24
	v_lshl_add_u64 v[24:25], s[8:9], 0, v[64:65]
	v_lshl_add_u64 v[16:17], v[16:17], 3, v[24:25]
	global_store_dword v[16:17], v82, off
.LBB0_453:
	s_or_b64 exec, exec, s[16:17]
	global_store_dword v[16:17], v19, off offset:4
	global_atomic_add_f32 v18, v19, s[6:7] offset:3084
.LBB0_454:
	s_andn2_saveexec_b64 s[14:15], s[14:15]
	v_or_b32_e32 v18, v24, v83
	v_lshl_add_u32 v16, v25, 3, v76
	ds_write_b64 v16, v[18:19]
.LBB0_456:
	s_or_b64 exec, exec, s[12:13]
	v_or_b32_e32 v16, v12, v13
	v_or3_b32 v16, v16, v15, v14
	v_cmp_ne_u32_e32 vcc, 0, v16
	s_and_saveexec_b64 s[12:13], vcc
	s_cbranch_execz .LBB0_493
	v_cmp_neq_f32_e32 vcc, 0, v12
	s_and_saveexec_b64 s[14:15], vcc
	s_cbranch_execz .LBB0_466
	ds_add_rtn_u32 v16, v77, v81
	v_or_b32_e32 v18, 0x400, v72
	s_waitcnt lgkmcnt(0)
	v_cmp_lt_i32_e32 vcc, s21, v16
	s_and_saveexec_b64 s[16:17], vcc
	s_xor_b64 s[16:17], exec, s[16:17]
	s_cbranch_execz .LBB0_464
	v_lshlrev_b32_e32 v19, 2, v18
	global_atomic_add v64, v19, v81, s[4:5] sc0
	s_waitcnt vmcnt(0)
	v_cmp_lt_i32_e32 vcc, 63, v64
	s_and_saveexec_b64 s[18:19], vcc
	s_xor_b64 s[18:19], exec, s[18:19]
	s_cbranch_execz .LBB0_461
	v_mov_b64_e32 v[16:17], s[10:11]
	v_mad_u64_u32 v[16:17], s[24:25], v18, s22, v[16:17]
	v_lshl_add_u64 v[16:17], v[64:65], 3, v[16:17]
	global_store_dword v[16:17], v82, off
.LBB0_461:
	s_andn2_saveexec_b64 s[18:19], s[18:19]
	s_cbranch_execz .LBB0_463
	v_ashrrev_i32_e32 v17, 31, v64
	v_mov_b32_e32 v16, v64
	v_lshlrev_b32_e32 v64, 9, v18
	v_lshl_add_u64 v[24:25], s[8:9], 0, v[64:65]
	v_lshl_add_u64 v[16:17], v[16:17], 3, v[24:25]
	global_store_dword v[16:17], v82, off
.LBB0_463:
	s_or_b64 exec, exec, s[18:19]
	global_store_dword v[16:17], v12, off offset:4
	global_atomic_add_f32 v19, v12, s[6:7]
.LBB0_464:
	s_andn2_saveexec_b64 s[16:17], s[16:17]
	v_or_b32_e32 v18, v18, v83
	v_lshl_add_u32 v16, v16, 3, v76
	v_mov_b32_e32 v19, v12
	ds_write_b64 v16, v[18:19]
.LBB0_466:
	s_or_b64 exec, exec, s[14:15]
	v_cmp_neq_f32_e32 vcc, 0, v13
	s_and_saveexec_b64 s[14:15], vcc
	s_cbranch_execz .LBB0_475
	ds_add_rtn_u32 v16, v77, v81
	v_or_b32_e32 v12, 0x401, v72
	s_waitcnt lgkmcnt(0)
	v_cmp_lt_i32_e32 vcc, s21, v16
	s_and_saveexec_b64 s[16:17], vcc
	s_xor_b64 s[16:17], exec, s[16:17]
	s_cbranch_execz .LBB0_473
	v_lshlrev_b32_e32 v18, 2, v12
	global_atomic_add v64, v18, v81, s[4:5] sc0
	s_waitcnt vmcnt(0)
	v_cmp_lt_i32_e32 vcc, 63, v64
	s_and_saveexec_b64 s[18:19], vcc
	s_xor_b64 s[18:19], exec, s[18:19]
	s_cbranch_execz .LBB0_470
	v_mov_b64_e32 v[16:17], s[10:11]
	v_mad_u64_u32 v[16:17], s[24:25], v12, s22, v[16:17]
	v_lshl_add_u64 v[16:17], v[64:65], 3, v[16:17]
	global_store_dword v[16:17], v82, off
.LBB0_470:
	s_andn2_saveexec_b64 s[18:19], s[18:19]
	s_cbranch_execz .LBB0_472
	v_ashrrev_i32_e32 v17, 31, v64
	v_mov_b32_e32 v16, v64
	v_lshlrev_b32_e32 v64, 9, v12
	v_lshl_add_u64 v[24:25], s[8:9], 0, v[64:65]
	v_lshl_add_u64 v[16:17], v[16:17], 3, v[24:25]
	global_store_dword v[16:17], v82, off
.LBB0_472:
	s_or_b64 exec, exec, s[18:19]
	global_store_dword v[16:17], v13, off offset:4
	global_atomic_add_f32 v18, v13, s[6:7]
.LBB0_473:
	s_andn2_saveexec_b64 s[16:17], s[16:17]
	v_or_b32_e32 v12, v12, v83
	v_lshl_add_u32 v16, v16, 3, v76
	ds_write_b64 v16, v[12:13]
.LBB0_475:
	s_or_b64 exec, exec, s[14:15]
	v_cmp_neq_f32_e32 vcc, 0, v14
	s_and_saveexec_b64 s[14:15], vcc
	s_cbranch_execz .LBB0_484
	ds_add_rtn_u32 v12, v77, v81
	v_or_b32_e32 v16, 0x402, v72
	s_waitcnt lgkmcnt(0)
	v_cmp_lt_i32_e32 vcc, s21, v12
	s_and_saveexec_b64 s[16:17], vcc
	s_xor_b64 s[16:17], exec, s[16:17]
	s_cbranch_execz .LBB0_482
	v_lshlrev_b32_e32 v17, 2, v16
	global_atomic_add v64, v17, v81, s[4:5] sc0
	s_waitcnt vmcnt(0)
	v_cmp_lt_i32_e32 vcc, 63, v64
	s_and_saveexec_b64 s[18:19], vcc
	s_xor_b64 s[18:19], exec, s[18:19]
	s_cbranch_execz .LBB0_479
	v_mov_b64_e32 v[12:13], s[10:11]
	v_mad_u64_u32 v[12:13], s[24:25], v16, s22, v[12:13]
	v_lshl_add_u64 v[12:13], v[64:65], 3, v[12:13]
	global_store_dword v[12:13], v82, off
.LBB0_479:
	s_andn2_saveexec_b64 s[18:19], s[18:19]
	s_cbranch_execz .LBB0_481
	v_ashrrev_i32_e32 v13, 31, v64
	v_mov_b32_e32 v12, v64
	v_lshlrev_b32_e32 v64, 9, v16
	v_lshl_add_u64 v[18:19], s[8:9], 0, v[64:65]
	v_lshl_add_u64 v[12:13], v[12:13], 3, v[18:19]
	global_store_dword v[12:13], v82, off
.LBB0_481:
	s_or_b64 exec, exec, s[18:19]
	global_store_dword v[12:13], v14, off offset:4
	global_atomic_add_f32 v17, v14, s[6:7]
.LBB0_482:
	s_andn2_saveexec_b64 s[16:17], s[16:17]
	v_or_b32_e32 v16, v16, v83
	v_lshl_add_u32 v12, v12, 3, v76
	v_mov_b32_e32 v17, v14
	ds_write_b64 v12, v[16:17]
.LBB0_484:
	s_or_b64 exec, exec, s[14:15]
	v_cmp_neq_f32_e32 vcc, 0, v15
	s_and_b64 exec, exec, vcc
	s_cbranch_execz .LBB0_493
	ds_add_rtn_u32 v17, v77, v81
	v_or_b32_e32 v16, 0x403, v72
	s_waitcnt lgkmcnt(0)
	v_cmp_lt_i32_e32 vcc, s21, v17
	s_and_saveexec_b64 s[14:15], vcc
	s_xor_b64 s[14:15], exec, s[14:15]
	s_cbranch_execz .LBB0_491
	v_lshlrev_b32_e32 v14, 2, v16
	global_atomic_add v64, v14, v81, s[4:5] sc0
	s_waitcnt vmcnt(0)
	v_cmp_lt_i32_e32 vcc, 63, v64
	s_and_saveexec_b64 s[16:17], vcc
	s_xor_b64 s[16:17], exec, s[16:17]
	s_cbranch_execz .LBB0_488
	v_mov_b64_e32 v[12:13], s[10:11]
	v_mad_u64_u32 v[12:13], s[18:19], v16, s22, v[12:13]
	v_lshl_add_u64 v[12:13], v[64:65], 3, v[12:13]
	global_store_dword v[12:13], v82, off
.LBB0_488:
	s_andn2_saveexec_b64 s[16:17], s[16:17]
	s_cbranch_execz .LBB0_490
	v_ashrrev_i32_e32 v13, 31, v64
	v_mov_b32_e32 v12, v64
	v_lshlrev_b32_e32 v64, 9, v16
	v_lshl_add_u64 v[16:17], s[8:9], 0, v[64:65]
	v_lshl_add_u64 v[12:13], v[12:13], 3, v[16:17]
	global_store_dword v[12:13], v82, off
.LBB0_490:
	s_or_b64 exec, exec, s[16:17]
	global_store_dword v[12:13], v15, off offset:4
	global_atomic_add_f32 v14, v15, s[6:7]
.LBB0_491:
	s_andn2_saveexec_b64 s[14:15], s[14:15]
	v_or_b32_e32 v14, v16, v83
	v_lshl_add_u32 v12, v17, 3, v76
	ds_write_b64 v12, v[14:15]
.LBB0_493:
	s_or_b64 exec, exec, s[12:13]
	v_or_b32_e32 v12, v8, v9
	v_or3_b32 v12, v12, v11, v10
	v_cmp_ne_u32_e32 vcc, 0, v12
	s_and_saveexec_b64 s[12:13], vcc
	s_cbranch_execz .LBB0_530
	v_cmp_neq_f32_e32 vcc, 0, v8
	s_and_saveexec_b64 s[14:15], vcc
	s_cbranch_execz .LBB0_503
	ds_add_rtn_u32 v12, v77, v81
	v_or_b32_e32 v14, 0x500, v72
	s_waitcnt lgkmcnt(0)
	v_cmp_lt_i32_e32 vcc, s21, v12
	s_and_saveexec_b64 s[16:17], vcc
	s_xor_b64 s[16:17], exec, s[16:17]
	s_cbranch_execz .LBB0_501
	v_lshlrev_b32_e32 v15, 2, v14
	global_atomic_add v64, v15, v81, s[4:5] sc0
	s_waitcnt vmcnt(0)
	v_cmp_lt_i32_e32 vcc, 63, v64
	s_and_saveexec_b64 s[18:19], vcc
	s_xor_b64 s[18:19], exec, s[18:19]
	s_cbranch_execz .LBB0_498
	v_mov_b64_e32 v[12:13], s[10:11]
	v_mad_u64_u32 v[12:13], s[24:25], v14, s22, v[12:13]
	v_lshl_add_u64 v[12:13], v[64:65], 3, v[12:13]
	global_store_dword v[12:13], v82, off
.LBB0_498:
	s_andn2_saveexec_b64 s[18:19], s[18:19]
	s_cbranch_execz .LBB0_500
	v_ashrrev_i32_e32 v13, 31, v64
	v_mov_b32_e32 v12, v64
	v_lshlrev_b32_e32 v64, 9, v14
	v_lshl_add_u64 v[16:17], s[8:9], 0, v[64:65]
	v_lshl_add_u64 v[12:13], v[12:13], 3, v[16:17]
	global_store_dword v[12:13], v82, off
.LBB0_500:
	s_or_b64 exec, exec, s[18:19]
	global_store_dword v[12:13], v8, off offset:4
	global_atomic_add_f32 v15, v8, s[6:7]
.LBB0_501:
	s_andn2_saveexec_b64 s[16:17], s[16:17]
	v_or_b32_e32 v14, v14, v83
	v_lshl_add_u32 v12, v12, 3, v76
	v_mov_b32_e32 v15, v8
	ds_write_b64 v12, v[14:15]
.LBB0_503:
	s_or_b64 exec, exec, s[14:15]
	v_cmp_neq_f32_e32 vcc, 0, v9
	s_and_saveexec_b64 s[14:15], vcc
	s_cbranch_execz .LBB0_512
	ds_add_rtn_u32 v12, v77, v81
	v_or_b32_e32 v8, 0x501, v72
	s_waitcnt lgkmcnt(0)
	v_cmp_lt_i32_e32 vcc, s21, v12
	s_and_saveexec_b64 s[16:17], vcc
	s_xor_b64 s[16:17], exec, s[16:17]
	s_cbranch_execz .LBB0_510
	v_lshlrev_b32_e32 v14, 2, v8
	global_atomic_add v64, v14, v81, s[4:5] sc0
	s_waitcnt vmcnt(0)
	v_cmp_lt_i32_e32 vcc, 63, v64
	s_and_saveexec_b64 s[18:19], vcc
	s_xor_b64 s[18:19], exec, s[18:19]
	s_cbranch_execz .LBB0_507
	v_mov_b64_e32 v[12:13], s[10:11]
	v_mad_u64_u32 v[12:13], s[24:25], v8, s22, v[12:13]
	v_lshl_add_u64 v[12:13], v[64:65], 3, v[12:13]
	global_store_dword v[12:13], v82, off
.LBB0_507:
	s_andn2_saveexec_b64 s[18:19], s[18:19]
	s_cbranch_execz .LBB0_509
	v_ashrrev_i32_e32 v13, 31, v64
	v_mov_b32_e32 v12, v64
	v_lshlrev_b32_e32 v64, 9, v8
	v_lshl_add_u64 v[16:17], s[8:9], 0, v[64:65]
	v_lshl_add_u64 v[12:13], v[12:13], 3, v[16:17]
	global_store_dword v[12:13], v82, off
.LBB0_509:
	s_or_b64 exec, exec, s[18:19]
	global_store_dword v[12:13], v9, off offset:4
	global_atomic_add_f32 v14, v9, s[6:7]
.LBB0_510:
	s_andn2_saveexec_b64 s[16:17], s[16:17]
	v_or_b32_e32 v8, v8, v83
	v_lshl_add_u32 v12, v12, 3, v76
	ds_write_b64 v12, v[8:9]
.LBB0_512:
	s_or_b64 exec, exec, s[14:15]
	v_cmp_neq_f32_e32 vcc, 0, v10
	s_and_saveexec_b64 s[14:15], vcc
	s_cbranch_execz .LBB0_521
	ds_add_rtn_u32 v8, v77, v81
	v_or_b32_e32 v12, 0x502, v72
	s_waitcnt lgkmcnt(0)
	v_cmp_lt_i32_e32 vcc, s21, v8
	s_and_saveexec_b64 s[16:17], vcc
	s_xor_b64 s[16:17], exec, s[16:17]
	s_cbranch_execz .LBB0_519
	v_lshlrev_b32_e32 v13, 2, v12
	global_atomic_add v64, v13, v81, s[4:5] sc0
	s_waitcnt vmcnt(0)
	v_cmp_lt_i32_e32 vcc, 63, v64
	s_and_saveexec_b64 s[18:19], vcc
	s_xor_b64 s[18:19], exec, s[18:19]
	s_cbranch_execz .LBB0_516
	v_mov_b64_e32 v[8:9], s[10:11]
	v_mad_u64_u32 v[8:9], s[24:25], v12, s22, v[8:9]
	v_lshl_add_u64 v[8:9], v[64:65], 3, v[8:9]
	global_store_dword v[8:9], v82, off
.LBB0_516:
	s_andn2_saveexec_b64 s[18:19], s[18:19]
	s_cbranch_execz .LBB0_518
	v_ashrrev_i32_e32 v9, 31, v64
	v_mov_b32_e32 v8, v64
	v_lshlrev_b32_e32 v64, 9, v12
	v_lshl_add_u64 v[14:15], s[8:9], 0, v[64:65]
	v_lshl_add_u64 v[8:9], v[8:9], 3, v[14:15]
	global_store_dword v[8:9], v82, off
.LBB0_518:
	s_or_b64 exec, exec, s[18:19]
	global_store_dword v[8:9], v10, off offset:4
	global_atomic_add_f32 v13, v10, s[6:7]
.LBB0_519:
	s_andn2_saveexec_b64 s[16:17], s[16:17]
	v_or_b32_e32 v12, v12, v83
	v_lshl_add_u32 v8, v8, 3, v76
	v_mov_b32_e32 v13, v10
	ds_write_b64 v8, v[12:13]
.LBB0_521:
	s_or_b64 exec, exec, s[14:15]
	v_cmp_neq_f32_e32 vcc, 0, v11
	s_and_b64 exec, exec, vcc
	s_cbranch_execz .LBB0_530
	ds_add_rtn_u32 v13, v77, v81
	v_or_b32_e32 v12, 0x503, v72
	s_waitcnt lgkmcnt(0)
	v_cmp_lt_i32_e32 vcc, s21, v13
	s_and_saveexec_b64 s[14:15], vcc
	s_xor_b64 s[14:15], exec, s[14:15]
	s_cbranch_execz .LBB0_528
	v_lshlrev_b32_e32 v10, 2, v12
	global_atomic_add v64, v10, v81, s[4:5] sc0
	s_waitcnt vmcnt(0)
	v_cmp_lt_i32_e32 vcc, 63, v64
	s_and_saveexec_b64 s[16:17], vcc
	s_xor_b64 s[16:17], exec, s[16:17]
	s_cbranch_execz .LBB0_525
	v_mov_b64_e32 v[8:9], s[10:11]
	v_mad_u64_u32 v[8:9], s[18:19], v12, s22, v[8:9]
	v_lshl_add_u64 v[8:9], v[64:65], 3, v[8:9]
	global_store_dword v[8:9], v82, off
.LBB0_525:
	s_andn2_saveexec_b64 s[16:17], s[16:17]
	s_cbranch_execz .LBB0_527
	v_ashrrev_i32_e32 v9, 31, v64
	v_mov_b32_e32 v8, v64
	v_lshlrev_b32_e32 v64, 9, v12
	v_lshl_add_u64 v[12:13], s[8:9], 0, v[64:65]
	v_lshl_add_u64 v[8:9], v[8:9], 3, v[12:13]
	global_store_dword v[8:9], v82, off
.LBB0_527:
	s_or_b64 exec, exec, s[16:17]
	global_store_dword v[8:9], v11, off offset:4
	global_atomic_add_f32 v10, v11, s[6:7]
.LBB0_528:
	s_andn2_saveexec_b64 s[14:15], s[14:15]
	v_or_b32_e32 v10, v12, v83
	v_lshl_add_u32 v8, v13, 3, v76
	ds_write_b64 v8, v[10:11]
.LBB0_530:
	s_or_b64 exec, exec, s[12:13]
	v_or_b32_e32 v8, v4, v5
	v_or3_b32 v8, v8, v7, v6
	v_cmp_ne_u32_e32 vcc, 0, v8
	s_and_saveexec_b64 s[12:13], vcc
	s_cbranch_execz .LBB0_567
	v_cmp_neq_f32_e32 vcc, 0, v4
	s_and_saveexec_b64 s[14:15], vcc
	s_cbranch_execz .LBB0_540
	ds_add_rtn_u32 v8, v77, v81
	v_or_b32_e32 v10, 0x600, v72
	s_waitcnt lgkmcnt(0)
	v_cmp_lt_i32_e32 vcc, s21, v8
	s_and_saveexec_b64 s[16:17], vcc
	s_xor_b64 s[16:17], exec, s[16:17]
	s_cbranch_execz .LBB0_538
	v_lshlrev_b32_e32 v11, 2, v10
	global_atomic_add v64, v11, v81, s[4:5] sc0
	s_waitcnt vmcnt(0)
	v_cmp_lt_i32_e32 vcc, 63, v64
	s_and_saveexec_b64 s[18:19], vcc
	s_xor_b64 s[18:19], exec, s[18:19]
	s_cbranch_execz .LBB0_535
	v_mov_b64_e32 v[8:9], s[10:11]
	v_mad_u64_u32 v[8:9], s[24:25], v10, s22, v[8:9]
	v_lshl_add_u64 v[8:9], v[64:65], 3, v[8:9]
	global_store_dword v[8:9], v82, off
.LBB0_535:
	s_andn2_saveexec_b64 s[18:19], s[18:19]
	s_cbranch_execz .LBB0_537
	v_ashrrev_i32_e32 v9, 31, v64
	v_mov_b32_e32 v8, v64
	v_lshlrev_b32_e32 v64, 9, v10
	v_lshl_add_u64 v[12:13], s[8:9], 0, v[64:65]
	v_lshl_add_u64 v[8:9], v[8:9], 3, v[12:13]
	global_store_dword v[8:9], v82, off
.LBB0_537:
	s_or_b64 exec, exec, s[18:19]
	global_store_dword v[8:9], v4, off offset:4
	global_atomic_add_f32 v11, v4, s[6:7]
.LBB0_538:
	s_andn2_saveexec_b64 s[16:17], s[16:17]
	v_or_b32_e32 v10, v10, v83
	v_lshl_add_u32 v8, v8, 3, v76
	v_mov_b32_e32 v11, v4
	ds_write_b64 v8, v[10:11]
.LBB0_540:
	s_or_b64 exec, exec, s[14:15]
	v_cmp_neq_f32_e32 vcc, 0, v5
	s_and_saveexec_b64 s[14:15], vcc
	s_cbranch_execz .LBB0_549
	ds_add_rtn_u32 v8, v77, v81
	v_or_b32_e32 v4, 0x601, v72
	s_waitcnt lgkmcnt(0)
	v_cmp_lt_i32_e32 vcc, s21, v8
	s_and_saveexec_b64 s[16:17], vcc
	s_xor_b64 s[16:17], exec, s[16:17]
	s_cbranch_execz .LBB0_547
	v_lshlrev_b32_e32 v10, 2, v4
	global_atomic_add v64, v10, v81, s[4:5] sc0
	s_waitcnt vmcnt(0)
	v_cmp_lt_i32_e32 vcc, 63, v64
	s_and_saveexec_b64 s[18:19], vcc
	s_xor_b64 s[18:19], exec, s[18:19]
	s_cbranch_execz .LBB0_544
	v_mov_b64_e32 v[8:9], s[10:11]
	v_mad_u64_u32 v[8:9], s[24:25], v4, s22, v[8:9]
	v_lshl_add_u64 v[8:9], v[64:65], 3, v[8:9]
	global_store_dword v[8:9], v82, off
.LBB0_544:
	s_andn2_saveexec_b64 s[18:19], s[18:19]
	s_cbranch_execz .LBB0_546
	v_ashrrev_i32_e32 v9, 31, v64
	v_mov_b32_e32 v8, v64
	v_lshlrev_b32_e32 v64, 9, v4
	v_lshl_add_u64 v[12:13], s[8:9], 0, v[64:65]
	v_lshl_add_u64 v[8:9], v[8:9], 3, v[12:13]
	global_store_dword v[8:9], v82, off
.LBB0_546:
	s_or_b64 exec, exec, s[18:19]
	global_store_dword v[8:9], v5, off offset:4
	global_atomic_add_f32 v10, v5, s[6:7]
.LBB0_547:
	s_andn2_saveexec_b64 s[16:17], s[16:17]
	v_or_b32_e32 v4, v4, v83
	v_lshl_add_u32 v8, v8, 3, v76
	ds_write_b64 v8, v[4:5]
.LBB0_549:
	s_or_b64 exec, exec, s[14:15]
	v_cmp_neq_f32_e32 vcc, 0, v6
	s_and_saveexec_b64 s[14:15], vcc
	s_cbranch_execz .LBB0_558
	ds_add_rtn_u32 v4, v77, v81
	v_or_b32_e32 v8, 0x602, v72
	s_waitcnt lgkmcnt(0)
	v_cmp_lt_i32_e32 vcc, s21, v4
	s_and_saveexec_b64 s[16:17], vcc
	s_xor_b64 s[16:17], exec, s[16:17]
	s_cbranch_execz .LBB0_556
	v_lshlrev_b32_e32 v9, 2, v8
	global_atomic_add v64, v9, v81, s[4:5] sc0
	s_waitcnt vmcnt(0)
	v_cmp_lt_i32_e32 vcc, 63, v64
	s_and_saveexec_b64 s[18:19], vcc
	s_xor_b64 s[18:19], exec, s[18:19]
	s_cbranch_execz .LBB0_553
	v_mov_b64_e32 v[4:5], s[10:11]
	v_mad_u64_u32 v[4:5], s[24:25], v8, s22, v[4:5]
	v_lshl_add_u64 v[4:5], v[64:65], 3, v[4:5]
	global_store_dword v[4:5], v82, off
.LBB0_553:
	s_andn2_saveexec_b64 s[18:19], s[18:19]
	s_cbranch_execz .LBB0_555
	v_ashrrev_i32_e32 v5, 31, v64
	v_mov_b32_e32 v4, v64
	v_lshlrev_b32_e32 v64, 9, v8
	v_lshl_add_u64 v[10:11], s[8:9], 0, v[64:65]
	v_lshl_add_u64 v[4:5], v[4:5], 3, v[10:11]
	global_store_dword v[4:5], v82, off
.LBB0_555:
	s_or_b64 exec, exec, s[18:19]
	global_store_dword v[4:5], v6, off offset:4
	global_atomic_add_f32 v9, v6, s[6:7]
.LBB0_556:
	s_andn2_saveexec_b64 s[16:17], s[16:17]
	v_or_b32_e32 v8, v8, v83
	v_lshl_add_u32 v4, v4, 3, v76
	v_mov_b32_e32 v9, v6
	ds_write_b64 v4, v[8:9]
.LBB0_558:
	s_or_b64 exec, exec, s[14:15]
	v_cmp_neq_f32_e32 vcc, 0, v7
	s_and_b64 exec, exec, vcc
	s_cbranch_execz .LBB0_567
	ds_add_rtn_u32 v9, v77, v81
	v_or_b32_e32 v8, 0x603, v72
	s_waitcnt lgkmcnt(0)
	v_cmp_lt_i32_e32 vcc, s21, v9
	s_and_saveexec_b64 s[14:15], vcc
	s_xor_b64 s[14:15], exec, s[14:15]
	s_cbranch_execz .LBB0_565
	v_lshlrev_b32_e32 v6, 2, v8
	global_atomic_add v64, v6, v81, s[4:5] sc0
	s_waitcnt vmcnt(0)
	v_cmp_lt_i32_e32 vcc, 63, v64
	s_and_saveexec_b64 s[16:17], vcc
	s_xor_b64 s[16:17], exec, s[16:17]
	s_cbranch_execz .LBB0_562
	v_mov_b64_e32 v[4:5], s[10:11]
	v_mad_u64_u32 v[4:5], s[18:19], v8, s22, v[4:5]
	v_lshl_add_u64 v[4:5], v[64:65], 3, v[4:5]
	global_store_dword v[4:5], v82, off
.LBB0_562:
	s_andn2_saveexec_b64 s[16:17], s[16:17]
	s_cbranch_execz .LBB0_564
	v_ashrrev_i32_e32 v5, 31, v64
	v_mov_b32_e32 v4, v64
	v_lshlrev_b32_e32 v64, 9, v8
	v_lshl_add_u64 v[8:9], s[8:9], 0, v[64:65]
	v_lshl_add_u64 v[4:5], v[4:5], 3, v[8:9]
	global_store_dword v[4:5], v82, off
.LBB0_564:
	s_or_b64 exec, exec, s[16:17]
	global_store_dword v[4:5], v7, off offset:4
	global_atomic_add_f32 v6, v7, s[6:7]
.LBB0_565:
	s_andn2_saveexec_b64 s[14:15], s[14:15]
	v_or_b32_e32 v6, v8, v83
	v_lshl_add_u32 v4, v9, 3, v76
	ds_write_b64 v4, v[6:7]
.LBB0_567:
	s_or_b64 exec, exec, s[12:13]
	v_cmp_ne_u32_e32 vcc, 0, v73
	s_and_b64 exec, exec, vcc
	s_cbranch_execz .LBB0_8
	v_cmp_neq_f32_e32 vcc, 0, v0
	s_and_saveexec_b64 s[12:13], vcc
	s_cbranch_execz .LBB0_577
	ds_add_rtn_u32 v4, v77, v81
	v_or_b32_e32 v6, 0x700, v72
	s_waitcnt lgkmcnt(0)
	v_cmp_lt_i32_e32 vcc, s21, v4
	s_and_saveexec_b64 s[14:15], vcc
	s_xor_b64 s[14:15], exec, s[14:15]
	s_cbranch_execz .LBB0_575
	v_lshlrev_b32_e32 v7, 2, v6
	global_atomic_add v64, v7, v81, s[4:5] sc0
	s_waitcnt vmcnt(0)
	v_cmp_lt_i32_e32 vcc, 63, v64
	s_and_saveexec_b64 s[16:17], vcc
	s_xor_b64 s[16:17], exec, s[16:17]
	s_cbranch_execz .LBB0_572
	v_mov_b64_e32 v[4:5], s[10:11]
	v_mad_u64_u32 v[4:5], s[18:19], v6, s22, v[4:5]
	v_lshl_add_u64 v[4:5], v[64:65], 3, v[4:5]
	global_store_dword v[4:5], v82, off
.LBB0_572:
	s_andn2_saveexec_b64 s[16:17], s[16:17]
	s_cbranch_execz .LBB0_574
	v_ashrrev_i32_e32 v5, 31, v64
	v_mov_b32_e32 v4, v64
	v_lshlrev_b32_e32 v64, 9, v6
	v_lshl_add_u64 v[8:9], s[8:9], 0, v[64:65]
	v_lshl_add_u64 v[4:5], v[4:5], 3, v[8:9]
	global_store_dword v[4:5], v82, off
.LBB0_574:
	s_or_b64 exec, exec, s[16:17]
	global_store_dword v[4:5], v0, off offset:4
	global_atomic_add_f32 v7, v0, s[6:7]
.LBB0_575:
	s_andn2_saveexec_b64 s[14:15], s[14:15]
	v_or_b32_e32 v6, v6, v83
	v_lshl_add_u32 v4, v4, 3, v76
	v_mov_b32_e32 v7, v0
	ds_write_b64 v4, v[6:7]
.LBB0_577:
	s_or_b64 exec, exec, s[12:13]
	v_cmp_neq_f32_e32 vcc, 0, v1
	s_and_saveexec_b64 s[12:13], vcc
	s_cbranch_execz .LBB0_586
	ds_add_rtn_u32 v4, v77, v81
	v_or_b32_e32 v0, 0x701, v72
	s_waitcnt lgkmcnt(0)
	v_cmp_lt_i32_e32 vcc, s21, v4
	s_and_saveexec_b64 s[14:15], vcc
	s_xor_b64 s[14:15], exec, s[14:15]
	s_cbranch_execz .LBB0_584
	v_lshlrev_b32_e32 v6, 2, v0
	global_atomic_add v64, v6, v81, s[4:5] sc0
	s_waitcnt vmcnt(0)
	v_cmp_lt_i32_e32 vcc, 63, v64
	s_and_saveexec_b64 s[16:17], vcc
	s_xor_b64 s[16:17], exec, s[16:17]
	s_cbranch_execz .LBB0_581
	v_mov_b64_e32 v[4:5], s[10:11]
	v_mad_u64_u32 v[4:5], s[18:19], v0, s22, v[4:5]
	v_lshl_add_u64 v[4:5], v[64:65], 3, v[4:5]
	global_store_dword v[4:5], v82, off
.LBB0_581:
	s_andn2_saveexec_b64 s[16:17], s[16:17]
	s_cbranch_execz .LBB0_583
	v_ashrrev_i32_e32 v5, 31, v64
	v_mov_b32_e32 v4, v64
	v_lshlrev_b32_e32 v64, 9, v0
	v_lshl_add_u64 v[8:9], s[8:9], 0, v[64:65]
	v_lshl_add_u64 v[4:5], v[4:5], 3, v[8:9]
	global_store_dword v[4:5], v82, off
.LBB0_583:
	s_or_b64 exec, exec, s[16:17]
	global_store_dword v[4:5], v1, off offset:4
	global_atomic_add_f32 v6, v1, s[6:7]
.LBB0_584:
	s_andn2_saveexec_b64 s[14:15], s[14:15]
	v_or_b32_e32 v0, v0, v83
	v_lshl_add_u32 v4, v4, 3, v76
	ds_write_b64 v4, v[0:1]
.LBB0_586:
	s_or_b64 exec, exec, s[12:13]
	v_cmp_neq_f32_e32 vcc, 0, v2
	s_and_saveexec_b64 s[12:13], vcc
	s_cbranch_execz .LBB0_595
	ds_add_rtn_u32 v0, v77, v81
	v_or_b32_e32 v4, 0x702, v72
	s_waitcnt lgkmcnt(0)
	v_cmp_lt_i32_e32 vcc, s21, v0
	s_and_saveexec_b64 s[14:15], vcc
	s_xor_b64 s[14:15], exec, s[14:15]
	s_cbranch_execz .LBB0_593
	v_lshlrev_b32_e32 v5, 2, v4
	global_atomic_add v64, v5, v81, s[4:5] sc0
	s_waitcnt vmcnt(0)
	v_cmp_lt_i32_e32 vcc, 63, v64
	s_and_saveexec_b64 s[16:17], vcc
	s_xor_b64 s[16:17], exec, s[16:17]
	s_cbranch_execz .LBB0_590
	v_mov_b64_e32 v[0:1], s[10:11]
	v_mad_u64_u32 v[0:1], s[18:19], v4, s22, v[0:1]
	v_lshl_add_u64 v[0:1], v[64:65], 3, v[0:1]
	global_store_dword v[0:1], v82, off
.LBB0_590:
	s_andn2_saveexec_b64 s[16:17], s[16:17]
	s_cbranch_execz .LBB0_592
	v_ashrrev_i32_e32 v1, 31, v64
	v_mov_b32_e32 v0, v64
	v_lshlrev_b32_e32 v64, 9, v4
	v_lshl_add_u64 v[6:7], s[8:9], 0, v[64:65]
	v_lshl_add_u64 v[0:1], v[0:1], 3, v[6:7]
	global_store_dword v[0:1], v82, off
.LBB0_592:
	s_or_b64 exec, exec, s[16:17]
	global_store_dword v[0:1], v2, off offset:4
	global_atomic_add_f32 v5, v2, s[6:7]
.LBB0_593:
	s_andn2_saveexec_b64 s[14:15], s[14:15]
	v_or_b32_e32 v4, v4, v83
	v_lshl_add_u32 v0, v0, 3, v76
	v_mov_b32_e32 v5, v2
	ds_write_b64 v0, v[4:5]
.LBB0_595:
	s_or_b64 exec, exec, s[12:13]
	v_cmp_neq_f32_e32 vcc, 0, v3
	s_and_b64 exec, exec, vcc
	s_cbranch_execz .LBB0_8
	ds_add_rtn_u32 v5, v77, v81
	v_or_b32_e32 v4, 0x703, v72
	s_waitcnt lgkmcnt(0)
	v_cmp_lt_i32_e32 vcc, s21, v5
	s_and_saveexec_b64 s[12:13], vcc
	s_xor_b64 s[12:13], exec, s[12:13]
	s_cbranch_execz .LBB0_602
	v_lshlrev_b32_e32 v2, 2, v4
	global_atomic_add v64, v2, v81, s[4:5] sc0
	s_waitcnt vmcnt(0)
	v_cmp_lt_i32_e32 vcc, 63, v64
	s_and_saveexec_b64 s[14:15], vcc
	s_xor_b64 s[14:15], exec, s[14:15]
	s_cbranch_execz .LBB0_599
	v_mov_b64_e32 v[0:1], s[10:11]
	v_mad_u64_u32 v[0:1], s[16:17], v4, s22, v[0:1]
	v_lshl_add_u64 v[0:1], v[64:65], 3, v[0:1]
	global_store_dword v[0:1], v82, off
.LBB0_599:
	s_andn2_saveexec_b64 s[14:15], s[14:15]
	s_cbranch_execz .LBB0_601
	v_ashrrev_i32_e32 v1, 31, v64
	v_mov_b32_e32 v0, v64
	v_lshlrev_b32_e32 v64, 9, v4
	v_lshl_add_u64 v[4:5], s[8:9], 0, v[64:65]
	v_lshl_add_u64 v[0:1], v[0:1], 3, v[4:5]
	global_store_dword v[0:1], v82, off
.LBB0_601:
	s_or_b64 exec, exec, s[14:15]
	global_store_dword v[0:1], v3, off offset:4
	global_atomic_add_f32 v2, v3, s[6:7]
.LBB0_602:
	s_andn2_saveexec_b64 s[12:13], s[12:13]
	s_cbranch_execz .LBB0_8
	v_or_b32_e32 v2, v4, v83
	v_lshl_add_u32 v0, v5, 3, v76
	ds_write_b64 v0, v[2:3]
	s_branch .LBB0_8
.LBB0_604:
	s_waitcnt vmcnt(13)
	v_or_b32_e32 v65, v53, v52
	v_or3_b32 v71, v65, v55, v54
	s_waitcnt vmcnt(12)
	v_or_b32_e32 v65, v48, v49
	v_or3_b32 v70, v65, v51, v50
	s_waitcnt vmcnt(11)
	v_or3_b32 v65, v70, v45, v44
	v_or3_b32 v65, v65, v47, v46
	s_waitcnt vmcnt(10)
	v_or3_b32 v65, v65, v37, v36
	v_or3_b32 v65, v65, v39, v38
	s_waitcnt vmcnt(9)
	v_or3_b32 v65, v65, v29, v28
	v_or3_b32 v65, v65, v31, v30
	s_waitcnt vmcnt(8)
	v_or3_b32 v65, v65, v21, v20
	v_or3_b32 v65, v65, v23, v22
	v_or_b32_e32 v64, v61, v60
	v_or3_b32 v65, v65, v57, v56
	v_or3_b32 v64, v64, v63, v62
	v_or3_b32 v65, v65, v59, v58
	v_add_u32_e32 v68, 5, v79
	v_or3_b32 v65, v65, v71, v64
	v_cmp_ne_u32_e32 vcc, 0, v65
	v_lshlrev_b32_e32 v69, 14, v68
	s_and_saveexec_b64 s[0:1], vcc
	s_cbranch_execz .LBB0_901
	v_cmp_ne_u32_e32 vcc, 0, v64
	s_and_saveexec_b64 s[2:3], vcc
	s_cbranch_execz .LBB0_642
	v_cmp_neq_f32_e32 vcc, 0, v60
	s_and_saveexec_b64 s[12:13], vcc
	s_cbranch_execz .LBB0_615
	v_mov_b32_e32 v65, 1
	ds_add_rtn_u32 v64, v77, v65
	s_movk_i32 s14, 0x7f
	v_or_b32_e32 v72, 0x2000, v78
	s_waitcnt lgkmcnt(0)
	v_cmp_lt_i32_e32 vcc, s14, v64
	s_and_saveexec_b64 s[14:15], vcc
	s_xor_b64 s[14:15], exec, s[14:15]
	s_cbranch_execz .LBB0_613
	v_lshlrev_b32_e32 v73, 2, v72
	global_atomic_add v64, v73, v65, s[4:5] sc0
	v_mov_b32_e32 v65, 0
	s_waitcnt vmcnt(0)
	v_cmp_lt_i32_e32 vcc, 63, v64
	s_and_saveexec_b64 s[16:17], vcc
	s_xor_b64 s[16:17], exec, s[16:17]
	s_cbranch_execz .LBB0_610
	s_mov_b32 s18, 0x18000
	v_mov_b64_e32 v[66:67], s[10:11]
	v_mad_u64_u32 v[66:67], s[18:19], v72, s18, v[66:67]
	v_lshl_add_u64 v[66:67], v[64:65], 3, v[66:67]
	global_store_dword v[66:67], v68, off
.LBB0_610:
	s_andn2_saveexec_b64 s[16:17], s[16:17]
	s_cbranch_execz .LBB0_612
	v_lshlrev_b32_e32 v66, 9, v72
	v_mov_b32_e32 v67, 0
	v_ashrrev_i32_e32 v65, 31, v64
	v_lshl_add_u64 v[66:67], s[8:9], 0, v[66:67]
	v_lshl_add_u64 v[66:67], v[64:65], 3, v[66:67]
	global_store_dword v[66:67], v68, off
.LBB0_612:
	s_or_b64 exec, exec, s[16:17]
	global_store_dword v[66:67], v60, off offset:4
	global_atomic_add_f32 v73, v60, s[6:7]
.LBB0_613:
	s_andn2_saveexec_b64 s[14:15], s[14:15]
	v_or_b32_e32 v66, v69, v72
	v_lshl_add_u32 v64, v64, 3, v76
	v_mov_b32_e32 v67, v60
	ds_write_b64 v64, v[66:67]
.LBB0_615:
	s_or_b64 exec, exec, s[12:13]
	v_cmp_neq_f32_e32 vcc, 0, v61
	s_and_saveexec_b64 s[12:13], vcc
	s_cbranch_execz .LBB0_624
	v_mov_b32_e32 v65, 1
	ds_add_rtn_u32 v64, v77, v65
	s_movk_i32 s14, 0x7f
	v_or_b32_e32 v60, 0x2001, v78
	s_waitcnt lgkmcnt(0)
	v_cmp_lt_i32_e32 vcc, s14, v64
	s_and_saveexec_b64 s[14:15], vcc
	s_xor_b64 s[14:15], exec, s[14:15]
	s_cbranch_execz .LBB0_622
	v_lshlrev_b32_e32 v72, 2, v60
	global_atomic_add v64, v72, v65, s[4:5] sc0
	v_mov_b32_e32 v65, 0
	s_waitcnt vmcnt(0)
	v_cmp_lt_i32_e32 vcc, 63, v64
	s_and_saveexec_b64 s[16:17], vcc
	s_xor_b64 s[16:17], exec, s[16:17]
	s_cbranch_execz .LBB0_619
	s_mov_b32 s18, 0x18000
	v_mov_b64_e32 v[66:67], s[10:11]
	v_mad_u64_u32 v[66:67], s[18:19], v60, s18, v[66:67]
	v_lshl_add_u64 v[66:67], v[64:65], 3, v[66:67]
	global_store_dword v[66:67], v68, off
.LBB0_619:
	s_andn2_saveexec_b64 s[16:17], s[16:17]
	s_cbranch_execz .LBB0_621
	v_lshlrev_b32_e32 v66, 9, v60
	v_mov_b32_e32 v67, 0
	v_ashrrev_i32_e32 v65, 31, v64
	v_lshl_add_u64 v[66:67], s[8:9], 0, v[66:67]
	v_lshl_add_u64 v[66:67], v[64:65], 3, v[66:67]
	global_store_dword v[66:67], v68, off
.LBB0_621:
	s_or_b64 exec, exec, s[16:17]
	global_store_dword v[66:67], v61, off offset:4
	global_atomic_add_f32 v72, v61, s[6:7]
.LBB0_622:
	s_andn2_saveexec_b64 s[14:15], s[14:15]
	v_or_b32_e32 v60, v69, v60
	v_lshl_add_u32 v64, v64, 3, v76
	ds_write_b64 v64, v[60:61]
.LBB0_624:
	s_or_b64 exec, exec, s[12:13]
	v_cmp_neq_f32_e32 vcc, 0, v62
	s_and_saveexec_b64 s[12:13], vcc
	s_cbranch_execz .LBB0_633
	v_mov_b32_e32 v61, 1
	ds_add_rtn_u32 v60, v77, v61
	s_movk_i32 s14, 0x7f
	v_or_b32_e32 v66, 0x2002, v78
	s_waitcnt lgkmcnt(0)
	v_cmp_lt_i32_e32 vcc, s14, v60
	s_and_saveexec_b64 s[14:15], vcc
	s_xor_b64 s[14:15], exec, s[14:15]
	s_cbranch_execz .LBB0_631
	v_lshlrev_b32_e32 v67, 2, v66
	global_atomic_add v60, v67, v61, s[4:5] sc0
	v_mov_b32_e32 v61, 0
	s_waitcnt vmcnt(0)
	v_cmp_lt_i32_e32 vcc, 63, v60
	s_and_saveexec_b64 s[16:17], vcc
	s_xor_b64 s[16:17], exec, s[16:17]
	s_cbranch_execz .LBB0_628
	s_mov_b32 s18, 0x18000
	v_mov_b64_e32 v[64:65], s[10:11]
	v_mad_u64_u32 v[64:65], s[18:19], v66, s18, v[64:65]
	v_lshl_add_u64 v[64:65], v[60:61], 3, v[64:65]
	global_store_dword v[64:65], v68, off
.LBB0_628:
	s_andn2_saveexec_b64 s[16:17], s[16:17]
	s_cbranch_execz .LBB0_630
	v_lshlrev_b32_e32 v64, 9, v66
	v_mov_b32_e32 v65, 0
	v_ashrrev_i32_e32 v61, 31, v60
	v_lshl_add_u64 v[64:65], s[8:9], 0, v[64:65]
	v_lshl_add_u64 v[64:65], v[60:61], 3, v[64:65]
	global_store_dword v[64:65], v68, off
.LBB0_630:
	s_or_b64 exec, exec, s[16:17]
	global_store_dword v[64:65], v62, off offset:4
	global_atomic_add_f32 v67, v62, s[6:7]
.LBB0_631:
	s_andn2_saveexec_b64 s[14:15], s[14:15]
	v_or_b32_e32 v64, v69, v66
	v_lshl_add_u32 v60, v60, 3, v76
	v_mov_b32_e32 v65, v62
	ds_write_b64 v60, v[64:65]
.LBB0_633:
	s_or_b64 exec, exec, s[12:13]
	v_cmp_neq_f32_e32 vcc, 0, v63
	s_and_b64 exec, exec, vcc
	s_cbranch_execz .LBB0_642
	v_mov_b32_e32 v61, 1
	ds_add_rtn_u32 v60, v77, v61
	s_movk_i32 s12, 0x7f
	v_or_b32_e32 v62, 0x2003, v78
	s_waitcnt lgkmcnt(0)
	v_cmp_lt_i32_e32 vcc, s12, v60
	s_and_saveexec_b64 s[12:13], vcc
	s_xor_b64 s[12:13], exec, s[12:13]
	s_cbranch_execz .LBB0_640
	v_lshlrev_b32_e32 v66, 2, v62
	global_atomic_add v60, v66, v61, s[4:5] sc0
	v_mov_b32_e32 v61, 0
	s_waitcnt vmcnt(0)
	v_cmp_lt_i32_e32 vcc, 63, v60
	s_and_saveexec_b64 s[14:15], vcc
	s_xor_b64 s[14:15], exec, s[14:15]
	s_cbranch_execz .LBB0_637
	s_mov_b32 s16, 0x18000
	v_mov_b64_e32 v[64:65], s[10:11]
	v_mad_u64_u32 v[64:65], s[16:17], v62, s16, v[64:65]
	v_lshl_add_u64 v[64:65], v[60:61], 3, v[64:65]
	global_store_dword v[64:65], v68, off
.LBB0_637:
	s_andn2_saveexec_b64 s[14:15], s[14:15]
	s_cbranch_execz .LBB0_639
	v_lshlrev_b32_e32 v64, 9, v62
	v_mov_b32_e32 v65, 0
	v_ashrrev_i32_e32 v61, 31, v60
	v_lshl_add_u64 v[64:65], s[8:9], 0, v[64:65]
	v_lshl_add_u64 v[64:65], v[60:61], 3, v[64:65]
	global_store_dword v[64:65], v68, off
.LBB0_639:
	s_or_b64 exec, exec, s[14:15]
	global_store_dword v[64:65], v63, off offset:4
	global_atomic_add_f32 v66, v63, s[6:7]
.LBB0_640:
	s_andn2_saveexec_b64 s[12:13], s[12:13]
	v_or_b32_e32 v62, v69, v62
	v_lshl_add_u32 v60, v60, 3, v76
	ds_write_b64 v60, v[62:63]
.LBB0_642:
	s_or_b64 exec, exec, s[2:3]
	v_or_b32_e32 v60, v56, v57
	v_or3_b32 v60, v60, v59, v58
	v_cmp_ne_u32_e32 vcc, 0, v60
	s_and_saveexec_b64 s[2:3], vcc
	s_cbranch_execz .LBB0_679
	v_cmp_neq_f32_e32 vcc, 0, v56
	s_and_saveexec_b64 s[12:13], vcc
	s_cbranch_execz .LBB0_652
	v_mov_b32_e32 v61, 1
	ds_add_rtn_u32 v60, v77, v61
	s_movk_i32 s14, 0x7f
	v_or_b32_e32 v64, 0x2100, v78
	s_waitcnt lgkmcnt(0)
	v_cmp_lt_i32_e32 vcc, s14, v60
	s_and_saveexec_b64 s[14:15], vcc
	s_xor_b64 s[14:15], exec, s[14:15]
	s_cbranch_execz .LBB0_650
	v_lshlrev_b32_e32 v65, 2, v64
	global_atomic_add v60, v65, v61, s[4:5] sc0
	v_mov_b32_e32 v61, 0
	s_waitcnt vmcnt(0)
	v_cmp_lt_i32_e32 vcc, 63, v60
	s_and_saveexec_b64 s[16:17], vcc
	s_xor_b64 s[16:17], exec, s[16:17]
	s_cbranch_execz .LBB0_647
	s_mov_b32 s18, 0x18000
	v_mov_b64_e32 v[62:63], s[10:11]
	v_mad_u64_u32 v[62:63], s[18:19], v64, s18, v[62:63]
	v_lshl_add_u64 v[62:63], v[60:61], 3, v[62:63]
	global_store_dword v[62:63], v68, off
.LBB0_647:
	s_andn2_saveexec_b64 s[16:17], s[16:17]
	s_cbranch_execz .LBB0_649
	v_lshlrev_b32_e32 v62, 9, v64
	v_mov_b32_e32 v63, 0
	v_ashrrev_i32_e32 v61, 31, v60
	v_lshl_add_u64 v[62:63], s[8:9], 0, v[62:63]
	v_lshl_add_u64 v[62:63], v[60:61], 3, v[62:63]
	global_store_dword v[62:63], v68, off
.LBB0_649:
	s_or_b64 exec, exec, s[16:17]
	global_store_dword v[62:63], v56, off offset:4
	global_atomic_add_f32 v65, v56, s[6:7]
.LBB0_650:
	s_andn2_saveexec_b64 s[14:15], s[14:15]
	v_or_b32_e32 v62, v69, v64
	v_lshl_add_u32 v60, v60, 3, v76
	v_mov_b32_e32 v63, v56
	ds_write_b64 v60, v[62:63]
.LBB0_652:
	s_or_b64 exec, exec, s[12:13]
	v_cmp_neq_f32_e32 vcc, 0, v57
	s_and_saveexec_b64 s[12:13], vcc
	s_cbranch_execz .LBB0_661
	v_mov_b32_e32 v61, 1
	ds_add_rtn_u32 v60, v77, v61
	s_movk_i32 s14, 0x7f
	v_or_b32_e32 v56, 0x2101, v78
	s_waitcnt lgkmcnt(0)
	v_cmp_lt_i32_e32 vcc, s14, v60
	s_and_saveexec_b64 s[14:15], vcc
	s_xor_b64 s[14:15], exec, s[14:15]
	s_cbranch_execz .LBB0_659
	v_lshlrev_b32_e32 v64, 2, v56
	global_atomic_add v60, v64, v61, s[4:5] sc0
	v_mov_b32_e32 v61, 0
	s_waitcnt vmcnt(0)
	v_cmp_lt_i32_e32 vcc, 63, v60
	s_and_saveexec_b64 s[16:17], vcc
	s_xor_b64 s[16:17], exec, s[16:17]
	s_cbranch_execz .LBB0_656
	s_mov_b32 s18, 0x18000
	v_mov_b64_e32 v[62:63], s[10:11]
	v_mad_u64_u32 v[62:63], s[18:19], v56, s18, v[62:63]
	v_lshl_add_u64 v[62:63], v[60:61], 3, v[62:63]
	global_store_dword v[62:63], v68, off
.LBB0_656:
	s_andn2_saveexec_b64 s[16:17], s[16:17]
	s_cbranch_execz .LBB0_658
	v_lshlrev_b32_e32 v62, 9, v56
	v_mov_b32_e32 v63, 0
	v_ashrrev_i32_e32 v61, 31, v60
	v_lshl_add_u64 v[62:63], s[8:9], 0, v[62:63]
	v_lshl_add_u64 v[62:63], v[60:61], 3, v[62:63]
	global_store_dword v[62:63], v68, off
.LBB0_658:
	s_or_b64 exec, exec, s[16:17]
	global_store_dword v[62:63], v57, off offset:4
	global_atomic_add_f32 v64, v57, s[6:7]
.LBB0_659:
	s_andn2_saveexec_b64 s[14:15], s[14:15]
	v_or_b32_e32 v56, v69, v56
	v_lshl_add_u32 v60, v60, 3, v76
	ds_write_b64 v60, v[56:57]
.LBB0_661:
	s_or_b64 exec, exec, s[12:13]
	v_cmp_neq_f32_e32 vcc, 0, v58
	s_and_saveexec_b64 s[12:13], vcc
	s_cbranch_execz .LBB0_670
	v_mov_b32_e32 v57, 1
	ds_add_rtn_u32 v56, v77, v57
	s_movk_i32 s14, 0x7f
	v_or_b32_e32 v62, 0x2102, v78
	s_waitcnt lgkmcnt(0)
	v_cmp_lt_i32_e32 vcc, s14, v56
	s_and_saveexec_b64 s[14:15], vcc
	s_xor_b64 s[14:15], exec, s[14:15]
	s_cbranch_execz .LBB0_668
	v_lshlrev_b32_e32 v63, 2, v62
	global_atomic_add v56, v63, v57, s[4:5] sc0
	v_mov_b32_e32 v57, 0
	s_waitcnt vmcnt(0)
	v_cmp_lt_i32_e32 vcc, 63, v56
	s_and_saveexec_b64 s[16:17], vcc
	s_xor_b64 s[16:17], exec, s[16:17]
	s_cbranch_execz .LBB0_665
	s_mov_b32 s18, 0x18000
	v_mov_b64_e32 v[60:61], s[10:11]
	v_mad_u64_u32 v[60:61], s[18:19], v62, s18, v[60:61]
	v_lshl_add_u64 v[60:61], v[56:57], 3, v[60:61]
	global_store_dword v[60:61], v68, off
.LBB0_665:
	s_andn2_saveexec_b64 s[16:17], s[16:17]
	s_cbranch_execz .LBB0_667
	v_lshlrev_b32_e32 v60, 9, v62
	v_mov_b32_e32 v61, 0
	v_ashrrev_i32_e32 v57, 31, v56
	v_lshl_add_u64 v[60:61], s[8:9], 0, v[60:61]
	v_lshl_add_u64 v[60:61], v[56:57], 3, v[60:61]
	global_store_dword v[60:61], v68, off
.LBB0_667:
	s_or_b64 exec, exec, s[16:17]
	global_store_dword v[60:61], v58, off offset:4
	global_atomic_add_f32 v63, v58, s[6:7]
.LBB0_668:
	s_andn2_saveexec_b64 s[14:15], s[14:15]
	v_or_b32_e32 v60, v69, v62
	v_lshl_add_u32 v56, v56, 3, v76
	v_mov_b32_e32 v61, v58
	ds_write_b64 v56, v[60:61]
.LBB0_670:
	s_or_b64 exec, exec, s[12:13]
	v_cmp_neq_f32_e32 vcc, 0, v59
	s_and_b64 exec, exec, vcc
	s_cbranch_execz .LBB0_679
	v_mov_b32_e32 v57, 1
	ds_add_rtn_u32 v56, v77, v57
	s_movk_i32 s12, 0x7f
	v_or_b32_e32 v58, 0x2103, v78
	s_waitcnt lgkmcnt(0)
	v_cmp_lt_i32_e32 vcc, s12, v56
	s_and_saveexec_b64 s[12:13], vcc
	s_xor_b64 s[12:13], exec, s[12:13]
	s_cbranch_execz .LBB0_677
	v_lshlrev_b32_e32 v62, 2, v58
	global_atomic_add v56, v62, v57, s[4:5] sc0
	v_mov_b32_e32 v57, 0
	s_waitcnt vmcnt(0)
	v_cmp_lt_i32_e32 vcc, 63, v56
	s_and_saveexec_b64 s[14:15], vcc
	s_xor_b64 s[14:15], exec, s[14:15]
	s_cbranch_execz .LBB0_674
	s_mov_b32 s16, 0x18000
	v_mov_b64_e32 v[60:61], s[10:11]
	v_mad_u64_u32 v[60:61], s[16:17], v58, s16, v[60:61]
	v_lshl_add_u64 v[60:61], v[56:57], 3, v[60:61]
	global_store_dword v[60:61], v68, off
.LBB0_674:
	s_andn2_saveexec_b64 s[14:15], s[14:15]
	s_cbranch_execz .LBB0_676
	v_lshlrev_b32_e32 v60, 9, v58
	v_mov_b32_e32 v61, 0
	v_ashrrev_i32_e32 v57, 31, v56
	v_lshl_add_u64 v[60:61], s[8:9], 0, v[60:61]
	v_lshl_add_u64 v[60:61], v[56:57], 3, v[60:61]
	global_store_dword v[60:61], v68, off
.LBB0_676:
	s_or_b64 exec, exec, s[14:15]
	global_store_dword v[60:61], v59, off offset:4
	global_atomic_add_f32 v62, v59, s[6:7]
.LBB0_677:
	s_andn2_saveexec_b64 s[12:13], s[12:13]
	v_or_b32_e32 v58, v69, v58
	v_lshl_add_u32 v56, v56, 3, v76
	ds_write_b64 v56, v[58:59]
.LBB0_679:
	s_or_b64 exec, exec, s[2:3]
	v_cmp_ne_u32_e32 vcc, 0, v71
	s_and_saveexec_b64 s[2:3], vcc
	s_cbranch_execz .LBB0_716
	v_cmp_neq_f32_e32 vcc, 0, v52
	s_and_saveexec_b64 s[12:13], vcc
	s_cbranch_execz .LBB0_689
	v_mov_b32_e32 v57, 1
	ds_add_rtn_u32 v56, v77, v57
	s_movk_i32 s14, 0x7f
	v_or_b32_e32 v60, 0x2200, v78
	s_waitcnt lgkmcnt(0)
	v_cmp_lt_i32_e32 vcc, s14, v56
	s_and_saveexec_b64 s[14:15], vcc
	s_xor_b64 s[14:15], exec, s[14:15]
	s_cbranch_execz .LBB0_687
	v_lshlrev_b32_e32 v61, 2, v60
	global_atomic_add v56, v61, v57, s[4:5] sc0
	v_mov_b32_e32 v57, 0
	s_waitcnt vmcnt(0)
	v_cmp_lt_i32_e32 vcc, 63, v56
	s_and_saveexec_b64 s[16:17], vcc
	s_xor_b64 s[16:17], exec, s[16:17]
	s_cbranch_execz .LBB0_684
	s_mov_b32 s18, 0x18000
	v_mov_b64_e32 v[58:59], s[10:11]
	v_mad_u64_u32 v[58:59], s[18:19], v60, s18, v[58:59]
	v_lshl_add_u64 v[58:59], v[56:57], 3, v[58:59]
	global_store_dword v[58:59], v68, off
.LBB0_684:
	s_andn2_saveexec_b64 s[16:17], s[16:17]
	s_cbranch_execz .LBB0_686
	v_lshlrev_b32_e32 v58, 9, v60
	v_mov_b32_e32 v59, 0
	v_ashrrev_i32_e32 v57, 31, v56
	v_lshl_add_u64 v[58:59], s[8:9], 0, v[58:59]
	v_lshl_add_u64 v[58:59], v[56:57], 3, v[58:59]
	global_store_dword v[58:59], v68, off
.LBB0_686:
	s_or_b64 exec, exec, s[16:17]
	global_store_dword v[58:59], v52, off offset:4
	global_atomic_add_f32 v61, v52, s[6:7]
.LBB0_687:
	s_andn2_saveexec_b64 s[14:15], s[14:15]
	v_or_b32_e32 v58, v69, v60
	v_lshl_add_u32 v56, v56, 3, v76
	v_mov_b32_e32 v59, v52
	ds_write_b64 v56, v[58:59]
.LBB0_689:
	s_or_b64 exec, exec, s[12:13]
	v_cmp_neq_f32_e32 vcc, 0, v53
	s_and_saveexec_b64 s[12:13], vcc
	s_cbranch_execz .LBB0_698
	v_mov_b32_e32 v57, 1
	ds_add_rtn_u32 v56, v77, v57
	s_movk_i32 s14, 0x7f
	v_or_b32_e32 v52, 0x2201, v78
	s_waitcnt lgkmcnt(0)
	v_cmp_lt_i32_e32 vcc, s14, v56
	s_and_saveexec_b64 s[14:15], vcc
	s_xor_b64 s[14:15], exec, s[14:15]
	s_cbranch_execz .LBB0_696
	v_lshlrev_b32_e32 v60, 2, v52
	global_atomic_add v56, v60, v57, s[4:5] sc0
	v_mov_b32_e32 v57, 0
	s_waitcnt vmcnt(0)
	v_cmp_lt_i32_e32 vcc, 63, v56
	s_and_saveexec_b64 s[16:17], vcc
	s_xor_b64 s[16:17], exec, s[16:17]
	s_cbranch_execz .LBB0_693
	s_mov_b32 s18, 0x18000
	v_mov_b64_e32 v[58:59], s[10:11]
	v_mad_u64_u32 v[58:59], s[18:19], v52, s18, v[58:59]
	v_lshl_add_u64 v[58:59], v[56:57], 3, v[58:59]
	global_store_dword v[58:59], v68, off
.LBB0_693:
	s_andn2_saveexec_b64 s[16:17], s[16:17]
	s_cbranch_execz .LBB0_695
	v_lshlrev_b32_e32 v58, 9, v52
	v_mov_b32_e32 v59, 0
	v_ashrrev_i32_e32 v57, 31, v56
	v_lshl_add_u64 v[58:59], s[8:9], 0, v[58:59]
	v_lshl_add_u64 v[58:59], v[56:57], 3, v[58:59]
	global_store_dword v[58:59], v68, off
.LBB0_695:
	s_or_b64 exec, exec, s[16:17]
	global_store_dword v[58:59], v53, off offset:4
	global_atomic_add_f32 v60, v53, s[6:7]
.LBB0_696:
	s_andn2_saveexec_b64 s[14:15], s[14:15]
	v_or_b32_e32 v52, v69, v52
	v_lshl_add_u32 v56, v56, 3, v76
	ds_write_b64 v56, v[52:53]
.LBB0_698:
	s_or_b64 exec, exec, s[12:13]
	v_cmp_neq_f32_e32 vcc, 0, v54
	s_and_saveexec_b64 s[12:13], vcc
	s_cbranch_execz .LBB0_707
	v_mov_b32_e32 v53, 1
	ds_add_rtn_u32 v52, v77, v53
	s_movk_i32 s14, 0x7f
	v_or_b32_e32 v58, 0x2202, v78
	s_waitcnt lgkmcnt(0)
	v_cmp_lt_i32_e32 vcc, s14, v52
	s_and_saveexec_b64 s[14:15], vcc
	s_xor_b64 s[14:15], exec, s[14:15]
	s_cbranch_execz .LBB0_705
	v_lshlrev_b32_e32 v59, 2, v58
	global_atomic_add v52, v59, v53, s[4:5] sc0
	v_mov_b32_e32 v53, 0
	s_waitcnt vmcnt(0)
	v_cmp_lt_i32_e32 vcc, 63, v52
	s_and_saveexec_b64 s[16:17], vcc
	s_xor_b64 s[16:17], exec, s[16:17]
	s_cbranch_execz .LBB0_702
	s_mov_b32 s18, 0x18000
	v_mov_b64_e32 v[56:57], s[10:11]
	v_mad_u64_u32 v[56:57], s[18:19], v58, s18, v[56:57]
	v_lshl_add_u64 v[56:57], v[52:53], 3, v[56:57]
	global_store_dword v[56:57], v68, off
.LBB0_702:
	s_andn2_saveexec_b64 s[16:17], s[16:17]
	s_cbranch_execz .LBB0_704
	v_lshlrev_b32_e32 v56, 9, v58
	v_mov_b32_e32 v57, 0
	v_ashrrev_i32_e32 v53, 31, v52
	v_lshl_add_u64 v[56:57], s[8:9], 0, v[56:57]
	v_lshl_add_u64 v[56:57], v[52:53], 3, v[56:57]
	global_store_dword v[56:57], v68, off
.LBB0_704:
	s_or_b64 exec, exec, s[16:17]
	global_store_dword v[56:57], v54, off offset:4
	global_atomic_add_f32 v59, v54, s[6:7]
.LBB0_705:
	s_andn2_saveexec_b64 s[14:15], s[14:15]
	v_or_b32_e32 v56, v69, v58
	v_lshl_add_u32 v52, v52, 3, v76
	v_mov_b32_e32 v57, v54
	ds_write_b64 v52, v[56:57]
.LBB0_707:
	s_or_b64 exec, exec, s[12:13]
	v_cmp_neq_f32_e32 vcc, 0, v55
	s_and_b64 exec, exec, vcc
	s_cbranch_execz .LBB0_716
	v_mov_b32_e32 v53, 1
	ds_add_rtn_u32 v52, v77, v53
	s_movk_i32 s12, 0x7f
	v_or_b32_e32 v54, 0x2203, v78
	s_waitcnt lgkmcnt(0)
	v_cmp_lt_i32_e32 vcc, s12, v52
	s_and_saveexec_b64 s[12:13], vcc
	s_xor_b64 s[12:13], exec, s[12:13]
	s_cbranch_execz .LBB0_714
	v_lshlrev_b32_e32 v58, 2, v54
	global_atomic_add v52, v58, v53, s[4:5] sc0
	v_mov_b32_e32 v53, 0
	s_waitcnt vmcnt(0)
	v_cmp_lt_i32_e32 vcc, 63, v52
	s_and_saveexec_b64 s[14:15], vcc
	s_xor_b64 s[14:15], exec, s[14:15]
	s_cbranch_execz .LBB0_711
	s_mov_b32 s16, 0x18000
	v_mov_b64_e32 v[56:57], s[10:11]
	v_mad_u64_u32 v[56:57], s[16:17], v54, s16, v[56:57]
	v_lshl_add_u64 v[56:57], v[52:53], 3, v[56:57]
	global_store_dword v[56:57], v68, off
.LBB0_711:
	s_andn2_saveexec_b64 s[14:15], s[14:15]
	s_cbranch_execz .LBB0_713
	v_lshlrev_b32_e32 v56, 9, v54
	v_mov_b32_e32 v57, 0
	v_ashrrev_i32_e32 v53, 31, v52
	v_lshl_add_u64 v[56:57], s[8:9], 0, v[56:57]
	v_lshl_add_u64 v[56:57], v[52:53], 3, v[56:57]
	global_store_dword v[56:57], v68, off
.LBB0_713:
	s_or_b64 exec, exec, s[14:15]
	global_store_dword v[56:57], v55, off offset:4
	global_atomic_add_f32 v58, v55, s[6:7]
.LBB0_714:
	s_andn2_saveexec_b64 s[12:13], s[12:13]
	v_or_b32_e32 v54, v69, v54
	v_lshl_add_u32 v52, v52, 3, v76
	ds_write_b64 v52, v[54:55]
.LBB0_716:
	s_or_b64 exec, exec, s[2:3]
	v_cmp_ne_u32_e32 vcc, 0, v70
	s_and_saveexec_b64 s[2:3], vcc
	s_cbranch_execz .LBB0_753
	v_cmp_neq_f32_e32 vcc, 0, v48
	s_and_saveexec_b64 s[12:13], vcc
	s_cbranch_execz .LBB0_726
	v_mov_b32_e32 v53, 1
	ds_add_rtn_u32 v52, v77, v53
	s_movk_i32 s14, 0x7f
	v_or_b32_e32 v56, 0x2300, v78
	s_waitcnt lgkmcnt(0)
	v_cmp_lt_i32_e32 vcc, s14, v52
	s_and_saveexec_b64 s[14:15], vcc
	s_xor_b64 s[14:15], exec, s[14:15]
	s_cbranch_execz .LBB0_724
	v_lshlrev_b32_e32 v57, 2, v56
	global_atomic_add v52, v57, v53, s[4:5] sc0
	v_mov_b32_e32 v53, 0
	s_waitcnt vmcnt(0)
	v_cmp_lt_i32_e32 vcc, 63, v52
	s_and_saveexec_b64 s[16:17], vcc
	s_xor_b64 s[16:17], exec, s[16:17]
	s_cbranch_execz .LBB0_721
	s_mov_b32 s18, 0x18000
	v_mov_b64_e32 v[54:55], s[10:11]
	v_mad_u64_u32 v[54:55], s[18:19], v56, s18, v[54:55]
	v_lshl_add_u64 v[54:55], v[52:53], 3, v[54:55]
	global_store_dword v[54:55], v68, off
.LBB0_721:
	s_andn2_saveexec_b64 s[16:17], s[16:17]
	s_cbranch_execz .LBB0_723
	v_lshlrev_b32_e32 v54, 9, v56
	v_mov_b32_e32 v55, 0
	v_ashrrev_i32_e32 v53, 31, v52
	v_lshl_add_u64 v[54:55], s[8:9], 0, v[54:55]
	v_lshl_add_u64 v[54:55], v[52:53], 3, v[54:55]
	global_store_dword v[54:55], v68, off
.LBB0_723:
	s_or_b64 exec, exec, s[16:17]
	global_store_dword v[54:55], v48, off offset:4
	global_atomic_add_f32 v57, v48, s[6:7]
.LBB0_724:
	s_andn2_saveexec_b64 s[14:15], s[14:15]
	v_or_b32_e32 v54, v69, v56
	v_lshl_add_u32 v52, v52, 3, v76
	v_mov_b32_e32 v55, v48
	ds_write_b64 v52, v[54:55]
.LBB0_726:
	s_or_b64 exec, exec, s[12:13]
	v_cmp_neq_f32_e32 vcc, 0, v49
	s_and_saveexec_b64 s[12:13], vcc
	s_cbranch_execz .LBB0_735
	v_mov_b32_e32 v53, 1
	ds_add_rtn_u32 v52, v77, v53
	s_movk_i32 s14, 0x7f
	v_or_b32_e32 v48, 0x2301, v78
	s_waitcnt lgkmcnt(0)
	v_cmp_lt_i32_e32 vcc, s14, v52
	s_and_saveexec_b64 s[14:15], vcc
	s_xor_b64 s[14:15], exec, s[14:15]
	s_cbranch_execz .LBB0_733
	v_lshlrev_b32_e32 v56, 2, v48
	global_atomic_add v52, v56, v53, s[4:5] sc0
	v_mov_b32_e32 v53, 0
	s_waitcnt vmcnt(0)
	v_cmp_lt_i32_e32 vcc, 63, v52
	s_and_saveexec_b64 s[16:17], vcc
	s_xor_b64 s[16:17], exec, s[16:17]
	s_cbranch_execz .LBB0_730
	s_mov_b32 s18, 0x18000
	v_mov_b64_e32 v[54:55], s[10:11]
	v_mad_u64_u32 v[54:55], s[18:19], v48, s18, v[54:55]
	v_lshl_add_u64 v[54:55], v[52:53], 3, v[54:55]
	global_store_dword v[54:55], v68, off
.LBB0_730:
	s_andn2_saveexec_b64 s[16:17], s[16:17]
	s_cbranch_execz .LBB0_732
	v_lshlrev_b32_e32 v54, 9, v48
	v_mov_b32_e32 v55, 0
	v_ashrrev_i32_e32 v53, 31, v52
	v_lshl_add_u64 v[54:55], s[8:9], 0, v[54:55]
	v_lshl_add_u64 v[54:55], v[52:53], 3, v[54:55]
	global_store_dword v[54:55], v68, off
.LBB0_732:
	s_or_b64 exec, exec, s[16:17]
	global_store_dword v[54:55], v49, off offset:4
	global_atomic_add_f32 v56, v49, s[6:7]
.LBB0_733:
	s_andn2_saveexec_b64 s[14:15], s[14:15]
	v_or_b32_e32 v48, v69, v48
	v_lshl_add_u32 v52, v52, 3, v76
	ds_write_b64 v52, v[48:49]
.LBB0_735:
	s_or_b64 exec, exec, s[12:13]
	v_cmp_neq_f32_e32 vcc, 0, v50
	s_and_saveexec_b64 s[12:13], vcc
	s_cbranch_execz .LBB0_744
	v_mov_b32_e32 v49, 1
	ds_add_rtn_u32 v48, v77, v49
	s_movk_i32 s14, 0x7f
	v_or_b32_e32 v54, 0x2302, v78
	s_waitcnt lgkmcnt(0)
	v_cmp_lt_i32_e32 vcc, s14, v48
	s_and_saveexec_b64 s[14:15], vcc
	s_xor_b64 s[14:15], exec, s[14:15]
	s_cbranch_execz .LBB0_742
	v_lshlrev_b32_e32 v55, 2, v54
	global_atomic_add v48, v55, v49, s[4:5] sc0
	v_mov_b32_e32 v49, 0
	s_waitcnt vmcnt(0)
	v_cmp_lt_i32_e32 vcc, 63, v48
	s_and_saveexec_b64 s[16:17], vcc
	s_xor_b64 s[16:17], exec, s[16:17]
	s_cbranch_execz .LBB0_739
	s_mov_b32 s18, 0x18000
	v_mov_b64_e32 v[52:53], s[10:11]
	v_mad_u64_u32 v[52:53], s[18:19], v54, s18, v[52:53]
	v_lshl_add_u64 v[52:53], v[48:49], 3, v[52:53]
	global_store_dword v[52:53], v68, off
.LBB0_739:
	s_andn2_saveexec_b64 s[16:17], s[16:17]
	s_cbranch_execz .LBB0_741
	v_lshlrev_b32_e32 v52, 9, v54
	v_mov_b32_e32 v53, 0
	v_ashrrev_i32_e32 v49, 31, v48
	v_lshl_add_u64 v[52:53], s[8:9], 0, v[52:53]
	v_lshl_add_u64 v[52:53], v[48:49], 3, v[52:53]
	global_store_dword v[52:53], v68, off
.LBB0_741:
	s_or_b64 exec, exec, s[16:17]
	global_store_dword v[52:53], v50, off offset:4
	global_atomic_add_f32 v55, v50, s[6:7]
.LBB0_742:
	s_andn2_saveexec_b64 s[14:15], s[14:15]
	v_or_b32_e32 v52, v69, v54
	v_lshl_add_u32 v48, v48, 3, v76
	v_mov_b32_e32 v53, v50
	ds_write_b64 v48, v[52:53]
.LBB0_744:
	s_or_b64 exec, exec, s[12:13]
	v_cmp_neq_f32_e32 vcc, 0, v51
	s_and_b64 exec, exec, vcc
	s_cbranch_execz .LBB0_753
	v_mov_b32_e32 v49, 1
	ds_add_rtn_u32 v48, v77, v49
	s_movk_i32 s12, 0x7f
	v_or_b32_e32 v50, 0x2303, v78
	s_waitcnt lgkmcnt(0)
	v_cmp_lt_i32_e32 vcc, s12, v48
	s_and_saveexec_b64 s[12:13], vcc
	s_xor_b64 s[12:13], exec, s[12:13]
	s_cbranch_execz .LBB0_751
	v_lshlrev_b32_e32 v54, 2, v50
	global_atomic_add v48, v54, v49, s[4:5] sc0
	v_mov_b32_e32 v49, 0
	s_waitcnt vmcnt(0)
	v_cmp_lt_i32_e32 vcc, 63, v48
	s_and_saveexec_b64 s[14:15], vcc
	s_xor_b64 s[14:15], exec, s[14:15]
	s_cbranch_execz .LBB0_748
	s_mov_b32 s16, 0x18000
	v_mov_b64_e32 v[52:53], s[10:11]
	v_mad_u64_u32 v[52:53], s[16:17], v50, s16, v[52:53]
	v_lshl_add_u64 v[52:53], v[48:49], 3, v[52:53]
	global_store_dword v[52:53], v68, off
.LBB0_748:
	s_andn2_saveexec_b64 s[14:15], s[14:15]
	s_cbranch_execz .LBB0_750
	v_lshlrev_b32_e32 v52, 9, v50
	v_mov_b32_e32 v53, 0
	v_ashrrev_i32_e32 v49, 31, v48
	v_lshl_add_u64 v[52:53], s[8:9], 0, v[52:53]
	v_lshl_add_u64 v[52:53], v[48:49], 3, v[52:53]
	global_store_dword v[52:53], v68, off
.LBB0_750:
	s_or_b64 exec, exec, s[14:15]
	global_store_dword v[52:53], v51, off offset:4
	global_atomic_add_f32 v54, v51, s[6:7]
.LBB0_751:
	s_andn2_saveexec_b64 s[12:13], s[12:13]
	v_or_b32_e32 v50, v69, v50
	v_lshl_add_u32 v48, v48, 3, v76
	ds_write_b64 v48, v[50:51]
.LBB0_753:
	s_or_b64 exec, exec, s[2:3]
	v_or_b32_e32 v48, v44, v45
	v_or3_b32 v48, v48, v47, v46
	v_cmp_ne_u32_e32 vcc, 0, v48
	s_and_saveexec_b64 s[2:3], vcc
	s_cbranch_execz .LBB0_790
	v_cmp_neq_f32_e32 vcc, 0, v44
	s_and_saveexec_b64 s[12:13], vcc
	s_cbranch_execz .LBB0_763
	v_mov_b32_e32 v49, 1
	ds_add_rtn_u32 v48, v77, v49
	s_movk_i32 s14, 0x7f
	v_or_b32_e32 v52, 0x2400, v78
	s_waitcnt lgkmcnt(0)
	v_cmp_lt_i32_e32 vcc, s14, v48
	s_and_saveexec_b64 s[14:15], vcc
	s_xor_b64 s[14:15], exec, s[14:15]
	s_cbranch_execz .LBB0_761
	v_lshlrev_b32_e32 v53, 2, v52
	global_atomic_add v48, v53, v49, s[4:5] sc0
	v_mov_b32_e32 v49, 0
	s_waitcnt vmcnt(0)
	v_cmp_lt_i32_e32 vcc, 63, v48
	s_and_saveexec_b64 s[16:17], vcc
	s_xor_b64 s[16:17], exec, s[16:17]
	s_cbranch_execz .LBB0_758
	s_mov_b32 s18, 0x18000
	v_mov_b64_e32 v[50:51], s[10:11]
	v_mad_u64_u32 v[50:51], s[18:19], v52, s18, v[50:51]
	v_lshl_add_u64 v[50:51], v[48:49], 3, v[50:51]
	global_store_dword v[50:51], v68, off
.LBB0_758:
	s_andn2_saveexec_b64 s[16:17], s[16:17]
	s_cbranch_execz .LBB0_760
	v_lshlrev_b32_e32 v50, 9, v52
	v_mov_b32_e32 v51, 0
	v_ashrrev_i32_e32 v49, 31, v48
	v_lshl_add_u64 v[50:51], s[8:9], 0, v[50:51]
	v_lshl_add_u64 v[50:51], v[48:49], 3, v[50:51]
	global_store_dword v[50:51], v68, off
.LBB0_760:
	s_or_b64 exec, exec, s[16:17]
	global_store_dword v[50:51], v44, off offset:4
	global_atomic_add_f32 v53, v44, s[6:7]
.LBB0_761:
	s_andn2_saveexec_b64 s[14:15], s[14:15]
	v_or_b32_e32 v50, v69, v52
	v_lshl_add_u32 v48, v48, 3, v76
	v_mov_b32_e32 v51, v44
	ds_write_b64 v48, v[50:51]
.LBB0_763:
	s_or_b64 exec, exec, s[12:13]
	v_cmp_neq_f32_e32 vcc, 0, v45
	s_and_saveexec_b64 s[12:13], vcc
	s_cbranch_execz .LBB0_772
	v_mov_b32_e32 v49, 1
	ds_add_rtn_u32 v48, v77, v49
	s_movk_i32 s14, 0x7f
	v_or_b32_e32 v44, 0x2401, v78
	s_waitcnt lgkmcnt(0)
	v_cmp_lt_i32_e32 vcc, s14, v48
	s_and_saveexec_b64 s[14:15], vcc
	s_xor_b64 s[14:15], exec, s[14:15]
	s_cbranch_execz .LBB0_770
	v_lshlrev_b32_e32 v52, 2, v44
	global_atomic_add v48, v52, v49, s[4:5] sc0
	v_mov_b32_e32 v49, 0
	s_waitcnt vmcnt(0)
	v_cmp_lt_i32_e32 vcc, 63, v48
	s_and_saveexec_b64 s[16:17], vcc
	s_xor_b64 s[16:17], exec, s[16:17]
	s_cbranch_execz .LBB0_767
	s_mov_b32 s18, 0x18000
	v_mov_b64_e32 v[50:51], s[10:11]
	v_mad_u64_u32 v[50:51], s[18:19], v44, s18, v[50:51]
	v_lshl_add_u64 v[50:51], v[48:49], 3, v[50:51]
	global_store_dword v[50:51], v68, off
.LBB0_767:
	s_andn2_saveexec_b64 s[16:17], s[16:17]
	s_cbranch_execz .LBB0_769
	v_lshlrev_b32_e32 v50, 9, v44
	v_mov_b32_e32 v51, 0
	v_ashrrev_i32_e32 v49, 31, v48
	v_lshl_add_u64 v[50:51], s[8:9], 0, v[50:51]
	v_lshl_add_u64 v[50:51], v[48:49], 3, v[50:51]
	global_store_dword v[50:51], v68, off
.LBB0_769:
	s_or_b64 exec, exec, s[16:17]
	global_store_dword v[50:51], v45, off offset:4
	global_atomic_add_f32 v52, v45, s[6:7]
.LBB0_770:
	s_andn2_saveexec_b64 s[14:15], s[14:15]
	v_or_b32_e32 v44, v69, v44
	v_lshl_add_u32 v48, v48, 3, v76
	ds_write_b64 v48, v[44:45]
.LBB0_772:
	s_or_b64 exec, exec, s[12:13]
	v_cmp_neq_f32_e32 vcc, 0, v46
	s_and_saveexec_b64 s[12:13], vcc
	s_cbranch_execz .LBB0_781
	v_mov_b32_e32 v45, 1
	ds_add_rtn_u32 v44, v77, v45
	s_movk_i32 s14, 0x7f
	v_or_b32_e32 v50, 0x2402, v78
	s_waitcnt lgkmcnt(0)
	v_cmp_lt_i32_e32 vcc, s14, v44
	s_and_saveexec_b64 s[14:15], vcc
	s_xor_b64 s[14:15], exec, s[14:15]
	s_cbranch_execz .LBB0_779
	v_lshlrev_b32_e32 v51, 2, v50
	global_atomic_add v44, v51, v45, s[4:5] sc0
	v_mov_b32_e32 v45, 0
	s_waitcnt vmcnt(0)
	v_cmp_lt_i32_e32 vcc, 63, v44
	s_and_saveexec_b64 s[16:17], vcc
	s_xor_b64 s[16:17], exec, s[16:17]
	s_cbranch_execz .LBB0_776
	s_mov_b32 s18, 0x18000
	v_mov_b64_e32 v[48:49], s[10:11]
	v_mad_u64_u32 v[48:49], s[18:19], v50, s18, v[48:49]
	v_lshl_add_u64 v[48:49], v[44:45], 3, v[48:49]
	global_store_dword v[48:49], v68, off
.LBB0_776:
	s_andn2_saveexec_b64 s[16:17], s[16:17]
	s_cbranch_execz .LBB0_778
	v_lshlrev_b32_e32 v48, 9, v50
	v_mov_b32_e32 v49, 0
	v_ashrrev_i32_e32 v45, 31, v44
	v_lshl_add_u64 v[48:49], s[8:9], 0, v[48:49]
	v_lshl_add_u64 v[48:49], v[44:45], 3, v[48:49]
	global_store_dword v[48:49], v68, off
.LBB0_778:
	s_or_b64 exec, exec, s[16:17]
	global_store_dword v[48:49], v46, off offset:4
	global_atomic_add_f32 v51, v46, s[6:7]
.LBB0_779:
	s_andn2_saveexec_b64 s[14:15], s[14:15]
	v_or_b32_e32 v48, v69, v50
	v_lshl_add_u32 v44, v44, 3, v76
	v_mov_b32_e32 v49, v46
	ds_write_b64 v44, v[48:49]
.LBB0_781:
	s_or_b64 exec, exec, s[12:13]
	v_cmp_neq_f32_e32 vcc, 0, v47
	s_and_b64 exec, exec, vcc
	s_cbranch_execz .LBB0_790
	v_mov_b32_e32 v45, 1
	ds_add_rtn_u32 v44, v77, v45
	s_movk_i32 s12, 0x7f
	v_or_b32_e32 v46, 0x2403, v78
	s_waitcnt lgkmcnt(0)
	v_cmp_lt_i32_e32 vcc, s12, v44
	s_and_saveexec_b64 s[12:13], vcc
	s_xor_b64 s[12:13], exec, s[12:13]
	s_cbranch_execz .LBB0_788
	v_lshlrev_b32_e32 v50, 2, v46
	global_atomic_add v44, v50, v45, s[4:5] sc0
	v_mov_b32_e32 v45, 0
	s_waitcnt vmcnt(0)
	v_cmp_lt_i32_e32 vcc, 63, v44
	s_and_saveexec_b64 s[14:15], vcc
	s_xor_b64 s[14:15], exec, s[14:15]
	s_cbranch_execz .LBB0_785
	s_mov_b32 s16, 0x18000
	v_mov_b64_e32 v[48:49], s[10:11]
	v_mad_u64_u32 v[48:49], s[16:17], v46, s16, v[48:49]
	v_lshl_add_u64 v[48:49], v[44:45], 3, v[48:49]
	global_store_dword v[48:49], v68, off
.LBB0_785:
	s_andn2_saveexec_b64 s[14:15], s[14:15]
	s_cbranch_execz .LBB0_787
	v_lshlrev_b32_e32 v48, 9, v46
	v_mov_b32_e32 v49, 0
	v_ashrrev_i32_e32 v45, 31, v44
	v_lshl_add_u64 v[48:49], s[8:9], 0, v[48:49]
	v_lshl_add_u64 v[48:49], v[44:45], 3, v[48:49]
	global_store_dword v[48:49], v68, off
.LBB0_787:
	s_or_b64 exec, exec, s[14:15]
	global_store_dword v[48:49], v47, off offset:4
	global_atomic_add_f32 v50, v47, s[6:7]
.LBB0_788:
	s_andn2_saveexec_b64 s[12:13], s[12:13]
	v_or_b32_e32 v46, v69, v46
	v_lshl_add_u32 v44, v44, 3, v76
	ds_write_b64 v44, v[46:47]
.LBB0_790:
	s_or_b64 exec, exec, s[2:3]
	v_or_b32_e32 v44, v36, v37
	v_or3_b32 v44, v44, v39, v38
	v_cmp_ne_u32_e32 vcc, 0, v44
	s_and_saveexec_b64 s[2:3], vcc
	s_cbranch_execz .LBB0_827
	v_cmp_neq_f32_e32 vcc, 0, v36
	s_and_saveexec_b64 s[12:13], vcc
	s_cbranch_execz .LBB0_800
	v_mov_b32_e32 v45, 1
	ds_add_rtn_u32 v44, v77, v45
	s_movk_i32 s14, 0x7f
	v_or_b32_e32 v48, 0x2500, v78
	s_waitcnt lgkmcnt(0)
	v_cmp_lt_i32_e32 vcc, s14, v44
	s_and_saveexec_b64 s[14:15], vcc
	s_xor_b64 s[14:15], exec, s[14:15]
	s_cbranch_execz .LBB0_798
	v_lshlrev_b32_e32 v49, 2, v48
	global_atomic_add v44, v49, v45, s[4:5] sc0
	v_mov_b32_e32 v45, 0
	s_waitcnt vmcnt(0)
	v_cmp_lt_i32_e32 vcc, 63, v44
	s_and_saveexec_b64 s[16:17], vcc
	s_xor_b64 s[16:17], exec, s[16:17]
	s_cbranch_execz .LBB0_795
	s_mov_b32 s18, 0x18000
	v_mov_b64_e32 v[46:47], s[10:11]
	v_mad_u64_u32 v[46:47], s[18:19], v48, s18, v[46:47]
	v_lshl_add_u64 v[46:47], v[44:45], 3, v[46:47]
	global_store_dword v[46:47], v68, off
.LBB0_795:
	s_andn2_saveexec_b64 s[16:17], s[16:17]
	s_cbranch_execz .LBB0_797
	v_lshlrev_b32_e32 v46, 9, v48
	v_mov_b32_e32 v47, 0
	v_ashrrev_i32_e32 v45, 31, v44
	v_lshl_add_u64 v[46:47], s[8:9], 0, v[46:47]
	v_lshl_add_u64 v[46:47], v[44:45], 3, v[46:47]
	global_store_dword v[46:47], v68, off
.LBB0_797:
	s_or_b64 exec, exec, s[16:17]
	global_store_dword v[46:47], v36, off offset:4
	global_atomic_add_f32 v49, v36, s[6:7]
.LBB0_798:
	s_andn2_saveexec_b64 s[14:15], s[14:15]
	v_or_b32_e32 v46, v69, v48
	v_lshl_add_u32 v44, v44, 3, v76
	v_mov_b32_e32 v47, v36
	ds_write_b64 v44, v[46:47]
.LBB0_800:
	s_or_b64 exec, exec, s[12:13]
	v_cmp_neq_f32_e32 vcc, 0, v37
	s_and_saveexec_b64 s[12:13], vcc
	s_cbranch_execz .LBB0_809
	v_mov_b32_e32 v45, 1
	ds_add_rtn_u32 v44, v77, v45
	s_movk_i32 s14, 0x7f
	v_or_b32_e32 v36, 0x2501, v78
	s_waitcnt lgkmcnt(0)
	v_cmp_lt_i32_e32 vcc, s14, v44
	s_and_saveexec_b64 s[14:15], vcc
	s_xor_b64 s[14:15], exec, s[14:15]
	s_cbranch_execz .LBB0_807
	v_lshlrev_b32_e32 v48, 2, v36
	global_atomic_add v44, v48, v45, s[4:5] sc0
	v_mov_b32_e32 v45, 0
	s_waitcnt vmcnt(0)
	v_cmp_lt_i32_e32 vcc, 63, v44
	s_and_saveexec_b64 s[16:17], vcc
	s_xor_b64 s[16:17], exec, s[16:17]
	s_cbranch_execz .LBB0_804
	s_mov_b32 s18, 0x18000
	v_mov_b64_e32 v[46:47], s[10:11]
	v_mad_u64_u32 v[46:47], s[18:19], v36, s18, v[46:47]
	v_lshl_add_u64 v[46:47], v[44:45], 3, v[46:47]
	global_store_dword v[46:47], v68, off
.LBB0_804:
	s_andn2_saveexec_b64 s[16:17], s[16:17]
	s_cbranch_execz .LBB0_806
	v_lshlrev_b32_e32 v46, 9, v36
	v_mov_b32_e32 v47, 0
	v_ashrrev_i32_e32 v45, 31, v44
	v_lshl_add_u64 v[46:47], s[8:9], 0, v[46:47]
	v_lshl_add_u64 v[46:47], v[44:45], 3, v[46:47]
	global_store_dword v[46:47], v68, off
.LBB0_806:
	s_or_b64 exec, exec, s[16:17]
	global_store_dword v[46:47], v37, off offset:4
	global_atomic_add_f32 v48, v37, s[6:7]
.LBB0_807:
	s_andn2_saveexec_b64 s[14:15], s[14:15]
	v_or_b32_e32 v36, v69, v36
	v_lshl_add_u32 v44, v44, 3, v76
	ds_write_b64 v44, v[36:37]
.LBB0_809:
	s_or_b64 exec, exec, s[12:13]
	v_cmp_neq_f32_e32 vcc, 0, v38
	s_and_saveexec_b64 s[12:13], vcc
	s_cbranch_execz .LBB0_818
	v_mov_b32_e32 v37, 1
	ds_add_rtn_u32 v36, v77, v37
	s_movk_i32 s14, 0x7f
	v_or_b32_e32 v46, 0x2502, v78
	s_waitcnt lgkmcnt(0)
	v_cmp_lt_i32_e32 vcc, s14, v36
	s_and_saveexec_b64 s[14:15], vcc
	s_xor_b64 s[14:15], exec, s[14:15]
	s_cbranch_execz .LBB0_816
	v_lshlrev_b32_e32 v47, 2, v46
	global_atomic_add v36, v47, v37, s[4:5] sc0
	v_mov_b32_e32 v37, 0
	s_waitcnt vmcnt(0)
	v_cmp_lt_i32_e32 vcc, 63, v36
	s_and_saveexec_b64 s[16:17], vcc
	s_xor_b64 s[16:17], exec, s[16:17]
	s_cbranch_execz .LBB0_813
	s_mov_b32 s18, 0x18000
	v_mov_b64_e32 v[44:45], s[10:11]
	v_mad_u64_u32 v[44:45], s[18:19], v46, s18, v[44:45]
	v_lshl_add_u64 v[44:45], v[36:37], 3, v[44:45]
	global_store_dword v[44:45], v68, off
.LBB0_813:
	s_andn2_saveexec_b64 s[16:17], s[16:17]
	s_cbranch_execz .LBB0_815
	v_lshlrev_b32_e32 v44, 9, v46
	v_mov_b32_e32 v45, 0
	v_ashrrev_i32_e32 v37, 31, v36
	v_lshl_add_u64 v[44:45], s[8:9], 0, v[44:45]
	v_lshl_add_u64 v[44:45], v[36:37], 3, v[44:45]
	global_store_dword v[44:45], v68, off
.LBB0_815:
	s_or_b64 exec, exec, s[16:17]
	global_store_dword v[44:45], v38, off offset:4
	global_atomic_add_f32 v47, v38, s[6:7]
.LBB0_816:
	s_andn2_saveexec_b64 s[14:15], s[14:15]
	v_or_b32_e32 v44, v69, v46
	v_lshl_add_u32 v36, v36, 3, v76
	v_mov_b32_e32 v45, v38
	ds_write_b64 v36, v[44:45]
.LBB0_818:
	s_or_b64 exec, exec, s[12:13]
	v_cmp_neq_f32_e32 vcc, 0, v39
	s_and_b64 exec, exec, vcc
	s_cbranch_execz .LBB0_827
	v_mov_b32_e32 v37, 1
	ds_add_rtn_u32 v36, v77, v37
	s_movk_i32 s12, 0x7f
	v_or_b32_e32 v38, 0x2503, v78
	s_waitcnt lgkmcnt(0)
	v_cmp_lt_i32_e32 vcc, s12, v36
	s_and_saveexec_b64 s[12:13], vcc
	s_xor_b64 s[12:13], exec, s[12:13]
	s_cbranch_execz .LBB0_825
	v_lshlrev_b32_e32 v46, 2, v38
	global_atomic_add v36, v46, v37, s[4:5] sc0
	v_mov_b32_e32 v37, 0
	s_waitcnt vmcnt(0)
	v_cmp_lt_i32_e32 vcc, 63, v36
	s_and_saveexec_b64 s[14:15], vcc
	s_xor_b64 s[14:15], exec, s[14:15]
	s_cbranch_execz .LBB0_822
	s_mov_b32 s16, 0x18000
	v_mov_b64_e32 v[44:45], s[10:11]
	v_mad_u64_u32 v[44:45], s[16:17], v38, s16, v[44:45]
	v_lshl_add_u64 v[44:45], v[36:37], 3, v[44:45]
	global_store_dword v[44:45], v68, off
.LBB0_822:
	s_andn2_saveexec_b64 s[14:15], s[14:15]
	s_cbranch_execz .LBB0_824
	v_lshlrev_b32_e32 v44, 9, v38
	v_mov_b32_e32 v45, 0
	v_ashrrev_i32_e32 v37, 31, v36
	v_lshl_add_u64 v[44:45], s[8:9], 0, v[44:45]
	v_lshl_add_u64 v[44:45], v[36:37], 3, v[44:45]
	global_store_dword v[44:45], v68, off
.LBB0_824:
	s_or_b64 exec, exec, s[14:15]
	global_store_dword v[44:45], v39, off offset:4
	global_atomic_add_f32 v46, v39, s[6:7]
.LBB0_825:
	s_andn2_saveexec_b64 s[12:13], s[12:13]
	v_or_b32_e32 v38, v69, v38
	v_lshl_add_u32 v36, v36, 3, v76
	ds_write_b64 v36, v[38:39]
.LBB0_827:
	s_or_b64 exec, exec, s[2:3]
	v_or_b32_e32 v36, v28, v29
	v_or3_b32 v36, v36, v31, v30
	v_cmp_ne_u32_e32 vcc, 0, v36
	s_and_saveexec_b64 s[2:3], vcc
	s_cbranch_execz .LBB0_864
	v_cmp_neq_f32_e32 vcc, 0, v28
	s_and_saveexec_b64 s[12:13], vcc
	s_cbranch_execz .LBB0_837
	v_mov_b32_e32 v37, 1
	ds_add_rtn_u32 v36, v77, v37
	s_movk_i32 s14, 0x7f
	v_or_b32_e32 v44, 0x2600, v78
	s_waitcnt lgkmcnt(0)
	v_cmp_lt_i32_e32 vcc, s14, v36
	s_and_saveexec_b64 s[14:15], vcc
	s_xor_b64 s[14:15], exec, s[14:15]
	s_cbranch_execz .LBB0_835
	v_lshlrev_b32_e32 v45, 2, v44
	global_atomic_add v36, v45, v37, s[4:5] sc0
	v_mov_b32_e32 v37, 0
	s_waitcnt vmcnt(0)
	v_cmp_lt_i32_e32 vcc, 63, v36
	s_and_saveexec_b64 s[16:17], vcc
	s_xor_b64 s[16:17], exec, s[16:17]
	s_cbranch_execz .LBB0_832
	s_mov_b32 s18, 0x18000
	v_mov_b64_e32 v[38:39], s[10:11]
	v_mad_u64_u32 v[38:39], s[18:19], v44, s18, v[38:39]
	v_lshl_add_u64 v[38:39], v[36:37], 3, v[38:39]
	global_store_dword v[38:39], v68, off
.LBB0_832:
	s_andn2_saveexec_b64 s[16:17], s[16:17]
	s_cbranch_execz .LBB0_834
	v_lshlrev_b32_e32 v38, 9, v44
	v_mov_b32_e32 v39, 0
	v_ashrrev_i32_e32 v37, 31, v36
	v_lshl_add_u64 v[38:39], s[8:9], 0, v[38:39]
	v_lshl_add_u64 v[38:39], v[36:37], 3, v[38:39]
	global_store_dword v[38:39], v68, off
.LBB0_834:
	s_or_b64 exec, exec, s[16:17]
	global_store_dword v[38:39], v28, off offset:4
	global_atomic_add_f32 v45, v28, s[6:7]
.LBB0_835:
	s_andn2_saveexec_b64 s[14:15], s[14:15]
	v_or_b32_e32 v38, v69, v44
	v_lshl_add_u32 v36, v36, 3, v76
	v_mov_b32_e32 v39, v28
	ds_write_b64 v36, v[38:39]
.LBB0_837:
	s_or_b64 exec, exec, s[12:13]
	v_cmp_neq_f32_e32 vcc, 0, v29
	s_and_saveexec_b64 s[12:13], vcc
	s_cbranch_execz .LBB0_846
	v_mov_b32_e32 v37, 1
	ds_add_rtn_u32 v36, v77, v37
	s_movk_i32 s14, 0x7f
	v_or_b32_e32 v28, 0x2601, v78
	s_waitcnt lgkmcnt(0)
	v_cmp_lt_i32_e32 vcc, s14, v36
	s_and_saveexec_b64 s[14:15], vcc
	s_xor_b64 s[14:15], exec, s[14:15]
	s_cbranch_execz .LBB0_844
	v_lshlrev_b32_e32 v44, 2, v28
	global_atomic_add v36, v44, v37, s[4:5] sc0
	v_mov_b32_e32 v37, 0
	s_waitcnt vmcnt(0)
	v_cmp_lt_i32_e32 vcc, 63, v36
	s_and_saveexec_b64 s[16:17], vcc
	s_xor_b64 s[16:17], exec, s[16:17]
	s_cbranch_execz .LBB0_841
	s_mov_b32 s18, 0x18000
	v_mov_b64_e32 v[38:39], s[10:11]
	v_mad_u64_u32 v[38:39], s[18:19], v28, s18, v[38:39]
	v_lshl_add_u64 v[38:39], v[36:37], 3, v[38:39]
	global_store_dword v[38:39], v68, off
.LBB0_841:
	s_andn2_saveexec_b64 s[16:17], s[16:17]
	s_cbranch_execz .LBB0_843
	v_lshlrev_b32_e32 v38, 9, v28
	v_mov_b32_e32 v39, 0
	v_ashrrev_i32_e32 v37, 31, v36
	v_lshl_add_u64 v[38:39], s[8:9], 0, v[38:39]
	v_lshl_add_u64 v[38:39], v[36:37], 3, v[38:39]
	global_store_dword v[38:39], v68, off
.LBB0_843:
	s_or_b64 exec, exec, s[16:17]
	global_store_dword v[38:39], v29, off offset:4
	global_atomic_add_f32 v44, v29, s[6:7]
.LBB0_844:
	s_andn2_saveexec_b64 s[14:15], s[14:15]
	v_or_b32_e32 v28, v69, v28
	v_lshl_add_u32 v36, v36, 3, v76
	ds_write_b64 v36, v[28:29]
.LBB0_846:
	s_or_b64 exec, exec, s[12:13]
	v_cmp_neq_f32_e32 vcc, 0, v30
	s_and_saveexec_b64 s[12:13], vcc
	s_cbranch_execz .LBB0_855
	v_mov_b32_e32 v29, 1
	ds_add_rtn_u32 v28, v77, v29
	s_movk_i32 s14, 0x7f
	v_or_b32_e32 v38, 0x2602, v78
	s_waitcnt lgkmcnt(0)
	v_cmp_lt_i32_e32 vcc, s14, v28
	s_and_saveexec_b64 s[14:15], vcc
	s_xor_b64 s[14:15], exec, s[14:15]
	s_cbranch_execz .LBB0_853
	v_lshlrev_b32_e32 v39, 2, v38
	global_atomic_add v28, v39, v29, s[4:5] sc0
	v_mov_b32_e32 v29, 0
	s_waitcnt vmcnt(0)
	v_cmp_lt_i32_e32 vcc, 63, v28
	s_and_saveexec_b64 s[16:17], vcc
	s_xor_b64 s[16:17], exec, s[16:17]
	s_cbranch_execz .LBB0_850
	s_mov_b32 s18, 0x18000
	v_mov_b64_e32 v[36:37], s[10:11]
	v_mad_u64_u32 v[36:37], s[18:19], v38, s18, v[36:37]
	v_lshl_add_u64 v[36:37], v[28:29], 3, v[36:37]
	global_store_dword v[36:37], v68, off
.LBB0_850:
	s_andn2_saveexec_b64 s[16:17], s[16:17]
	s_cbranch_execz .LBB0_852
	v_lshlrev_b32_e32 v36, 9, v38
	v_mov_b32_e32 v37, 0
	v_ashrrev_i32_e32 v29, 31, v28
	v_lshl_add_u64 v[36:37], s[8:9], 0, v[36:37]
	v_lshl_add_u64 v[36:37], v[28:29], 3, v[36:37]
	global_store_dword v[36:37], v68, off
.LBB0_852:
	s_or_b64 exec, exec, s[16:17]
	global_store_dword v[36:37], v30, off offset:4
	global_atomic_add_f32 v39, v30, s[6:7]
.LBB0_853:
	s_andn2_saveexec_b64 s[14:15], s[14:15]
	v_or_b32_e32 v36, v69, v38
	v_lshl_add_u32 v28, v28, 3, v76
	v_mov_b32_e32 v37, v30
	ds_write_b64 v28, v[36:37]
.LBB0_855:
	s_or_b64 exec, exec, s[12:13]
	v_cmp_neq_f32_e32 vcc, 0, v31
	s_and_b64 exec, exec, vcc
	s_cbranch_execz .LBB0_864
	v_mov_b32_e32 v29, 1
	ds_add_rtn_u32 v28, v77, v29
	s_movk_i32 s12, 0x7f
	v_or_b32_e32 v30, 0x2603, v78
	s_waitcnt lgkmcnt(0)
	v_cmp_lt_i32_e32 vcc, s12, v28
	s_and_saveexec_b64 s[12:13], vcc
	s_xor_b64 s[12:13], exec, s[12:13]
	s_cbranch_execz .LBB0_862
	v_lshlrev_b32_e32 v38, 2, v30
	global_atomic_add v28, v38, v29, s[4:5] sc0
	v_mov_b32_e32 v29, 0
	s_waitcnt vmcnt(0)
	v_cmp_lt_i32_e32 vcc, 63, v28
	s_and_saveexec_b64 s[14:15], vcc
	s_xor_b64 s[14:15], exec, s[14:15]
	s_cbranch_execz .LBB0_859
	s_mov_b32 s16, 0x18000
	v_mov_b64_e32 v[36:37], s[10:11]
	v_mad_u64_u32 v[36:37], s[16:17], v30, s16, v[36:37]
	v_lshl_add_u64 v[36:37], v[28:29], 3, v[36:37]
	global_store_dword v[36:37], v68, off
.LBB0_859:
	s_andn2_saveexec_b64 s[14:15], s[14:15]
	s_cbranch_execz .LBB0_861
	v_lshlrev_b32_e32 v36, 9, v30
	v_mov_b32_e32 v37, 0
	v_ashrrev_i32_e32 v29, 31, v28
	v_lshl_add_u64 v[36:37], s[8:9], 0, v[36:37]
	v_lshl_add_u64 v[36:37], v[28:29], 3, v[36:37]
	global_store_dword v[36:37], v68, off
.LBB0_861:
	s_or_b64 exec, exec, s[14:15]
	global_store_dword v[36:37], v31, off offset:4
	global_atomic_add_f32 v38, v31, s[6:7]
.LBB0_862:
	s_andn2_saveexec_b64 s[12:13], s[12:13]
	v_or_b32_e32 v30, v69, v30
	v_lshl_add_u32 v28, v28, 3, v76
	ds_write_b64 v28, v[30:31]
.LBB0_864:
	s_or_b64 exec, exec, s[2:3]
	v_or_b32_e32 v28, v20, v21
	v_or3_b32 v28, v28, v23, v22
	v_cmp_ne_u32_e32 vcc, 0, v28
	s_and_b64 exec, exec, vcc
	s_cbranch_execz .LBB0_901
	v_cmp_neq_f32_e32 vcc, 0, v20
	s_and_saveexec_b64 s[2:3], vcc
	s_cbranch_execz .LBB0_874
	v_mov_b32_e32 v29, 1
	ds_add_rtn_u32 v28, v77, v29
	s_movk_i32 s12, 0x7f
	v_or_b32_e32 v36, 0x2700, v78
	s_waitcnt lgkmcnt(0)
	v_cmp_lt_i32_e32 vcc, s12, v28
	s_and_saveexec_b64 s[12:13], vcc
	s_xor_b64 s[12:13], exec, s[12:13]
	s_cbranch_execz .LBB0_872
	v_lshlrev_b32_e32 v37, 2, v36
	global_atomic_add v28, v37, v29, s[4:5] sc0
	v_mov_b32_e32 v29, 0
	s_waitcnt vmcnt(0)
	v_cmp_lt_i32_e32 vcc, 63, v28
	s_and_saveexec_b64 s[14:15], vcc
	s_xor_b64 s[14:15], exec, s[14:15]
	s_cbranch_execz .LBB0_869
	s_mov_b32 s16, 0x18000
	v_mov_b64_e32 v[30:31], s[10:11]
	v_mad_u64_u32 v[30:31], s[16:17], v36, s16, v[30:31]
	v_lshl_add_u64 v[30:31], v[28:29], 3, v[30:31]
	global_store_dword v[30:31], v68, off
.LBB0_869:
	s_andn2_saveexec_b64 s[14:15], s[14:15]
	s_cbranch_execz .LBB0_871
	v_lshlrev_b32_e32 v30, 9, v36
	v_mov_b32_e32 v31, 0
	v_ashrrev_i32_e32 v29, 31, v28
	v_lshl_add_u64 v[30:31], s[8:9], 0, v[30:31]
	v_lshl_add_u64 v[30:31], v[28:29], 3, v[30:31]
	global_store_dword v[30:31], v68, off
.LBB0_871:
	s_or_b64 exec, exec, s[14:15]
	global_store_dword v[30:31], v20, off offset:4
	global_atomic_add_f32 v37, v20, s[6:7]
.LBB0_872:
	s_andn2_saveexec_b64 s[12:13], s[12:13]
	v_or_b32_e32 v30, v69, v36
	v_lshl_add_u32 v28, v28, 3, v76
	v_mov_b32_e32 v31, v20
	ds_write_b64 v28, v[30:31]
.LBB0_874:
	s_or_b64 exec, exec, s[2:3]
	v_cmp_neq_f32_e32 vcc, 0, v21
	s_and_saveexec_b64 s[2:3], vcc
	s_cbranch_execz .LBB0_883
	v_mov_b32_e32 v29, 1
	ds_add_rtn_u32 v28, v77, v29
	s_movk_i32 s12, 0x7f
	v_or_b32_e32 v20, 0x2701, v78
	s_waitcnt lgkmcnt(0)
	v_cmp_lt_i32_e32 vcc, s12, v28
	s_and_saveexec_b64 s[12:13], vcc
	s_xor_b64 s[12:13], exec, s[12:13]
	s_cbranch_execz .LBB0_881
	v_lshlrev_b32_e32 v36, 2, v20
	global_atomic_add v28, v36, v29, s[4:5] sc0
	v_mov_b32_e32 v29, 0
	s_waitcnt vmcnt(0)
	v_cmp_lt_i32_e32 vcc, 63, v28
	s_and_saveexec_b64 s[14:15], vcc
	s_xor_b64 s[14:15], exec, s[14:15]
	s_cbranch_execz .LBB0_878
	s_mov_b32 s16, 0x18000
	v_mov_b64_e32 v[30:31], s[10:11]
	v_mad_u64_u32 v[30:31], s[16:17], v20, s16, v[30:31]
	v_lshl_add_u64 v[30:31], v[28:29], 3, v[30:31]
	global_store_dword v[30:31], v68, off
.LBB0_878:
	s_andn2_saveexec_b64 s[14:15], s[14:15]
	s_cbranch_execz .LBB0_880
	v_lshlrev_b32_e32 v30, 9, v20
	v_mov_b32_e32 v31, 0
	v_ashrrev_i32_e32 v29, 31, v28
	v_lshl_add_u64 v[30:31], s[8:9], 0, v[30:31]
	v_lshl_add_u64 v[30:31], v[28:29], 3, v[30:31]
	global_store_dword v[30:31], v68, off
.LBB0_880:
	s_or_b64 exec, exec, s[14:15]
	global_store_dword v[30:31], v21, off offset:4
	global_atomic_add_f32 v36, v21, s[6:7]
.LBB0_881:
	s_andn2_saveexec_b64 s[12:13], s[12:13]
	v_or_b32_e32 v20, v69, v20
	v_lshl_add_u32 v28, v28, 3, v76
	ds_write_b64 v28, v[20:21]
.LBB0_883:
	s_or_b64 exec, exec, s[2:3]
	v_cmp_neq_f32_e32 vcc, 0, v22
	s_and_saveexec_b64 s[2:3], vcc
	s_cbranch_execz .LBB0_892
	v_mov_b32_e32 v21, 1
	ds_add_rtn_u32 v20, v77, v21
	s_movk_i32 s12, 0x7f
	v_or_b32_e32 v30, 0x2702, v78
	s_waitcnt lgkmcnt(0)
	v_cmp_lt_i32_e32 vcc, s12, v20
	s_and_saveexec_b64 s[12:13], vcc
	s_xor_b64 s[12:13], exec, s[12:13]
	s_cbranch_execz .LBB0_890
	v_lshlrev_b32_e32 v31, 2, v30
	global_atomic_add v20, v31, v21, s[4:5] sc0
	v_mov_b32_e32 v21, 0
	s_waitcnt vmcnt(0)
	v_cmp_lt_i32_e32 vcc, 63, v20
	s_and_saveexec_b64 s[14:15], vcc
	s_xor_b64 s[14:15], exec, s[14:15]
	s_cbranch_execz .LBB0_887
	s_mov_b32 s16, 0x18000
	v_mov_b64_e32 v[28:29], s[10:11]
	v_mad_u64_u32 v[28:29], s[16:17], v30, s16, v[28:29]
	v_lshl_add_u64 v[28:29], v[20:21], 3, v[28:29]
	global_store_dword v[28:29], v68, off
.LBB0_887:
	s_andn2_saveexec_b64 s[14:15], s[14:15]
	s_cbranch_execz .LBB0_889
	v_lshlrev_b32_e32 v28, 9, v30
	v_mov_b32_e32 v29, 0
	v_ashrrev_i32_e32 v21, 31, v20
	v_lshl_add_u64 v[28:29], s[8:9], 0, v[28:29]
	v_lshl_add_u64 v[28:29], v[20:21], 3, v[28:29]
	global_store_dword v[28:29], v68, off
.LBB0_889:
	s_or_b64 exec, exec, s[14:15]
	global_store_dword v[28:29], v22, off offset:4
	global_atomic_add_f32 v31, v22, s[6:7]
.LBB0_890:
	s_andn2_saveexec_b64 s[12:13], s[12:13]
	v_or_b32_e32 v28, v69, v30
	v_lshl_add_u32 v20, v20, 3, v76
	v_mov_b32_e32 v29, v22
	ds_write_b64 v20, v[28:29]
.LBB0_892:
	s_or_b64 exec, exec, s[2:3]
	v_cmp_neq_f32_e32 vcc, 0, v23
	s_and_b64 exec, exec, vcc
	s_cbranch_execz .LBB0_901
	v_mov_b32_e32 v21, 1
	ds_add_rtn_u32 v20, v77, v21
	s_movk_i32 s2, 0x7f
	v_or_b32_e32 v22, 0x2703, v78
	s_waitcnt lgkmcnt(0)
	v_cmp_lt_i32_e32 vcc, s2, v20
	s_and_saveexec_b64 s[2:3], vcc
	s_xor_b64 s[2:3], exec, s[2:3]
	s_cbranch_execz .LBB0_899
	v_lshlrev_b32_e32 v30, 2, v22
	global_atomic_add v20, v30, v21, s[4:5] sc0
	v_mov_b32_e32 v21, 0
	s_waitcnt vmcnt(0)
	v_cmp_lt_i32_e32 vcc, 63, v20
	s_and_saveexec_b64 s[12:13], vcc
	s_xor_b64 s[12:13], exec, s[12:13]
	s_cbranch_execz .LBB0_896
	s_mov_b32 s14, 0x18000
	v_mov_b64_e32 v[28:29], s[10:11]
	v_mad_u64_u32 v[28:29], s[14:15], v22, s14, v[28:29]
	v_lshl_add_u64 v[28:29], v[20:21], 3, v[28:29]
	global_store_dword v[28:29], v68, off
.LBB0_896:
	s_andn2_saveexec_b64 s[12:13], s[12:13]
	s_cbranch_execz .LBB0_898
	v_lshlrev_b32_e32 v28, 9, v22
	v_mov_b32_e32 v29, 0
	v_ashrrev_i32_e32 v21, 31, v20
	v_lshl_add_u64 v[28:29], s[8:9], 0, v[28:29]
	v_lshl_add_u64 v[28:29], v[20:21], 3, v[28:29]
	global_store_dword v[28:29], v68, off
.LBB0_898:
	s_or_b64 exec, exec, s[12:13]
	global_store_dword v[28:29], v23, off offset:4
	global_atomic_add_f32 v30, v23, s[6:7]
.LBB0_899:
	s_andn2_saveexec_b64 s[2:3], s[2:3]
	v_or_b32_e32 v22, v69, v22
	v_lshl_add_u32 v20, v20, 3, v76
	ds_write_b64 v20, v[22:23]
.LBB0_901:
	s_or_b64 exec, exec, s[0:1]
	s_waitcnt vmcnt(5)
	v_or_b32_e32 v21, v25, v24
	v_or3_b32 v29, v21, v27, v26
	s_waitcnt vmcnt(0)
	v_or_b32_e32 v21, v0, v1
	v_or3_b32 v28, v21, v3, v2
	v_or3_b32 v21, v28, v5, v4
	v_or3_b32 v21, v21, v7, v6
	v_or3_b32 v21, v21, v9, v8
	v_or3_b32 v21, v21, v11, v10
	v_or3_b32 v21, v21, v13, v12
	v_or3_b32 v21, v21, v15, v14
	v_or3_b32 v21, v21, v17, v16
	v_or3_b32 v21, v21, v19, v18
	v_or_b32_e32 v20, v41, v40
	v_or3_b32 v21, v21, v33, v32
	v_or3_b32 v20, v20, v43, v42
	v_or3_b32 v21, v21, v35, v34
	v_or3_b32 v21, v21, v29, v20
	v_cmp_ne_u32_e32 vcc, 0, v21
	s_and_saveexec_b64 s[0:1], vcc
	s_cbranch_execz .LBB0_1198
	v_cmp_ne_u32_e32 vcc, 0, v20
	s_and_saveexec_b64 s[2:3], vcc
	s_cbranch_execz .LBB0_939
	v_cmp_neq_f32_e32 vcc, 0, v40
	s_and_saveexec_b64 s[12:13], vcc
	s_cbranch_execz .LBB0_912
	v_mov_b32_e32 v21, 1
	ds_add_rtn_u32 v20, v77, v21
	s_movk_i32 s14, 0x7f
	v_or_b32_e32 v30, 0x2800, v78
	s_waitcnt lgkmcnt(0)
	v_cmp_lt_i32_e32 vcc, s14, v20
	s_and_saveexec_b64 s[14:15], vcc
	s_xor_b64 s[14:15], exec, s[14:15]
	s_cbranch_execz .LBB0_910
	v_lshlrev_b32_e32 v31, 2, v30
	global_atomic_add v20, v31, v21, s[4:5] sc0
	v_mov_b32_e32 v21, 0
	s_waitcnt vmcnt(0)
	v_cmp_lt_i32_e32 vcc, 63, v20
	s_and_saveexec_b64 s[16:17], vcc
	s_xor_b64 s[16:17], exec, s[16:17]
	s_cbranch_execz .LBB0_907
	s_mov_b32 s18, 0x18000
	v_mov_b64_e32 v[22:23], s[10:11]
	v_mad_u64_u32 v[22:23], s[18:19], v30, s18, v[22:23]
	v_lshl_add_u64 v[22:23], v[20:21], 3, v[22:23]
	global_store_dword v[22:23], v68, off
.LBB0_907:
	s_andn2_saveexec_b64 s[16:17], s[16:17]
	s_cbranch_execz .LBB0_909
	v_lshlrev_b32_e32 v22, 9, v30
	v_mov_b32_e32 v23, 0
	v_ashrrev_i32_e32 v21, 31, v20
	v_lshl_add_u64 v[22:23], s[8:9], 0, v[22:23]
	v_lshl_add_u64 v[22:23], v[20:21], 3, v[22:23]
	global_store_dword v[22:23], v68, off
.LBB0_909:
	s_or_b64 exec, exec, s[16:17]
	global_store_dword v[22:23], v40, off offset:4
	global_atomic_add_f32 v31, v40, s[6:7]
.LBB0_910:
	s_andn2_saveexec_b64 s[14:15], s[14:15]
	v_or_b32_e32 v22, v69, v30
	v_lshl_add_u32 v20, v20, 3, v76
	v_mov_b32_e32 v23, v40
	ds_write_b64 v20, v[22:23]
.LBB0_912:
	s_or_b64 exec, exec, s[12:13]
	v_cmp_neq_f32_e32 vcc, 0, v41
	s_and_saveexec_b64 s[12:13], vcc
	s_cbranch_execz .LBB0_921
	v_mov_b32_e32 v21, 1
	ds_add_rtn_u32 v20, v77, v21
	s_movk_i32 s14, 0x7f
	v_or_b32_e32 v30, 0x2801, v78
	s_waitcnt lgkmcnt(0)
	v_cmp_lt_i32_e32 vcc, s14, v20
	s_and_saveexec_b64 s[14:15], vcc
	s_xor_b64 s[14:15], exec, s[14:15]
	s_cbranch_execz .LBB0_919
	v_lshlrev_b32_e32 v31, 2, v30
	global_atomic_add v20, v31, v21, s[4:5] sc0
	v_mov_b32_e32 v21, 0
	s_waitcnt vmcnt(0)
	v_cmp_lt_i32_e32 vcc, 63, v20
	s_and_saveexec_b64 s[16:17], vcc
	s_xor_b64 s[16:17], exec, s[16:17]
	s_cbranch_execz .LBB0_916
	s_mov_b32 s18, 0x18000
	v_mov_b64_e32 v[22:23], s[10:11]
	v_mad_u64_u32 v[22:23], s[18:19], v30, s18, v[22:23]
	v_lshl_add_u64 v[22:23], v[20:21], 3, v[22:23]
	global_store_dword v[22:23], v68, off

.LBB0_918:
	s_or_b64 exec, exec, s[16:17]
	global_store_dword v[22:23], v41, off offset:4
	global_atomic_add_f32 v31, v41, s[6:7]
.LBB0_919:
	s_andn2_saveexec_b64 s[14:15], s[14:15]
	v_or_b32_e32 v40, v69, v30
	v_lshl_add_u32 v20, v20, 3, v76
	ds_write_b64 v20, v[40:41]
.LBB0_921:
	s_or_b64 exec, exec, s[12:13]
	v_cmp_neq_f32_e32 vcc, 0, v42
	s_and_saveexec_b64 s[12:13], vcc
	s_cbranch_execz .LBB0_930
	v_mov_b32_e32 v21, 1
	ds_add_rtn_u32 v20, v77, v21
	s_movk_i32 s14, 0x7f
	v_or_b32_e32 v30, 0x2802, v78
	s_waitcnt lgkmcnt(0)
	v_cmp_lt_i32_e32 vcc, s14, v20
	s_and_saveexec_b64 s[14:15], vcc
	s_xor_b64 s[14:15], exec, s[14:15]
	s_cbranch_execz .LBB0_928
	v_lshlrev_b32_e32 v31, 2, v30
	global_atomic_add v20, v31, v21, s[4:5] sc0
	v_mov_b32_e32 v21, 0
	s_waitcnt vmcnt(0)
	v_cmp_lt_i32_e32 vcc, 63, v20
	s_and_saveexec_b64 s[16:17], vcc
	s_xor_b64 s[16:17], exec, s[16:17]
	s_cbranch_execz .LBB0_925
	s_mov_b32 s18, 0x18000
	v_mov_b64_e32 v[22:23], s[10:11]
	v_mad_u64_u32 v[22:23], s[18:19], v30, s18, v[22:23]
	v_lshl_add_u64 v[22:23], v[20:21], 3, v[22:23]
	global_store_dword v[22:23], v68, off

.LBB0_927:
	s_or_b64 exec, exec, s[16:17]
	global_store_dword v[22:23], v42, off offset:4
	global_atomic_add_f32 v31, v42, s[6:7]
.LBB0_928:
	s_andn2_saveexec_b64 s[14:15], s[14:15]
	v_or_b32_e32 v22, v69, v30
	v_lshl_add_u32 v20, v20, 3, v76
	v_mov_b32_e32 v23, v42
	ds_write_b64 v20, v[22:23]
.LBB0_930:
	s_or_b64 exec, exec, s[12:13]
	v_cmp_neq_f32_e32 vcc, 0, v43
	s_and_b64 exec, exec, vcc
	s_cbranch_execz .LBB0_939
	v_mov_b32_e32 v21, 1
	ds_add_rtn_u32 v20, v77, v21
	s_movk_i32 s12, 0x7f
	v_or_b32_e32 v30, 0x2803, v78
	s_waitcnt lgkmcnt(0)
	v_cmp_lt_i32_e32 vcc, s12, v20
	s_and_saveexec_b64 s[12:13], vcc
	s_xor_b64 s[12:13], exec, s[12:13]
	s_cbranch_execz .LBB0_937
	v_lshlrev_b32_e32 v31, 2, v30
	global_atomic_add v20, v31, v21, s[4:5] sc0
	v_mov_b32_e32 v21, 0
	s_waitcnt vmcnt(0)
	v_cmp_lt_i32_e32 vcc, 63, v20
	s_and_saveexec_b64 s[14:15], vcc
	s_xor_b64 s[14:15], exec, s[14:15]
	s_cbranch_execz .LBB0_934
	s_mov_b32 s16, 0x18000
	v_mov_b64_e32 v[22:23], s[10:11]
	v_mad_u64_u32 v[22:23], s[16:17], v30, s16, v[22:23]
	v_lshl_add_u64 v[22:23], v[20:21], 3, v[22:23]
	global_store_dword v[22:23], v68, off
.LBB0_934:
	s_andn2_saveexec_b64 s[14:15], s[14:15]
	s_cbranch_execz .LBB0_936
	v_lshlrev_b32_e32 v22, 9, v30
	v_mov_b32_e32 v23, 0
	v_ashrrev_i32_e32 v21, 31, v20
	v_lshl_add_u64 v[22:23], s[8:9], 0, v[22:23]
	v_lshl_add_u64 v[22:23], v[20:21], 3, v[22:23]
	global_store_dword v[22:23], v68, off
.LBB0_936:
	s_or_b64 exec, exec, s[14:15]
	global_store_dword v[22:23], v43, off offset:4
	global_atomic_add_f32 v31, v43, s[6:7]
.LBB0_937:
	s_andn2_saveexec_b64 s[12:13], s[12:13]
	v_or_b32_e32 v42, v69, v30
	v_lshl_add_u32 v20, v20, 3, v76
	ds_write_b64 v20, v[42:43]
.LBB0_939:
	s_or_b64 exec, exec, s[2:3]
	v_or_b32_e32 v20, v32, v33
	v_or3_b32 v20, v20, v35, v34
	v_cmp_ne_u32_e32 vcc, 0, v20
	s_and_saveexec_b64 s[2:3], vcc
	s_cbranch_execz .LBB0_976
	v_cmp_neq_f32_e32 vcc, 0, v32
	s_and_saveexec_b64 s[12:13], vcc
	s_cbranch_execz .LBB0_949
	v_mov_b32_e32 v21, 1
	ds_add_rtn_u32 v20, v77, v21
	s_movk_i32 s14, 0x7f
	v_or_b32_e32 v30, 0x2900, v78
	s_waitcnt lgkmcnt(0)
	v_cmp_lt_i32_e32 vcc, s14, v20
	s_and_saveexec_b64 s[14:15], vcc
	s_xor_b64 s[14:15], exec, s[14:15]
	s_cbranch_execz .LBB0_947
	v_lshlrev_b32_e32 v31, 2, v30
	global_atomic_add v20, v31, v21, s[4:5] sc0
	v_mov_b32_e32 v21, 0
	s_waitcnt vmcnt(0)
	v_cmp_lt_i32_e32 vcc, 63, v20
	s_and_saveexec_b64 s[16:17], vcc
	s_xor_b64 s[16:17], exec, s[16:17]
	s_cbranch_execz .LBB0_944
	s_mov_b32 s18, 0x18000
	v_mov_b64_e32 v[22:23], s[10:11]
	v_mad_u64_u32 v[22:23], s[18:19], v30, s18, v[22:23]
	v_lshl_add_u64 v[22:23], v[20:21], 3, v[22:23]
	global_store_dword v[22:23], v68, off

.LBB0_946:
	s_or_b64 exec, exec, s[16:17]
	global_store_dword v[22:23], v32, off offset:4
	global_atomic_add_f32 v31, v32, s[6:7]
.LBB0_947:
	s_andn2_saveexec_b64 s[14:15], s[14:15]
	v_or_b32_e32 v22, v69, v30
	v_lshl_add_u32 v20, v20, 3, v76
	v_mov_b32_e32 v23, v32
	ds_write_b64 v20, v[22:23]
.LBB0_949:
	s_or_b64 exec, exec, s[12:13]
	v_cmp_neq_f32_e32 vcc, 0, v33
	s_and_saveexec_b64 s[12:13], vcc
	s_cbranch_execz .LBB0_958
	v_mov_b32_e32 v21, 1
	ds_add_rtn_u32 v20, v77, v21
	s_movk_i32 s14, 0x7f
	v_or_b32_e32 v30, 0x2901, v78
	s_waitcnt lgkmcnt(0)
	v_cmp_lt_i32_e32 vcc, s14, v20
	s_and_saveexec_b64 s[14:15], vcc
	s_xor_b64 s[14:15], exec, s[14:15]
	s_cbranch_execz .LBB0_956
	v_lshlrev_b32_e32 v31, 2, v30
	global_atomic_add v20, v31, v21, s[4:5] sc0
	v_mov_b32_e32 v21, 0
	s_waitcnt vmcnt(0)
	v_cmp_lt_i32_e32 vcc, 63, v20
	s_and_saveexec_b64 s[16:17], vcc
	s_xor_b64 s[16:17], exec, s[16:17]
	s_cbranch_execz .LBB0_953
	s_mov_b32 s18, 0x18000
	v_mov_b64_e32 v[22:23], s[10:11]
	v_mad_u64_u32 v[22:23], s[18:19], v30, s18, v[22:23]
	v_lshl_add_u64 v[22:23], v[20:21], 3, v[22:23]
	global_store_dword v[22:23], v68, off

.LBB0_955:
	s_or_b64 exec, exec, s[16:17]
	global_store_dword v[22:23], v33, off offset:4
	global_atomic_add_f32 v31, v33, s[6:7]
.LBB0_956:
	s_andn2_saveexec_b64 s[14:15], s[14:15]
	v_or_b32_e32 v32, v69, v30
	v_lshl_add_u32 v20, v20, 3, v76
	ds_write_b64 v20, v[32:33]
.LBB0_958:
	s_or_b64 exec, exec, s[12:13]
	v_cmp_neq_f32_e32 vcc, 0, v34
	s_and_saveexec_b64 s[12:13], vcc
	s_cbranch_execz .LBB0_967
	v_mov_b32_e32 v21, 1
	ds_add_rtn_u32 v20, v77, v21
	s_movk_i32 s14, 0x7f
	v_or_b32_e32 v30, 0x2902, v78
	s_waitcnt lgkmcnt(0)
	v_cmp_lt_i32_e32 vcc, s14, v20
	s_and_saveexec_b64 s[14:15], vcc
	s_xor_b64 s[14:15], exec, s[14:15]
	s_cbranch_execz .LBB0_965
	v_lshlrev_b32_e32 v31, 2, v30
	global_atomic_add v20, v31, v21, s[4:5] sc0
	v_mov_b32_e32 v21, 0
	s_waitcnt vmcnt(0)
	v_cmp_lt_i32_e32 vcc, 63, v20
	s_and_saveexec_b64 s[16:17], vcc
	s_xor_b64 s[16:17], exec, s[16:17]
	s_cbranch_execz .LBB0_962
	s_mov_b32 s18, 0x18000
	v_mov_b64_e32 v[22:23], s[10:11]
	v_mad_u64_u32 v[22:23], s[18:19], v30, s18, v[22:23]
	v_lshl_add_u64 v[22:23], v[20:21], 3, v[22:23]
	global_store_dword v[22:23], v68, off

.LBB0_964:
	s_or_b64 exec, exec, s[16:17]
	global_store_dword v[22:23], v34, off offset:4
	global_atomic_add_f32 v31, v34, s[6:7]
.LBB0_965:
	s_andn2_saveexec_b64 s[14:15], s[14:15]
	v_or_b32_e32 v22, v69, v30
	v_lshl_add_u32 v20, v20, 3, v76
	v_mov_b32_e32 v23, v34
	ds_write_b64 v20, v[22:23]
.LBB0_967:
	s_or_b64 exec, exec, s[12:13]
	v_cmp_neq_f32_e32 vcc, 0, v35
	s_and_b64 exec, exec, vcc
	s_cbranch_execz .LBB0_976
	v_mov_b32_e32 v21, 1
	ds_add_rtn_u32 v20, v77, v21
	s_movk_i32 s12, 0x7f
	v_or_b32_e32 v30, 0x2903, v78
	s_waitcnt lgkmcnt(0)
	v_cmp_lt_i32_e32 vcc, s12, v20
	s_and_saveexec_b64 s[12:13], vcc
	s_xor_b64 s[12:13], exec, s[12:13]
	s_cbranch_execz .LBB0_974
	v_lshlrev_b32_e32 v31, 2, v30
	global_atomic_add v20, v31, v21, s[4:5] sc0
	v_mov_b32_e32 v21, 0
	s_waitcnt vmcnt(0)
	v_cmp_lt_i32_e32 vcc, 63, v20
	s_and_saveexec_b64 s[14:15], vcc
	s_xor_b64 s[14:15], exec, s[14:15]
	s_cbranch_execz .LBB0_971
	s_mov_b32 s16, 0x18000
	v_mov_b64_e32 v[22:23], s[10:11]
	v_mad_u64_u32 v[22:23], s[16:17], v30, s16, v[22:23]
	v_lshl_add_u64 v[22:23], v[20:21], 3, v[22:23]
	global_store_dword v[22:23], v68, off

.LBB0_973:
	s_or_b64 exec, exec, s[14:15]
	global_store_dword v[22:23], v35, off offset:4
	global_atomic_add_f32 v31, v35, s[6:7]
.LBB0_974:
	s_andn2_saveexec_b64 s[12:13], s[12:13]
	v_or_b32_e32 v34, v69, v30
	v_lshl_add_u32 v20, v20, 3, v76
	ds_write_b64 v20, v[34:35]
.LBB0_976:
	s_or_b64 exec, exec, s[2:3]
	v_cmp_ne_u32_e32 vcc, 0, v29
	s_and_saveexec_b64 s[2:3], vcc
	s_cbranch_execz .LBB0_1013
	v_cmp_neq_f32_e32 vcc, 0, v24
	s_and_saveexec_b64 s[12:13], vcc
	s_cbranch_execz .LBB0_986
	v_mov_b32_e32 v21, 1
	ds_add_rtn_u32 v20, v77, v21
	s_movk_i32 s14, 0x7f
	v_or_b32_e32 v29, 0x2a00, v78
	s_waitcnt lgkmcnt(0)
	v_cmp_lt_i32_e32 vcc, s14, v20
	s_and_saveexec_b64 s[14:15], vcc
	s_xor_b64 s[14:15], exec, s[14:15]
	s_cbranch_execz .LBB0_984
	v_lshlrev_b32_e32 v30, 2, v29
	global_atomic_add v20, v30, v21, s[4:5] sc0
	v_mov_b32_e32 v21, 0
	s_waitcnt vmcnt(0)
	v_cmp_lt_i32_e32 vcc, 63, v20
	s_and_saveexec_b64 s[16:17], vcc
	s_xor_b64 s[16:17], exec, s[16:17]
	s_cbranch_execz .LBB0_981
	s_mov_b32 s18, 0x18000
	v_mov_b64_e32 v[22:23], s[10:11]
	v_mad_u64_u32 v[22:23], s[18:19], v29, s18, v[22:23]
	v_lshl_add_u64 v[22:23], v[20:21], 3, v[22:23]
	global_store_dword v[22:23], v68, off
.LBB0_981:
	s_andn2_saveexec_b64 s[16:17], s[16:17]
	s_cbranch_execz .LBB0_983
	v_lshlrev_b32_e32 v22, 9, v29
	v_mov_b32_e32 v23, 0
	v_ashrrev_i32_e32 v21, 31, v20
	v_lshl_add_u64 v[22:23], s[8:9], 0, v[22:23]
	v_lshl_add_u64 v[22:23], v[20:21], 3, v[22:23]
	global_store_dword v[22:23], v68, off
.LBB0_983:
	s_or_b64 exec, exec, s[16:17]
	global_store_dword v[22:23], v24, off offset:4
	global_atomic_add_f32 v30, v24, s[6:7]
.LBB0_984:
	s_andn2_saveexec_b64 s[14:15], s[14:15]
	v_or_b32_e32 v22, v69, v29
	v_lshl_add_u32 v20, v20, 3, v76
	v_mov_b32_e32 v23, v24
	ds_write_b64 v20, v[22:23]
.LBB0_986:
	s_or_b64 exec, exec, s[12:13]
	v_cmp_neq_f32_e32 vcc, 0, v25
	s_and_saveexec_b64 s[12:13], vcc
	s_cbranch_execz .LBB0_995
	v_mov_b32_e32 v21, 1
	ds_add_rtn_u32 v20, v77, v21
	s_movk_i32 s14, 0x7f
	v_or_b32_e32 v24, 0x2a01, v78
	s_waitcnt lgkmcnt(0)
	v_cmp_lt_i32_e32 vcc, s14, v20
	s_and_saveexec_b64 s[14:15], vcc
	s_xor_b64 s[14:15], exec, s[14:15]
	s_cbranch_execz .LBB0_993
	v_lshlrev_b32_e32 v29, 2, v24
	global_atomic_add v20, v29, v21, s[4:5] sc0
	v_mov_b32_e32 v21, 0
	s_waitcnt vmcnt(0)
	v_cmp_lt_i32_e32 vcc, 63, v20
	s_and_saveexec_b64 s[16:17], vcc
	s_xor_b64 s[16:17], exec, s[16:17]
	s_cbranch_execz .LBB0_990
	s_mov_b32 s18, 0x18000
	v_mov_b64_e32 v[22:23], s[10:11]
	v_mad_u64_u32 v[22:23], s[18:19], v24, s18, v[22:23]
	v_lshl_add_u64 v[22:23], v[20:21], 3, v[22:23]
	global_store_dword v[22:23], v68, off
.LBB0_990:
	s_andn2_saveexec_b64 s[16:17], s[16:17]
	s_cbranch_execz .LBB0_992
	v_lshlrev_b32_e32 v22, 9, v24
	v_mov_b32_e32 v23, 0
	v_ashrrev_i32_e32 v21, 31, v20
	v_lshl_add_u64 v[22:23], s[8:9], 0, v[22:23]
	v_lshl_add_u64 v[22:23], v[20:21], 3, v[22:23]
	global_store_dword v[22:23], v68, off
.LBB0_992:
	s_or_b64 exec, exec, s[16:17]
	global_store_dword v[22:23], v25, off offset:4
	global_atomic_add_f32 v29, v25, s[6:7]
.LBB0_993:
	s_andn2_saveexec_b64 s[14:15], s[14:15]
	v_or_b32_e32 v24, v69, v24
	v_lshl_add_u32 v20, v20, 3, v76
	ds_write_b64 v20, v[24:25]
.LBB0_995:
	s_or_b64 exec, exec, s[12:13]
	v_cmp_neq_f32_e32 vcc, 0, v26
	s_and_saveexec_b64 s[12:13], vcc
	s_cbranch_execz .LBB0_1004
	v_mov_b32_e32 v21, 1
	ds_add_rtn_u32 v20, v77, v21
	s_movk_i32 s14, 0x7f
	v_or_b32_e32 v24, 0x2a02, v78
	s_waitcnt lgkmcnt(0)
	v_cmp_lt_i32_e32 vcc, s14, v20
	s_and_saveexec_b64 s[14:15], vcc
	s_xor_b64 s[14:15], exec, s[14:15]
	s_cbranch_execz .LBB0_1002
	v_lshlrev_b32_e32 v25, 2, v24
	global_atomic_add v20, v25, v21, s[4:5] sc0
	v_mov_b32_e32 v21, 0
	s_waitcnt vmcnt(0)
	v_cmp_lt_i32_e32 vcc, 63, v20
	s_and_saveexec_b64 s[16:17], vcc
	s_xor_b64 s[16:17], exec, s[16:17]
	s_cbranch_execz .LBB0_999
	s_mov_b32 s18, 0x18000
	v_mov_b64_e32 v[22:23], s[10:11]
	v_mad_u64_u32 v[22:23], s[18:19], v24, s18, v[22:23]
	v_lshl_add_u64 v[22:23], v[20:21], 3, v[22:23]
	global_store_dword v[22:23], v68, off

.LBB0_1001:
	s_or_b64 exec, exec, s[16:17]
	global_store_dword v[22:23], v26, off offset:4
	global_atomic_add_f32 v25, v26, s[6:7]
.LBB0_1002:
	s_andn2_saveexec_b64 s[14:15], s[14:15]
	v_or_b32_e32 v22, v69, v24
	v_lshl_add_u32 v20, v20, 3, v76
	v_mov_b32_e32 v23, v26
	ds_write_b64 v20, v[22:23]
.LBB0_1004:
	s_or_b64 exec, exec, s[12:13]
	v_cmp_neq_f32_e32 vcc, 0, v27
	s_and_b64 exec, exec, vcc
	s_cbranch_execz .LBB0_1013
	v_mov_b32_e32 v21, 1
	ds_add_rtn_u32 v20, v77, v21
	s_movk_i32 s12, 0x7f
	v_or_b32_e32 v24, 0x2a03, v78
	s_waitcnt lgkmcnt(0)
	v_cmp_lt_i32_e32 vcc, s12, v20
	s_and_saveexec_b64 s[12:13], vcc
	s_xor_b64 s[12:13], exec, s[12:13]
	s_cbranch_execz .LBB0_1011
	v_lshlrev_b32_e32 v25, 2, v24
	global_atomic_add v20, v25, v21, s[4:5] sc0
	v_mov_b32_e32 v21, 0
	s_waitcnt vmcnt(0)
	v_cmp_lt_i32_e32 vcc, 63, v20
	s_and_saveexec_b64 s[14:15], vcc
	s_xor_b64 s[14:15], exec, s[14:15]
	s_cbranch_execz .LBB0_1008
	s_mov_b32 s16, 0x18000
	v_mov_b64_e32 v[22:23], s[10:11]
	v_mad_u64_u32 v[22:23], s[16:17], v24, s16, v[22:23]
	v_lshl_add_u64 v[22:23], v[20:21], 3, v[22:23]
	global_store_dword v[22:23], v68, off
.LBB0_1008:
	s_andn2_saveexec_b64 s[14:15], s[14:15]
	s_cbranch_execz .LBB0_1010
	v_lshlrev_b32_e32 v22, 9, v24
	v_mov_b32_e32 v23, 0
	v_ashrrev_i32_e32 v21, 31, v20
	v_lshl_add_u64 v[22:23], s[8:9], 0, v[22:23]
	v_lshl_add_u64 v[22:23], v[20:21], 3, v[22:23]
	global_store_dword v[22:23], v68, off
.LBB0_1010:
	s_or_b64 exec, exec, s[14:15]
	global_store_dword v[22:23], v27, off offset:4
	global_atomic_add_f32 v25, v27, s[6:7]
.LBB0_1011:
	s_andn2_saveexec_b64 s[12:13], s[12:13]
	v_or_b32_e32 v26, v69, v24
	v_lshl_add_u32 v20, v20, 3, v76
	ds_write_b64 v20, v[26:27]
.LBB0_1013:
	s_or_b64 exec, exec, s[2:3]
	v_or_b32_e32 v20, v16, v17
	v_or3_b32 v20, v20, v19, v18
	v_cmp_ne_u32_e32 vcc, 0, v20
	s_and_saveexec_b64 s[2:3], vcc
	s_cbranch_execz .LBB0_1050
	v_cmp_neq_f32_e32 vcc, 0, v16
	s_and_saveexec_b64 s[12:13], vcc
	s_cbranch_execz .LBB0_1023
	v_mov_b32_e32 v21, 1
	ds_add_rtn_u32 v20, v77, v21
	s_movk_i32 s14, 0x7f
	v_or_b32_e32 v24, 0x2b00, v78
	s_waitcnt lgkmcnt(0)
	v_cmp_lt_i32_e32 vcc, s14, v20
	s_and_saveexec_b64 s[14:15], vcc
	s_xor_b64 s[14:15], exec, s[14:15]
	s_cbranch_execz .LBB0_1021
	v_lshlrev_b32_e32 v25, 2, v24
	global_atomic_add v20, v25, v21, s[4:5] sc0
	v_mov_b32_e32 v21, 0
	s_waitcnt vmcnt(0)
	v_cmp_lt_i32_e32 vcc, 63, v20
	s_and_saveexec_b64 s[16:17], vcc
	s_xor_b64 s[16:17], exec, s[16:17]
	s_cbranch_execz .LBB0_1018
	s_mov_b32 s18, 0x18000
	v_mov_b64_e32 v[22:23], s[10:11]
	v_mad_u64_u32 v[22:23], s[18:19], v24, s18, v[22:23]
	v_lshl_add_u64 v[22:23], v[20:21], 3, v[22:23]
	global_store_dword v[22:23], v68, off

.LBB0_1020:
	s_or_b64 exec, exec, s[16:17]
	global_store_dword v[22:23], v16, off offset:4
	global_atomic_add_f32 v25, v16, s[6:7]
.LBB0_1021:
	s_andn2_saveexec_b64 s[14:15], s[14:15]
	v_or_b32_e32 v22, v69, v24
	v_lshl_add_u32 v20, v20, 3, v76
	v_mov_b32_e32 v23, v16
	ds_write_b64 v20, v[22:23]
.LBB0_1023:
	s_or_b64 exec, exec, s[12:13]
	v_cmp_neq_f32_e32 vcc, 0, v17
	s_and_saveexec_b64 s[12:13], vcc
	s_cbranch_execz .LBB0_1032
	v_mov_b32_e32 v21, 1
	ds_add_rtn_u32 v20, v77, v21
	s_movk_i32 s14, 0x7f
	v_or_b32_e32 v16, 0x2b01, v78
	s_waitcnt lgkmcnt(0)
	v_cmp_lt_i32_e32 vcc, s14, v20
	s_and_saveexec_b64 s[14:15], vcc
	s_xor_b64 s[14:15], exec, s[14:15]
	s_cbranch_execz .LBB0_1030
	v_lshlrev_b32_e32 v24, 2, v16
	global_atomic_add v20, v24, v21, s[4:5] sc0
	v_mov_b32_e32 v21, 0
	s_waitcnt vmcnt(0)
	v_cmp_lt_i32_e32 vcc, 63, v20
	s_and_saveexec_b64 s[16:17], vcc
	s_xor_b64 s[16:17], exec, s[16:17]
	s_cbranch_execz .LBB0_1027
	s_mov_b32 s18, 0x18000
	v_mov_b64_e32 v[22:23], s[10:11]
	v_mad_u64_u32 v[22:23], s[18:19], v16, s18, v[22:23]
	v_lshl_add_u64 v[22:23], v[20:21], 3, v[22:23]
	global_store_dword v[22:23], v68, off
.LBB0_1027:
	s_andn2_saveexec_b64 s[16:17], s[16:17]
	s_cbranch_execz .LBB0_1029
	v_lshlrev_b32_e32 v22, 9, v16
	v_mov_b32_e32 v23, 0
	v_ashrrev_i32_e32 v21, 31, v20
	v_lshl_add_u64 v[22:23], s[8:9], 0, v[22:23]
	v_lshl_add_u64 v[22:23], v[20:21], 3, v[22:23]
	global_store_dword v[22:23], v68, off
.LBB0_1029:
	s_or_b64 exec, exec, s[16:17]
	global_store_dword v[22:23], v17, off offset:4
	global_atomic_add_f32 v24, v17, s[6:7]
.LBB0_1030:
	s_andn2_saveexec_b64 s[14:15], s[14:15]
	v_or_b32_e32 v16, v69, v16
	v_lshl_add_u32 v20, v20, 3, v76
	ds_write_b64 v20, v[16:17]
.LBB0_1032:
	s_or_b64 exec, exec, s[12:13]
	v_cmp_neq_f32_e32 vcc, 0, v18
	s_and_saveexec_b64 s[12:13], vcc
	s_cbranch_execz .LBB0_1041
	v_mov_b32_e32 v17, 1
	ds_add_rtn_u32 v16, v77, v17
	s_movk_i32 s14, 0x7f
	v_or_b32_e32 v22, 0x2b02, v78
	s_waitcnt lgkmcnt(0)
	v_cmp_lt_i32_e32 vcc, s14, v16
	s_and_saveexec_b64 s[14:15], vcc
	s_xor_b64 s[14:15], exec, s[14:15]
	s_cbranch_execz .LBB0_1039
	v_lshlrev_b32_e32 v23, 2, v22
	global_atomic_add v16, v23, v17, s[4:5] sc0
	v_mov_b32_e32 v17, 0
	s_waitcnt vmcnt(0)
	v_cmp_lt_i32_e32 vcc, 63, v16
	s_and_saveexec_b64 s[16:17], vcc
	s_xor_b64 s[16:17], exec, s[16:17]
	s_cbranch_execz .LBB0_1036
	s_mov_b32 s18, 0x18000
	v_mov_b64_e32 v[20:21], s[10:11]
	v_mad_u64_u32 v[20:21], s[18:19], v22, s18, v[20:21]
	v_lshl_add_u64 v[20:21], v[16:17], 3, v[20:21]
	global_store_dword v[20:21], v68, off
.LBB0_1036:
	s_andn2_saveexec_b64 s[16:17], s[16:17]
	s_cbranch_execz .LBB0_1038
	v_lshlrev_b32_e32 v20, 9, v22
	v_mov_b32_e32 v21, 0
	v_ashrrev_i32_e32 v17, 31, v16
	v_lshl_add_u64 v[20:21], s[8:9], 0, v[20:21]
	v_lshl_add_u64 v[20:21], v[16:17], 3, v[20:21]
	global_store_dword v[20:21], v68, off
.LBB0_1038:
	s_or_b64 exec, exec, s[16:17]
	global_store_dword v[20:21], v18, off offset:4
	global_atomic_add_f32 v23, v18, s[6:7]
.LBB0_1039:
	s_andn2_saveexec_b64 s[14:15], s[14:15]
	v_or_b32_e32 v20, v69, v22
	v_lshl_add_u32 v16, v16, 3, v76
	v_mov_b32_e32 v21, v18
	ds_write_b64 v16, v[20:21]
.LBB0_1041:
	s_or_b64 exec, exec, s[12:13]
	v_cmp_neq_f32_e32 vcc, 0, v19
	s_and_b64 exec, exec, vcc
	s_cbranch_execz .LBB0_1050
	v_mov_b32_e32 v17, 1
	ds_add_rtn_u32 v16, v77, v17
	s_movk_i32 s12, 0x7f
	v_or_b32_e32 v18, 0x2b03, v78
	s_waitcnt lgkmcnt(0)
	v_cmp_lt_i32_e32 vcc, s12, v16
	s_and_saveexec_b64 s[12:13], vcc
	s_xor_b64 s[12:13], exec, s[12:13]
	s_cbranch_execz .LBB0_1048
	v_lshlrev_b32_e32 v22, 2, v18
	global_atomic_add v16, v22, v17, s[4:5] sc0
	v_mov_b32_e32 v17, 0
	s_waitcnt vmcnt(0)
	v_cmp_lt_i32_e32 vcc, 63, v16
	s_and_saveexec_b64 s[14:15], vcc
	s_xor_b64 s[14:15], exec, s[14:15]
	s_cbranch_execz .LBB0_1045
	s_mov_b32 s16, 0x18000
	v_mov_b64_e32 v[20:21], s[10:11]
	v_mad_u64_u32 v[20:21], s[16:17], v18, s16, v[20:21]
	v_lshl_add_u64 v[20:21], v[16:17], 3, v[20:21]
	global_store_dword v[20:21], v68, off
.LBB0_1045:
	s_andn2_saveexec_b64 s[14:15], s[14:15]
	s_cbranch_execz .LBB0_1047
	v_lshlrev_b32_e32 v20, 9, v18
	v_mov_b32_e32 v21, 0
	v_ashrrev_i32_e32 v17, 31, v16
	v_lshl_add_u64 v[20:21], s[8:9], 0, v[20:21]
	v_lshl_add_u64 v[20:21], v[16:17], 3, v[20:21]
	global_store_dword v[20:21], v68, off
.LBB0_1047:
	s_or_b64 exec, exec, s[14:15]
	global_store_dword v[20:21], v19, off offset:4
	global_atomic_add_f32 v22, v19, s[6:7]
.LBB0_1048:
	s_andn2_saveexec_b64 s[12:13], s[12:13]
	v_or_b32_e32 v18, v69, v18
	v_lshl_add_u32 v16, v16, 3, v76
	ds_write_b64 v16, v[18:19]
.LBB0_1050:
	s_or_b64 exec, exec, s[2:3]
	v_or_b32_e32 v16, v12, v13
	v_or3_b32 v16, v16, v15, v14
	v_cmp_ne_u32_e32 vcc, 0, v16
	s_and_saveexec_b64 s[2:3], vcc
	s_cbranch_execz .LBB0_1087
	v_cmp_neq_f32_e32 vcc, 0, v12
	s_and_saveexec_b64 s[12:13], vcc
	s_cbranch_execz .LBB0_1060
	v_mov_b32_e32 v17, 1
	ds_add_rtn_u32 v16, v77, v17
	s_movk_i32 s14, 0x7f
	v_or_b32_e32 v20, 0x2c00, v78
	s_waitcnt lgkmcnt(0)
	v_cmp_lt_i32_e32 vcc, s14, v16
	s_and_saveexec_b64 s[14:15], vcc
	s_xor_b64 s[14:15], exec, s[14:15]
	s_cbranch_execz .LBB0_1058
	v_lshlrev_b32_e32 v21, 2, v20
	global_atomic_add v16, v21, v17, s[4:5] sc0
	v_mov_b32_e32 v17, 0
	s_waitcnt vmcnt(0)
	v_cmp_lt_i32_e32 vcc, 63, v16
	s_and_saveexec_b64 s[16:17], vcc
	s_xor_b64 s[16:17], exec, s[16:17]
	s_cbranch_execz .LBB0_1055
	s_mov_b32 s18, 0x18000
	v_mov_b64_e32 v[18:19], s[10:11]
	v_mad_u64_u32 v[18:19], s[18:19], v20, s18, v[18:19]
	v_lshl_add_u64 v[18:19], v[16:17], 3, v[18:19]
	global_store_dword v[18:19], v68, off
.LBB0_1055:
	s_andn2_saveexec_b64 s[16:17], s[16:17]
	s_cbranch_execz .LBB0_1057
	v_lshlrev_b32_e32 v18, 9, v20
	v_mov_b32_e32 v19, 0
	v_ashrrev_i32_e32 v17, 31, v16
	v_lshl_add_u64 v[18:19], s[8:9], 0, v[18:19]
	v_lshl_add_u64 v[18:19], v[16:17], 3, v[18:19]
	global_store_dword v[18:19], v68, off
.LBB0_1057:
	s_or_b64 exec, exec, s[16:17]
	global_store_dword v[18:19], v12, off offset:4
	global_atomic_add_f32 v21, v12, s[6:7]
.LBB0_1058:
	s_andn2_saveexec_b64 s[14:15], s[14:15]
	v_or_b32_e32 v18, v69, v20
	v_lshl_add_u32 v16, v16, 3, v76
	v_mov_b32_e32 v19, v12
	ds_write_b64 v16, v[18:19]
.LBB0_1060:
	s_or_b64 exec, exec, s[12:13]
	v_cmp_neq_f32_e32 vcc, 0, v13
	s_and_saveexec_b64 s[12:13], vcc
	s_cbranch_execz .LBB0_1069
	v_mov_b32_e32 v17, 1
	ds_add_rtn_u32 v16, v77, v17
	s_movk_i32 s14, 0x7f
	v_or_b32_e32 v12, 0x2c01, v78
	s_waitcnt lgkmcnt(0)
	v_cmp_lt_i32_e32 vcc, s14, v16
	s_and_saveexec_b64 s[14:15], vcc
	s_xor_b64 s[14:15], exec, s[14:15]
	s_cbranch_execz .LBB0_1067
	v_lshlrev_b32_e32 v20, 2, v12
	global_atomic_add v16, v20, v17, s[4:5] sc0
	v_mov_b32_e32 v17, 0
	s_waitcnt vmcnt(0)
	v_cmp_lt_i32_e32 vcc, 63, v16
	s_and_saveexec_b64 s[16:17], vcc
	s_xor_b64 s[16:17], exec, s[16:17]
	s_cbranch_execz .LBB0_1064
	s_mov_b32 s18, 0x18000
	v_mov_b64_e32 v[18:19], s[10:11]
	v_mad_u64_u32 v[18:19], s[18:19], v12, s18, v[18:19]
	v_lshl_add_u64 v[18:19], v[16:17], 3, v[18:19]
	global_store_dword v[18:19], v68, off
.LBB0_1064:
	s_andn2_saveexec_b64 s[16:17], s[16:17]
	s_cbranch_execz .LBB0_1066
	v_lshlrev_b32_e32 v18, 9, v12
	v_mov_b32_e32 v19, 0
	v_ashrrev_i32_e32 v17, 31, v16
	v_lshl_add_u64 v[18:19], s[8:9], 0, v[18:19]
	v_lshl_add_u64 v[18:19], v[16:17], 3, v[18:19]
	global_store_dword v[18:19], v68, off
.LBB0_1066:
	s_or_b64 exec, exec, s[16:17]
	global_store_dword v[18:19], v13, off offset:4
	global_atomic_add_f32 v20, v13, s[6:7]
.LBB0_1067:
	s_andn2_saveexec_b64 s[14:15], s[14:15]
	v_or_b32_e32 v12, v69, v12
	v_lshl_add_u32 v16, v16, 3, v76
	ds_write_b64 v16, v[12:13]
.LBB0_1069:
	s_or_b64 exec, exec, s[12:13]
	v_cmp_neq_f32_e32 vcc, 0, v14
	s_and_saveexec_b64 s[12:13], vcc
	s_cbranch_execz .LBB0_1078
	v_mov_b32_e32 v13, 1
	ds_add_rtn_u32 v12, v77, v13
	s_movk_i32 s14, 0x7f
	v_or_b32_e32 v18, 0x2c02, v78
	s_waitcnt lgkmcnt(0)
	v_cmp_lt_i32_e32 vcc, s14, v12
	s_and_saveexec_b64 s[14:15], vcc
	s_xor_b64 s[14:15], exec, s[14:15]
	s_cbranch_execz .LBB0_1076
	v_lshlrev_b32_e32 v19, 2, v18
	global_atomic_add v12, v19, v13, s[4:5] sc0
	v_mov_b32_e32 v13, 0
	s_waitcnt vmcnt(0)
	v_cmp_lt_i32_e32 vcc, 63, v12
	s_and_saveexec_b64 s[16:17], vcc
	s_xor_b64 s[16:17], exec, s[16:17]
	s_cbranch_execz .LBB0_1073
	s_mov_b32 s18, 0x18000
	v_mov_b64_e32 v[16:17], s[10:11]
	v_mad_u64_u32 v[16:17], s[18:19], v18, s18, v[16:17]
	v_lshl_add_u64 v[16:17], v[12:13], 3, v[16:17]
	global_store_dword v[16:17], v68, off
.LBB0_1073:
	s_andn2_saveexec_b64 s[16:17], s[16:17]
	s_cbranch_execz .LBB0_1075
	v_lshlrev_b32_e32 v16, 9, v18
	v_mov_b32_e32 v17, 0
	v_ashrrev_i32_e32 v13, 31, v12
	v_lshl_add_u64 v[16:17], s[8:9], 0, v[16:17]
	v_lshl_add_u64 v[16:17], v[12:13], 3, v[16:17]
	global_store_dword v[16:17], v68, off
.LBB0_1075:
	s_or_b64 exec, exec, s[16:17]
	global_store_dword v[16:17], v14, off offset:4
	global_atomic_add_f32 v19, v14, s[6:7]
.LBB0_1076:
	s_andn2_saveexec_b64 s[14:15], s[14:15]
	v_or_b32_e32 v16, v69, v18
	v_lshl_add_u32 v12, v12, 3, v76
	v_mov_b32_e32 v17, v14
	ds_write_b64 v12, v[16:17]
.LBB0_1078:
	s_or_b64 exec, exec, s[12:13]
	v_cmp_neq_f32_e32 vcc, 0, v15
	s_and_b64 exec, exec, vcc
	s_cbranch_execz .LBB0_1087
	v_mov_b32_e32 v13, 1
	ds_add_rtn_u32 v12, v77, v13
	s_movk_i32 s12, 0x7f
	v_or_b32_e32 v14, 0x2c03, v78
	s_waitcnt lgkmcnt(0)
	v_cmp_lt_i32_e32 vcc, s12, v12
	s_and_saveexec_b64 s[12:13], vcc
	s_xor_b64 s[12:13], exec, s[12:13]
	s_cbranch_execz .LBB0_1085
	v_lshlrev_b32_e32 v18, 2, v14
	global_atomic_add v12, v18, v13, s[4:5] sc0
	v_mov_b32_e32 v13, 0
	s_waitcnt vmcnt(0)
	v_cmp_lt_i32_e32 vcc, 63, v12
	s_and_saveexec_b64 s[14:15], vcc
	s_xor_b64 s[14:15], exec, s[14:15]
	s_cbranch_execz .LBB0_1082
	s_mov_b32 s16, 0x18000
	v_mov_b64_e32 v[16:17], s[10:11]
	v_mad_u64_u32 v[16:17], s[16:17], v14, s16, v[16:17]
	v_lshl_add_u64 v[16:17], v[12:13], 3, v[16:17]
	global_store_dword v[16:17], v68, off
.LBB0_1082:
	s_andn2_saveexec_b64 s[14:15], s[14:15]
	s_cbranch_execz .LBB0_1084
	v_lshlrev_b32_e32 v16, 9, v14
	v_mov_b32_e32 v17, 0
	v_ashrrev_i32_e32 v13, 31, v12
	v_lshl_add_u64 v[16:17], s[8:9], 0, v[16:17]
	v_lshl_add_u64 v[16:17], v[12:13], 3, v[16:17]
	global_store_dword v[16:17], v68, off
.LBB0_1084:
	s_or_b64 exec, exec, s[14:15]
	global_store_dword v[16:17], v15, off offset:4
	global_atomic_add_f32 v18, v15, s[6:7]
.LBB0_1085:
	s_andn2_saveexec_b64 s[12:13], s[12:13]
	v_or_b32_e32 v14, v69, v14
	v_lshl_add_u32 v12, v12, 3, v76
	ds_write_b64 v12, v[14:15]
.LBB0_1087:
	s_or_b64 exec, exec, s[2:3]
	v_or_b32_e32 v12, v8, v9
	v_or3_b32 v12, v12, v11, v10
	v_cmp_ne_u32_e32 vcc, 0, v12
	s_and_saveexec_b64 s[2:3], vcc
	s_cbranch_execz .LBB0_1124
	v_cmp_neq_f32_e32 vcc, 0, v8
	s_and_saveexec_b64 s[12:13], vcc
	s_cbranch_execz .LBB0_1097
	v_mov_b32_e32 v13, 1
	ds_add_rtn_u32 v12, v77, v13
	s_movk_i32 s14, 0x7f
	v_or_b32_e32 v16, 0x2d00, v78
	s_waitcnt lgkmcnt(0)
	v_cmp_lt_i32_e32 vcc, s14, v12
	s_and_saveexec_b64 s[14:15], vcc
	s_xor_b64 s[14:15], exec, s[14:15]
	s_cbranch_execz .LBB0_1095
	v_lshlrev_b32_e32 v17, 2, v16
	global_atomic_add v12, v17, v13, s[4:5] sc0
	v_mov_b32_e32 v13, 0
	s_waitcnt vmcnt(0)
	v_cmp_lt_i32_e32 vcc, 63, v12
	s_and_saveexec_b64 s[16:17], vcc
	s_xor_b64 s[16:17], exec, s[16:17]
	s_cbranch_execz .LBB0_1092
	s_mov_b32 s18, 0x18000
	v_mov_b64_e32 v[14:15], s[10:11]
	v_mad_u64_u32 v[14:15], s[18:19], v16, s18, v[14:15]
	v_lshl_add_u64 v[14:15], v[12:13], 3, v[14:15]
	global_store_dword v[14:15], v68, off
.LBB0_1092:
	s_andn2_saveexec_b64 s[16:17], s[16:17]
	s_cbranch_execz .LBB0_1094
	v_lshlrev_b32_e32 v14, 9, v16
	v_mov_b32_e32 v15, 0
	v_ashrrev_i32_e32 v13, 31, v12
	v_lshl_add_u64 v[14:15], s[8:9], 0, v[14:15]
	v_lshl_add_u64 v[14:15], v[12:13], 3, v[14:15]
	global_store_dword v[14:15], v68, off
.LBB0_1094:
	s_or_b64 exec, exec, s[16:17]
	global_store_dword v[14:15], v8, off offset:4
	global_atomic_add_f32 v17, v8, s[6:7]
.LBB0_1095:
	s_andn2_saveexec_b64 s[14:15], s[14:15]
	v_or_b32_e32 v14, v69, v16
	v_lshl_add_u32 v12, v12, 3, v76
	v_mov_b32_e32 v15, v8
	ds_write_b64 v12, v[14:15]
.LBB0_1097:
	s_or_b64 exec, exec, s[12:13]
	v_cmp_neq_f32_e32 vcc, 0, v9
	s_and_saveexec_b64 s[12:13], vcc
	s_cbranch_execz .LBB0_1106
	v_mov_b32_e32 v13, 1
	ds_add_rtn_u32 v12, v77, v13
	s_movk_i32 s14, 0x7f
	v_or_b32_e32 v8, 0x2d01, v78
	s_waitcnt lgkmcnt(0)
	v_cmp_lt_i32_e32 vcc, s14, v12
	s_and_saveexec_b64 s[14:15], vcc
	s_xor_b64 s[14:15], exec, s[14:15]
	s_cbranch_execz .LBB0_1104
	v_lshlrev_b32_e32 v16, 2, v8
	global_atomic_add v12, v16, v13, s[4:5] sc0
	v_mov_b32_e32 v13, 0
	s_waitcnt vmcnt(0)
	v_cmp_lt_i32_e32 vcc, 63, v12
	s_and_saveexec_b64 s[16:17], vcc
	s_xor_b64 s[16:17], exec, s[16:17]
	s_cbranch_execz .LBB0_1101
	s_mov_b32 s18, 0x18000
	v_mov_b64_e32 v[14:15], s[10:11]
	v_mad_u64_u32 v[14:15], s[18:19], v8, s18, v[14:15]
	v_lshl_add_u64 v[14:15], v[12:13], 3, v[14:15]
	global_store_dword v[14:15], v68, off
.LBB0_1101:
	s_andn2_saveexec_b64 s[16:17], s[16:17]
	s_cbranch_execz .LBB0_1103
	v_lshlrev_b32_e32 v14, 9, v8
	v_mov_b32_e32 v15, 0
	v_ashrrev_i32_e32 v13, 31, v12
	v_lshl_add_u64 v[14:15], s[8:9], 0, v[14:15]
	v_lshl_add_u64 v[14:15], v[12:13], 3, v[14:15]
	global_store_dword v[14:15], v68, off
.LBB0_1103:
	s_or_b64 exec, exec, s[16:17]
	global_store_dword v[14:15], v9, off offset:4
	global_atomic_add_f32 v16, v9, s[6:7]
.LBB0_1104:
	s_andn2_saveexec_b64 s[14:15], s[14:15]
	v_or_b32_e32 v8, v69, v8
	v_lshl_add_u32 v12, v12, 3, v76
	ds_write_b64 v12, v[8:9]
.LBB0_1106:
	s_or_b64 exec, exec, s[12:13]
	v_cmp_neq_f32_e32 vcc, 0, v10
	s_and_saveexec_b64 s[12:13], vcc
	s_cbranch_execz .LBB0_1115
	v_mov_b32_e32 v9, 1
	ds_add_rtn_u32 v8, v77, v9
	s_movk_i32 s14, 0x7f
	v_or_b32_e32 v14, 0x2d02, v78
	s_waitcnt lgkmcnt(0)
	v_cmp_lt_i32_e32 vcc, s14, v8
	s_and_saveexec_b64 s[14:15], vcc
	s_xor_b64 s[14:15], exec, s[14:15]
	s_cbranch_execz .LBB0_1113
	v_lshlrev_b32_e32 v15, 2, v14
	global_atomic_add v8, v15, v9, s[4:5] sc0
	v_mov_b32_e32 v9, 0
	s_waitcnt vmcnt(0)
	v_cmp_lt_i32_e32 vcc, 63, v8
	s_and_saveexec_b64 s[16:17], vcc
	s_xor_b64 s[16:17], exec, s[16:17]
	s_cbranch_execz .LBB0_1110
	s_mov_b32 s18, 0x18000
	v_mov_b64_e32 v[12:13], s[10:11]
	v_mad_u64_u32 v[12:13], s[18:19], v14, s18, v[12:13]
	v_lshl_add_u64 v[12:13], v[8:9], 3, v[12:13]
	global_store_dword v[12:13], v68, off
.LBB0_1110:
	s_andn2_saveexec_b64 s[16:17], s[16:17]
	s_cbranch_execz .LBB0_1112
	v_lshlrev_b32_e32 v12, 9, v14
	v_mov_b32_e32 v13, 0
	v_ashrrev_i32_e32 v9, 31, v8
	v_lshl_add_u64 v[12:13], s[8:9], 0, v[12:13]
	v_lshl_add_u64 v[12:13], v[8:9], 3, v[12:13]
	global_store_dword v[12:13], v68, off
.LBB0_1112:
	s_or_b64 exec, exec, s[16:17]
	global_store_dword v[12:13], v10, off offset:4
	global_atomic_add_f32 v15, v10, s[6:7]
.LBB0_1113:
	s_andn2_saveexec_b64 s[14:15], s[14:15]
	v_or_b32_e32 v12, v69, v14
	v_lshl_add_u32 v8, v8, 3, v76
	v_mov_b32_e32 v13, v10
	ds_write_b64 v8, v[12:13]
.LBB0_1115:
	s_or_b64 exec, exec, s[12:13]
	v_cmp_neq_f32_e32 vcc, 0, v11
	s_and_b64 exec, exec, vcc
	s_cbranch_execz .LBB0_1124
	v_mov_b32_e32 v9, 1
	ds_add_rtn_u32 v8, v77, v9
	s_movk_i32 s12, 0x7f
	v_or_b32_e32 v10, 0x2d03, v78
	s_waitcnt lgkmcnt(0)
	v_cmp_lt_i32_e32 vcc, s12, v8
	s_and_saveexec_b64 s[12:13], vcc
	s_xor_b64 s[12:13], exec, s[12:13]
	s_cbranch_execz .LBB0_1122
	v_lshlrev_b32_e32 v14, 2, v10
	global_atomic_add v8, v14, v9, s[4:5] sc0
	v_mov_b32_e32 v9, 0
	s_waitcnt vmcnt(0)
	v_cmp_lt_i32_e32 vcc, 63, v8
	s_and_saveexec_b64 s[14:15], vcc
	s_xor_b64 s[14:15], exec, s[14:15]
	s_cbranch_execz .LBB0_1119
	s_mov_b32 s16, 0x18000
	v_mov_b64_e32 v[12:13], s[10:11]
	v_mad_u64_u32 v[12:13], s[16:17], v10, s16, v[12:13]
	v_lshl_add_u64 v[12:13], v[8:9], 3, v[12:13]
	global_store_dword v[12:13], v68, off
.LBB0_1119:
	s_andn2_saveexec_b64 s[14:15], s[14:15]
	s_cbranch_execz .LBB0_1121
	v_lshlrev_b32_e32 v12, 9, v10
	v_mov_b32_e32 v13, 0
	v_ashrrev_i32_e32 v9, 31, v8
	v_lshl_add_u64 v[12:13], s[8:9], 0, v[12:13]
	v_lshl_add_u64 v[12:13], v[8:9], 3, v[12:13]
	global_store_dword v[12:13], v68, off
.LBB0_1121:
	s_or_b64 exec, exec, s[14:15]
	global_store_dword v[12:13], v11, off offset:4
	global_atomic_add_f32 v14, v11, s[6:7]
.LBB0_1122:
	s_andn2_saveexec_b64 s[12:13], s[12:13]
	v_or_b32_e32 v10, v69, v10
	v_lshl_add_u32 v8, v8, 3, v76
	ds_write_b64 v8, v[10:11]
.LBB0_1124:
	s_or_b64 exec, exec, s[2:3]
	v_or_b32_e32 v8, v4, v5
	v_or3_b32 v8, v8, v7, v6
	v_cmp_ne_u32_e32 vcc, 0, v8
	s_and_saveexec_b64 s[2:3], vcc
	s_cbranch_execz .LBB0_1161
	v_cmp_neq_f32_e32 vcc, 0, v4
	s_and_saveexec_b64 s[12:13], vcc
	s_cbranch_execz .LBB0_1134
	v_mov_b32_e32 v9, 1
	ds_add_rtn_u32 v8, v77, v9
	s_movk_i32 s14, 0x7f
	v_or_b32_e32 v12, 0x2e00, v78
	s_waitcnt lgkmcnt(0)
	v_cmp_lt_i32_e32 vcc, s14, v8
	s_and_saveexec_b64 s[14:15], vcc
	s_xor_b64 s[14:15], exec, s[14:15]
	s_cbranch_execz .LBB0_1132
	v_lshlrev_b32_e32 v13, 2, v12
	global_atomic_add v8, v13, v9, s[4:5] sc0
	v_mov_b32_e32 v9, 0
	s_waitcnt vmcnt(0)
	v_cmp_lt_i32_e32 vcc, 63, v8
	s_and_saveexec_b64 s[16:17], vcc
	s_xor_b64 s[16:17], exec, s[16:17]
	s_cbranch_execz .LBB0_1129
	s_mov_b32 s18, 0x18000
	v_mov_b64_e32 v[10:11], s[10:11]
	v_mad_u64_u32 v[10:11], s[18:19], v12, s18, v[10:11]
	v_lshl_add_u64 v[10:11], v[8:9], 3, v[10:11]
	global_store_dword v[10:11], v68, off
.LBB0_1129:
	s_andn2_saveexec_b64 s[16:17], s[16:17]
	s_cbranch_execz .LBB0_1131
	v_lshlrev_b32_e32 v10, 9, v12
	v_mov_b32_e32 v11, 0
	v_ashrrev_i32_e32 v9, 31, v8
	v_lshl_add_u64 v[10:11], s[8:9], 0, v[10:11]
	v_lshl_add_u64 v[10:11], v[8:9], 3, v[10:11]
	global_store_dword v[10:11], v68, off
.LBB0_1131:
	s_or_b64 exec, exec, s[16:17]
	global_store_dword v[10:11], v4, off offset:4
	global_atomic_add_f32 v13, v4, s[6:7]
.LBB0_1132:
	s_andn2_saveexec_b64 s[14:15], s[14:15]
	v_or_b32_e32 v10, v69, v12
	v_lshl_add_u32 v8, v8, 3, v76
	v_mov_b32_e32 v11, v4
	ds_write_b64 v8, v[10:11]
.LBB0_1134:
	s_or_b64 exec, exec, s[12:13]
	v_cmp_neq_f32_e32 vcc, 0, v5
	s_and_saveexec_b64 s[12:13], vcc
	s_cbranch_execz .LBB0_1143
	v_mov_b32_e32 v9, 1
	ds_add_rtn_u32 v8, v77, v9
	s_movk_i32 s14, 0x7f
	v_or_b32_e32 v4, 0x2e01, v78
	s_waitcnt lgkmcnt(0)
	v_cmp_lt_i32_e32 vcc, s14, v8
	s_and_saveexec_b64 s[14:15], vcc
	s_xor_b64 s[14:15], exec, s[14:15]
	s_cbranch_execz .LBB0_1141
	v_lshlrev_b32_e32 v12, 2, v4
	global_atomic_add v8, v12, v9, s[4:5] sc0
	v_mov_b32_e32 v9, 0
	s_waitcnt vmcnt(0)
	v_cmp_lt_i32_e32 vcc, 63, v8
	s_and_saveexec_b64 s[16:17], vcc
	s_xor_b64 s[16:17], exec, s[16:17]
	s_cbranch_execz .LBB0_1138
	s_mov_b32 s18, 0x18000
	v_mov_b64_e32 v[10:11], s[10:11]
	v_mad_u64_u32 v[10:11], s[18:19], v4, s18, v[10:11]
	v_lshl_add_u64 v[10:11], v[8:9], 3, v[10:11]
	global_store_dword v[10:11], v68, off
.LBB0_1138:
	s_andn2_saveexec_b64 s[16:17], s[16:17]
	s_cbranch_execz .LBB0_1140
	v_lshlrev_b32_e32 v10, 9, v4
	v_mov_b32_e32 v11, 0
	v_ashrrev_i32_e32 v9, 31, v8
	v_lshl_add_u64 v[10:11], s[8:9], 0, v[10:11]
	v_lshl_add_u64 v[10:11], v[8:9], 3, v[10:11]
	global_store_dword v[10:11], v68, off
.LBB0_1140:
	s_or_b64 exec, exec, s[16:17]
	global_store_dword v[10:11], v5, off offset:4
	global_atomic_add_f32 v12, v5, s[6:7]
.LBB0_1141:
	s_andn2_saveexec_b64 s[14:15], s[14:15]
	v_or_b32_e32 v4, v69, v4
	v_lshl_add_u32 v8, v8, 3, v76
	ds_write_b64 v8, v[4:5]
.LBB0_1143:
	s_or_b64 exec, exec, s[12:13]
	v_cmp_neq_f32_e32 vcc, 0, v6
	s_and_saveexec_b64 s[12:13], vcc
	s_cbranch_execz .LBB0_1152
	v_mov_b32_e32 v5, 1
	ds_add_rtn_u32 v4, v77, v5
	s_movk_i32 s14, 0x7f
	v_or_b32_e32 v10, 0x2e02, v78
	s_waitcnt lgkmcnt(0)
	v_cmp_lt_i32_e32 vcc, s14, v4
	s_and_saveexec_b64 s[14:15], vcc
	s_xor_b64 s[14:15], exec, s[14:15]
	s_cbranch_execz .LBB0_1150
	v_lshlrev_b32_e32 v11, 2, v10
	global_atomic_add v4, v11, v5, s[4:5] sc0
	v_mov_b32_e32 v5, 0
	s_waitcnt vmcnt(0)
	v_cmp_lt_i32_e32 vcc, 63, v4
	s_and_saveexec_b64 s[16:17], vcc
	s_xor_b64 s[16:17], exec, s[16:17]
	s_cbranch_execz .LBB0_1147
	s_mov_b32 s18, 0x18000
	v_mov_b64_e32 v[8:9], s[10:11]
	v_mad_u64_u32 v[8:9], s[18:19], v10, s18, v[8:9]
	v_lshl_add_u64 v[8:9], v[4:5], 3, v[8:9]
	global_store_dword v[8:9], v68, off
.LBB0_1147:
	s_andn2_saveexec_b64 s[16:17], s[16:17]
	s_cbranch_execz .LBB0_1149
	v_lshlrev_b32_e32 v8, 9, v10
	v_mov_b32_e32 v9, 0
	v_ashrrev_i32_e32 v5, 31, v4
	v_lshl_add_u64 v[8:9], s[8:9], 0, v[8:9]
	v_lshl_add_u64 v[8:9], v[4:5], 3, v[8:9]
	global_store_dword v[8:9], v68, off
.LBB0_1149:
	s_or_b64 exec, exec, s[16:17]
	global_store_dword v[8:9], v6, off offset:4
	global_atomic_add_f32 v11, v6, s[6:7]
.LBB0_1150:
	s_andn2_saveexec_b64 s[14:15], s[14:15]
	v_or_b32_e32 v8, v69, v10
	v_lshl_add_u32 v4, v4, 3, v76
	v_mov_b32_e32 v9, v6
	ds_write_b64 v4, v[8:9]
.LBB0_1152:
	s_or_b64 exec, exec, s[12:13]
	v_cmp_neq_f32_e32 vcc, 0, v7
	s_and_b64 exec, exec, vcc
	s_cbranch_execz .LBB0_1161
	v_mov_b32_e32 v5, 1
	ds_add_rtn_u32 v4, v77, v5
	s_movk_i32 s12, 0x7f
	v_or_b32_e32 v6, 0x2e03, v78
	s_waitcnt lgkmcnt(0)
	v_cmp_lt_i32_e32 vcc, s12, v4
	s_and_saveexec_b64 s[12:13], vcc
	s_xor_b64 s[12:13], exec, s[12:13]
	s_cbranch_execz .LBB0_1159
	v_lshlrev_b32_e32 v10, 2, v6
	global_atomic_add v4, v10, v5, s[4:5] sc0
	v_mov_b32_e32 v5, 0
	s_waitcnt vmcnt(0)
	v_cmp_lt_i32_e32 vcc, 63, v4
	s_and_saveexec_b64 s[14:15], vcc
	s_xor_b64 s[14:15], exec, s[14:15]
	s_cbranch_execz .LBB0_1156
	s_mov_b32 s16, 0x18000
	v_mov_b64_e32 v[8:9], s[10:11]
	v_mad_u64_u32 v[8:9], s[16:17], v6, s16, v[8:9]
	v_lshl_add_u64 v[8:9], v[4:5], 3, v[8:9]
	global_store_dword v[8:9], v68, off
.LBB0_1156:
	s_andn2_saveexec_b64 s[14:15], s[14:15]
	s_cbranch_execz .LBB0_1158
	v_lshlrev_b32_e32 v8, 9, v6
	v_mov_b32_e32 v9, 0
	v_ashrrev_i32_e32 v5, 31, v4
	v_lshl_add_u64 v[8:9], s[8:9], 0, v[8:9]
	v_lshl_add_u64 v[8:9], v[4:5], 3, v[8:9]
	global_store_dword v[8:9], v68, off
.LBB0_1158:
	s_or_b64 exec, exec, s[14:15]
	global_store_dword v[8:9], v7, off offset:4
	global_atomic_add_f32 v10, v7, s[6:7]
.LBB0_1159:
	s_andn2_saveexec_b64 s[12:13], s[12:13]
	v_or_b32_e32 v6, v69, v6
	v_lshl_add_u32 v4, v4, 3, v76
	ds_write_b64 v4, v[6:7]
.LBB0_1161:
	s_or_b64 exec, exec, s[2:3]
	v_cmp_ne_u32_e32 vcc, 0, v28
	s_and_b64 exec, exec, vcc
	s_cbranch_execz .LBB0_1198
	v_cmp_neq_f32_e32 vcc, 0, v0
	s_and_saveexec_b64 s[2:3], vcc
	s_cbranch_execz .LBB0_1171
	v_mov_b32_e32 v5, 1
	ds_add_rtn_u32 v4, v77, v5
	s_movk_i32 s12, 0x7f
	v_or_b32_e32 v8, 0x2f00, v78
	s_waitcnt lgkmcnt(0)
	v_cmp_lt_i32_e32 vcc, s12, v4
	s_and_saveexec_b64 s[12:13], vcc
	s_xor_b64 s[12:13], exec, s[12:13]
	s_cbranch_execz .LBB0_1169
	v_lshlrev_b32_e32 v9, 2, v8
	global_atomic_add v4, v9, v5, s[4:5] sc0
	v_mov_b32_e32 v5, 0
	s_waitcnt vmcnt(0)
	v_cmp_lt_i32_e32 vcc, 63, v4
	s_and_saveexec_b64 s[14:15], vcc
	s_xor_b64 s[14:15], exec, s[14:15]
	s_cbranch_execz .LBB0_1166
	s_mov_b32 s16, 0x18000
	v_mov_b64_e32 v[6:7], s[10:11]
	v_mad_u64_u32 v[6:7], s[16:17], v8, s16, v[6:7]
	v_lshl_add_u64 v[6:7], v[4:5], 3, v[6:7]
	global_store_dword v[6:7], v68, off
.LBB0_1166:
	s_andn2_saveexec_b64 s[14:15], s[14:15]
	s_cbranch_execz .LBB0_1168
	v_lshlrev_b32_e32 v6, 9, v8
	v_mov_b32_e32 v7, 0
	v_ashrrev_i32_e32 v5, 31, v4
	v_lshl_add_u64 v[6:7], s[8:9], 0, v[6:7]
	v_lshl_add_u64 v[6:7], v[4:5], 3, v[6:7]
	global_store_dword v[6:7], v68, off
.LBB0_1168:
	s_or_b64 exec, exec, s[14:15]
	global_store_dword v[6:7], v0, off offset:4
	global_atomic_add_f32 v9, v0, s[6:7]
.LBB0_1169:
	s_andn2_saveexec_b64 s[12:13], s[12:13]
	v_or_b32_e32 v6, v69, v8
	v_lshl_add_u32 v4, v4, 3, v76
	v_mov_b32_e32 v7, v0
	ds_write_b64 v4, v[6:7]
.LBB0_1171:
	s_or_b64 exec, exec, s[2:3]
	v_cmp_neq_f32_e32 vcc, 0, v1
	s_and_saveexec_b64 s[2:3], vcc
	s_cbranch_execz .LBB0_1180
	v_mov_b32_e32 v5, 1
	ds_add_rtn_u32 v4, v77, v5
	s_movk_i32 s12, 0x7f
	v_or_b32_e32 v0, 0x2f01, v78
	s_waitcnt lgkmcnt(0)
	v_cmp_lt_i32_e32 vcc, s12, v4
	s_and_saveexec_b64 s[12:13], vcc
	s_xor_b64 s[12:13], exec, s[12:13]
	s_cbranch_execz .LBB0_1178
	v_lshlrev_b32_e32 v8, 2, v0
	global_atomic_add v4, v8, v5, s[4:5] sc0
	v_mov_b32_e32 v5, 0
	s_waitcnt vmcnt(0)
	v_cmp_lt_i32_e32 vcc, 63, v4
	s_and_saveexec_b64 s[14:15], vcc
	s_xor_b64 s[14:15], exec, s[14:15]
	s_cbranch_execz .LBB0_1175
	s_mov_b32 s16, 0x18000
	v_mov_b64_e32 v[6:7], s[10:11]
	v_mad_u64_u32 v[6:7], s[16:17], v0, s16, v[6:7]
	v_lshl_add_u64 v[6:7], v[4:5], 3, v[6:7]
	global_store_dword v[6:7], v68, off
.LBB0_1175:
	s_andn2_saveexec_b64 s[14:15], s[14:15]
	s_cbranch_execz .LBB0_1177
	v_lshlrev_b32_e32 v6, 9, v0
	v_mov_b32_e32 v7, 0
	v_ashrrev_i32_e32 v5, 31, v4
	v_lshl_add_u64 v[6:7], s[8:9], 0, v[6:7]
	v_lshl_add_u64 v[6:7], v[4:5], 3, v[6:7]
	global_store_dword v[6:7], v68, off
.LBB0_1177:
	s_or_b64 exec, exec, s[14:15]
	global_store_dword v[6:7], v1, off offset:4
	global_atomic_add_f32 v8, v1, s[6:7]
.LBB0_1178:
	s_andn2_saveexec_b64 s[12:13], s[12:13]
	v_or_b32_e32 v0, v69, v0
	v_lshl_add_u32 v4, v4, 3, v76
	ds_write_b64 v4, v[0:1]
.LBB0_1180:
	s_or_b64 exec, exec, s[2:3]
	v_cmp_neq_f32_e32 vcc, 0, v2
	s_and_saveexec_b64 s[2:3], vcc
	s_cbranch_execz .LBB0_1189
	v_mov_b32_e32 v1, 1
	ds_add_rtn_u32 v0, v77, v1
	s_movk_i32 s12, 0x7f
	v_or_b32_e32 v6, 0x2f02, v78
	s_waitcnt lgkmcnt(0)
	v_cmp_lt_i32_e32 vcc, s12, v0
	s_and_saveexec_b64 s[12:13], vcc
	s_xor_b64 s[12:13], exec, s[12:13]
	s_cbranch_execz .LBB0_1187
	v_lshlrev_b32_e32 v7, 2, v6
	global_atomic_add v0, v7, v1, s[4:5] sc0
	v_mov_b32_e32 v1, 0
	s_waitcnt vmcnt(0)
	v_cmp_lt_i32_e32 vcc, 63, v0
	s_and_saveexec_b64 s[14:15], vcc
	s_xor_b64 s[14:15], exec, s[14:15]
	s_cbranch_execz .LBB0_1184
	s_mov_b32 s16, 0x18000
	v_mov_b64_e32 v[4:5], s[10:11]
	v_mad_u64_u32 v[4:5], s[16:17], v6, s16, v[4:5]
	v_lshl_add_u64 v[4:5], v[0:1], 3, v[4:5]
	global_store_dword v[4:5], v68, off
.LBB0_1184:
	s_andn2_saveexec_b64 s[14:15], s[14:15]
	s_cbranch_execz .LBB0_1186
	v_lshlrev_b32_e32 v4, 9, v6
	v_mov_b32_e32 v5, 0
	v_ashrrev_i32_e32 v1, 31, v0
	v_lshl_add_u64 v[4:5], s[8:9], 0, v[4:5]
	v_lshl_add_u64 v[4:5], v[0:1], 3, v[4:5]
	global_store_dword v[4:5], v68, off
.LBB0_1186:
	s_or_b64 exec, exec, s[14:15]
	global_store_dword v[4:5], v2, off offset:4
	global_atomic_add_f32 v7, v2, s[6:7]
.LBB0_1187:
	s_andn2_saveexec_b64 s[12:13], s[12:13]
	v_or_b32_e32 v4, v69, v6
	v_lshl_add_u32 v0, v0, 3, v76
	v_mov_b32_e32 v5, v2
	ds_write_b64 v0, v[4:5]
.LBB0_1189:
	s_or_b64 exec, exec, s[2:3]
	v_cmp_neq_f32_e32 vcc, 0, v3
	s_and_b64 exec, exec, vcc
	s_cbranch_execz .LBB0_1198
	v_mov_b32_e32 v1, 1
	ds_add_rtn_u32 v0, v77, v1
	s_movk_i32 s2, 0x7f
	v_or_b32_e32 v2, 0x2f03, v78
	s_waitcnt lgkmcnt(0)
	v_cmp_lt_i32_e32 vcc, s2, v0
	s_and_saveexec_b64 s[2:3], vcc
	s_xor_b64 s[2:3], exec, s[2:3]
	s_cbranch_execz .LBB0_1196
	v_lshlrev_b32_e32 v6, 2, v2
	global_atomic_add v0, v6, v1, s[4:5] sc0
	v_mov_b32_e32 v1, 0
	s_waitcnt vmcnt(0)
	v_cmp_lt_i32_e32 vcc, 63, v0
	s_and_saveexec_b64 s[12:13], vcc
	s_xor_b64 s[12:13], exec, s[12:13]
	s_cbranch_execz .LBB0_1193
	s_mov_b32 s14, 0x18000
	v_mov_b64_e32 v[4:5], s[10:11]
	v_mad_u64_u32 v[4:5], s[14:15], v2, s14, v[4:5]
	v_lshl_add_u64 v[4:5], v[0:1], 3, v[4:5]
	global_store_dword v[4:5], v68, off
.LBB0_1193:
	s_andn2_saveexec_b64 s[12:13], s[12:13]
	s_cbranch_execz .LBB0_1195
	v_lshlrev_b32_e32 v4, 9, v2
	v_mov_b32_e32 v5, 0
	v_ashrrev_i32_e32 v1, 31, v0
	v_lshl_add_u64 v[4:5], s[8:9], 0, v[4:5]
	v_lshl_add_u64 v[4:5], v[0:1], 3, v[4:5]
	global_store_dword v[4:5], v68, off
.LBB0_1195:
	s_or_b64 exec, exec, s[12:13]
	global_store_dword v[4:5], v3, off offset:4
	global_atomic_add_f32 v6, v3, s[6:7]
.LBB0_1196:
	s_andn2_saveexec_b64 s[2:3], s[2:3]
	v_or_b32_e32 v2, v69, v2
	v_lshl_add_u32 v0, v0, 3, v76
	ds_write_b64 v0, v[2:3]
.LBB0_1198:
	s_or_b64 exec, exec, s[0:1]
	s_waitcnt lgkmcnt(0)
	ds_read_b32 v1, v77
	v_mov_b32_e32 v5, 0
	v_mov_b32_e32 v0, 0
	v_lshl_add_u32 v2, v80, 3, v76
	v_mov_b32_e32 v4, 0
	s_waitcnt lgkmcnt(0)
	v_cmp_gt_i32_e64 s[0:1], v1, v80
	s_and_saveexec_b64 s[2:3], s[0:1]
	ds_read_b64 v[4:5], v2
	s_or_b64 exec, exec, s[2:3]
	v_min_i32_e32 v1, 0x80, v1
	v_or_b32_e32 v3, 64, v80
	v_cmp_lt_i32_e32 vcc, v3, v1
	v_mov_b32_e32 v1, 0
	s_and_saveexec_b64 s[2:3], vcc
	ds_read_b64 v[0:1], v2 offset:512
	s_or_b64 exec, exec, s[2:3]
	s_waitcnt lgkmcnt(0)
	v_and_b32_e32 v12, 0x3fff, v4
	v_mov_b32_e32 v2, 0
	v_lshlrev_b32_e32 v3, 2, v12
	v_mov_b32_e32 v6, 0
	s_and_saveexec_b64 s[2:3], s[0:1]
	s_cbranch_execz .LBB0_1204
	v_mov_b32_e32 v6, 1
	global_atomic_add v6, v3, v6, s[4:5] sc0
.LBB0_1204:
	s_or_b64 exec, exec, s[2:3]
	v_and_b32_e32 v11, 0x3fff, v0
	v_lshlrev_b32_e32 v10, 2, v11
	s_and_saveexec_b64 s[2:3], vcc
	s_cbranch_execnz .LBB0_1208
	s_or_b64 exec, exec, s[2:3]
	s_and_saveexec_b64 s[2:3], s[0:1]
	s_cbranch_execnz .LBB0_1209
.LBB0_1206:
	s_or_b64 exec, exec, s[2:3]
	s_and_saveexec_b64 s[0:1], vcc
	s_cbranch_execnz .LBB0_1214

.LBB0_1208:
	v_mov_b32_e32 v2, 1
	global_atomic_add v2, v10, v2, s[4:5] sc0
	s_or_b64 exec, exec, s[2:3]
	s_and_saveexec_b64 s[2:3], s[0:1]
	s_cbranch_execz .LBB0_1206
.LBB0_1209:
	v_lshrrev_b32_e32 v4, 14, v4
	s_waitcnt vmcnt(0)
	v_cmp_lt_i32_e64 s[0:1], 63, v6
	s_and_saveexec_b64 s[4:5], s[0:1]
	s_xor_b64 s[0:1], exec, s[4:5]
	s_cbranch_execz .LBB0_1211
	s_movk_i32 s4, 0x3000
	v_mad_u32_u24 v6, v12, s4, v6
	v_mov_b32_e32 v7, 0
	v_lshl_add_u64 v[8:9], v[6:7], 3, s[10:11]
	global_store_dword v[8:9], v4, off
.LBB0_1211:
	s_andn2_saveexec_b64 s[0:1], s[0:1]
	s_cbranch_execz .LBB0_1213
	v_lshlrev_b32_e32 v8, 9, v12
	v_mov_b32_e32 v9, 0
	v_ashrrev_i32_e32 v7, 31, v6
	v_lshl_add_u64 v[8:9], s[8:9], 0, v[8:9]
	v_lshl_add_u64 v[8:9], v[6:7], 3, v[8:9]
	global_store_dword v[8:9], v4, off
.LBB0_1213:
	s_or_b64 exec, exec, s[0:1]
	global_store_dword v[8:9], v5, off offset:4
	global_atomic_add_f32 v3, v5, s[6:7]
	s_or_b64 exec, exec, s[2:3]
	s_and_saveexec_b64 s[0:1], vcc
	s_cbranch_execz .LBB0_1207
.LBB0_1214:
	v_lshrrev_b32_e32 v0, 14, v0
	s_waitcnt vmcnt(0)
	v_cmp_lt_i32_e32 vcc, 63, v2
	s_and_saveexec_b64 s[0:1], vcc
	s_xor_b64 s[0:1], exec, s[0:1]
	s_cbranch_execz .LBB0_1216
	s_movk_i32 s2, 0x3000
	v_mad_u32_u24 v2, v11, s2, v2
	v_mov_b32_e32 v3, 0
	v_lshl_add_u64 v[4:5], v[2:3], 3, s[10:11]
	global_store_dword v[4:5], v0, off
.LBB0_1216:
	s_andn2_saveexec_b64 s[0:1], s[0:1]
	s_cbranch_execz .LBB0_1218
	v_lshlrev_b32_e32 v4, 9, v11
	v_mov_b32_e32 v5, 0
	v_ashrrev_i32_e32 v3, 31, v2
	v_lshl_add_u64 v[4:5], s[8:9], 0, v[4:5]
	v_lshl_add_u64 v[4:5], v[2:3], 3, v[4:5]
	global_store_dword v[4:5], v0, off
.LBB0_1218:
	s_or_b64 exec, exec, s[0:1]
	global_store_dword v[4:5], v1, off offset:4
	global_atomic_add_f32 v10, v1, s[6:7]
	s_endpgm

	.amdhsa_kernel _Z9k1_kernelPKfS0_S0_PDF16_PiPfP15HIP_vector_typeIiLj2EES6_
		.amdhsa_group_segment_fixed_size 37392
		.amdhsa_private_segment_fixed_size 0
		.amdhsa_kernarg_size 64
		.amdhsa_user_sgpr_count 2
		.amdhsa_user_sgpr_dispatch_ptr 0
		.amdhsa_user_sgpr_queue_ptr 0
		.amdhsa_user_sgpr_kernarg_segment_ptr 1
		.amdhsa_user_sgpr_dispatch_id 0
		.amdhsa_user_sgpr_kernarg_preload_length 0
		.amdhsa_user_sgpr_kernarg_preload_offset 0
		.amdhsa_user_sgpr_private_segment_size 0
		.amdhsa_uses_dynamic_stack 0
		.amdhsa_enable_private_segment 0
		.amdhsa_system_sgpr_workgroup_id_x 1
		.amdhsa_system_sgpr_workgroup_id_y 0
		.amdhsa_system_sgpr_workgroup_id_z 0
		.amdhsa_system_sgpr_workgroup_info 0
		.amdhsa_system_vgpr_workitem_id 0
		.amdhsa_next_free_vgpr 120
		.amdhsa_next_free_sgpr 96
		.amdhsa_accum_offset 120
		.amdhsa_reserve_vcc 1
		.amdhsa_float_round_mode_32 0
		.amdhsa_float_round_mode_16_64 0
		.amdhsa_float_denorm_mode_32 3
		.amdhsa_float_denorm_mode_16_64 3
		.amdhsa_dx10_clamp 1
		.amdhsa_ieee_mode 1
		.amdhsa_fp16_overflow 0
		.amdhsa_tg_split 0
		.amdhsa_exception_fp_ieee_invalid_op 0
		.amdhsa_exception_fp_denorm_src 0
		.amdhsa_exception_fp_ieee_div_zero 0
		.amdhsa_exception_fp_ieee_overflow 0
		.amdhsa_exception_fp_ieee_underflow 0
		.amdhsa_exception_fp_ieee_inexact 0
		.amdhsa_exception_int_div_zero 0
	.end_amdhsa_kernel

.Lfunc_end0:
	.size	_Z9k1_kernelPKfS0_S0_PDF16_PiPfP15HIP_vector_typeIiLj2EES6_, .Lfunc_end0-_Z9k1_kernelPKfS0_S0_PDF16_PiPfP15HIP_vector_typeIiLj2EES6_
	.set _Z9k1_kernelPKfS0_S0_PDF16_PiPfP15HIP_vector_typeIiLj2EES6_.num_vgpr, 120
	.set _Z9k1_kernelPKfS0_S0_PDF16_PiPfP15HIP_vector_typeIiLj2EES6_.num_agpr, 0
	.set _Z9k1_kernelPKfS0_S0_PDF16_PiPfP15HIP_vector_typeIiLj2EES6_.numbered_sgpr, 26
	.set _Z9k1_kernelPKfS0_S0_PDF16_PiPfP15HIP_vector_typeIiLj2EES6_.num_named_barrier, 0
	.set _Z9k1_kernelPKfS0_S0_PDF16_PiPfP15HIP_vector_typeIiLj2EES6_.private_seg_size, 0
	.set _Z9k1_kernelPKfS0_S0_PDF16_PiPfP15HIP_vector_typeIiLj2EES6_.uses_vcc, 1
	.set _Z9k1_kernelPKfS0_S0_PDF16_PiPfP15HIP_vector_typeIiLj2EES6_.uses_flat_scratch, 0
	.set _Z9k1_kernelPKfS0_S0_PDF16_PiPfP15HIP_vector_typeIiLj2EES6_.has_dyn_sized_stack, 0
	.set _Z9k1_kernelPKfS0_S0_PDF16_PiPfP15HIP_vector_typeIiLj2EES6_.has_recursion, 0
	.set _Z9k1_kernelPKfS0_S0_PDF16_PiPfP15HIP_vector_typeIiLj2EES6_.has_indirect_call, 0

_Z10agg_kernelILi128ELb1EEvPKiPKfP15HIP_vector_typeIiLj2EES6_PKDF16_S3_PDF16_Pf:
	s_load_dwordx4 s[4:7], s[0:1], 0x0
	s_load_dwordx2 s[8:9], s[0:1], 0x10
	s_load_dwordx4 s[12:15], s[0:1], 0x20
	s_load_dwordx4 s[16:19], s[0:1], 0x30
	v_readfirstlane_b32 s3, v0
	v_and_b32_e32 v1, 63, v0
	v_and_b32_e32 v2, 15, v0
	v_bfe_u32 v9, v0, 4, 1
	v_lshrrev_b32_e32 v1, 5, v1
	s_lshr_b32 s3, s3, 6
	s_lshl_b32 s24, s2, 4
	s_lshl_b32 s25, s3, 1
	s_add_u32 s24, s24, s25
	v_add_u32_e32 v1, s24, v1
	v_lshlrev_b32_e32 v8, 2, v1
	v_lshlrev_b32_e32 v2, 4, v2
	v_lshl_add_u32 v6, v1, 6, v9
	v_lshlrev_b32_e32 v6, 3, v6
	v_lshl_add_u32 v10, v1, 8, v2
	s_mov_b32 s33, 0x800000
	s_mov_b32 s34, 0xc0000
	s_mov_b32 s20, 0
	v_mov_b32_e32 v72, 0
	v_mov_b32_e32 v73, 0
	v_mov_b32_e32 v74, 0
	v_mov_b32_e32 v75, 0
	v_mov_b32_e32 v76, 0
	v_mov_b32_e32 v77, 0
	v_mov_b32_e32 v78, 0
	v_mov_b32_e32 v79, 0
	s_waitcnt lgkmcnt(0)
	global_load_dword v7, v8, s[4:5]
	global_load_dword v5, v8, s[6:7]
	global_load_dwordx2 v[16:17], v6, s[8:9] offset:0
	global_load_dwordx2 v[18:19], v6, s[8:9] offset:16
	global_load_dwordx2 v[20:21], v6, s[8:9] offset:32
	global_load_dwordx2 v[22:23], v6, s[8:9] offset:48
	global_load_dwordx2 v[24:25], v6, s[8:9] offset:64
	global_load_dwordx2 v[26:27], v6, s[8:9] offset:80
	global_load_dwordx2 v[28:29], v6, s[8:9] offset:96
	global_load_dwordx2 v[30:31], v6, s[8:9] offset:112
	global_load_dwordx4 v[12:15], v10, s[12:13]
	s_waitcnt vmcnt(9)
	v_sub_u32_e32 v3, v7, v9
	v_cmp_eq_u32_e32 vcc, 0, v2
	s_nop 1
	v_cndmask_b32_e32 v4, 0, v7, vcc
	v_sub_u32_e32 v4, v4, v9
.Lagg_loop:
	s_waitcnt vmcnt(0)
	s_add_u32 s21, s20, 0
	v_cmp_lt_i32_e64 s[40:41], s21, v3
	s_add_u32 s21, s20, 2
	v_cmp_lt_i32_e64 s[42:43], s21, v3
	s_add_u32 s21, s20, 4
	v_cmp_lt_i32_e64 s[44:45], s21, v3
	s_add_u32 s21, s20, 6
	v_cmp_lt_i32_e64 s[46:47], s21, v3
	s_add_u32 s21, s20, 8
	v_cmp_lt_i32_e64 s[48:49], s21, v3
	s_add_u32 s21, s20, 10
	v_cmp_lt_i32_e64 s[50:51], s21, v3
	s_add_u32 s21, s20, 12
	v_cmp_lt_i32_e64 s[52:53], s21, v3
	s_add_u32 s21, s20, 14
	v_cmp_lt_i32_e64 s[54:55], s21, v3
	v_cndmask_b32_e64 v16, v1, v16, s[40:41]
	v_cndmask_b32_e64 v17, 0, v17, s[40:41]
	v_lshlrev_b32_e32 v32, 2, v16
	v_lshl_add_u32 v16, v16, 8, v2
	global_load_dword v32, v32, s[6:7]
	global_load_dwordx4 v[40:43], v16, s[12:13]
	v_cndmask_b32_e64 v18, v1, v18, s[42:43]
	v_cndmask_b32_e64 v19, 0, v19, s[42:43]
	v_lshlrev_b32_e32 v33, 2, v18
	v_lshl_add_u32 v18, v18, 8, v2
	global_load_dword v33, v33, s[6:7]
	global_load_dwordx4 v[44:47], v18, s[12:13]
	v_cndmask_b32_e64 v20, v1, v20, s[44:45]
	v_cndmask_b32_e64 v21, 0, v21, s[44:45]
	v_lshlrev_b32_e32 v34, 2, v20
	v_lshl_add_u32 v20, v20, 8, v2
	global_load_dword v34, v34, s[6:7]
	global_load_dwordx4 v[48:51], v20, s[12:13]
	v_cndmask_b32_e64 v22, v1, v22, s[46:47]
	v_cndmask_b32_e64 v23, 0, v23, s[46:47]
	v_lshlrev_b32_e32 v35, 2, v22
	v_lshl_add_u32 v22, v22, 8, v2
	global_load_dword v35, v35, s[6:7]
	global_load_dwordx4 v[52:55], v22, s[12:13]
	v_cndmask_b32_e64 v24, v1, v24, s[48:49]
	v_cndmask_b32_e64 v25, 0, v25, s[48:49]
	v_lshlrev_b32_e32 v36, 2, v24
	v_lshl_add_u32 v24, v24, 8, v2
	global_load_dword v36, v36, s[6:7]
	global_load_dwordx4 v[56:59], v24, s[12:13]
	v_cndmask_b32_e64 v26, v1, v26, s[50:51]
	v_cndmask_b32_e64 v27, 0, v27, s[50:51]
	v_lshlrev_b32_e32 v37, 2, v26
	v_lshl_add_u32 v26, v26, 8, v2
	global_load_dword v37, v37, s[6:7]
	global_load_dwordx4 v[60:63], v26, s[12:13]
	v_cndmask_b32_e64 v28, v1, v28, s[52:53]
	v_cndmask_b32_e64 v29, 0, v29, s[52:53]
	v_lshlrev_b32_e32 v38, 2, v28
	v_lshl_add_u32 v28, v28, 8, v2
	global_load_dword v38, v38, s[6:7]
	global_load_dwordx4 v[64:67], v28, s[12:13]
	v_cndmask_b32_e64 v30, v1, v30, s[54:55]
	v_cndmask_b32_e64 v31, 0, v31, s[54:55]
	v_lshlrev_b32_e32 v39, 2, v30
	v_lshl_add_u32 v30, v30, 8, v2
	global_load_dword v39, v39, s[6:7]
	global_load_dwordx4 v[68:71], v30, s[12:13]
	s_waitcnt vmcnt(15)
	v_add_f32_e32 v8, 1.0, v32
	v_mul_f32_e32 v10, 0x4b800000, v8
	v_cmp_gt_f32_e32 vcc, s33, v8
	s_nop 1
	v_cndmask_b32_e32 v10, v8, v10, vcc
	v_rsq_f32_e32 v9, v10
	s_nop 0
	v_mul_f32_e32 v10, 0x45800000, v9
	v_cndmask_b32_e32 v9, v9, v10, vcc
	v_cmp_lt_f32_e32 vcc, 0, v8
	s_nop 1
	v_cndmask_b32_e32 v9, 0, v9, vcc
	v_mul_f32_e32 v32, v17, v9
	s_waitcnt vmcnt(13)
	v_add_f32_e32 v8, 1.0, v33
	v_mul_f32_e32 v10, 0x4b800000, v8
	v_cmp_gt_f32_e32 vcc, s33, v8
	s_nop 1
	v_cndmask_b32_e32 v10, v8, v10, vcc
	v_rsq_f32_e32 v9, v10
	s_nop 0
	v_mul_f32_e32 v10, 0x45800000, v9
	v_cndmask_b32_e32 v9, v9, v10, vcc
	v_cmp_lt_f32_e32 vcc, 0, v8
	s_nop 1
	v_cndmask_b32_e32 v9, 0, v9, vcc
	v_mul_f32_e32 v33, v19, v9
	s_waitcnt vmcnt(11)
	v_add_f32_e32 v8, 1.0, v34
	v_mul_f32_e32 v10, 0x4b800000, v8
	v_cmp_gt_f32_e32 vcc, s33, v8
	s_nop 1
	v_cndmask_b32_e32 v10, v8, v10, vcc
	v_rsq_f32_e32 v9, v10
	s_nop 0
	v_mul_f32_e32 v10, 0x45800000, v9
	v_cndmask_b32_e32 v9, v9, v10, vcc
	v_cmp_lt_f32_e32 vcc, 0, v8
	s_nop 1
	v_cndmask_b32_e32 v9, 0, v9, vcc
	v_mul_f32_e32 v34, v21, v9
	s_waitcnt vmcnt(9)
	v_add_f32_e32 v8, 1.0, v35
	v_mul_f32_e32 v10, 0x4b800000, v8
	v_cmp_gt_f32_e32 vcc, s33, v8
	s_nop 1
	v_cndmask_b32_e32 v10, v8, v10, vcc
	v_rsq_f32_e32 v9, v10
	s_nop 0
	v_mul_f32_e32 v10, 0x45800000, v9
	v_cndmask_b32_e32 v9, v9, v10, vcc
	v_cmp_lt_f32_e32 vcc, 0, v8
	s_nop 1
	v_cndmask_b32_e32 v9, 0, v9, vcc
	v_mul_f32_e32 v35, v23, v9
	s_waitcnt vmcnt(7)
	v_add_f32_e32 v8, 1.0, v36
	v_mul_f32_e32 v10, 0x4b800000, v8
	v_cmp_gt_f32_e32 vcc, s33, v8
	s_nop 1
	v_cndmask_b32_e32 v10, v8, v10, vcc
	v_rsq_f32_e32 v9, v10
	s_nop 0
	v_mul_f32_e32 v10, 0x45800000, v9
	v_cndmask_b32_e32 v9, v9, v10, vcc
	v_cmp_lt_f32_e32 vcc, 0, v8
	s_nop 1
	v_cndmask_b32_e32 v9, 0, v9, vcc
	v_mul_f32_e32 v36, v25, v9
	s_waitcnt vmcnt(5)
	v_add_f32_e32 v8, 1.0, v37
	v_mul_f32_e32 v10, 0x4b800000, v8
	v_cmp_gt_f32_e32 vcc, s33, v8
	s_nop 1
	v_cndmask_b32_e32 v10, v8, v10, vcc
	v_rsq_f32_e32 v9, v10
	s_nop 0
	v_mul_f32_e32 v10, 0x45800000, v9
	v_cndmask_b32_e32 v9, v9, v10, vcc
	v_cmp_lt_f32_e32 vcc, 0, v8
	s_nop 1
	v_cndmask_b32_e32 v9, 0, v9, vcc
	v_mul_f32_e32 v37, v27, v9
	s_waitcnt vmcnt(3)
	v_add_f32_e32 v8, 1.0, v38
	v_mul_f32_e32 v10, 0x4b800000, v8
	v_cmp_gt_f32_e32 vcc, s33, v8
	s_nop 1
	v_cndmask_b32_e32 v10, v8, v10, vcc
	v_rsq_f32_e32 v9, v10
	s_nop 0
	v_mul_f32_e32 v10, 0x45800000, v9
	v_cndmask_b32_e32 v9, v9, v10, vcc
	v_cmp_lt_f32_e32 vcc, 0, v8
	s_nop 1
	v_cndmask_b32_e32 v9, 0, v9, vcc
	v_mul_f32_e32 v38, v29, v9
	s_waitcnt vmcnt(1)
	v_add_f32_e32 v8, 1.0, v39
	v_mul_f32_e32 v10, 0x4b800000, v8
	v_cmp_gt_f32_e32 vcc, s33, v8
	s_nop 1
	v_cndmask_b32_e32 v10, v8, v10, vcc
	v_rsq_f32_e32 v9, v10
	s_nop 0
	v_mul_f32_e32 v10, 0x45800000, v9
	v_cndmask_b32_e32 v9, v9, v10, vcc
	v_cmp_lt_f32_e32 vcc, 0, v8
	s_nop 1
	v_cndmask_b32_e32 v9, 0, v9, vcc
	v_mul_f32_e32 v39, v31, v9
	s_add_u32 s21, s20, 0
	v_cmp_lt_i32_e32 vcc, s21, v4
	s_and_saveexec_b64 s[22:23], vcc
	global_store_dword v6, v32, s[8:9] offset:4
	s_mov_b64 exec, s[22:23]
	s_add_u32 s21, s20, 2
	v_cmp_lt_i32_e32 vcc, s21, v4
	s_and_saveexec_b64 s[22:23], vcc
	global_store_dword v6, v33, s[8:9] offset:20
	s_mov_b64 exec, s[22:23]
	s_add_u32 s21, s20, 4
	v_cmp_lt_i32_e32 vcc, s21, v4
	s_and_saveexec_b64 s[22:23], vcc
	global_store_dword v6, v34, s[8:9] offset:36
	s_mov_b64 exec, s[22:23]
	s_add_u32 s21, s20, 6
	v_cmp_lt_i32_e32 vcc, s21, v4
	s_and_saveexec_b64 s[22:23], vcc
	global_store_dword v6, v35, s[8:9] offset:52
	s_mov_b64 exec, s[22:23]
	s_add_u32 s21, s20, 8
	v_cmp_lt_i32_e32 vcc, s21, v4
	s_and_saveexec_b64 s[22:23], vcc
	global_store_dword v6, v36, s[8:9] offset:68
	s_mov_b64 exec, s[22:23]
	s_add_u32 s21, s20, 10
	v_cmp_lt_i32_e32 vcc, s21, v4
	s_and_saveexec_b64 s[22:23], vcc
	global_store_dword v6, v37, s[8:9] offset:84
	s_mov_b64 exec, s[22:23]
	s_add_u32 s21, s20, 12
	v_cmp_lt_i32_e32 vcc, s21, v4
	s_and_saveexec_b64 s[22:23], vcc
	global_store_dword v6, v38, s[8:9] offset:100
	s_mov_b64 exec, s[22:23]
	s_add_u32 s21, s20, 14
	v_cmp_lt_i32_e32 vcc, s21, v4
	s_and_saveexec_b64 s[22:23], vcc
	global_store_dword v6, v39, s[8:9] offset:116
	s_mov_b64 exec, s[22:23]
	s_waitcnt vmcnt(8)
	s_add_u32 s20, s20, 16
	v_add_u32_e32 v6, 0x80, v6
	v_cmp_lt_u32_e32 vcc, s20, v7
	s_cbranch_vccz .Lagg_lastc
	s_cmp_ge_u32 s20, 64
	s_cbranch_scc1 .Lagg_c_noload
	global_load_dwordx2 v[16:17], v6, s[8:9] offset:0
	global_load_dwordx2 v[18:19], v6, s[8:9] offset:16
	global_load_dwordx2 v[20:21], v6, s[8:9] offset:32
	global_load_dwordx2 v[22:23], v6, s[8:9] offset:48
	global_load_dwordx2 v[24:25], v6, s[8:9] offset:64
	global_load_dwordx2 v[26:27], v6, s[8:9] offset:80
	global_load_dwordx2 v[28:29], v6, s[8:9] offset:96
	global_load_dwordx2 v[30:31], v6, s[8:9] offset:112
.Lagg_c_noload:
	v_cvt_f32_f16_sdwa v9, v40 dst_sel:DWORD dst_unused:UNUSED_PAD src0_sel:WORD_1
	v_cvt_f32_f16_e32 v8, v40
	v_fmac_f32_e32 v72, v32, v8
	v_fmac_f32_e32 v73, v32, v9
	v_cvt_f32_f16_sdwa v9, v41 dst_sel:DWORD dst_unused:UNUSED_PAD src0_sel:WORD_1
	v_cvt_f32_f16_e32 v8, v41
	v_fmac_f32_e32 v74, v32, v8
	v_fmac_f32_e32 v75, v32, v9
	v_cvt_f32_f16_sdwa v9, v42 dst_sel:DWORD dst_unused:UNUSED_PAD src0_sel:WORD_1
	v_cvt_f32_f16_e32 v8, v42
	v_fmac_f32_e32 v76, v32, v8
	v_fmac_f32_e32 v77, v32, v9
	v_cvt_f32_f16_sdwa v9, v43 dst_sel:DWORD dst_unused:UNUSED_PAD src0_sel:WORD_1
	v_cvt_f32_f16_e32 v8, v43
	v_fmac_f32_e32 v78, v32, v8
	v_fmac_f32_e32 v79, v32, v9
	v_cvt_f32_f16_sdwa v9, v44 dst_sel:DWORD dst_unused:UNUSED_PAD src0_sel:WORD_1
	v_cvt_f32_f16_e32 v8, v44
	v_fmac_f32_e32 v72, v33, v8
	v_fmac_f32_e32 v73, v33, v9
	v_cvt_f32_f16_sdwa v9, v45 dst_sel:DWORD dst_unused:UNUSED_PAD src0_sel:WORD_1
	v_cvt_f32_f16_e32 v8, v45
	v_fmac_f32_e32 v74, v33, v8
	v_fmac_f32_e32 v75, v33, v9
	v_cvt_f32_f16_sdwa v9, v46 dst_sel:DWORD dst_unused:UNUSED_PAD src0_sel:WORD_1
	v_cvt_f32_f16_e32 v8, v46
	v_fmac_f32_e32 v76, v33, v8
	v_fmac_f32_e32 v77, v33, v9
	v_cvt_f32_f16_sdwa v9, v47 dst_sel:DWORD dst_unused:UNUSED_PAD src0_sel:WORD_1
	v_cvt_f32_f16_e32 v8, v47
	v_fmac_f32_e32 v78, v33, v8
	v_fmac_f32_e32 v79, v33, v9
	v_cvt_f32_f16_sdwa v9, v48 dst_sel:DWORD dst_unused:UNUSED_PAD src0_sel:WORD_1
	v_cvt_f32_f16_e32 v8, v48
	v_fmac_f32_e32 v72, v34, v8
	v_fmac_f32_e32 v73, v34, v9
	v_cvt_f32_f16_sdwa v9, v49 dst_sel:DWORD dst_unused:UNUSED_PAD src0_sel:WORD_1
	v_cvt_f32_f16_e32 v8, v49
	v_fmac_f32_e32 v74, v34, v8
	v_fmac_f32_e32 v75, v34, v9
	v_cvt_f32_f16_sdwa v9, v50 dst_sel:DWORD dst_unused:UNUSED_PAD src0_sel:WORD_1
	v_cvt_f32_f16_e32 v8, v50
	v_fmac_f32_e32 v76, v34, v8
	v_fmac_f32_e32 v77, v34, v9
	v_cvt_f32_f16_sdwa v9, v51 dst_sel:DWORD dst_unused:UNUSED_PAD src0_sel:WORD_1
	v_cvt_f32_f16_e32 v8, v51
	v_fmac_f32_e32 v78, v34, v8
	v_fmac_f32_e32 v79, v34, v9
	v_cvt_f32_f16_sdwa v9, v52 dst_sel:DWORD dst_unused:UNUSED_PAD src0_sel:WORD_1
	v_cvt_f32_f16_e32 v8, v52
	v_fmac_f32_e32 v72, v35, v8
	v_fmac_f32_e32 v73, v35, v9
	v_cvt_f32_f16_sdwa v9, v53 dst_sel:DWORD dst_unused:UNUSED_PAD src0_sel:WORD_1
	v_cvt_f32_f16_e32 v8, v53
	v_fmac_f32_e32 v74, v35, v8
	v_fmac_f32_e32 v75, v35, v9
	v_cvt_f32_f16_sdwa v9, v54 dst_sel:DWORD dst_unused:UNUSED_PAD src0_sel:WORD_1
	v_cvt_f32_f16_e32 v8, v54
	v_fmac_f32_e32 v76, v35, v8
	v_fmac_f32_e32 v77, v35, v9
	v_cvt_f32_f16_sdwa v9, v55 dst_sel:DWORD dst_unused:UNUSED_PAD src0_sel:WORD_1
	v_cvt_f32_f16_e32 v8, v55
	v_fmac_f32_e32 v78, v35, v8
	v_fmac_f32_e32 v79, v35, v9
	v_cvt_f32_f16_sdwa v9, v56 dst_sel:DWORD dst_unused:UNUSED_PAD src0_sel:WORD_1
	v_cvt_f32_f16_e32 v8, v56
	v_fmac_f32_e32 v72, v36, v8
	v_fmac_f32_e32 v73, v36, v9
	v_cvt_f32_f16_sdwa v9, v57 dst_sel:DWORD dst_unused:UNUSED_PAD src0_sel:WORD_1
	v_cvt_f32_f16_e32 v8, v57
	v_fmac_f32_e32 v74, v36, v8
	v_fmac_f32_e32 v75, v36, v9
	v_cvt_f32_f16_sdwa v9, v58 dst_sel:DWORD dst_unused:UNUSED_PAD src0_sel:WORD_1
	v_cvt_f32_f16_e32 v8, v58
	v_fmac_f32_e32 v76, v36, v8
	v_fmac_f32_e32 v77, v36, v9
	v_cvt_f32_f16_sdwa v9, v59 dst_sel:DWORD dst_unused:UNUSED_PAD src0_sel:WORD_1
	v_cvt_f32_f16_e32 v8, v59
	v_fmac_f32_e32 v78, v36, v8
	v_fmac_f32_e32 v79, v36, v9
	v_cvt_f32_f16_sdwa v9, v60 dst_sel:DWORD dst_unused:UNUSED_PAD src0_sel:WORD_1
	v_cvt_f32_f16_e32 v8, v60
	v_fmac_f32_e32 v72, v37, v8
	v_fmac_f32_e32 v73, v37, v9
	v_cvt_f32_f16_sdwa v9, v61 dst_sel:DWORD dst_unused:UNUSED_PAD src0_sel:WORD_1
	v_cvt_f32_f16_e32 v8, v61
	v_fmac_f32_e32 v74, v37, v8
	v_fmac_f32_e32 v75, v37, v9
	v_cvt_f32_f16_sdwa v9, v62 dst_sel:DWORD dst_unused:UNUSED_PAD src0_sel:WORD_1
	v_cvt_f32_f16_e32 v8, v62
	v_fmac_f32_e32 v76, v37, v8
	v_fmac_f32_e32 v77, v37, v9
	v_cvt_f32_f16_sdwa v9, v63 dst_sel:DWORD dst_unused:UNUSED_PAD src0_sel:WORD_1
	v_cvt_f32_f16_e32 v8, v63
	v_fmac_f32_e32 v78, v37, v8
	v_fmac_f32_e32 v79, v37, v9
	v_cvt_f32_f16_sdwa v9, v64 dst_sel:DWORD dst_unused:UNUSED_PAD src0_sel:WORD_1
	v_cvt_f32_f16_e32 v8, v64
	v_fmac_f32_e32 v72, v38, v8
	v_fmac_f32_e32 v73, v38, v9
	v_cvt_f32_f16_sdwa v9, v65 dst_sel:DWORD dst_unused:UNUSED_PAD src0_sel:WORD_1
	v_cvt_f32_f16_e32 v8, v65
	v_fmac_f32_e32 v74, v38, v8
	v_fmac_f32_e32 v75, v38, v9
	v_cvt_f32_f16_sdwa v9, v66 dst_sel:DWORD dst_unused:UNUSED_PAD src0_sel:WORD_1
	v_cvt_f32_f16_e32 v8, v66
	v_fmac_f32_e32 v76, v38, v8
	v_fmac_f32_e32 v77, v38, v9
	v_cvt_f32_f16_sdwa v9, v67 dst_sel:DWORD dst_unused:UNUSED_PAD src0_sel:WORD_1
	v_cvt_f32_f16_e32 v8, v67
	v_fmac_f32_e32 v78, v38, v8
	v_fmac_f32_e32 v79, v38, v9
	v_cvt_f32_f16_sdwa v9, v68 dst_sel:DWORD dst_unused:UNUSED_PAD src0_sel:WORD_1
	v_cvt_f32_f16_e32 v8, v68
	v_fmac_f32_e32 v72, v39, v8
	v_fmac_f32_e32 v73, v39, v9
	v_cvt_f32_f16_sdwa v9, v69 dst_sel:DWORD dst_unused:UNUSED_PAD src0_sel:WORD_1
	v_cvt_f32_f16_e32 v8, v69
	v_fmac_f32_e32 v74, v39, v8
	v_fmac_f32_e32 v75, v39, v9
	v_cvt_f32_f16_sdwa v9, v70 dst_sel:DWORD dst_unused:UNUSED_PAD src0_sel:WORD_1
	v_cvt_f32_f16_e32 v8, v70
	v_fmac_f32_e32 v76, v39, v8
	v_fmac_f32_e32 v77, v39, v9
	v_cvt_f32_f16_sdwa v9, v71 dst_sel:DWORD dst_unused:UNUSED_PAD src0_sel:WORD_1
	v_cvt_f32_f16_e32 v8, v71
	v_fmac_f32_e32 v78, v39, v8
	v_fmac_f32_e32 v79, v39, v9
	s_cmp_lt_u32 s20, 64
	s_cbranch_scc1 .Lagg_loop
	s_branch .Lagg_slow
.Lagg_lastc:
	v_lshlrev_b32_e32 v24, 1, v2
	global_load_dwordx4 v[16:19], v24, s[14:15]
	global_load_dwordx4 v[20:23], v24, s[14:15] offset:16
	v_cvt_f32_f16_sdwa v9, v40 dst_sel:DWORD dst_unused:UNUSED_PAD src0_sel:WORD_1
	v_cvt_f32_f16_e32 v8, v40
	v_fmac_f32_e32 v72, v32, v8
	v_fmac_f32_e32 v73, v32, v9
	v_cvt_f32_f16_sdwa v9, v41 dst_sel:DWORD dst_unused:UNUSED_PAD src0_sel:WORD_1
	v_cvt_f32_f16_e32 v8, v41
	v_fmac_f32_e32 v74, v32, v8
	v_fmac_f32_e32 v75, v32, v9
	v_cvt_f32_f16_sdwa v9, v42 dst_sel:DWORD dst_unused:UNUSED_PAD src0_sel:WORD_1
	v_cvt_f32_f16_e32 v8, v42
	v_fmac_f32_e32 v76, v32, v8
	v_fmac_f32_e32 v77, v32, v9
	v_cvt_f32_f16_sdwa v9, v43 dst_sel:DWORD dst_unused:UNUSED_PAD src0_sel:WORD_1
	v_cvt_f32_f16_e32 v8, v43
	v_fmac_f32_e32 v78, v32, v8
	v_fmac_f32_e32 v79, v32, v9
	v_cvt_f32_f16_sdwa v9, v44 dst_sel:DWORD dst_unused:UNUSED_PAD src0_sel:WORD_1
	v_cvt_f32_f16_e32 v8, v44
	v_fmac_f32_e32 v72, v33, v8
	v_fmac_f32_e32 v73, v33, v9
	v_cvt_f32_f16_sdwa v9, v45 dst_sel:DWORD dst_unused:UNUSED_PAD src0_sel:WORD_1
	v_cvt_f32_f16_e32 v8, v45
	v_fmac_f32_e32 v74, v33, v8
	v_fmac_f32_e32 v75, v33, v9
	v_cvt_f32_f16_sdwa v9, v46 dst_sel:DWORD dst_unused:UNUSED_PAD src0_sel:WORD_1
	v_cvt_f32_f16_e32 v8, v46
	v_fmac_f32_e32 v76, v33, v8
	v_fmac_f32_e32 v77, v33, v9
	v_cvt_f32_f16_sdwa v9, v47 dst_sel:DWORD dst_unused:UNUSED_PAD src0_sel:WORD_1
	v_cvt_f32_f16_e32 v8, v47
	v_fmac_f32_e32 v78, v33, v8
	v_fmac_f32_e32 v79, v33, v9
	v_cvt_f32_f16_sdwa v9, v48 dst_sel:DWORD dst_unused:UNUSED_PAD src0_sel:WORD_1
	v_cvt_f32_f16_e32 v8, v48
	v_fmac_f32_e32 v72, v34, v8
	v_fmac_f32_e32 v73, v34, v9
	v_cvt_f32_f16_sdwa v9, v49 dst_sel:DWORD dst_unused:UNUSED_PAD src0_sel:WORD_1
	v_cvt_f32_f16_e32 v8, v49
	v_fmac_f32_e32 v74, v34, v8
	v_fmac_f32_e32 v75, v34, v9
	v_cvt_f32_f16_sdwa v9, v50 dst_sel:DWORD dst_unused:UNUSED_PAD src0_sel:WORD_1
	v_cvt_f32_f16_e32 v8, v50
	v_fmac_f32_e32 v76, v34, v8
	v_fmac_f32_e32 v77, v34, v9
	v_cvt_f32_f16_sdwa v9, v51 dst_sel:DWORD dst_unused:UNUSED_PAD src0_sel:WORD_1
	v_cvt_f32_f16_e32 v8, v51
	v_fmac_f32_e32 v78, v34, v8
	v_fmac_f32_e32 v79, v34, v9
	v_cvt_f32_f16_sdwa v9, v52 dst_sel:DWORD dst_unused:UNUSED_PAD src0_sel:WORD_1
	v_cvt_f32_f16_e32 v8, v52
	v_fmac_f32_e32 v72, v35, v8
	v_fmac_f32_e32 v73, v35, v9
	v_cvt_f32_f16_sdwa v9, v53 dst_sel:DWORD dst_unused:UNUSED_PAD src0_sel:WORD_1
	v_cvt_f32_f16_e32 v8, v53
	v_fmac_f32_e32 v74, v35, v8
	v_fmac_f32_e32 v75, v35, v9
	v_cvt_f32_f16_sdwa v9, v54 dst_sel:DWORD dst_unused:UNUSED_PAD src0_sel:WORD_1
	v_cvt_f32_f16_e32 v8, v54
	v_fmac_f32_e32 v76, v35, v8
	v_fmac_f32_e32 v77, v35, v9
	v_cvt_f32_f16_sdwa v9, v55 dst_sel:DWORD dst_unused:UNUSED_PAD src0_sel:WORD_1
	v_cvt_f32_f16_e32 v8, v55
	v_fmac_f32_e32 v78, v35, v8
	v_fmac_f32_e32 v79, v35, v9
	v_cvt_f32_f16_sdwa v9, v56 dst_sel:DWORD dst_unused:UNUSED_PAD src0_sel:WORD_1
	v_cvt_f32_f16_e32 v8, v56
	v_fmac_f32_e32 v72, v36, v8
	v_fmac_f32_e32 v73, v36, v9
	v_cvt_f32_f16_sdwa v9, v57 dst_sel:DWORD dst_unused:UNUSED_PAD src0_sel:WORD_1
	v_cvt_f32_f16_e32 v8, v57
	v_fmac_f32_e32 v74, v36, v8
	v_fmac_f32_e32 v75, v36, v9
	v_cvt_f32_f16_sdwa v9, v58 dst_sel:DWORD dst_unused:UNUSED_PAD src0_sel:WORD_1
	v_cvt_f32_f16_e32 v8, v58
	v_fmac_f32_e32 v76, v36, v8
	v_fmac_f32_e32 v77, v36, v9
	v_cvt_f32_f16_sdwa v9, v59 dst_sel:DWORD dst_unused:UNUSED_PAD src0_sel:WORD_1
	v_cvt_f32_f16_e32 v8, v59
	v_fmac_f32_e32 v78, v36, v8
	v_fmac_f32_e32 v79, v36, v9
	v_cvt_f32_f16_sdwa v9, v60 dst_sel:DWORD dst_unused:UNUSED_PAD src0_sel:WORD_1
	v_cvt_f32_f16_e32 v8, v60
	v_fmac_f32_e32 v72, v37, v8
	v_fmac_f32_e32 v73, v37, v9
	v_cvt_f32_f16_sdwa v9, v61 dst_sel:DWORD dst_unused:UNUSED_PAD src0_sel:WORD_1
	v_cvt_f32_f16_e32 v8, v61
	v_fmac_f32_e32 v74, v37, v8
	v_fmac_f32_e32 v75, v37, v9
	v_cvt_f32_f16_sdwa v9, v62 dst_sel:DWORD dst_unused:UNUSED_PAD src0_sel:WORD_1
	v_cvt_f32_f16_e32 v8, v62
	v_fmac_f32_e32 v76, v37, v8
	v_fmac_f32_e32 v77, v37, v9
	v_cvt_f32_f16_sdwa v9, v63 dst_sel:DWORD dst_unused:UNUSED_PAD src0_sel:WORD_1
	v_cvt_f32_f16_e32 v8, v63
	v_fmac_f32_e32 v78, v37, v8
	v_fmac_f32_e32 v79, v37, v9
	v_cvt_f32_f16_sdwa v9, v64 dst_sel:DWORD dst_unused:UNUSED_PAD src0_sel:WORD_1
	v_cvt_f32_f16_e32 v8, v64
	v_fmac_f32_e32 v72, v38, v8
	v_fmac_f32_e32 v73, v38, v9
	v_cvt_f32_f16_sdwa v9, v65 dst_sel:DWORD dst_unused:UNUSED_PAD src0_sel:WORD_1
	v_cvt_f32_f16_e32 v8, v65
	v_fmac_f32_e32 v74, v38, v8
	v_fmac_f32_e32 v75, v38, v9
	v_cvt_f32_f16_sdwa v9, v66 dst_sel:DWORD dst_unused:UNUSED_PAD src0_sel:WORD_1
	v_cvt_f32_f16_e32 v8, v66
	v_fmac_f32_e32 v76, v38, v8
	v_fmac_f32_e32 v77, v38, v9
	v_cvt_f32_f16_sdwa v9, v67 dst_sel:DWORD dst_unused:UNUSED_PAD src0_sel:WORD_1
	v_cvt_f32_f16_e32 v8, v67
	v_fmac_f32_e32 v78, v38, v8
	v_fmac_f32_e32 v79, v38, v9
	v_cvt_f32_f16_sdwa v9, v68 dst_sel:DWORD dst_unused:UNUSED_PAD src0_sel:WORD_1
	v_cvt_f32_f16_e32 v8, v68
	v_fmac_f32_e32 v72, v39, v8
	v_fmac_f32_e32 v73, v39, v9
	v_cvt_f32_f16_sdwa v9, v69 dst_sel:DWORD dst_unused:UNUSED_PAD src0_sel:WORD_1
	v_cvt_f32_f16_e32 v8, v69
	v_fmac_f32_e32 v74, v39, v8
	v_fmac_f32_e32 v75, v39, v9
	v_cvt_f32_f16_sdwa v9, v70 dst_sel:DWORD dst_unused:UNUSED_PAD src0_sel:WORD_1
	v_cvt_f32_f16_e32 v8, v70
	v_fmac_f32_e32 v76, v39, v8
	v_fmac_f32_e32 v77, v39, v9
	v_cvt_f32_f16_sdwa v9, v71 dst_sel:DWORD dst_unused:UNUSED_PAD src0_sel:WORD_1
	v_cvt_f32_f16_e32 v8, v71
	v_fmac_f32_e32 v78, v39, v8
	v_fmac_f32_e32 v79, v39, v9
	s_branch .Lagg_epi
.Lagg_slow:
	s_waitcnt vmcnt(0)
	v_bfe_u32 v34, v0, 4, 1
.Lagg_slow_loop:
	v_cmp_lt_u32_e32 vcc, s20, v7
	s_cbranch_vccz .Lagg_slow_done
	v_add_u32_e32 v35, s20, v34
	v_mul_u32_u24_e32 v36, 0x3000, v1
	v_add3_u32 v36, v36, v35, s34
	v_lshlrev_b32_e32 v36, 3, v36
	global_load_dwordx2 v[16:17], v36, s[8:9]
	v_cmp_lt_u32_e64 s[40:41], v35, v7
	s_waitcnt vmcnt(0)
	v_cndmask_b32_e64 v16, v1, v16, s[40:41]
	v_cndmask_b32_e64 v17, 0, v17, s[40:41]
	v_lshlrev_b32_e32 v32, 2, v16
	v_lshl_add_u32 v16, v16, 8, v2
	global_load_dword v32, v32, s[6:7]
	global_load_dwordx4 v[40:43], v16, s[12:13]
	s_waitcnt vmcnt(0)
	v_add_f32_e32 v8, 1.0, v32
	v_mul_f32_e32 v10, 0x4b800000, v8
	v_cmp_gt_f32_e32 vcc, s33, v8
	s_nop 1
	v_cndmask_b32_e32 v10, v8, v10, vcc
	v_rsq_f32_e32 v11, v10
	s_nop 0
	v_mul_f32_e32 v10, 0x45800000, v11
	v_cndmask_b32_e32 v11, v11, v10, vcc
	v_cmp_lt_f32_e32 vcc, 0, v8
	s_nop 1
	v_cndmask_b32_e32 v11, 0, v11, vcc
	v_mul_f32_e32 v32, v17, v11
	v_cmp_eq_u32_e32 vcc, 0, v2
	s_and_b64 vcc, vcc, s[40:41]
	s_and_saveexec_b64 s[22:23], vcc
	global_store_dword v36, v32, s[8:9] offset:4
	s_mov_b64 exec, s[22:23]
	v_cvt_f32_f16_sdwa v11, v40 dst_sel:DWORD dst_unused:UNUSED_PAD src0_sel:WORD_1
	v_cvt_f32_f16_e32 v8, v40
	v_fmac_f32_e32 v72, v32, v8
	v_fmac_f32_e32 v73, v32, v11
	v_cvt_f32_f16_sdwa v11, v41 dst_sel:DWORD dst_unused:UNUSED_PAD src0_sel:WORD_1
	v_cvt_f32_f16_e32 v8, v41
	v_fmac_f32_e32 v74, v32, v8
	v_fmac_f32_e32 v75, v32, v11
	v_cvt_f32_f16_sdwa v11, v42 dst_sel:DWORD dst_unused:UNUSED_PAD src0_sel:WORD_1
	v_cvt_f32_f16_e32 v8, v42
	v_fmac_f32_e32 v76, v32, v8
	v_fmac_f32_e32 v77, v32, v11
	v_cvt_f32_f16_sdwa v11, v43 dst_sel:DWORD dst_unused:UNUSED_PAD src0_sel:WORD_1
	v_cvt_f32_f16_e32 v8, v43
	v_fmac_f32_e32 v78, v32, v8
	v_fmac_f32_e32 v79, v32, v11
	s_add_u32 s20, s20, 2
	s_branch .Lagg_slow_loop
.Lagg_slow_done:
	v_lshlrev_b32_e32 v24, 1, v2
	global_load_dwordx4 v[16:19], v24, s[14:15]
	global_load_dwordx4 v[20:23], v24, s[14:15] offset:16
.Lagg_epi:
	v_mov_b32_e32 v32, v72
	v_mov_b32_e32 v33, v73
	v_mov_b32_e32 v34, v74
	v_mov_b32_e32 v35, v75
	v_mov_b32_e32 v36, v76
	v_mov_b32_e32 v37, v77
	v_mov_b32_e32 v38, v78
	v_mov_b32_e32 v39, v79
	s_nop 1
	v_permlane16_swap_b32_e32 v72, v32
	v_permlane16_swap_b32_e32 v73, v33
	v_permlane16_swap_b32_e32 v74, v34
	v_permlane16_swap_b32_e32 v75, v35
	v_permlane16_swap_b32_e32 v76, v36
	v_permlane16_swap_b32_e32 v77, v37
	v_permlane16_swap_b32_e32 v78, v38
	v_permlane16_swap_b32_e32 v79, v39
	v_add_f32_e32 v72, v72, v32
	v_add_f32_e32 v73, v73, v33
	v_add_f32_e32 v74, v74, v34
	v_add_f32_e32 v75, v75, v35
	v_add_f32_e32 v76, v76, v36
	v_add_f32_e32 v77, v77, v37
	v_add_f32_e32 v78, v78, v38
	v_add_f32_e32 v79, v79, v39
	v_add_f32_e32 v8, 1.0, v5
	v_mul_f32_e32 v10, 0x4b800000, v8
	v_cmp_gt_f32_e32 vcc, s33, v8
	s_nop 1
	v_cndmask_b32_e32 v10, v8, v10, vcc
	v_rsq_f32_e32 v11, v10
	s_nop 0
	v_mul_f32_e32 v10, 0x45800000, v11
	v_cndmask_b32_e32 v11, v11, v10, vcc
	v_cmp_lt_f32_e32 vcc, 0, v8
	s_nop 1
	v_cndmask_b32_e32 v5, 0, v11, vcc
	s_waitcnt vmcnt(0)
	v_cvt_f32_f16_sdwa v9, v12 dst_sel:DWORD dst_unused:UNUSED_PAD src0_sel:WORD_1
	v_cvt_f32_f16_e32 v8, v12
	v_fma_f32 v8, v5, v8, v72
	v_fma_f32 v9, v5, v9, v73
	v_fma_f32 v40, v5, v8, v16
	v_fma_f32 v41, v5, v9, v17
	v_cvt_f32_f16_sdwa v9, v13 dst_sel:DWORD dst_unused:UNUSED_PAD src0_sel:WORD_1
	v_cvt_f32_f16_e32 v8, v13
	v_fma_f32 v8, v5, v8, v74
	v_fma_f32 v9, v5, v9, v75
	v_fma_f32 v42, v5, v8, v18
	v_fma_f32 v43, v5, v9, v19
	v_cvt_f32_f16_sdwa v9, v14 dst_sel:DWORD dst_unused:UNUSED_PAD src0_sel:WORD_1
	v_cvt_f32_f16_e32 v8, v14
	v_fma_f32 v8, v5, v8, v76
	v_fma_f32 v9, v5, v9, v77
	v_fma_f32 v44, v5, v8, v20
	v_fma_f32 v45, v5, v9, v21
	v_cvt_f32_f16_sdwa v9, v15 dst_sel:DWORD dst_unused:UNUSED_PAD src0_sel:WORD_1
	v_cvt_f32_f16_e32 v8, v15
	v_fma_f32 v8, v5, v8, v78
	v_fma_f32 v9, v5, v9, v79
	v_fma_f32 v46, v5, v8, v22
	v_fma_f32 v47, v5, v9, v23
	v_cvt_pk_f16_f32 v24, v40, v41
	v_cvt_pk_f16_f32 v25, v42, v43
	v_cvt_pk_f16_f32 v26, v44, v45
	v_cvt_pk_f16_f32 v27, v46, v47
	v_lshl_add_u32 v8, v1, 8, v2
	v_bfe_u32 v9, v0, 4, 1
	v_cmp_eq_u32_e32 vcc, 0, v9
	s_and_saveexec_b64 s[22:23], vcc
	global_store_dwordx4 v8, v[24:27], s[16:17]
	s_mov_b64 exec, s[22:23]
	v_mul_f32_e32 v48, v40, v40
	v_mul_f32_e32 v49, v41, v41
	v_mul_f32_e32 v50, v42, v42
	v_mul_f32_e32 v51, v43, v43
	v_mul_f32_e32 v52, v44, v44
	v_mul_f32_e32 v53, v45, v45
	v_mul_f32_e32 v54, v46, v46
	v_mul_f32_e32 v55, v47, v47
	v_mov_b32_e32 v56, v40
	v_mov_b32_e32 v64, v48
	v_mov_b32_e32 v57, v41
	v_mov_b32_e32 v65, v49
	v_mov_b32_e32 v58, v42
	v_mov_b32_e32 v66, v50
	v_mov_b32_e32 v59, v43
	v_mov_b32_e32 v67, v51
	v_mov_b32_e32 v60, v44
	v_mov_b32_e32 v68, v52
	v_mov_b32_e32 v61, v45
	v_mov_b32_e32 v69, v53
	v_mov_b32_e32 v62, v46
	v_mov_b32_e32 v70, v54
	v_mov_b32_e32 v63, v47
	v_mov_b32_e32 v71, v55
	s_nop 1
	v_permlane32_swap_b32_e32 v40, v56
	v_permlane32_swap_b32_e32 v48, v64
	v_permlane32_swap_b32_e32 v41, v57
	v_permlane32_swap_b32_e32 v49, v65
	v_permlane32_swap_b32_e32 v42, v58
	v_permlane32_swap_b32_e32 v50, v66
	v_permlane32_swap_b32_e32 v43, v59
	v_permlane32_swap_b32_e32 v51, v67
	v_permlane32_swap_b32_e32 v44, v60
	v_permlane32_swap_b32_e32 v52, v68
	v_permlane32_swap_b32_e32 v45, v61
	v_permlane32_swap_b32_e32 v53, v69
	v_permlane32_swap_b32_e32 v46, v62
	v_permlane32_swap_b32_e32 v54, v70
	v_permlane32_swap_b32_e32 v47, v63
	v_permlane32_swap_b32_e32 v55, v71
	v_add_f32_e32 v40, v40, v56
	v_add_f32_e32 v48, v48, v64
	v_add_f32_e32 v41, v41, v57
	v_add_f32_e32 v49, v49, v65
	v_add_f32_e32 v42, v42, v58
	v_add_f32_e32 v50, v50, v66
	v_add_f32_e32 v43, v43, v59
	v_add_f32_e32 v51, v51, v67
	v_add_f32_e32 v44, v44, v60
	v_add_f32_e32 v52, v52, v68
	v_add_f32_e32 v45, v45, v61
	v_add_f32_e32 v53, v53, v69
	v_add_f32_e32 v46, v46, v62
	v_add_f32_e32 v54, v54, v70
	v_add_f32_e32 v47, v47, v63
	v_add_f32_e32 v55, v55, v71
	s_lshl_b32 s25, s3, 10
	v_lshl_add_u32 v8, v2, 1, s25
	v_and_b32_e32 v9, 63, v0
	v_cmp_gt_u32_e32 vcc, 16, v9
	s_and_saveexec_b64 s[22:23], vcc
	ds_write_b128 v8, v[40:43]
	ds_write_b128 v8, v[44:47] offset:16
	ds_write_b128 v8, v[48:51] offset:512
	ds_write_b128 v8, v[52:55] offset:528
	s_mov_b64 exec, s[22:23]
	s_waitcnt lgkmcnt(0)
	s_barrier
	v_cmp_gt_u32_e32 vcc, 0x100, v0
	s_and_saveexec_b64 s[22:23], vcc
	s_cbranch_execz .Lagg_end
	v_lshlrev_b32_e32 v8, 2, v0
	ds_read_b32 v16, v8 offset:0
	ds_read_b32 v17, v8 offset:1024
	ds_read_b32 v18, v8 offset:2048
	ds_read_b32 v19, v8 offset:3072
	ds_read_b32 v20, v8 offset:4096
	ds_read_b32 v21, v8 offset:5120
	ds_read_b32 v22, v8 offset:6144
	ds_read_b32 v23, v8 offset:7168
	s_and_b32 s25, s2, 7
	s_lshl_b32 s25, s25, 10
	v_add_u32_e32 v8, s25, v8
	s_waitcnt lgkmcnt(0)
	v_add_f32_e32 v16, v16, v17
	v_add_f32_e32 v18, v18, v19
	v_add_f32_e32 v20, v20, v21
	v_add_f32_e32 v22, v22, v23
	v_add_f32_e32 v16, v16, v18
	v_add_f32_e32 v20, v20, v22
	v_add_f32_e32 v16, v16, v20
	global_atomic_add_f32 v8, v16, s[18:19]

	.amdhsa_kernel _Z10agg_kernelILi128ELb1EEvPKiPKfP15HIP_vector_typeIiLj2EES6_PKDF16_S3_PDF16_Pf
		.amdhsa_group_segment_fixed_size 8192
		.amdhsa_private_segment_fixed_size 0
		.amdhsa_kernarg_size 64
		.amdhsa_user_sgpr_count 2
		.amdhsa_user_sgpr_dispatch_ptr 0
		.amdhsa_user_sgpr_queue_ptr 0
		.amdhsa_user_sgpr_kernarg_segment_ptr 1
		.amdhsa_user_sgpr_dispatch_id 0
		.amdhsa_user_sgpr_kernarg_preload_length 0
		.amdhsa_user_sgpr_kernarg_preload_offset 0
		.amdhsa_user_sgpr_private_segment_size 0
		.amdhsa_uses_dynamic_stack 0
		.amdhsa_enable_private_segment 0
		.amdhsa_system_sgpr_workgroup_id_x 1
		.amdhsa_system_sgpr_workgroup_id_y 0
		.amdhsa_system_sgpr_workgroup_id_z 0
		.amdhsa_system_sgpr_workgroup_info 0
		.amdhsa_system_vgpr_workitem_id 0
		.amdhsa_next_free_vgpr 80
		.amdhsa_next_free_sgpr 60
		.amdhsa_accum_offset 80
		.amdhsa_reserve_vcc 1
		.amdhsa_float_round_mode_32 0
		.amdhsa_float_round_mode_16_64 0
		.amdhsa_float_denorm_mode_32 3
		.amdhsa_float_denorm_mode_16_64 3
		.amdhsa_dx10_clamp 1
		.amdhsa_ieee_mode 1
		.amdhsa_fp16_overflow 0
		.amdhsa_tg_split 0
		.amdhsa_exception_fp_ieee_invalid_op 0
		.amdhsa_exception_fp_denorm_src 0
		.amdhsa_exception_fp_ieee_div_zero 0
		.amdhsa_exception_fp_ieee_overflow 0
		.amdhsa_exception_fp_ieee_underflow 0
		.amdhsa_exception_fp_ieee_inexact 0
		.amdhsa_exception_int_div_zero 0
	.end_amdhsa_kernel

amdhsa.kernels:
  - .agpr_count:     0
    .args:
      - .actual_access:  read_only
        .address_space:  global
        .offset:         0
        .size:           8
        .value_kind:     global_buffer
      - .actual_access:  read_only
        .address_space:  global
        .offset:         8
        .size:           8
        .value_kind:     global_buffer
      - .actual_access:  read_only
        .address_space:  global
        .offset:         16
        .size:           8
        .value_kind:     global_buffer
      - .actual_access:  write_only
        .address_space:  global
        .offset:         24
        .size:           8
        .value_kind:     global_buffer
      - .address_space:  global
        .offset:         32
        .size:           8
        .value_kind:     global_buffer
      - .address_space:  global
        .offset:         40
        .size:           8
        .value_kind:     global_buffer
      - .actual_access:  write_only
        .address_space:  global
        .offset:         48
        .size:           8
        .value_kind:     global_buffer
      - .actual_access:  write_only
        .address_space:  global
        .offset:         56
        .size:           8
        .value_kind:     global_buffer
    .group_segment_fixed_size: 37392
    .kernarg_segment_align: 8
    .kernarg_segment_size: 64
    .language:       OpenCL C
    .language_version:
      - 2
      - 0
    .max_flat_workgroup_size: 256
    .name:           _Z9k1_kernelPKfS0_S0_PDF16_PiPfP15HIP_vector_typeIiLj2EES6_
    .private_segment_fixed_size: 0
    .sgpr_count:     32
    .sgpr_spill_count: 0
    .symbol:         _Z9k1_kernelPKfS0_S0_PDF16_PiPfP15HIP_vector_typeIiLj2EES6_.kd
    .uniform_work_group_size: 1
    .uses_dynamic_stack: false
    .vgpr_count:     120
    .vgpr_spill_count: 0
    .wavefront_size: 64
  - .agpr_count:     0
    .args:
      - .actual_access:  read_only
        .address_space:  global
        .offset:         0
        .size:           8
        .value_kind:     global_buffer
      - .actual_access:  read_only
        .address_space:  global
        .offset:         8
        .size:           8
        .value_kind:     global_buffer
      - .actual_access:  read_only
        .address_space:  global
        .offset:         16
        .size:           8
        .value_kind:     global_buffer
      - .actual_access:  read_only
        .address_space:  global
        .offset:         24
        .size:           8
        .value_kind:     global_buffer
      - .actual_access:  read_only
        .address_space:  global
        .offset:         32
        .size:           8
        .value_kind:     global_buffer
      - .actual_access:  read_only
        .address_space:  global
        .offset:         40
        .size:           8
        .value_kind:     global_buffer
      - .actual_access:  read_only
        .address_space:  global
        .offset:         48
        .size:           8
        .value_kind:     global_buffer
      - .actual_access:  read_only
        .address_space:  global
        .offset:         56
        .size:           8
        .value_kind:     global_buffer
      - .actual_access:  read_only
        .address_space:  global
        .offset:         64
        .size:           8
        .value_kind:     global_buffer
      - .actual_access:  write_only
        .address_space:  global
        .offset:         72
        .size:           8
        .value_kind:     global_buffer
      - .address_space:  global
        .offset:         80
        .size:           8
        .value_kind:     global_buffer
    .group_segment_fixed_size: 44224
    .kernarg_segment_align: 8
    .kernarg_segment_size: 88
    .language:       OpenCL C
    .language_version:
      - 2
      - 0
    .max_flat_workgroup_size: 512
    .name:           _Z11agg2_kernelPKiPKfPK15HIP_vector_typeIiLj2EEPKDF16_S2_S2_S2_S2_S2_PfS9_
    .private_segment_fixed_size: 0
    .sgpr_count:     41
    .sgpr_spill_count: 0
    .symbol:         _Z11agg2_kernelPKiPKfPK15HIP_vector_typeIiLj2EEPKDF16_S2_S2_S2_S2_S2_PfS9_.kd
    .uniform_work_group_size: 1
    .uses_dynamic_stack: false
    .vgpr_count:     80
    .vgpr_spill_count: 0
    .wavefront_size: 64
  - .agpr_count:     0
    .args:
      - .actual_access:  read_only
        .address_space:  global
        .offset:         0
        .size:           8
        .value_kind:     global_buffer
      - .actual_access:  read_only
        .address_space:  global
        .offset:         8
        .size:           8
        .value_kind:     global_buffer
      - .actual_access:  read_only
        .address_space:  global
        .offset:         16
        .size:           8
        .value_kind:     global_buffer
      - .actual_access:  read_only
        .address_space:  global
        .offset:         24
        .size:           8
        .value_kind:     global_buffer
      - .actual_access:  write_only
        .address_space:  global
        .offset:         32
        .size:           8
        .value_kind:     global_buffer
      - .offset:         40
        .size:           4
        .value_kind:     hidden_block_count_x
      - .offset:         44
        .size:           4
        .value_kind:     hidden_block_count_y
      - .offset:         48
        .size:           4
        .value_kind:     hidden_block_count_z
      - .offset:         52
        .size:           2
        .value_kind:     hidden_group_size_x
      - .offset:         54
        .size:           2
        .value_kind:     hidden_group_size_y
      - .offset:         56
        .size:           2
        .value_kind:     hidden_group_size_z
      - .offset:         58
        .size:           2
        .value_kind:     hidden_remainder_x
      - .offset:         60
        .size:           2
        .value_kind:     hidden_remainder_y
      - .offset:         62
        .size:           2
        .value_kind:     hidden_remainder_z
      - .offset:         80
        .size:           8
        .value_kind:     hidden_global_offset_x
      - .offset:         88
        .size:           8
        .value_kind:     hidden_global_offset_y
      - .offset:         96
        .size:           8
        .value_kind:     hidden_global_offset_z
      - .offset:         104
        .size:           2
        .value_kind:     hidden_grid_dims
    .group_segment_fixed_size: 512
    .kernarg_segment_align: 8
    .kernarg_segment_size: 296
    .language:       OpenCL C
    .language_version:
      - 2
      - 0
    .max_flat_workgroup_size: 256
    .name:           _Z12final_kernelPKfS0_S0_S0_Pf
    .private_segment_fixed_size: 0
    .sgpr_count:     18
    .sgpr_spill_count: 0
    .symbol:         _Z12final_kernelPKfS0_S0_S0_Pf.kd
    .uniform_work_group_size: 1
    .uses_dynamic_stack: false
    .vgpr_count:     36
    .vgpr_spill_count: 0
    .wavefront_size: 64
  - .agpr_count:     0
    .args:
      - .actual_access:  read_only
        .address_space:  global
        .offset:         0
        .size:           8
        .value_kind:     global_buffer
      - .actual_access:  read_only
        .address_space:  global
        .offset:         8
        .size:           8
        .value_kind:     global_buffer
      - .address_space:  global
        .offset:         16
        .size:           8
        .value_kind:     global_buffer
      - .address_space:  global
        .offset:         24
        .size:           8
        .value_kind:     global_buffer
      - .actual_access:  read_only
        .address_space:  global
        .offset:         32
        .size:           8
        .value_kind:     global_buffer
      - .actual_access:  read_only
        .address_space:  global
        .offset:         40
        .size:           8
        .value_kind:     global_buffer
      - .actual_access:  write_only
        .address_space:  global
        .offset:         48
        .size:           8
        .value_kind:     global_buffer
      - .address_space:  global
        .offset:         56
        .size:           8
        .value_kind:     global_buffer
    .group_segment_fixed_size: 8192
    .kernarg_segment_align: 8
    .kernarg_segment_size: 64
    .language:       OpenCL C
    .language_version:
      - 2
      - 0
    .max_flat_workgroup_size: 512
    .name:           _Z10agg_kernelILi128ELb1EEvPKiPKfP15HIP_vector_typeIiLj2EES6_PKDF16_S3_PDF16_Pf
    .private_segment_fixed_size: 0
    .sgpr_count:     66
    .sgpr_spill_count: 0
    .symbol:         _Z10agg_kernelILi128ELb1EEvPKiPKfP15HIP_vector_typeIiLj2EES6_PKDF16_S3_PDF16_Pf.kd
    .uniform_work_group_size: 1
    .uses_dynamic_stack: false
    .vgpr_count:     80
    .vgpr_spill_count: 0
    .wavefront_size: 64
